# all packed f32 VALU ops replaced by scalar halves (blanket), on top of v102
# baseline (speedup 1.0000x reference)
.LBB0_184:
	s_lshl_b32 s12, s12, 6
	s_ashr_i32 s13, s12, 31
	s_lshl_b64 s[12:13], s[12:13], 1
	s_add_u32 s12, s0, s12
	s_addc_u32 s13, s1, s13
	v_mov_b32_e32 v139, v44
	v_add_u32_e32 v45, s14, v144
	v_lshl_add_u64 v[46:47], s[12:13], 0, v[138:139]
	v_cmp_gt_i32_e32 vcc, s26, v45
	v_add_u32_e32 v45, 0x400, v145
	s_and_saveexec_b64 s[12:13], vcc
	s_cbranch_execz .LBB0_186
	ds_read2_b32 v[140:141], v45 offset0:152 offset1:220
	ds_read2_b32 v[158:159], v45 offset0:16 offset1:84
	ds_read2_b32 v[162:163], v145 offset0:136 offset1:204
	ds_read2_b32 v[164:165], v145 offset1:68
	v_add_u32_e32 v137, s3, v144
	s_waitcnt lgkmcnt(3)
	v_mul_f32_e64 v140, s2, v140
	v_mul_f32_e64 v141, s2, v141
	s_waitcnt lgkmcnt(2)
	v_mul_f32_e64 v158, s2, v158
	v_mul_f32_e64 v159, s2, v159
	v_cvt_pk_bf16_f32 v161, v140, v141
	s_waitcnt lgkmcnt(1)
	v_mul_f32_e64 v140, s2, v162
	v_mul_f32_e64 v141, s2, v163
	v_cvt_pk_bf16_f32 v160, v158, v159
	v_cvt_pk_bf16_f32 v159, v140, v141
	s_waitcnt lgkmcnt(0)
	v_mul_f32_e64 v140, s2, v164
	v_mul_f32_e64 v141, s2, v165
	v_cvt_pk_bf16_f32 v158, v140, v141
	v_mad_u64_u32 v[140:141], s[16:17], v137, s23, 0
	v_ashrrev_i32_e32 v139, 31, v137
	v_mov_b32_e32 v162, v141
	v_mad_u64_u32 v[162:163], s[16:17], v139, s23, v[162:163]
	v_mov_b32_e32 v141, v162
	v_lshl_add_u64 v[140:141], v[140:141], 1, v[46:47]
	global_store_dwordx4 v[140:141], v[158:161], off
.LBB0_186:
	s_or_b64 exec, exec, s[12:13]
	v_add_u32_e32 v137, s14, v146
	v_cmp_gt_i32_e32 vcc, s26, v137
	s_and_saveexec_b64 s[12:13], vcc
	s_cbranch_execz .LBB0_188
	ds_read2_b32 v[140:141], v45 offset0:160 offset1:228
	ds_read2_b32 v[158:159], v45 offset0:24 offset1:92
	ds_read2_b32 v[162:163], v145 offset0:144 offset1:212
	ds_read2_b32 v[164:165], v145 offset0:8 offset1:76
	v_add_u32_e32 v137, s3, v146
	s_waitcnt lgkmcnt(3)
	v_mul_f32_e64 v140, s2, v140
	v_mul_f32_e64 v141, s2, v141
	s_waitcnt lgkmcnt(2)
	v_mul_f32_e64 v158, s2, v158
	v_mul_f32_e64 v159, s2, v159
	v_cvt_pk_bf16_f32 v161, v140, v141
	s_waitcnt lgkmcnt(1)
	v_mul_f32_e64 v140, s2, v162
	v_mul_f32_e64 v141, s2, v163
	v_cvt_pk_bf16_f32 v160, v158, v159
	v_cvt_pk_bf16_f32 v159, v140, v141
	s_waitcnt lgkmcnt(0)
	v_mul_f32_e64 v140, s2, v164
	v_mul_f32_e64 v141, s2, v165
	v_cvt_pk_bf16_f32 v158, v140, v141
	v_mad_u64_u32 v[140:141], s[16:17], v137, s23, 0
	v_ashrrev_i32_e32 v139, 31, v137
	v_mov_b32_e32 v162, v141
	v_mad_u64_u32 v[162:163], s[16:17], v139, s23, v[162:163]
	v_mov_b32_e32 v141, v162
	v_lshl_add_u64 v[140:141], v[140:141], 1, v[46:47]
	global_store_dwordx4 v[140:141], v[158:161], off
.LBB0_188:
	s_or_b64 exec, exec, s[12:13]
	v_add_u32_e32 v137, s14, v147
	v_cmp_gt_i32_e32 vcc, s26, v137
	s_and_saveexec_b64 s[12:13], vcc
	s_cbranch_execz .LBB0_190
	ds_read2_b32 v[140:141], v45 offset0:168 offset1:236
	ds_read2_b32 v[158:159], v45 offset0:32 offset1:100
	ds_read2_b32 v[162:163], v145 offset0:152 offset1:220
	ds_read2_b32 v[164:165], v145 offset0:16 offset1:84
	v_add_u32_e32 v137, s3, v147
	s_waitcnt lgkmcnt(3)
	v_mul_f32_e64 v140, s2, v140
	v_mul_f32_e64 v141, s2, v141
	s_waitcnt lgkmcnt(2)
	v_mul_f32_e64 v158, s2, v158
	v_mul_f32_e64 v159, s2, v159
	v_cvt_pk_bf16_f32 v161, v140, v141
	s_waitcnt lgkmcnt(1)
	v_mul_f32_e64 v140, s2, v162
	v_mul_f32_e64 v141, s2, v163
	v_cvt_pk_bf16_f32 v160, v158, v159
	v_cvt_pk_bf16_f32 v159, v140, v141
	s_waitcnt lgkmcnt(0)
	v_mul_f32_e64 v140, s2, v164
	v_mul_f32_e64 v141, s2, v165
	v_cvt_pk_bf16_f32 v158, v140, v141
	v_mad_u64_u32 v[140:141], s[16:17], v137, s23, 0
	v_ashrrev_i32_e32 v139, 31, v137
	v_mov_b32_e32 v162, v141
	v_mad_u64_u32 v[162:163], s[16:17], v139, s23, v[162:163]
	v_mov_b32_e32 v141, v162
	v_lshl_add_u64 v[140:141], v[140:141], 1, v[46:47]
	global_store_dwordx4 v[140:141], v[158:161], off
.LBB0_190:
	s_or_b64 exec, exec, s[12:13]
	v_add_u32_e32 v137, s14, v148
	v_cmp_gt_i32_e32 vcc, s26, v137
	s_and_saveexec_b64 s[12:13], vcc
	s_cbranch_execz .LBB0_192
	ds_read2_b32 v[140:141], v45 offset0:176 offset1:244
	ds_read2_b32 v[158:159], v45 offset0:40 offset1:108
	ds_read2_b32 v[162:163], v145 offset0:160 offset1:228
	ds_read2_b32 v[164:165], v145 offset0:24 offset1:92
	v_add_u32_e32 v137, s3, v148
	s_waitcnt lgkmcnt(3)
	v_mul_f32_e64 v140, s2, v140
	v_mul_f32_e64 v141, s2, v141
	s_waitcnt lgkmcnt(2)
	v_mul_f32_e64 v158, s2, v158
	v_mul_f32_e64 v159, s2, v159
	v_cvt_pk_bf16_f32 v161, v140, v141
	s_waitcnt lgkmcnt(1)
	v_mul_f32_e64 v140, s2, v162
	v_mul_f32_e64 v141, s2, v163
	v_cvt_pk_bf16_f32 v160, v158, v159
	v_cvt_pk_bf16_f32 v159, v140, v141
	s_waitcnt lgkmcnt(0)
	v_mul_f32_e64 v140, s2, v164
	v_mul_f32_e64 v141, s2, v165
	v_cvt_pk_bf16_f32 v158, v140, v141
	v_mad_u64_u32 v[140:141], s[16:17], v137, s23, 0
	v_ashrrev_i32_e32 v139, 31, v137
	v_mov_b32_e32 v162, v141
	v_mad_u64_u32 v[162:163], s[16:17], v139, s23, v[162:163]
	v_mov_b32_e32 v141, v162
	v_lshl_add_u64 v[140:141], v[140:141], 1, v[46:47]
	global_store_dwordx4 v[140:141], v[158:161], off
.LBB0_192:
	s_or_b64 exec, exec, s[12:13]
	v_add_u32_e32 v137, s14, v149
	v_cmp_gt_i32_e32 vcc, s26, v137
	s_and_saveexec_b64 s[12:13], vcc
	s_cbranch_execz .LBB0_194
	ds_read2_b32 v[140:141], v45 offset0:184 offset1:252
	ds_read2_b32 v[158:159], v45 offset0:48 offset1:116
	ds_read2_b32 v[162:163], v145 offset0:168 offset1:236
	ds_read2_b32 v[164:165], v145 offset0:32 offset1:100
	v_add_u32_e32 v137, s3, v149
	s_waitcnt lgkmcnt(3)
	v_mul_f32_e64 v140, s2, v140
	v_mul_f32_e64 v141, s2, v141
	s_waitcnt lgkmcnt(2)
	v_mul_f32_e64 v158, s2, v158
	v_mul_f32_e64 v159, s2, v159
	v_cvt_pk_bf16_f32 v161, v140, v141
	s_waitcnt lgkmcnt(1)
	v_mul_f32_e64 v140, s2, v162
	v_mul_f32_e64 v141, s2, v163
	v_cvt_pk_bf16_f32 v160, v158, v159
	v_cvt_pk_bf16_f32 v159, v140, v141
	s_waitcnt lgkmcnt(0)
	v_mul_f32_e64 v140, s2, v164
	v_mul_f32_e64 v141, s2, v165
	v_cvt_pk_bf16_f32 v158, v140, v141
	v_mad_u64_u32 v[140:141], s[16:17], v137, s23, 0
	v_ashrrev_i32_e32 v139, 31, v137
	v_mov_b32_e32 v162, v141
	v_mad_u64_u32 v[162:163], s[16:17], v139, s23, v[162:163]
	v_mov_b32_e32 v141, v162
	v_lshl_add_u64 v[140:141], v[140:141], 1, v[46:47]
	global_store_dwordx4 v[140:141], v[158:161], off
.LBB0_194:
	s_or_b64 exec, exec, s[12:13]
	v_add_u32_e32 v137, s14, v150
	v_cmp_gt_i32_e32 vcc, s26, v137
	v_add_u32_e32 v137, 0x600, v145
	s_and_saveexec_b64 s[12:13], vcc
	s_cbranch_execz .LBB0_196
	ds_read2_b32 v[140:141], v137 offset0:64 offset1:132
	ds_read2_b32 v[158:159], v45 offset0:56 offset1:124
	ds_read2_b32 v[162:163], v145 offset0:176 offset1:244
	ds_read2_b32 v[164:165], v145 offset0:40 offset1:108
	v_add_u32_e32 v139, s3, v150
	s_waitcnt lgkmcnt(3)
	v_mul_f32_e64 v140, s2, v140
	v_mul_f32_e64 v141, s2, v141
	s_waitcnt lgkmcnt(2)
	v_mul_f32_e64 v158, s2, v158
	v_mul_f32_e64 v159, s2, v159
	v_cvt_pk_bf16_f32 v161, v140, v141
	s_waitcnt lgkmcnt(1)
	v_mul_f32_e64 v140, s2, v162
	v_mul_f32_e64 v141, s2, v163
	v_cvt_pk_bf16_f32 v160, v158, v159
	v_cvt_pk_bf16_f32 v159, v140, v141
	s_waitcnt lgkmcnt(0)
	v_mul_f32_e64 v140, s2, v164
	v_mul_f32_e64 v141, s2, v165
	v_cvt_pk_bf16_f32 v158, v140, v141
	v_mad_u64_u32 v[140:141], s[16:17], v139, s23, 0
	v_ashrrev_i32_e32 v157, 31, v139
	v_mov_b32_e32 v162, v141
	v_mad_u64_u32 v[162:163], s[16:17], v157, s23, v[162:163]
	v_mov_b32_e32 v141, v162
	v_lshl_add_u64 v[140:141], v[140:141], 1, v[46:47]
	global_store_dwordx4 v[140:141], v[158:161], off
.LBB0_196:
	s_or_b64 exec, exec, s[12:13]
	v_add_u32_e32 v139, s14, v151
	v_cmp_gt_i32_e32 vcc, s26, v139
	s_and_saveexec_b64 s[12:13], vcc
	s_cbranch_execz .LBB0_198
	ds_read2_b32 v[140:141], v137 offset0:72 offset1:140
	ds_read2_b32 v[158:159], v45 offset0:64 offset1:132
	ds_read2_b32 v[162:163], v145 offset0:184 offset1:252
	ds_read2_b32 v[164:165], v145 offset0:48 offset1:116
	v_add_u32_e32 v139, s3, v151
	s_waitcnt lgkmcnt(3)
	v_mul_f32_e64 v140, s2, v140
	v_mul_f32_e64 v141, s2, v141
	s_waitcnt lgkmcnt(2)
	v_mul_f32_e64 v158, s2, v158
	v_mul_f32_e64 v159, s2, v159
	v_cvt_pk_bf16_f32 v161, v140, v141
	s_waitcnt lgkmcnt(1)
	v_mul_f32_e64 v140, s2, v162
	v_mul_f32_e64 v141, s2, v163
	v_cvt_pk_bf16_f32 v160, v158, v159
	v_cvt_pk_bf16_f32 v159, v140, v141
	s_waitcnt lgkmcnt(0)
	v_mul_f32_e64 v140, s2, v164
	v_mul_f32_e64 v141, s2, v165
	v_cvt_pk_bf16_f32 v158, v140, v141
	v_mad_u64_u32 v[140:141], s[16:17], v139, s23, 0
	v_ashrrev_i32_e32 v157, 31, v139
	v_mov_b32_e32 v162, v141
	v_mad_u64_u32 v[162:163], s[16:17], v157, s23, v[162:163]
	v_mov_b32_e32 v141, v162
	v_lshl_add_u64 v[140:141], v[140:141], 1, v[46:47]
	global_store_dwordx4 v[140:141], v[158:161], off
.LBB0_198:
	s_or_b64 exec, exec, s[12:13]
	v_add_u32_e32 v139, s14, v152
	v_cmp_gt_i32_e32 vcc, s26, v139
	s_and_saveexec_b64 s[12:13], vcc
	s_cbranch_execz .LBB0_200
	ds_read2_b32 v[140:141], v137 offset0:80 offset1:148
	ds_read2_b32 v[158:159], v45 offset0:72 offset1:140
	v_add_u32_e32 v45, 0x200, v145
	ds_read2_b32 v[162:163], v145 offset0:56 offset1:124
	ds_read2_b32 v[164:165], v45 offset0:64 offset1:132
	v_add_u32_e32 v45, s3, v152
	s_waitcnt lgkmcnt(3)
	v_mul_f32_e64 v140, s2, v140
	v_mul_f32_e64 v141, s2, v141
	v_cvt_pk_bf16_f32 v161, v140, v141
	s_waitcnt lgkmcnt(2)
	v_mul_f32_e64 v140, s2, v158
	v_mul_f32_e64 v141, s2, v159
	v_cvt_pk_bf16_f32 v160, v140, v141
	s_waitcnt lgkmcnt(0)
	v_mul_f32_e64 v140, s2, v164
	v_mul_f32_e64 v141, s2, v165
	v_cvt_pk_bf16_f32 v159, v140, v141
	v_mul_f32_e64 v140, s2, v162
	v_mul_f32_e64 v141, s2, v163
	v_cvt_pk_bf16_f32 v158, v140, v141
	v_mad_u64_u32 v[140:141], s[2:3], v45, s23, 0
	v_ashrrev_i32_e32 v137, 31, v45
	v_mov_b32_e32 v162, v141
	v_mad_u64_u32 v[162:163], s[2:3], v137, s23, v[162:163]
	v_mov_b32_e32 v141, v162
	v_lshl_add_u64 v[46:47], v[140:141], 1, v[46:47]
	global_store_dwordx4 v[46:47], v[158:161], off

.LBB0_255:
	v_and_b32_e32 v4, 30, v1
	v_cvt_f32_ubyte0_e32 v4, v4
	v_mul_f32_e32 v4, 0xbd000000, v4
	v_cmp_eq_f32_e32 vcc, 0, v4
	v_ashrrev_i32_e32 v16, 4, v0
	s_nop 0
	v_cndmask_b32_e64 v17, v7, 1.0, vcc
	v_frexp_mant_f32_e32 v18, v17
	v_cmp_gt_f32_e64 s[0:1], s25, v18
	s_nop 1
	v_cndmask_b32_e64 v19, 1.0, 2.0, s[0:1]
	v_mul_f32_e32 v18, v18, v19
	v_add_f32_e32 v21, 1.0, v18
	v_rcp_f32_e32 v26, v21
	v_add_f32_e32 v19, -1.0, v21
	v_sub_f32_e32 v23, v18, v19
	v_add_f32_e32 v19, -1.0, v18
	v_mul_f32_e32 v27, v19, v26
	v_mul_f32_e32 v20, v21, v27
	v_fma_f32 v22, v27, v21, -v20
	v_fmac_f32_e32 v22, v27, v23
	v_add_f32_e32 v18, v20, v22
	v_sub_f32_e32 v21, v19, v18
	v_add_f32_e64 v24, v18, -v20
	v_add_f32_e64 v25, v19, -v21
	v_mov_b32_e32 v23, v18
	v_add_f32_e64 v18, v24, -v22
	v_add_f32_e64 v19, v25, -v23
	s_nop 0
	v_add_f32_e32 v18, v18, v19
	v_add_f32_e32 v18, v21, v18
	v_mul_f32_e32 v19, v26, v18
	v_add_f32_e32 v18, v27, v19
	v_sub_f32_e32 v20, v18, v27
	v_sub_f32_e32 v28, v19, v20
	v_mul_f32_e32 v19, v18, v18
	v_fma_f32 v21, v18, v18, -v19
	v_add_f32_e32 v20, v28, v28
	v_fmac_f32_e32 v21, v18, v20
	v_add_f32_e32 v20, v19, v21
	v_fmamk_f32 v22, v20, 0x3e76c4e1, v8
	v_fmaak_f32 v22, v20, v22, 0x3ecccdef
	v_sub_f32_e32 v19, v20, v19
	v_sub_f32_e32 v29, v21, v19
	v_mul_f32_e32 v19, v20, v22
	v_fma_f32 v21, v20, v22, -v19
	v_fmac_f32_e32 v21, v29, v22
	v_add_f32_e32 v22, v19, v21
	v_add_f32_e32 v23, 0x3f2aaaaa, v22
	v_sub_f32_e32 v19, v22, v19
	v_sub_f32_e32 v19, v21, v19
	v_add_f32_e32 v21, 0xbf2aaaaa, v23
	v_add_f32_e32 v19, 0x31739010, v19
	v_sub_f32_e32 v21, v22, v21
	v_mul_f32_e64 v24, v18, v20
	v_mul_f32_e64 v25, v19, v21
	v_add_f32_e64 v26, v18, v20
	v_add_f32_e64 v27, v19, v21
	v_fma_f32 v22, v20, v18, -v24
	v_fmac_f32_e32 v22, v20, v28
	v_mov_b32_e32 v25, v27
	v_fmac_f32_e32 v22, v29, v18
	v_add_f32_e64 v20, v24, v22
	v_add_f32_e64 v21, v25, v23
	v_ldexp_f32 v28, v28, 1
	v_sub_f32_e32 v19, v20, v24
	v_sub_f32_e32 v19, v22, v19
	v_sub_f32_e32 v22, v23, v21
	v_add_f32_e32 v25, v27, v22
	v_cvt_f64_f32_e32 v[26:27], v17
	v_frexp_exp_i32_f64_e32 v17, v[26:27]
	v_mul_f32_e64 v22, v20, v21
	v_mul_f32_e64 v23, v21, v20
	v_subbrev_co_u32_e64 v17, s[0:1], 0, v17, s[0:1]
	v_cvt_f32_i32_e32 v23, v17
	v_ashrrev_i32_e32 v17, 31, v16
	v_lshl_add_u64 v[16:17], v[16:17], 2, s[16:17]
	global_load_dword v30, v[16:17], off
	v_fma_f32 v24, v20, v21, -v22
	v_fmac_f32_e32 v24, v20, v25
	v_mul_f32_e32 v16, 0x3f317218, v23
	v_fmac_f32_e32 v24, v19, v21
	v_fma_f32 v20, v23, s26, -v16
	v_fmac_f32_e32 v20, 0xb102e308, v23
	v_ldexp_f32 v21, v18, 1
	v_add_f32_e32 v17, v22, v24
	v_add_f32_e64 v18, v16, v20
	v_add_f32_e64 v19, v17, v21
	v_mov_b32_e32 v26, v17
	v_mov_b32_e32 v27, v19
	v_mov_b32_e32 v23, v21
	v_add_f32_e64 v22, v26, -v22
	v_add_f32_e64 v23, v27, -v23
	v_mov_b32_e32 v25, v17
	v_add_f32_e64 v22, v24, -v22
	v_add_f32_e64 v23, v25, -v23
	v_mov_b32_e32 v21, v18
	v_add_f32_e32 v17, v28, v22
	v_add_f32_e32 v17, v17, v23
	v_add_f32_e64 v22, v18, -v16
	v_add_f32_e64 v23, v19, -v17
	v_add_f32_e64 v24, v18, v16
	v_add_f32_e64 v25, v19, v17
	v_mov_b32_e32 v16, v17
	v_mov_b32_e32 v23, v25
	v_add_f32_e64 v26, v20, -v22
	v_add_f32_e64 v27, v21, -v23
	v_add_f32_e64 v20, v20, v22
	v_add_f32_e64 v21, v21, v23
	v_mov_b32_e32 v17, v18
	v_add_f32_e64 v22, v21, -v18
	v_add_f32_e64 v23, v20, -v19
	v_add_f32_e64 v28, v24, -v22
	v_add_f32_e64 v29, v25, -v22
	v_mov_b32_e32 v24, v25
	v_mov_b32_e32 v25, v21
	v_pk_mov_b32 v[22:23], v[18:19], v[22:23] op_sel:[1,0]
	v_mov_b32_e32 v28, v26
	v_add_f32_e64 v22, v24, -v22
	v_add_f32_e64 v23, v25, -v23
	v_mov_b32_e32 v27, v21
	v_add_f32_e64 v16, v16, -v22
	v_add_f32_e64 v17, v17, -v23
	s_nop 0
	v_add_f32_e64 v18, v28, v16
	v_add_f32_e64 v19, v29, v17
	s_nop 0
	v_add_f32_e64 v22, v18, v19
	v_add_f32_e64 v23, v19, v18
	s_nop 0
	v_pk_add_f32 v[20:21], v[20:21], v[22:23] op_sel:[1,0] op_sel_hi:[0,1]
	v_mov_b32_e32 v19, v20
	v_add_f32_e64 v24, v18, -v26
	v_add_f32_e64 v25, v19, -v27
	v_mov_b32_e32 v17, v22
	v_sub_f32_e32 v18, v18, v24
	v_add_f32_e64 v16, v16, -v24
	v_add_f32_e64 v17, v17, -v25
	v_sub_f32_e32 v18, v26, v18
	v_add_f32_e32 v16, v16, v18
	v_add_f32_e32 v16, v16, v17
	v_add_f32_e32 v17, v20, v16
	v_sub_f32_e32 v18, v17, v20
	v_sub_f32_e32 v16, v16, v18
	v_mul_f32_e32 v18, v4, v17
	v_fma_f32 v17, v4, v17, -v18
	v_fmac_f32_e32 v17, v4, v16
	v_add_f32_e32 v16, v18, v17
	v_cmp_class_f32_e64 s[0:1], v18, s27
	v_sub_f32_e32 v19, v16, v18
	v_sub_f32_e32 v17, v17, v19
	v_cndmask_b32_e64 v16, v16, v18, s[0:1]
	v_cmp_eq_f32_e64 s[0:1], s29, v16
	s_nop 1
	v_cndmask_b32_e64 v18, 0, v9, s[0:1]
	v_sub_f32_e32 v19, v16, v18
	v_mul_f32_e32 v20, 0x3fb8aa3b, v19
	v_fma_f32 v21, v19, s34, -v20
	v_rndne_f32_e32 v22, v20
	v_fmac_f32_e32 v21, 0x32a5705f, v19
	v_sub_f32_e32 v20, v20, v22
	v_add_f32_e32 v20, v20, v21
	v_exp_f32_e32 v20, v20
	v_cvt_i32_f32_e32 v21, v22
	v_cmp_neq_f32_e64 s[0:1], |v16|, s28
	s_nop 1
	v_cndmask_b32_e64 v16, 0, v17, s[0:1]
	v_ldexp_f32 v17, v20, v21
	v_cmp_ngt_f32_e64 s[0:1], s35, v19
	v_add_f32_e32 v16, v18, v16
	s_waitcnt vmcnt(0)
	v_cvt_f32_i32_e32 v18, v30
	v_cndmask_b32_e64 v17, 0, v17, s[0:1]
	v_cmp_nlt_f32_e64 s[0:1], s29, v19
	s_nop 1
	v_cndmask_b32_e64 v17, v10, v17, s[0:1]
	v_fma_f32 v16, v17, v16, v17
	v_cmp_class_f32_e64 s[0:1], v17, s27
	s_nop 1
	v_cndmask_b32_e64 v16, v16, v17, s[0:1]
	v_cmp_neq_f32_e64 s[0:1], v4, |v4|
	s_nop 1
	v_cndmask_b32_e64 v17, v10, 0, s[0:1]
	v_cndmask_b32_e64 v17, v17, 1.0, vcc
	v_cmp_class_f32_e64 s[0:1], v4, s27
	s_nop 1
	v_cndmask_b32_e64 v4, |v16|, v17, s[0:1]
	v_mul_f32_e32 v16, v4, v18
	v_and_b32_e32 v17, 0x7fffffff, v16
	v_lshrrev_b32_e32 v4, 23, v17
	v_and_b32_e32 v18, 0x7fffff, v17
	v_cmp_nlt_f32_e64 s[6:7], |v16|, s37
	v_add_u32_e32 v19, 0xffffff88, v4
	v_or_b32_e32 v18, 0x800000, v18
	s_and_saveexec_b64 s[0:1], s[6:7]
	s_xor_b64 s[22:23], exec, s[0:1]
	s_cbranch_execz .LBB0_257
	v_cmp_lt_u32_e32 vcc, 63, v19
	s_nop 1
	v_cndmask_b32_e32 v4, 0, v13, vcc
	v_add_u32_e32 v4, v4, v19
	v_cmp_lt_u32_e64 s[0:1], 31, v4
	s_nop 1
	v_cndmask_b32_e64 v20, 0, v14, s[0:1]
	v_add_u32_e32 v4, v20, v4
	v_cmp_lt_u32_e64 s[2:3], 31, v4
	s_nop 1
	v_cndmask_b32_e64 v20, 0, v14, s[2:3]
	v_add_u32_e32 v34, v20, v4
	v_mad_u64_u32 v[20:21], s[4:5], v18, s38, 0
	v_mov_b32_e32 v4, v21
	v_mad_u64_u32 v[22:23], s[4:5], v18, s39, v[4:5]
	v_mov_b32_e32 v4, v23
	v_mad_u64_u32 v[24:25], s[4:5], v18, s40, v[4:5]
	v_mov_b32_e32 v4, v25
	v_mad_u64_u32 v[26:27], s[4:5], v18, s41, v[4:5]
	v_mov_b32_e32 v4, v27
	v_mad_u64_u32 v[28:29], s[4:5], v18, s42, v[4:5]
	v_mov_b32_e32 v4, v29
	v_mad_u64_u32 v[30:31], s[4:5], v18, s43, v[4:5]
	v_mov_b32_e32 v4, v31
	v_mad_u64_u32 v[32:33], s[4:5], v18, s44, v[4:5]
	v_cndmask_b32_e32 v21, v30, v26, vcc
	v_cndmask_b32_e32 v4, v32, v28, vcc
	v_cndmask_b32_e32 v25, v33, v30, vcc
	v_cndmask_b32_e64 v23, v4, v21, s[0:1]
	v_cndmask_b32_e64 v4, v25, v4, s[0:1]
	v_cndmask_b32_e32 v25, v28, v24, vcc
	v_cndmask_b32_e64 v21, v21, v25, s[0:1]
	v_cndmask_b32_e32 v22, v26, v22, vcc
	v_cndmask_b32_e64 v4, v4, v23, s[2:3]
	v_cndmask_b32_e64 v23, v23, v21, s[2:3]
	v_sub_u32_e32 v27, 32, v34
	v_cndmask_b32_e64 v25, v25, v22, s[0:1]
	v_alignbit_b32 v28, v4, v23, v27
	v_cmp_eq_u32_e64 s[4:5], 0, v34
	v_cndmask_b32_e64 v21, v21, v25, s[2:3]
	v_cndmask_b32_e32 v20, v24, v20, vcc
	v_cndmask_b32_e64 v4, v28, v4, s[4:5]
	v_alignbit_b32 v26, v23, v21, v27
	v_cndmask_b32_e64 v20, v22, v20, s[0:1]
	v_cndmask_b32_e64 v23, v26, v23, s[4:5]
	v_bfe_u32 v29, v4, 29, 1
	v_cndmask_b32_e64 v20, v25, v20, s[2:3]
	v_alignbit_b32 v26, v4, v23, 30
	v_sub_u32_e32 v30, 0, v29
	v_alignbit_b32 v22, v21, v20, v27
	v_xor_b32_e32 v26, v26, v30
	v_cndmask_b32_e64 v21, v22, v21, s[4:5]
	v_alignbit_b32 v22, v23, v21, 30
	v_ffbh_u32_e32 v23, v26
	v_min_u32_e32 v23, 32, v23
	v_alignbit_b32 v20, v21, v20, 30
	v_xor_b32_e32 v22, v22, v30
	v_sub_u32_e32 v24, 31, v23
	v_xor_b32_e32 v20, v20, v30
	v_alignbit_b32 v25, v26, v22, v24
	v_alignbit_b32 v20, v22, v20, v24
	v_alignbit_b32 v21, v25, v20, 9
	v_ffbh_u32_e32 v22, v21
	v_min_u32_e32 v22, 32, v22
	v_lshrrev_b32_e32 v28, 29, v4
	v_not_b32_e32 v24, v22
	v_alignbit_b32 v20, v21, v20, v24
	v_lshlrev_b32_e32 v21, 31, v28
	v_or_b32_e32 v24, 0x33000000, v21
	v_add_lshl_u32 v22, v22, v23, 23
	v_lshrrev_b32_e32 v20, 9, v20
	v_sub_u32_e32 v22, v24, v22
	v_or_b32_e32 v21, 0.5, v21
	v_lshlrev_b32_e32 v23, 23, v23
	v_or_b32_e32 v20, v22, v20
	v_lshrrev_b32_e32 v22, 9, v25
	v_sub_u32_e32 v21, v21, v23
	v_or_b32_e32 v21, v22, v21
	v_mul_f32_e32 v22, 0x3fc90fda, v21
	v_fma_f32 v23, v21, s45, -v22
	v_fmac_f32_e32 v23, 0x33a22168, v21
	v_fmac_f32_e32 v23, 0x3fc90fda, v20
	v_lshrrev_b32_e32 v4, 30, v4
	v_add_f32_e32 v21, v22, v23
	v_add_u32_e32 v20, v29, v4

.LBB0_270:
	v_lshl_add_u64 v[14:15], v[2:3], 0, s[6:7]
	v_add_co_u32_e64 v16, s[0:1], s10, v14
	global_load_dword v46, v[14:15], off
	s_nop 0
	v_addc_co_u32_e64 v17, s[0:1], 0, v15, s[0:1]
	v_add_co_u32_e64 v18, s[0:1], s13, v14
	v_mov_b32_e32 v1, s20
	s_nop 0
	v_addc_co_u32_e64 v19, s[0:1], 0, v15, s[0:1]
	v_add_co_u32_e64 v20, s[0:1], s14, v14
	s_add_u32 s6, s6, 0x30000
	s_nop 0
	v_addc_co_u32_e64 v21, s[0:1], 0, v15, s[0:1]
	v_add_co_u32_e64 v22, s[0:1], s15, v14
	s_addc_u32 s7, s7, 0
	s_nop 0
	v_addc_co_u32_e64 v23, s[0:1], 0, v15, s[0:1]
	v_add_co_u32_e64 v24, s[0:1], s16, v14
	s_addk_i32 s20, 0x80
	s_nop 0
	v_addc_co_u32_e64 v25, s[0:1], 0, v15, s[0:1]
	v_add_co_u32_e64 v26, s[0:1], s17, v14
	s_cmp_lg_u32 s6, 0x300000
	s_nop 0
	v_addc_co_u32_e64 v27, s[0:1], 0, v15, s[0:1]
	v_add_co_u32_e64 v14, s[0:1], s18, v14
	s_nop 1
	v_addc_co_u32_e64 v15, s[0:1], 0, v15, s[0:1]
	global_load_dword v48, v[16:17], off
	global_load_dword v50, v[18:19], off
	global_load_dword v52, v[20:21], off
	global_load_dword v54, v[22:23], off
	global_load_dword v56, v[24:25], off
	global_load_dword v58, v[26:27], off
	global_load_dword v60, v[14:15], off
	ds_read_b128 v[14:17], v1
	ds_read_b128 v[18:21], v1 offset:16
	ds_read_b128 v[22:25], v1 offset:32
	ds_read_b128 v[26:29], v1 offset:48
	ds_read_b128 v[30:33], v1 offset:64
	ds_read_b128 v[34:37], v1 offset:80
	ds_read_b128 v[38:41], v1 offset:96
	ds_read_b128 v[42:45], v1 offset:112
	s_waitcnt vmcnt(7) lgkmcnt(7)
	v_fma_f32 v4, v46, v14, v4
	v_fma_f32 v5, v46, v15, v5
	v_fma_f32 v8, v46, v16, v8
	v_fma_f32 v9, v46, v17, v9
	s_waitcnt vmcnt(6) lgkmcnt(6)
	v_fma_f32 v4, v48, v18, v4
	v_fma_f32 v5, v48, v19, v5
	v_fma_f32 v8, v48, v20, v8
	v_fma_f32 v9, v48, v21, v9
	s_waitcnt vmcnt(5) lgkmcnt(5)
	v_fma_f32 v4, v50, v22, v4
	v_fma_f32 v5, v50, v23, v5
	v_fma_f32 v8, v50, v24, v8
	v_fma_f32 v9, v50, v25, v9
	s_waitcnt vmcnt(4) lgkmcnt(4)
	v_fma_f32 v4, v52, v26, v4
	v_fma_f32 v5, v52, v27, v5
	v_fma_f32 v8, v52, v28, v8
	v_fma_f32 v9, v52, v29, v9
	s_waitcnt vmcnt(3) lgkmcnt(3)
	v_fma_f32 v4, v54, v30, v4
	v_fma_f32 v5, v54, v31, v5
	v_fma_f32 v8, v54, v32, v8
	v_fma_f32 v9, v54, v33, v9
	s_waitcnt vmcnt(2) lgkmcnt(2)
	v_fma_f32 v4, v56, v34, v4
	v_fma_f32 v5, v56, v35, v5
	v_fma_f32 v8, v56, v36, v8
	v_fma_f32 v9, v56, v37, v9
	s_waitcnt vmcnt(1) lgkmcnt(1)
	v_fma_f32 v4, v58, v38, v4
	v_fma_f32 v5, v58, v39, v5
	v_fma_f32 v8, v58, v40, v8
	v_fma_f32 v9, v58, v41, v9
	s_waitcnt vmcnt(0) lgkmcnt(0)
	v_fma_f32 v4, v60, v42, v4
	v_fma_f32 v5, v60, v43, v5
	v_fma_f32 v8, v60, v44, v8
	v_fma_f32 v9, v60, v45, v9
	s_cbranch_scc1 .LBB0_270
	ds_write2st64_b32 v12, v4, v5 offset1:1
	ds_write2st64_b32 v12, v8, v9 offset0:2 offset1:3
	s_waitcnt lgkmcnt(0)
	s_barrier
	s_and_saveexec_b64 s[0:1], vcc
	s_cbranch_execz .LBB0_268
	s_load_dwordx2 s[6:7], s[8:9], 0x20
	s_lshl_b32 s20, s19, 6
	v_or_b32_e32 v2, s20, v7
	v_ashrrev_i32_e32 v3, 31, v2
	v_add_u32_e32 v16, s20, v11
	s_waitcnt lgkmcnt(0)
	v_lshl_add_u64 v[2:3], v[2:3], 2, s[6:7]
	global_load_dword v1, v[2:3], off
	ds_read2st64_b32 v[2:3], v10 offset1:4
	ds_read2st64_b32 v[4:5], v10 offset0:8 offset1:12
	ds_read2st64_b32 v[8:9], v10 offset0:16 offset1:20
	ds_read2st64_b32 v[14:15], v10 offset0:24 offset1:28
	v_ashrrev_i32_e32 v17, 31, v16
	s_waitcnt vmcnt(0) lgkmcnt(3)
	v_add_f32_e32 v1, v1, v2
	v_add_f32_e32 v1, v1, v3
	s_waitcnt lgkmcnt(2)
	v_add_f32_e32 v1, v1, v4
	v_add_f32_e32 v1, v1, v5
	s_waitcnt lgkmcnt(1)
	v_add_f32_e32 v1, v1, v8
	v_add_f32_e32 v1, v1, v9
	s_waitcnt lgkmcnt(0)
	v_add_f32_e32 v1, v1, v14
	v_add_f32_e32 v1, v1, v15
	v_lshl_add_u64 v[2:3], v[16:17], 2, s[2:3]
	global_store_dword v[2:3], v1, off
	s_branch .LBB0_268

.LBB0_339:
	v_mul_f32_e32 v80, v29, v29
	v_mul_f32_e32 v81, v25, v25
	v_fmac_f32_e32 v80, v28, v28
	v_fmac_f32_e32 v81, v24, v24
	v_fmac_f32_e32 v80, v30, v30
	v_fmac_f32_e32 v81, v26, v26
	v_fmac_f32_e32 v80, v31, v31
	v_fmac_f32_e32 v81, v27, v27
	v_add_f32_e32 v80, v80, v81
	v_mul_f32_e32 v81, v21, v21
	v_fmac_f32_e32 v81, v20, v20
	v_fmac_f32_e32 v81, v22, v22
	v_fmac_f32_e32 v81, v23, v23
	v_add_f32_e32 v80, v81, v80
	v_mul_f32_e32 v81, v5, v5
	v_fmac_f32_e32 v81, v4, v4
	v_fmac_f32_e32 v81, v6, v6
	v_fmac_f32_e32 v81, v7, v7
	v_add_f32_e32 v80, v81, v80
	ds_swizzle_b32 v81, v80 offset:swizzle(SWAP,1)
	s_lshl_b64 s[16:17], s[16:17], 11
	s_add_u32 s10, s10, 0x1000
	s_addc_u32 s11, s11, 0
	s_add_u32 s2, s2, 0x1000
	s_waitcnt lgkmcnt(0)
	v_add_f32_e32 v80, v80, v81
	ds_swizzle_b32 v81, v80 offset:swizzle(SWAP,2)
	s_addc_u32 s3, s3, 0
	s_add_i32 s12, s12, 2
	s_waitcnt lgkmcnt(0)
	v_add_f32_e32 v80, v80, v81
	ds_swizzle_b32 v81, v80 offset:swizzle(SWAP,4)
	s_waitcnt lgkmcnt(0)
	v_add_f32_e32 v80, v80, v81
	ds_swizzle_b32 v81, v80 offset:swizzle(SWAP,8)
	s_waitcnt lgkmcnt(0)
	v_add_f32_e32 v80, v80, v81
	ds_swizzle_b32 v81, v80 offset:swizzle(SWAP,16)
	s_waitcnt lgkmcnt(0)
	v_add_f32_e32 v80, v80, v81
	v_mov_b32_e32 v81, v80
	s_nop 1
	v_permlane32_swap_b32_e32 v80, v81
	v_add_f32_e32 v80, v80, v81
	v_fmamk_f32 v80, v80, 0x3a800000, v210
	v_mul_f32_e32 v81, 0x4b800000, v80
	v_cmp_gt_f32_e32 vcc, s56, v80
	s_nop 1
	v_cndmask_b32_e32 v80, v80, v81, vcc
	v_rsq_f32_e32 v82, v80
	v_lshl_add_u64 v[80:81], v[118:119], 0, s[16:17]
	s_mov_b64 s[16:17], s[0:1]
	v_mul_f32_e32 v83, 0x45800000, v82
	v_cndmask_b32_e32 v82, v82, v83, vcc
	v_mul_f32_e64 v28, v28, v82
	v_mul_f32_e64 v29, v29, v82
	v_mul_f32_e64 v30, v30, v82
	v_mul_f32_e64 v31, v31, v82
	v_mul_f32_e64 v24, v24, v82
	v_mul_f32_e64 v25, v25, v82
	v_mul_f32_e64 v26, v26, v82
	v_mul_f32_e64 v27, v27, v82
	v_mul_f32_e64 v20, v20, v82
	v_mul_f32_e64 v21, v21, v82
	v_mul_f32_e64 v22, v22, v82
	v_mul_f32_e64 v23, v23, v82
	v_mul_f32_e64 v4, v4, v82
	v_mul_f32_e64 v5, v5, v82
	v_mul_f32_e64 v6, v6, v82
	v_mul_f32_e64 v7, v7, v82
	v_fma_f32 v30, v50, v30, v54
	v_fma_f32 v31, v51, v31, v55
	v_fma_f32 v28, v48, v28, v52
	v_fma_f32 v29, v49, v29, v53
	v_fma_f32 v26, v42, v26, v46
	v_fma_f32 v27, v43, v27, v47
	v_fma_f32 v24, v40, v24, v44
	v_fma_f32 v25, v41, v25, v45
	v_fma_f32 v22, v34, v22, v38
	v_fma_f32 v23, v35, v23, v39
	v_fma_f32 v20, v32, v20, v36
	v_fma_f32 v21, v33, v21, v37
	v_fma_f32 v6, v58, v6, v62
	v_fma_f32 v7, v59, v7, v63
	v_fma_f32 v4, v56, v4, v60
	v_fma_f32 v5, v57, v5, v61
	v_cvt_pk_bf16_f32 v28, v28, v29
	v_cvt_pk_bf16_f32 v29, v30, v31
	v_cvt_pk_bf16_f32 v24, v24, v25
	v_cvt_pk_bf16_f32 v25, v26, v27
	v_cvt_pk_bf16_f32 v20, v20, v21
	v_cvt_pk_bf16_f32 v21, v22, v23
	v_cvt_pk_bf16_f32 v4, v4, v5
	v_cvt_pk_bf16_f32 v5, v6, v7
	global_store_dwordx2 v[80:81], v[28:29], off
	global_store_dwordx2 v[80:81], v[24:25], off offset:512
	global_store_dwordx2 v[80:81], v[20:21], off offset:1024
	global_store_dwordx2 v[80:81], v[4:5], off offset:1536
	s_waitcnt vmcnt(4)
	v_mov_b64_e32 v[4:5], v[76:77]
	v_mov_b64_e32 v[20:21], v[72:73]
	v_mov_b64_e32 v[24:25], v[68:69]
	v_mov_b64_e32 v[28:29], v[64:65]
	s_andn2_b64 vcc, exec, s[18:19]
	v_mov_b64_e32 v[6:7], v[78:79]
	v_mov_b64_e32 v[22:23], v[74:75]
	v_mov_b64_e32 v[26:27], v[70:71]
	v_mov_b64_e32 v[30:31], v[66:67]
	s_cbranch_vccz .LBB0_356
.LBB0_340:
	s_ashr_i32 s40, s16, 31
	s_lshr_b32 s0, s40, 20
	s_add_i32 s0, s16, s0
	s_ashr_i32 s13, s0, 12
	s_cmp_eq_u32 s13, s39
	s_cbranch_scc1 .LBB0_350
	s_mul_i32 s0, s13, 0x1800
	s_ashr_i32 s1, s0, 31
	s_lshl_b64 s[0:1], s[0:1], 2
	s_load_dwordx2 s[20:21], s[4:5], 0x30
	s_add_u32 s0, s29, s0
	s_addc_u32 s1, s30, s1
	s_add_u32 s18, s0, 0x5000
	v_lshlrev_b32_e32 v208, 2, v114
	s_addc_u32 s19, s1, 0
	v_lshl_add_u64 v[72:73], s[0:1], 0, v[208:209]
	s_waitcnt lgkmcnt(0)
	s_add_u32 s20, s20, s14
	v_add_co_u32_e32 v32, vcc, 0x1000, v72
	s_addc_u32 s21, s21, s15
	s_nop 0
	v_addc_co_u32_e32 v33, vcc, 0, v73, vcc
	global_load_dwordx4 v[48:51], v208, s[20:21]
	global_load_dwordx4 v[64:67], v[32:33], off
	global_load_dwordx4 v[52:55], v208, s[0:1]
	global_load_dwordx4 v[60:63], v[122:123], off
	global_load_dwordx4 v[56:59], v[120:121], off
	v_cndmask_b32_e64 v32, 0, 1, s[6:7]
	v_cmp_ne_u32_e64 s[0:1], 1, v32
	s_andn2_b64 vcc, exec, s[6:7]
	s_cbranch_vccnz .LBB0_343
	global_load_dwordx4 v[16:19], v208, s[18:19]
	global_load_dwordx4 v[32:35], v[124:125], off
	s_waitcnt vmcnt(0)
	v_add_f32_e64 v18, v18, v34
	v_add_f32_e64 v19, v19, v35
	v_add_f32_e64 v16, v16, v32
	v_add_f32_e64 v17, v17, v33
.LBB0_343:
	v_lshl_add_u64 v[74:75], s[20:21], 0, v[208:209]
	s_mov_b64 s[20:21], 0x1000
	v_lshl_add_u64 v[76:77], v[72:73], 0, s[20:21]
	global_load_dwordx4 v[40:43], v[74:75], off offset:1024
	global_load_dwordx4 v[88:91], v[76:77], off offset:1024
	global_load_dwordx4 v[44:47], v[72:73], off offset:1024
	global_load_dwordx4 v[84:87], v[122:123], off offset:1024
	global_load_dwordx4 v[68:71], v[120:121], off offset:1024
	s_and_b64 vcc, exec, s[0:1]
	s_cbranch_vccnz .LBB0_345
	global_load_dwordx4 v[12:15], v128, s[18:19]
	global_load_dwordx4 v[32:35], v[124:125], off offset:1024
	s_waitcnt vmcnt(0)
	v_add_f32_e64 v14, v14, v34
	v_add_f32_e64 v15, v15, v35
	v_add_f32_e64 v12, v12, v32
	v_add_f32_e64 v13, v13, v33
.LBB0_345:
	global_load_dwordx4 v[32:35], v[74:75], off offset:2048
	global_load_dwordx4 v[108:111], v[76:77], off offset:2048
	global_load_dwordx4 v[36:39], v[72:73], off offset:2048
	global_load_dwordx4 v[104:107], v[122:123], off offset:2048
	global_load_dwordx4 v[100:103], v[120:121], off offset:2048
	s_and_b64 vcc, exec, s[0:1]
	s_cbranch_vccnz .LBB0_347
	global_load_dwordx4 v[8:11], v129, s[18:19]
	global_load_dwordx4 v[78:81], v[124:125], off offset:2048
	s_waitcnt vmcnt(0)
	v_add_f32_e64 v10, v10, v80
	v_add_f32_e64 v11, v11, v81
	v_add_f32_e64 v8, v8, v78
	v_add_f32_e64 v9, v9, v79
.LBB0_347:
	global_load_dwordx4 v[80:83], v[74:75], off offset:3072
	global_load_dwordx4 v[96:99], v[76:77], off offset:3072
	s_nop 0
	global_load_dwordx4 v[72:75], v[72:73], off offset:3072
	s_nop 0
	global_load_dwordx4 v[92:95], v[122:123], off offset:3072
	global_load_dwordx4 v[76:79], v[120:121], off offset:3072
	s_and_b64 vcc, exec, s[0:1]
	s_cbranch_vccnz .LBB0_349
	global_load_dwordx4 v[0:3], v130, s[18:19]
	global_load_dwordx4 v[132:135], v[124:125], off offset:3072
	s_waitcnt vmcnt(0)
	v_add_f32_e64 v2, v2, v134
	v_add_f32_e64 v3, v3, v135
	v_add_f32_e64 v0, v0, v132
	v_add_f32_e64 v1, v1, v133
.LBB0_349:
	s_waitcnt vmcnt(0)
	v_add_f32_e64 v64, v64, 1.0
	v_add_f32_e64 v65, v65, 1.0
	s_waitcnt vmcnt(8)
	v_add_f32_e64 v110, v110, 1.0
	v_add_f32_e64 v111, v111, 1.0
	v_add_f32_e64 v108, v108, 1.0
	v_add_f32_e64 v109, v109, 1.0
	v_add_f32_e64 v90, v90, 1.0
	v_add_f32_e64 v91, v91, 1.0
	v_add_f32_e64 v88, v88, 1.0
	v_add_f32_e64 v89, v89, 1.0
	v_add_f32_e64 v66, v66, 1.0
	v_add_f32_e64 v67, v67, 1.0
	v_add_f32_e64 v60, v64, v60
	v_add_f32_e64 v61, v65, v61
	v_add_f32_e64 v54, v54, v58
	v_add_f32_e64 v55, v55, v59
	v_add_f32_e64 v52, v52, v56
	v_add_f32_e64 v53, v53, v57
	s_waitcnt vmcnt(3)
	v_add_f32_e64 v56, v98, 1.0
	v_add_f32_e64 v57, v99, 1.0
	v_add_f32_e64 v58, v96, 1.0
	v_add_f32_e64 v59, v97, 1.0
	v_add_f32_e64 v106, v110, v106
	v_add_f32_e64 v107, v111, v107
	v_add_f32_e64 v104, v108, v104
	v_add_f32_e64 v105, v109, v105
	v_add_f32_e64 v86, v90, v86
	v_add_f32_e64 v87, v91, v87
	v_add_f32_e64 v84, v88, v84
	v_add_f32_e64 v85, v89, v85
	v_add_f32_e64 v62, v66, v62
	v_add_f32_e64 v63, v67, v63
	v_mul_f32_e64 v48, v48, v60
	v_mul_f32_e64 v49, v49, v61
	s_waitcnt vmcnt(1)
	v_add_f32_e64 v56, v56, v94
	v_add_f32_e64 v57, v57, v95
	v_add_f32_e64 v60, v58, v92
	v_add_f32_e64 v61, v59, v93
	v_mul_f32_e64 v34, v34, v106
	v_mul_f32_e64 v35, v35, v107
	v_mul_f32_e64 v32, v32, v104
	v_mul_f32_e64 v33, v33, v105
	v_add_f32_e64 v38, v38, v102
	v_add_f32_e64 v39, v39, v103
	v_add_f32_e64 v36, v36, v100
	v_add_f32_e64 v37, v37, v101
	v_mul_f32_e64 v42, v42, v86
	v_mul_f32_e64 v43, v43, v87
	v_mul_f32_e64 v40, v40, v84
	v_mul_f32_e64 v41, v41, v85
	v_add_f32_e64 v46, v46, v70
	v_add_f32_e64 v47, v47, v71
	v_add_f32_e64 v44, v44, v68
	v_add_f32_e64 v45, v45, v69
	v_mul_f32_e64 v50, v50, v62
	v_mul_f32_e64 v51, v51, v63
	v_mul_f32_e64 v58, v82, v56
	v_mul_f32_e64 v59, v83, v57
	v_mul_f32_e64 v56, v80, v60
	v_mul_f32_e64 v57, v81, v61
	s_waitcnt vmcnt(0)
	v_add_f32_e64 v62, v74, v78
	v_add_f32_e64 v63, v75, v79
	v_add_f32_e64 v60, v72, v76
	v_add_f32_e64 v61, v73, v77
	s_mov_b32 s39, s13

.LBB0_355:
	s_ashr_i32 s13, s12, 31
	s_lshl_b64 s[20:21], s[12:13], 2
	s_add_u32 s42, s31, s20
	s_addc_u32 s43, s34, s21
	global_load_dwordx2 v[80:81], v209, s[42:43]
	s_add_u32 s42, s35, s20
	s_addc_u32 s43, s36, s21
	s_add_u32 s20, s37, s20
	s_addc_u32 s21, s38, s21
	global_load_dword v83, v209, s[42:43]
	global_load_dword v82, v209, s[20:21]
	v_lshl_add_u64 v[100:101], s[2:3], 0, v[112:113]
	s_waitcnt vmcnt(2)
	v_readfirstlane_b32 s13, v80
	s_cmp_eq_u32 s13, 1
	s_cselect_b32 s17, s23, 0
	s_cmp_eq_u32 s13, 2
	s_cselect_b32 s17, s24, s17
	s_cmp_eq_u32 s13, 3
	s_cselect_b32 s17, s25, s17
	s_cmp_eq_u32 s13, 4
	s_cselect_b32 s17, s26, s17
	s_cmp_eq_u32 s13, 5
	s_cselect_b32 s17, s27, s17
	s_cmp_eq_u32 s13, 6
	v_mov_b32_e32 v80, s17
	s_cselect_b64 vcc, -1, 0
	s_cmp_eq_u32 s13, 7
	v_cndmask_b32_e32 v80, v80, v115, vcc
	s_cselect_b64 vcc, -1, 0
	s_add_i32 s20, s12, 1
	s_ashr_i32 s21, s20, 31
	s_lshl_b64 s[20:21], s[20:21], 2
	s_add_u32 s42, s35, s20
	s_addc_u32 s43, s36, s21
	global_load_dword v91, v209, s[42:43]
	s_add_u32 s20, s37, s20
	v_readfirstlane_b32 s13, v81
	s_addc_u32 s21, s38, s21
	s_cmp_eq_u32 s13, 1
	s_cselect_b32 s17, s23, 0
	s_cmp_eq_u32 s13, 2
	s_cselect_b32 s17, s24, s17
	s_cmp_eq_u32 s13, 3
	s_cselect_b32 s17, s25, s17
	s_cmp_eq_u32 s13, 4
	s_cselect_b32 s17, s26, s17
	s_cmp_eq_u32 s13, 5
	v_cndmask_b32_e32 v80, v80, v126, vcc
	s_cselect_b32 s17, s27, s17
	s_cmp_eq_u32 s13, 6
	s_waitcnt vmcnt(2)
	v_add_u32_e32 v84, v80, v83
	v_mov_b32_e32 v83, s17
	s_cselect_b64 vcc, -1, 0
	s_cmp_eq_u32 s13, 7
	v_cndmask_b32_e32 v83, v83, v115, vcc
	s_cselect_b64 vcc, -1, 0
	v_cndmask_b32_e32 v83, v83, v126, vcc
	v_ashrrev_i32_e32 v85, 31, v84
	v_lshlrev_b64 v[84:85], 11, v[84:85]
	v_lshl_add_u64 v[84:85], v[116:117], 0, v[84:85]
	global_load_dwordx2 v[86:87], v[84:85], off
	global_load_dwordx2 v[88:89], v[84:85], off offset:512
	global_load_dwordx2 v[80:81], v[84:85], off offset:1024
	s_nop 0
	global_load_dwordx2 v[84:85], v[84:85], off offset:1536
	s_waitcnt vmcnt(5)
	v_mul_f32_e64 v102, v18, v82
	v_mul_f32_e64 v103, v19, v82
	global_load_dword v90, v209, s[20:21]
	v_mul_f32_e64 v104, v16, v82
	v_mul_f32_e64 v105, v17, v82
	v_mul_f32_e64 v106, v14, v82
	v_mul_f32_e64 v107, v15, v82
	v_mul_f32_e64 v108, v12, v82
	v_mul_f32_e64 v109, v13, v82
	v_mul_f32_e64 v110, v10, v82
	v_mul_f32_e64 v111, v11, v82
	v_mul_f32_e64 v132, v8, v82
	v_mul_f32_e64 v133, v9, v82
	v_mul_f32_e64 v134, v2, v82
	v_mul_f32_e64 v135, v3, v82
	s_mov_b32 s17, s40
	s_waitcnt vmcnt(5)
	v_add_u32_e32 v92, v83, v91
	v_ashrrev_i32_e32 v93, 31, v92
	v_lshlrev_b64 v[92:93], 11, v[92:93]
	v_lshl_add_u64 v[92:93], v[116:117], 0, v[92:93]
	global_load_dwordx2 v[94:95], v[92:93], off
	global_load_dwordx2 v[96:97], v[92:93], off offset:512
	global_load_dwordx2 v[98:99], v[92:93], off offset:1024
	s_nop 0
	global_load_dwordx2 v[92:93], v[92:93], off offset:1536
	v_mul_f32_e64 v83, v1, v82
	v_mul_f32_e64 v82, v0, v82
	s_waitcnt vmcnt(8)
	v_lshlrev_b32_e32 v136, 16, v86
	v_and_b32_e32 v137, 0xffff0000, v86
	v_lshlrev_b32_e32 v86, 16, v87
	v_and_b32_e32 v87, 0xffff0000, v87
	s_waitcnt vmcnt(7)
	v_lshlrev_b32_e32 v138, 16, v88
	v_and_b32_e32 v139, 0xffff0000, v88
	v_lshlrev_b32_e32 v88, 16, v89
	v_and_b32_e32 v89, 0xffff0000, v89
	s_waitcnt vmcnt(6)
	v_lshlrev_b32_e32 v140, 16, v80
	v_and_b32_e32 v141, 0xffff0000, v80
	v_lshlrev_b32_e32 v80, 16, v81
	v_and_b32_e32 v81, 0xffff0000, v81
	s_waitcnt vmcnt(5)
	v_lshlrev_b32_e32 v142, 16, v84
	v_and_b32_e32 v143, 0xffff0000, v84
	v_lshlrev_b32_e32 v84, 16, v85
	v_and_b32_e32 v85, 0xffff0000, v85
	v_fma_f32 v28, v104, v136, v28
	v_fma_f32 v29, v105, v137, v29
	v_fma_f32 v30, v102, v86, v30
	v_fma_f32 v31, v103, v87, v31
	v_fma_f32 v24, v108, v138, v24
	v_fma_f32 v25, v109, v139, v25
	v_fma_f32 v26, v106, v88, v26
	v_fma_f32 v27, v107, v89, v27
	v_fma_f32 v20, v132, v140, v20
	v_fma_f32 v21, v133, v141, v21
	v_fma_f32 v22, v110, v80, v22
	v_fma_f32 v23, v111, v81, v23
	v_fma_f32 v4, v82, v142, v4
	v_fma_f32 v5, v83, v143, v5
	v_fma_f32 v6, v134, v84, v6
	v_fma_f32 v7, v135, v85, v7
	s_waitcnt vmcnt(4)
	v_mul_f32_e64 v80, v16, v90
	v_mul_f32_e64 v81, v17, v90
	v_mul_f32_e64 v82, v18, v90
	v_mul_f32_e64 v83, v19, v90
	v_mul_f32_e64 v84, v12, v90
	v_mul_f32_e64 v85, v13, v90
	v_mul_f32_e64 v86, v14, v90
	v_mul_f32_e64 v87, v15, v90
	v_mul_f32_e64 v88, v8, v90
	v_mul_f32_e64 v89, v9, v90
	v_mul_f32_e64 v102, v10, v90
	v_mul_f32_e64 v103, v11, v90
	v_mul_f32_e64 v104, v0, v90
	v_mul_f32_e64 v105, v1, v90
	v_mul_f32_e64 v91, v3, v90
	v_mul_f32_e64 v90, v2, v90
	s_waitcnt vmcnt(3)
	v_lshlrev_b32_e32 v106, 16, v94
	v_and_b32_e32 v107, 0xffff0000, v94
	v_lshlrev_b32_e32 v94, 16, v95
	v_and_b32_e32 v95, 0xffff0000, v95
	s_waitcnt vmcnt(2)
	v_lshlrev_b32_e32 v108, 16, v96
	v_and_b32_e32 v109, 0xffff0000, v96
	v_lshlrev_b32_e32 v96, 16, v97
	v_and_b32_e32 v97, 0xffff0000, v97
	s_waitcnt vmcnt(1)
	v_lshlrev_b32_e32 v110, 16, v98
	v_and_b32_e32 v111, 0xffff0000, v98
	v_lshlrev_b32_e32 v98, 16, v99
	v_and_b32_e32 v99, 0xffff0000, v99
	s_waitcnt vmcnt(0)
	v_lshlrev_b32_e32 v132, 16, v92
	v_and_b32_e32 v133, 0xffff0000, v92
	v_lshlrev_b32_e32 v92, 16, v93
	v_and_b32_e32 v93, 0xffff0000, v93
	v_fma_f32 v30, v82, v94, v30
	v_fma_f32 v31, v83, v95, v31
	v_fma_f32 v28, v80, v106, v28
	v_fma_f32 v29, v81, v107, v29
	v_fma_f32 v26, v86, v96, v26
	v_fma_f32 v27, v87, v97, v27
	v_fma_f32 v24, v84, v108, v24
	v_fma_f32 v25, v85, v109, v25
	v_fma_f32 v22, v102, v98, v22
	v_fma_f32 v23, v103, v99, v23
	v_fma_f32 v20, v88, v110, v20
	v_fma_f32 v21, v89, v111, v21
	v_fma_f32 v6, v90, v92, v6
	v_fma_f32 v7, v91, v93, v7
	v_fma_f32 v4, v104, v132, v4
	v_fma_f32 v5, v105, v133, v5
	global_store_dwordx4 v[100:101], v[28:31], off
	global_store_dwordx4 v[100:101], v[24:27], off offset:1024
	global_store_dwordx4 v[100:101], v[20:23], off offset:2048
	global_store_dwordx4 v[100:101], v[4:7], off offset:3072
	s_branch .LBB0_339

.LBB0_491:
	s_or_b64 exec, exec, s[0:1]
	s_waitcnt lgkmcnt(0)
	s_barrier
	ds_read2st64_b32 v[118:119], v104 offset1:4
	ds_read2st64_b32 v[120:121], v104 offset0:8 offset1:12
	ds_read2st64_b32 v[70:71], v104 offset0:16 offset1:20
	ds_read2st64_b32 v[68:69], v104 offset0:24 offset1:28
	ds_read2st64_b32 v[66:67], v104 offset0:32 offset1:36
	ds_read2st64_b32 v[64:65], v104 offset0:40 offset1:44
	ds_read2st64_b32 v[62:63], v104 offset0:48 offset1:52
	s_waitcnt vmcnt(0)
	ds_read2st64_b32 v[46:47], v104 offset0:56 offset1:60
	ds_read2st64_b32 v[44:45], v104 offset0:64 offset1:68
	ds_read2st64_b32 v[42:43], v104 offset0:72 offset1:76
	ds_read2st64_b32 v[40:41], v104 offset0:80 offset1:84
	ds_read2st64_b32 v[38:39], v104 offset0:88 offset1:92
	ds_read2st64_b32 v[36:37], v104 offset0:96 offset1:100
	ds_read2st64_b32 v[34:35], v104 offset0:104 offset1:108
	ds_read2st64_b32 v[32:33], v104 offset0:112 offset1:116
	ds_read2st64_b32 v[30:31], v104 offset0:120 offset1:124
	ds_read2st64_b32 v[28:29], v104 offset0:128 offset1:132
	ds_read2st64_b32 v[26:27], v104 offset0:136 offset1:140
	ds_read2st64_b32 v[24:25], v104 offset0:144 offset1:148
	ds_read2st64_b32 v[22:23], v104 offset0:152 offset1:156
	ds_read2st64_b32 v[20:21], v104 offset0:160 offset1:164
	ds_read2st64_b32 v[18:19], v104 offset0:168 offset1:172
	ds_read2st64_b32 v[16:17], v104 offset0:176 offset1:180
	ds_read2st64_b32 v[14:15], v104 offset0:184 offset1:188
	ds_read2st64_b32 v[12:13], v104 offset0:192 offset1:196
	ds_read2st64_b32 v[10:11], v104 offset0:200 offset1:204
	ds_read2st64_b32 v[8:9], v104 offset0:208 offset1:212
	ds_read2st64_b32 v[6:7], v104 offset0:216 offset1:220
	ds_read2st64_b32 v[4:5], v104 offset0:224 offset1:228
	ds_read2st64_b32 v[2:3], v104 offset0:232 offset1:236
	ds_read2st64_b32 v[0:1], v104 offset0:240 offset1:244
	s_waitcnt lgkmcnt(14)
	v_fma_f32 v117, v51, v118, v103
	v_fmac_f32_e32 v117, v72, v119
	v_fma_f32 v118, v51, v119, v103
	v_fmac_f32_e32 v117, v73, v120
	v_fmac_f32_e32 v118, v72, v120
	v_fma_f32 v119, v51, v120, v103
	v_fmac_f32_e32 v117, v74, v121
	v_fmac_f32_e32 v118, v73, v121
	v_fmac_f32_e32 v119, v72, v121
	v_fma_f32 v120, v51, v121, v103
	v_fmac_f32_e32 v117, v75, v70
	v_fmac_f32_e32 v118, v74, v70
	v_fmac_f32_e32 v119, v73, v70
	v_fmac_f32_e32 v120, v72, v70
	v_fma_f32 v70, v51, v70, v103
	v_fmac_f32_e32 v117, v76, v71
	v_fmac_f32_e32 v118, v75, v71
	v_fmac_f32_e32 v119, v74, v71
	v_fmac_f32_e32 v120, v73, v71
	v_fmac_f32_e32 v70, v72, v71
	v_fma_f32 v71, v51, v71, v103
	v_fmac_f32_e32 v117, v77, v68
	v_fmac_f32_e32 v118, v76, v68
	v_fmac_f32_e32 v119, v75, v68
	v_fmac_f32_e32 v120, v74, v68
	v_fmac_f32_e32 v70, v73, v68
	v_fmac_f32_e32 v71, v72, v68
	v_fma_f32 v68, v51, v68, v103
	v_fmac_f32_e32 v117, v78, v69
	v_fmac_f32_e32 v118, v77, v69
	v_fmac_f32_e32 v119, v76, v69
	v_fmac_f32_e32 v120, v75, v69
	v_fmac_f32_e32 v70, v74, v69
	v_fmac_f32_e32 v71, v73, v69
	v_fmac_f32_e32 v68, v72, v69
	v_fma_f32 v69, v51, v69, v103
	v_fmac_f32_e32 v117, v79, v66
	v_fmac_f32_e32 v118, v78, v66
	v_fmac_f32_e32 v119, v77, v66
	v_fmac_f32_e32 v120, v76, v66
	v_fmac_f32_e32 v70, v75, v66
	v_fmac_f32_e32 v71, v74, v66
	v_fmac_f32_e32 v68, v73, v66
	v_fmac_f32_e32 v69, v72, v66
	v_fma_f32 v66, v51, v66, v103
	v_fmac_f32_e32 v117, v80, v67
	v_fmac_f32_e32 v118, v79, v67
	v_fmac_f32_e32 v119, v78, v67
	v_fmac_f32_e32 v120, v77, v67
	v_fmac_f32_e32 v70, v76, v67
	v_fmac_f32_e32 v71, v75, v67
	v_fmac_f32_e32 v68, v74, v67
	v_fmac_f32_e32 v69, v73, v67
	v_fmac_f32_e32 v66, v72, v67
	v_fma_f32 v67, v51, v67, v103
	v_fmac_f32_e32 v117, v81, v64
	v_fmac_f32_e32 v118, v80, v64
	v_fmac_f32_e32 v119, v79, v64
	v_fmac_f32_e32 v120, v78, v64
	v_fmac_f32_e32 v70, v77, v64
	v_fmac_f32_e32 v71, v76, v64
	v_fmac_f32_e32 v68, v75, v64
	v_fmac_f32_e32 v69, v74, v64
	v_fmac_f32_e32 v66, v73, v64
	v_fmac_f32_e32 v67, v72, v64
	v_fma_f32 v64, v51, v64, v103
	v_fmac_f32_e32 v117, v82, v65
	v_fmac_f32_e32 v118, v81, v65
	v_fmac_f32_e32 v119, v80, v65
	v_fmac_f32_e32 v120, v79, v65
	v_fmac_f32_e32 v70, v78, v65
	v_fmac_f32_e32 v71, v77, v65
	v_fmac_f32_e32 v68, v76, v65
	v_fmac_f32_e32 v69, v75, v65
	v_fmac_f32_e32 v66, v74, v65
	v_fmac_f32_e32 v67, v73, v65
	v_fmac_f32_e32 v64, v72, v65
	v_fma_f32 v65, v51, v65, v103
	v_fmac_f32_e32 v117, v83, v62
	v_fmac_f32_e32 v118, v82, v62
	v_fmac_f32_e32 v119, v81, v62
	v_fmac_f32_e32 v120, v80, v62
	v_fmac_f32_e32 v70, v79, v62
	v_fmac_f32_e32 v71, v78, v62
	v_fmac_f32_e32 v68, v77, v62
	v_fmac_f32_e32 v69, v76, v62
	v_fmac_f32_e32 v66, v75, v62
	v_fmac_f32_e32 v67, v74, v62
	v_fmac_f32_e32 v64, v73, v62
	v_fmac_f32_e32 v65, v72, v62
	v_fma_f32 v62, v51, v62, v103
	v_fmac_f32_e32 v117, v84, v63
	v_fmac_f32_e32 v118, v83, v63
	v_fmac_f32_e32 v119, v82, v63
	v_fmac_f32_e32 v120, v81, v63
	v_fmac_f32_e32 v70, v80, v63
	v_fmac_f32_e32 v71, v79, v63
	v_fmac_f32_e32 v68, v78, v63
	v_fmac_f32_e32 v69, v77, v63
	v_fmac_f32_e32 v66, v76, v63
	v_fmac_f32_e32 v67, v75, v63
	v_fmac_f32_e32 v64, v74, v63
	v_fmac_f32_e32 v65, v73, v63
	v_fmac_f32_e32 v62, v72, v63
	v_fma_f32 v63, v51, v63, v103
	v_fmac_f32_e32 v117, v85, v46
	v_fmac_f32_e32 v118, v84, v46
	v_fmac_f32_e32 v119, v83, v46
	v_fmac_f32_e32 v120, v82, v46
	v_fmac_f32_e32 v70, v81, v46
	v_fmac_f32_e32 v71, v80, v46
	v_fmac_f32_e32 v68, v79, v46
	v_fmac_f32_e32 v69, v78, v46
	v_fmac_f32_e32 v66, v77, v46
	v_fmac_f32_e32 v67, v76, v46
	v_fmac_f32_e32 v64, v75, v46
	v_fmac_f32_e32 v65, v74, v46
	v_fmac_f32_e32 v62, v73, v46
	v_fmac_f32_e32 v63, v72, v46
	v_fma_f32 v46, v51, v46, v103
	v_fmac_f32_e32 v117, v86, v47
	v_fmac_f32_e32 v118, v85, v47
	v_fmac_f32_e32 v119, v84, v47
	v_fmac_f32_e32 v120, v83, v47
	v_fmac_f32_e32 v70, v82, v47
	v_fmac_f32_e32 v71, v81, v47
	v_fmac_f32_e32 v68, v80, v47
	v_fmac_f32_e32 v69, v79, v47
	v_fmac_f32_e32 v66, v78, v47
	v_fmac_f32_e32 v67, v77, v47
	v_fmac_f32_e32 v64, v76, v47
	v_fmac_f32_e32 v65, v75, v47
	v_fmac_f32_e32 v62, v74, v47
	v_fmac_f32_e32 v63, v73, v47
	v_fmac_f32_e32 v46, v72, v47
	v_fma_f32 v47, v51, v47, v103
	v_fmac_f32_e32 v117, v87, v44
	v_fmac_f32_e32 v118, v86, v44
	v_fmac_f32_e32 v119, v85, v44
	v_fmac_f32_e32 v120, v84, v44
	v_fmac_f32_e32 v70, v83, v44
	v_fmac_f32_e32 v71, v82, v44
	v_fmac_f32_e32 v68, v81, v44
	v_fmac_f32_e32 v69, v80, v44
	v_fmac_f32_e32 v66, v79, v44
	v_fmac_f32_e32 v67, v78, v44
	v_fmac_f32_e32 v64, v77, v44
	v_fmac_f32_e32 v65, v76, v44
	v_fmac_f32_e32 v62, v75, v44
	v_fmac_f32_e32 v63, v74, v44
	v_fmac_f32_e32 v46, v73, v44
	v_fmac_f32_e32 v47, v72, v44
	v_fma_f32 v44, v51, v44, v103
	v_fmac_f32_e32 v117, v88, v45
	v_fmac_f32_e32 v118, v87, v45
	v_fmac_f32_e32 v119, v86, v45
	v_fmac_f32_e32 v120, v85, v45
	v_fmac_f32_e32 v70, v84, v45
	v_fmac_f32_e32 v71, v83, v45
	v_fmac_f32_e32 v68, v82, v45
	v_fmac_f32_e32 v69, v81, v45
	v_fmac_f32_e32 v66, v80, v45
	v_fmac_f32_e32 v67, v79, v45
	v_fmac_f32_e32 v64, v78, v45
	v_fmac_f32_e32 v65, v77, v45
	v_fmac_f32_e32 v62, v76, v45
	v_fmac_f32_e32 v63, v75, v45
	v_fmac_f32_e32 v46, v74, v45
	v_fmac_f32_e32 v47, v73, v45
	v_fmac_f32_e32 v44, v72, v45
	v_fma_f32 v45, v51, v45, v103
	v_fmac_f32_e32 v117, v89, v42
	v_fmac_f32_e32 v118, v88, v42
	v_fmac_f32_e32 v119, v87, v42
	v_fmac_f32_e32 v120, v86, v42
	v_fmac_f32_e32 v70, v85, v42
	v_fmac_f32_e32 v71, v84, v42
	v_fmac_f32_e32 v68, v83, v42
	v_fmac_f32_e32 v69, v82, v42
	v_fmac_f32_e32 v66, v81, v42
	v_fmac_f32_e32 v67, v80, v42
	v_fmac_f32_e32 v64, v79, v42
	v_fmac_f32_e32 v65, v78, v42
	v_fmac_f32_e32 v62, v77, v42
	v_fmac_f32_e32 v63, v76, v42
	v_fmac_f32_e32 v46, v75, v42
	v_fmac_f32_e32 v47, v74, v42
	v_fmac_f32_e32 v44, v73, v42
	v_fmac_f32_e32 v45, v72, v42
	v_fma_f32 v42, v51, v42, v103
	v_fmac_f32_e32 v117, v90, v43
	v_fmac_f32_e32 v118, v89, v43
	v_fmac_f32_e32 v119, v88, v43
	v_fmac_f32_e32 v120, v87, v43
	v_fmac_f32_e32 v70, v86, v43
	v_fmac_f32_e32 v71, v85, v43
	v_fmac_f32_e32 v68, v84, v43
	v_fmac_f32_e32 v69, v83, v43
	v_fmac_f32_e32 v66, v82, v43
	v_fmac_f32_e32 v67, v81, v43
	v_fmac_f32_e32 v64, v80, v43
	v_fmac_f32_e32 v65, v79, v43
	v_fmac_f32_e32 v62, v78, v43
	v_fmac_f32_e32 v63, v77, v43
	v_fmac_f32_e32 v46, v76, v43
	v_fmac_f32_e32 v47, v75, v43
	v_fmac_f32_e32 v44, v74, v43
	v_fmac_f32_e32 v45, v73, v43
	v_fmac_f32_e32 v42, v72, v43
	v_fma_f32 v43, v51, v43, v103
	v_fmac_f32_e32 v117, v91, v40
	v_fmac_f32_e32 v118, v90, v40
	v_fmac_f32_e32 v119, v89, v40
	v_fmac_f32_e32 v120, v88, v40
	v_fmac_f32_e32 v70, v87, v40
	v_fmac_f32_e32 v71, v86, v40
	v_fmac_f32_e32 v68, v85, v40
	v_fmac_f32_e32 v69, v84, v40
	v_fmac_f32_e32 v66, v83, v40
	v_fmac_f32_e32 v67, v82, v40
	v_fmac_f32_e32 v64, v81, v40
	v_fmac_f32_e32 v65, v80, v40
	v_fmac_f32_e32 v62, v79, v40
	v_fmac_f32_e32 v63, v78, v40
	v_fmac_f32_e32 v46, v77, v40
	v_fmac_f32_e32 v47, v76, v40
	v_fmac_f32_e32 v44, v75, v40
	v_fmac_f32_e32 v45, v74, v40
	v_fmac_f32_e32 v42, v73, v40
	v_fmac_f32_e32 v43, v72, v40
	v_fma_f32 v40, v51, v40, v103
	v_fmac_f32_e32 v117, v92, v41
	v_fmac_f32_e32 v118, v91, v41
	v_fmac_f32_e32 v119, v90, v41
	v_fmac_f32_e32 v120, v89, v41
	v_fmac_f32_e32 v70, v88, v41
	v_fmac_f32_e32 v71, v87, v41
	v_fmac_f32_e32 v68, v86, v41
	v_fmac_f32_e32 v69, v85, v41
	v_fmac_f32_e32 v66, v84, v41
	v_fmac_f32_e32 v67, v83, v41
	v_fmac_f32_e32 v64, v82, v41
	v_fmac_f32_e32 v65, v81, v41
	v_fmac_f32_e32 v62, v80, v41
	v_fmac_f32_e32 v63, v79, v41
	v_fmac_f32_e32 v46, v78, v41
	v_fmac_f32_e32 v47, v77, v41
	v_fmac_f32_e32 v44, v76, v41
	v_fmac_f32_e32 v45, v75, v41
	v_fmac_f32_e32 v42, v74, v41
	v_fmac_f32_e32 v43, v73, v41
	v_fmac_f32_e32 v40, v72, v41
	v_fma_f32 v41, v51, v41, v103
	v_fmac_f32_e32 v117, v93, v38
	v_fmac_f32_e32 v118, v92, v38
	v_fmac_f32_e32 v119, v91, v38
	v_fmac_f32_e32 v120, v90, v38
	v_fmac_f32_e32 v70, v89, v38
	v_fmac_f32_e32 v71, v88, v38
	v_fmac_f32_e32 v68, v87, v38
	v_fmac_f32_e32 v69, v86, v38
	v_fmac_f32_e32 v66, v85, v38
	v_fmac_f32_e32 v67, v84, v38
	v_fmac_f32_e32 v64, v83, v38
	v_fmac_f32_e32 v65, v82, v38
	v_fmac_f32_e32 v62, v81, v38
	v_fmac_f32_e32 v63, v80, v38
	v_fmac_f32_e32 v46, v79, v38
	v_fmac_f32_e32 v47, v78, v38
	v_fmac_f32_e32 v44, v77, v38
	v_fmac_f32_e32 v45, v76, v38
	v_fmac_f32_e32 v42, v75, v38
	v_fmac_f32_e32 v43, v74, v38
	v_fmac_f32_e32 v40, v73, v38
	v_fmac_f32_e32 v41, v72, v38
	v_fma_f32 v38, v51, v38, v103
	v_fmac_f32_e32 v117, v94, v39
	v_fmac_f32_e32 v118, v93, v39
	v_fmac_f32_e32 v119, v92, v39
	v_fmac_f32_e32 v120, v91, v39
	v_fmac_f32_e32 v70, v90, v39
	v_fmac_f32_e32 v71, v89, v39
	v_fmac_f32_e32 v68, v88, v39
	v_fmac_f32_e32 v69, v87, v39
	v_fmac_f32_e32 v66, v86, v39
	v_fmac_f32_e32 v67, v85, v39
	v_fmac_f32_e32 v64, v84, v39
	v_fmac_f32_e32 v65, v83, v39
	v_fmac_f32_e32 v62, v82, v39
	v_fmac_f32_e32 v63, v81, v39
	v_fmac_f32_e32 v46, v80, v39
	v_fmac_f32_e32 v47, v79, v39
	v_fmac_f32_e32 v44, v78, v39
	v_fmac_f32_e32 v45, v77, v39
	v_fmac_f32_e32 v42, v76, v39
	v_fmac_f32_e32 v43, v75, v39
	v_fmac_f32_e32 v40, v74, v39
	v_fmac_f32_e32 v41, v73, v39
	v_fmac_f32_e32 v38, v72, v39
	v_fma_f32 v39, v51, v39, v103
	v_fmac_f32_e32 v117, v95, v36
	v_fmac_f32_e32 v118, v94, v36
	v_fmac_f32_e32 v119, v93, v36
	v_fmac_f32_e32 v120, v92, v36
	v_fmac_f32_e32 v70, v91, v36
	v_fmac_f32_e32 v71, v90, v36
	v_fmac_f32_e32 v68, v89, v36
	v_fmac_f32_e32 v69, v88, v36
	v_fmac_f32_e32 v66, v87, v36
	v_fmac_f32_e32 v67, v86, v36
	v_fmac_f32_e32 v64, v85, v36
	v_fmac_f32_e32 v65, v84, v36
	v_fmac_f32_e32 v62, v83, v36
	v_fmac_f32_e32 v63, v82, v36
	v_fmac_f32_e32 v46, v81, v36
	v_fmac_f32_e32 v47, v80, v36
	v_fmac_f32_e32 v44, v79, v36
	v_fmac_f32_e32 v45, v78, v36
	v_fmac_f32_e32 v42, v77, v36
	v_fmac_f32_e32 v43, v76, v36
	v_fmac_f32_e32 v40, v75, v36
	v_fmac_f32_e32 v41, v74, v36
	v_fmac_f32_e32 v38, v73, v36
	v_fmac_f32_e32 v39, v72, v36
	v_fma_f32 v36, v51, v36, v103
	v_fmac_f32_e32 v117, v96, v37
	v_fmac_f32_e32 v118, v95, v37
	v_fmac_f32_e32 v119, v94, v37
	v_fmac_f32_e32 v120, v93, v37
	v_fmac_f32_e32 v70, v92, v37
	v_fmac_f32_e32 v71, v91, v37
	v_fmac_f32_e32 v68, v90, v37
	v_fmac_f32_e32 v69, v89, v37
	v_fmac_f32_e32 v66, v88, v37
	v_fmac_f32_e32 v67, v87, v37
	v_fmac_f32_e32 v64, v86, v37
	v_fmac_f32_e32 v65, v85, v37
	v_fmac_f32_e32 v62, v84, v37
	v_fmac_f32_e32 v63, v83, v37
	v_fmac_f32_e32 v46, v82, v37
	v_fmac_f32_e32 v47, v81, v37
	v_fmac_f32_e32 v44, v80, v37
	v_fmac_f32_e32 v45, v79, v37
	v_fmac_f32_e32 v42, v78, v37
	v_fmac_f32_e32 v43, v77, v37
	v_fmac_f32_e32 v40, v76, v37
	v_fmac_f32_e32 v41, v75, v37
	v_fmac_f32_e32 v38, v74, v37
	v_fmac_f32_e32 v39, v73, v37
	v_fmac_f32_e32 v36, v72, v37
	v_fma_f32 v37, v51, v37, v103
	v_fmac_f32_e32 v117, v97, v34
	v_fmac_f32_e32 v118, v96, v34
	v_fmac_f32_e32 v119, v95, v34
	v_fmac_f32_e32 v120, v94, v34
	v_fmac_f32_e32 v70, v93, v34
	v_fmac_f32_e32 v71, v92, v34
	v_fmac_f32_e32 v68, v91, v34
	v_fmac_f32_e32 v69, v90, v34
	v_fmac_f32_e32 v66, v89, v34
	v_fmac_f32_e32 v67, v88, v34
	v_fmac_f32_e32 v64, v87, v34
	v_fmac_f32_e32 v65, v86, v34
	v_fmac_f32_e32 v62, v85, v34
	v_fmac_f32_e32 v63, v84, v34
	v_fmac_f32_e32 v46, v83, v34
	v_fmac_f32_e32 v47, v82, v34
	v_fmac_f32_e32 v44, v81, v34
	v_fmac_f32_e32 v45, v80, v34
	v_fmac_f32_e32 v42, v79, v34
	v_fmac_f32_e32 v43, v78, v34
	v_fmac_f32_e32 v40, v77, v34
	v_fmac_f32_e32 v41, v76, v34
	v_fmac_f32_e32 v38, v75, v34
	v_fmac_f32_e32 v39, v74, v34
	v_fmac_f32_e32 v36, v73, v34
	v_fmac_f32_e32 v37, v72, v34
	v_fma_f32 v34, v51, v34, v103
	v_fmac_f32_e32 v117, v98, v35
	v_fmac_f32_e32 v118, v97, v35
	v_fmac_f32_e32 v119, v96, v35
	v_fmac_f32_e32 v120, v95, v35
	v_fmac_f32_e32 v70, v94, v35
	v_fmac_f32_e32 v71, v93, v35
	v_fmac_f32_e32 v68, v92, v35
	v_fmac_f32_e32 v69, v91, v35
	v_fmac_f32_e32 v66, v90, v35
	v_fmac_f32_e32 v67, v89, v35
	v_fmac_f32_e32 v64, v88, v35
	v_fmac_f32_e32 v65, v87, v35
	v_fmac_f32_e32 v62, v86, v35
	v_fmac_f32_e32 v63, v85, v35
	v_fmac_f32_e32 v46, v84, v35
	v_fmac_f32_e32 v47, v83, v35
	v_fmac_f32_e32 v44, v82, v35
	v_fmac_f32_e32 v45, v81, v35
	v_fmac_f32_e32 v42, v80, v35
	v_fmac_f32_e32 v43, v79, v35
	v_fmac_f32_e32 v40, v78, v35
	v_fmac_f32_e32 v41, v77, v35
	v_fmac_f32_e32 v38, v76, v35
	v_fmac_f32_e32 v39, v75, v35
	v_fmac_f32_e32 v36, v74, v35
	v_fmac_f32_e32 v37, v73, v35
	v_fmac_f32_e32 v34, v72, v35
	v_fma_f32 v35, v51, v35, v103
	v_fmac_f32_e32 v117, v99, v32
	v_fmac_f32_e32 v118, v98, v32
	v_fmac_f32_e32 v119, v97, v32
	v_fmac_f32_e32 v120, v96, v32
	v_fmac_f32_e32 v70, v95, v32
	v_fmac_f32_e32 v71, v94, v32
	v_fmac_f32_e32 v68, v93, v32
	v_fmac_f32_e32 v69, v92, v32
	v_fmac_f32_e32 v66, v91, v32
	v_fmac_f32_e32 v67, v90, v32
	v_fmac_f32_e32 v64, v89, v32
	v_fmac_f32_e32 v65, v88, v32
	v_fmac_f32_e32 v62, v87, v32
	v_fmac_f32_e32 v63, v86, v32
	v_fmac_f32_e32 v46, v85, v32
	v_fmac_f32_e32 v47, v84, v32
	v_fmac_f32_e32 v44, v83, v32
	v_fmac_f32_e32 v45, v82, v32
	v_fmac_f32_e32 v42, v81, v32
	v_fmac_f32_e32 v43, v80, v32
	v_fmac_f32_e32 v40, v79, v32
	v_fmac_f32_e32 v41, v78, v32
	v_fmac_f32_e32 v38, v77, v32
	v_fmac_f32_e32 v39, v76, v32
	v_fmac_f32_e32 v36, v75, v32
	v_fmac_f32_e32 v37, v74, v32
	v_fmac_f32_e32 v34, v73, v32
	v_fmac_f32_e32 v35, v72, v32
	v_fma_f32 v32, v51, v32, v103
	v_fmac_f32_e32 v117, v101, v33
	v_fmac_f32_e32 v118, v99, v33
	v_fmac_f32_e32 v119, v98, v33
	v_fmac_f32_e32 v120, v97, v33
	v_fmac_f32_e32 v70, v96, v33
	v_fmac_f32_e32 v71, v95, v33
	v_fmac_f32_e32 v68, v94, v33
	v_fmac_f32_e32 v69, v93, v33
	v_fmac_f32_e32 v66, v92, v33
	v_fmac_f32_e32 v67, v91, v33
	v_fmac_f32_e32 v64, v90, v33
	v_fmac_f32_e32 v65, v89, v33
	v_fmac_f32_e32 v62, v88, v33
	v_fmac_f32_e32 v63, v87, v33
	v_fmac_f32_e32 v46, v86, v33
	v_fmac_f32_e32 v47, v85, v33
	v_fmac_f32_e32 v44, v84, v33
	v_fmac_f32_e32 v45, v83, v33
	v_fmac_f32_e32 v42, v82, v33
	v_fmac_f32_e32 v43, v81, v33
	v_fmac_f32_e32 v40, v80, v33
	v_fmac_f32_e32 v41, v79, v33
	v_fmac_f32_e32 v38, v78, v33
	v_fmac_f32_e32 v39, v77, v33
	v_fmac_f32_e32 v36, v76, v33
	v_fmac_f32_e32 v37, v75, v33
	v_fmac_f32_e32 v34, v74, v33
	v_fmac_f32_e32 v35, v73, v33
	v_fmac_f32_e32 v32, v72, v33
	v_fma_f32 v33, v51, v33, v103
	v_fmac_f32_e32 v117, v102, v30
	v_fmac_f32_e32 v118, v101, v30
	v_fmac_f32_e32 v119, v99, v30
	v_fmac_f32_e32 v120, v98, v30
	v_fmac_f32_e32 v70, v97, v30
	v_fmac_f32_e32 v71, v96, v30
	v_fmac_f32_e32 v68, v95, v30
	v_fmac_f32_e32 v69, v94, v30
	v_fmac_f32_e32 v66, v93, v30
	v_fmac_f32_e32 v67, v92, v30
	v_fmac_f32_e32 v64, v91, v30
	v_fmac_f32_e32 v65, v90, v30
	v_fmac_f32_e32 v62, v89, v30
	v_fmac_f32_e32 v63, v88, v30
	v_fmac_f32_e32 v46, v87, v30
	v_fmac_f32_e32 v47, v86, v30
	v_fmac_f32_e32 v44, v85, v30
	v_fmac_f32_e32 v45, v84, v30
	v_fmac_f32_e32 v42, v83, v30
	v_fmac_f32_e32 v43, v82, v30
	v_fmac_f32_e32 v40, v81, v30
	v_fmac_f32_e32 v41, v80, v30
	v_fmac_f32_e32 v38, v79, v30
	v_fmac_f32_e32 v39, v78, v30
	v_fmac_f32_e32 v36, v77, v30
	v_fmac_f32_e32 v37, v76, v30
	v_fmac_f32_e32 v34, v75, v30
	v_fmac_f32_e32 v35, v74, v30
	v_fmac_f32_e32 v32, v73, v30
	v_fmac_f32_e32 v33, v72, v30
	v_fma_f32 v30, v51, v30, v103
	v_fmac_f32_e32 v118, v102, v31
	v_fmac_f32_e32 v119, v101, v31
	v_fmac_f32_e32 v120, v99, v31
	v_fmac_f32_e32 v70, v98, v31
	v_fmac_f32_e32 v71, v97, v31
	v_fmac_f32_e32 v68, v96, v31
	v_fmac_f32_e32 v69, v95, v31
	v_fmac_f32_e32 v66, v94, v31
	v_fmac_f32_e32 v67, v93, v31
	v_fmac_f32_e32 v64, v92, v31
	v_fmac_f32_e32 v65, v91, v31
	v_fmac_f32_e32 v62, v90, v31
	v_fmac_f32_e32 v63, v89, v31
	v_fmac_f32_e32 v46, v88, v31
	v_fmac_f32_e32 v47, v87, v31
	v_fmac_f32_e32 v44, v86, v31
	v_fmac_f32_e32 v45, v85, v31
	v_fmac_f32_e32 v42, v84, v31
	v_fmac_f32_e32 v43, v83, v31
	v_fmac_f32_e32 v40, v82, v31
	v_fmac_f32_e32 v41, v81, v31
	v_fmac_f32_e32 v38, v80, v31
	v_fmac_f32_e32 v39, v79, v31
	v_fmac_f32_e32 v36, v78, v31
	v_fmac_f32_e32 v37, v77, v31
	v_fmac_f32_e32 v34, v76, v31
	v_fmac_f32_e32 v35, v75, v31
	v_fmac_f32_e32 v32, v74, v31
	v_fmac_f32_e32 v33, v73, v31
	v_fmac_f32_e32 v30, v72, v31
	v_fma_f32 v31, v51, v31, v103
	v_fmac_f32_e32 v30, v73, v28
	v_fmac_f32_e32 v31, v72, v28
	v_fmac_f32_e32 v30, v74, v29
	v_fmac_f32_e32 v31, v73, v29
	v_fmac_f32_e32 v33, v74, v28
	s_waitcnt lgkmcnt(13)
	v_fmac_f32_e32 v30, v75, v26
	v_fmac_f32_e32 v31, v74, v26
	v_fmac_f32_e32 v32, v75, v28
	v_fmac_f32_e32 v33, v75, v29
	v_fmac_f32_e32 v30, v76, v27
	v_fmac_f32_e32 v31, v75, v27
	v_fmac_f32_e32 v35, v76, v28
	v_fmac_f32_e32 v32, v76, v29
	v_fmac_f32_e32 v33, v76, v26
	s_waitcnt lgkmcnt(12)
	v_fmac_f32_e32 v30, v77, v24
	v_fmac_f32_e32 v31, v76, v24
	v_fmac_f32_e32 v34, v77, v28
	v_fmac_f32_e32 v35, v77, v29
	v_fmac_f32_e32 v32, v77, v26
	v_fmac_f32_e32 v33, v77, v27
	v_fmac_f32_e32 v30, v78, v25
	v_fmac_f32_e32 v31, v77, v25
	v_fmac_f32_e32 v37, v78, v28
	v_fmac_f32_e32 v34, v78, v29
	v_fmac_f32_e32 v35, v78, v26
	v_fmac_f32_e32 v32, v78, v27
	v_fmac_f32_e32 v33, v78, v24
	s_waitcnt lgkmcnt(11)
	v_fmac_f32_e32 v30, v79, v22
	v_fmac_f32_e32 v31, v78, v22
	v_fmac_f32_e32 v36, v79, v28
	v_fmac_f32_e32 v37, v79, v29
	v_fmac_f32_e32 v34, v79, v26
	v_fmac_f32_e32 v35, v79, v27
	v_fmac_f32_e32 v32, v79, v24
	v_fmac_f32_e32 v33, v79, v25
	v_fmac_f32_e32 v30, v80, v23
	v_fmac_f32_e32 v31, v79, v23
	v_fmac_f32_e32 v39, v80, v28
	v_fmac_f32_e32 v36, v80, v29
	v_fmac_f32_e32 v37, v80, v26
	v_fmac_f32_e32 v34, v80, v27
	v_fmac_f32_e32 v35, v80, v24
	v_fmac_f32_e32 v32, v80, v25
	v_fmac_f32_e32 v33, v80, v22
	s_waitcnt lgkmcnt(10)
	v_fmac_f32_e32 v30, v81, v20
	v_fmac_f32_e32 v31, v80, v20
	v_fmac_f32_e32 v38, v81, v28
	v_fmac_f32_e32 v39, v81, v29
	v_fmac_f32_e32 v36, v81, v26
	v_fmac_f32_e32 v37, v81, v27
	v_fmac_f32_e32 v34, v81, v24
	v_fmac_f32_e32 v35, v81, v25
	v_fmac_f32_e32 v32, v81, v22
	v_fmac_f32_e32 v33, v81, v23
	v_fmac_f32_e32 v30, v82, v21
	v_fmac_f32_e32 v31, v81, v21
	v_fmac_f32_e32 v41, v82, v28
	v_fmac_f32_e32 v38, v82, v29
	v_fmac_f32_e32 v39, v82, v26
	v_fmac_f32_e32 v36, v82, v27
	v_fmac_f32_e32 v37, v82, v24
	v_fmac_f32_e32 v34, v82, v25
	v_fmac_f32_e32 v35, v82, v22
	v_fmac_f32_e32 v32, v82, v23
	v_fmac_f32_e32 v33, v82, v20
	s_waitcnt lgkmcnt(9)
	v_fmac_f32_e32 v30, v83, v18
	v_fmac_f32_e32 v31, v82, v18
	v_fmac_f32_e32 v40, v83, v28
	v_fmac_f32_e32 v41, v83, v29
	v_fmac_f32_e32 v38, v83, v26
	v_fmac_f32_e32 v39, v83, v27
	v_fmac_f32_e32 v36, v83, v24
	v_fmac_f32_e32 v37, v83, v25
	v_fmac_f32_e32 v34, v83, v22
	v_fmac_f32_e32 v35, v83, v23
	v_fmac_f32_e32 v32, v83, v20
	v_fmac_f32_e32 v33, v83, v21
	v_fmac_f32_e32 v30, v84, v19
	v_fmac_f32_e32 v31, v83, v19
	v_fmac_f32_e32 v43, v84, v28
	v_fmac_f32_e32 v40, v84, v29
	v_fmac_f32_e32 v41, v84, v26
	v_fmac_f32_e32 v38, v84, v27
	v_fmac_f32_e32 v39, v84, v24
	v_fmac_f32_e32 v36, v84, v25
	v_fmac_f32_e32 v37, v84, v22
	v_fmac_f32_e32 v34, v84, v23
	v_fmac_f32_e32 v35, v84, v20
	v_fmac_f32_e32 v32, v84, v21
	v_fmac_f32_e32 v33, v84, v18
	s_waitcnt lgkmcnt(8)
	v_fmac_f32_e32 v30, v85, v16
	v_fmac_f32_e32 v31, v84, v16
	v_fmac_f32_e32 v42, v85, v28
	v_fmac_f32_e32 v43, v85, v29
	v_fmac_f32_e32 v40, v85, v26
	v_fmac_f32_e32 v41, v85, v27
	v_fmac_f32_e32 v38, v85, v24
	v_fmac_f32_e32 v39, v85, v25
	v_fmac_f32_e32 v36, v85, v22
	v_fmac_f32_e32 v37, v85, v23
	v_fmac_f32_e32 v34, v85, v20
	v_fmac_f32_e32 v35, v85, v21
	v_fmac_f32_e32 v32, v85, v18
	v_fmac_f32_e32 v33, v85, v19
	v_fmac_f32_e32 v30, v86, v17
	v_fmac_f32_e32 v31, v85, v17
	v_fmac_f32_e32 v45, v86, v28
	v_fmac_f32_e32 v42, v86, v29
	v_fmac_f32_e32 v43, v86, v26
	v_fmac_f32_e32 v40, v86, v27
	v_fmac_f32_e32 v41, v86, v24
	v_fmac_f32_e32 v38, v86, v25
	v_fmac_f32_e32 v39, v86, v22
	v_fmac_f32_e32 v36, v86, v23
	v_fmac_f32_e32 v37, v86, v20
	v_fmac_f32_e32 v34, v86, v21
	v_fmac_f32_e32 v35, v86, v18
	v_fmac_f32_e32 v32, v86, v19
	v_fmac_f32_e32 v33, v86, v16
	s_waitcnt lgkmcnt(7)
	v_fmac_f32_e32 v30, v87, v14
	v_fmac_f32_e32 v31, v86, v14
	v_fmac_f32_e32 v44, v87, v28
	v_fmac_f32_e32 v45, v87, v29
	v_fmac_f32_e32 v42, v87, v26
	v_fmac_f32_e32 v43, v87, v27
	v_fmac_f32_e32 v40, v87, v24
	v_fmac_f32_e32 v41, v87, v25
	v_fmac_f32_e32 v38, v87, v22
	v_fmac_f32_e32 v39, v87, v23
	v_fmac_f32_e32 v36, v87, v20
	v_fmac_f32_e32 v37, v87, v21
	v_fmac_f32_e32 v34, v87, v18
	v_fmac_f32_e32 v35, v87, v19
	v_fmac_f32_e32 v32, v87, v16
	v_fmac_f32_e32 v33, v87, v17
	v_fmac_f32_e32 v30, v88, v15
	v_fmac_f32_e32 v31, v87, v15
	v_fmac_f32_e32 v47, v88, v28
	v_fmac_f32_e32 v44, v88, v29
	v_fmac_f32_e32 v45, v88, v26
	v_fmac_f32_e32 v42, v88, v27
	v_fmac_f32_e32 v43, v88, v24
	v_fmac_f32_e32 v40, v88, v25
	v_fmac_f32_e32 v41, v88, v22
	v_fmac_f32_e32 v38, v88, v23
	v_fmac_f32_e32 v39, v88, v20
	v_fmac_f32_e32 v36, v88, v21
	v_fmac_f32_e32 v37, v88, v18
	v_fmac_f32_e32 v34, v88, v19
	v_fmac_f32_e32 v35, v88, v16
	v_fmac_f32_e32 v32, v88, v17
	v_fmac_f32_e32 v33, v88, v14
	s_waitcnt lgkmcnt(6)
	v_fmac_f32_e32 v30, v89, v12
	v_fmac_f32_e32 v31, v88, v12
	v_fmac_f32_e32 v46, v89, v28
	v_fmac_f32_e32 v47, v89, v29
	v_fmac_f32_e32 v44, v89, v26
	v_fmac_f32_e32 v45, v89, v27
	v_fmac_f32_e32 v42, v89, v24
	v_fmac_f32_e32 v43, v89, v25
	v_fmac_f32_e32 v40, v89, v22
	v_fmac_f32_e32 v41, v89, v23
	v_fmac_f32_e32 v38, v89, v20
	v_fmac_f32_e32 v39, v89, v21
	v_fmac_f32_e32 v36, v89, v18
	v_fmac_f32_e32 v37, v89, v19
	v_fmac_f32_e32 v34, v89, v16
	v_fmac_f32_e32 v35, v89, v17
	v_fmac_f32_e32 v32, v89, v14
	v_fmac_f32_e32 v33, v89, v15
	v_fmac_f32_e32 v30, v90, v13
	v_fmac_f32_e32 v31, v89, v13
	v_fmac_f32_e32 v63, v90, v28
	v_fmac_f32_e32 v46, v90, v29
	v_fmac_f32_e32 v47, v90, v26
	v_fmac_f32_e32 v44, v90, v27
	v_fmac_f32_e32 v45, v90, v24
	v_fmac_f32_e32 v42, v90, v25
	v_fmac_f32_e32 v43, v90, v22
	v_fmac_f32_e32 v40, v90, v23
	v_fmac_f32_e32 v41, v90, v20
	v_fmac_f32_e32 v38, v90, v21
	v_fmac_f32_e32 v39, v90, v18
	v_fmac_f32_e32 v36, v90, v19
	v_fmac_f32_e32 v37, v90, v16
	v_fmac_f32_e32 v34, v90, v17
	v_fmac_f32_e32 v35, v90, v14
	v_fmac_f32_e32 v32, v90, v15
	v_fmac_f32_e32 v33, v90, v12
	s_waitcnt lgkmcnt(5)
	v_fmac_f32_e32 v30, v91, v10
	v_fmac_f32_e32 v31, v90, v10
	v_fmac_f32_e32 v62, v91, v28
	v_fmac_f32_e32 v63, v91, v29
	v_fmac_f32_e32 v46, v91, v26
	v_fmac_f32_e32 v47, v91, v27
	v_fmac_f32_e32 v44, v91, v24
	v_fmac_f32_e32 v45, v91, v25
	v_fmac_f32_e32 v42, v91, v22
	v_fmac_f32_e32 v43, v91, v23
	v_fmac_f32_e32 v40, v91, v20
	v_fmac_f32_e32 v41, v91, v21
	v_fmac_f32_e32 v38, v91, v18
	v_fmac_f32_e32 v39, v91, v19
	v_fmac_f32_e32 v36, v91, v16
	v_fmac_f32_e32 v37, v91, v17
	v_fmac_f32_e32 v34, v91, v14
	v_fmac_f32_e32 v35, v91, v15
	v_fmac_f32_e32 v32, v91, v12
	v_fmac_f32_e32 v33, v91, v13
	v_fmac_f32_e32 v30, v92, v11
	v_fmac_f32_e32 v31, v91, v11
	v_fmac_f32_e32 v65, v92, v28
	v_fmac_f32_e32 v62, v92, v29
	v_fmac_f32_e32 v63, v92, v26
	v_fmac_f32_e32 v46, v92, v27
	v_fmac_f32_e32 v47, v92, v24
	v_fmac_f32_e32 v44, v92, v25
	v_fmac_f32_e32 v45, v92, v22
	v_fmac_f32_e32 v42, v92, v23
	v_fmac_f32_e32 v43, v92, v20
	v_fmac_f32_e32 v40, v92, v21
	v_fmac_f32_e32 v41, v92, v18
	v_fmac_f32_e32 v38, v92, v19
	v_fmac_f32_e32 v39, v92, v16
	v_fmac_f32_e32 v36, v92, v17
	v_fmac_f32_e32 v37, v92, v14
	v_fmac_f32_e32 v34, v92, v15
	v_fmac_f32_e32 v35, v92, v12
	v_fmac_f32_e32 v32, v92, v13
	v_fmac_f32_e32 v33, v92, v10
	s_waitcnt lgkmcnt(4)
	v_fmac_f32_e32 v30, v93, v8
	v_fmac_f32_e32 v31, v92, v8
	v_fmac_f32_e32 v64, v93, v28
	v_fmac_f32_e32 v65, v93, v29
	v_fmac_f32_e32 v62, v93, v26
	v_fmac_f32_e32 v63, v93, v27
	v_fmac_f32_e32 v46, v93, v24
	v_fmac_f32_e32 v47, v93, v25
	v_fmac_f32_e32 v44, v93, v22
	v_fmac_f32_e32 v45, v93, v23
	v_fmac_f32_e32 v42, v93, v20
	v_fmac_f32_e32 v43, v93, v21
	v_fmac_f32_e32 v40, v93, v18
	v_fmac_f32_e32 v41, v93, v19
	v_fmac_f32_e32 v38, v93, v16
	v_fmac_f32_e32 v39, v93, v17
	v_fmac_f32_e32 v36, v93, v14
	v_fmac_f32_e32 v37, v93, v15
	v_fmac_f32_e32 v34, v93, v12
	v_fmac_f32_e32 v35, v93, v13
	v_fmac_f32_e32 v32, v93, v10
	v_fmac_f32_e32 v33, v93, v11
	v_fmac_f32_e32 v30, v94, v9
	v_fmac_f32_e32 v31, v93, v9
	v_fmac_f32_e32 v67, v94, v28
	v_fmac_f32_e32 v64, v94, v29
	v_fmac_f32_e32 v65, v94, v26
	v_fmac_f32_e32 v62, v94, v27
	v_fmac_f32_e32 v63, v94, v24
	v_fmac_f32_e32 v46, v94, v25
	v_fmac_f32_e32 v47, v94, v22
	v_fmac_f32_e32 v44, v94, v23
	v_fmac_f32_e32 v45, v94, v20
	v_fmac_f32_e32 v42, v94, v21
	v_fmac_f32_e32 v43, v94, v18
	v_fmac_f32_e32 v40, v94, v19
	v_fmac_f32_e32 v41, v94, v16
	v_fmac_f32_e32 v38, v94, v17
	v_fmac_f32_e32 v39, v94, v14
	v_fmac_f32_e32 v36, v94, v15
	v_fmac_f32_e32 v37, v94, v12
	v_fmac_f32_e32 v34, v94, v13
	v_fmac_f32_e32 v35, v94, v10
	v_fmac_f32_e32 v32, v94, v11
	v_fmac_f32_e32 v33, v94, v8
	s_waitcnt lgkmcnt(3)
	v_fmac_f32_e32 v30, v95, v6
	v_fmac_f32_e32 v31, v94, v6
	v_fmac_f32_e32 v66, v95, v28
	v_fmac_f32_e32 v67, v95, v29
	v_fmac_f32_e32 v64, v95, v26
	v_fmac_f32_e32 v65, v95, v27
	v_fmac_f32_e32 v62, v95, v24
	v_fmac_f32_e32 v63, v95, v25
	v_fmac_f32_e32 v46, v95, v22
	v_fmac_f32_e32 v47, v95, v23
	v_fmac_f32_e32 v44, v95, v20
	v_fmac_f32_e32 v45, v95, v21
	v_fmac_f32_e32 v42, v95, v18
	v_fmac_f32_e32 v43, v95, v19
	v_fmac_f32_e32 v40, v95, v16
	v_fmac_f32_e32 v41, v95, v17
	v_fmac_f32_e32 v38, v95, v14
	v_fmac_f32_e32 v39, v95, v15
	v_fmac_f32_e32 v36, v95, v12
	v_fmac_f32_e32 v37, v95, v13
	v_fmac_f32_e32 v34, v95, v10
	v_fmac_f32_e32 v35, v95, v11
	v_fmac_f32_e32 v32, v95, v8
	v_fmac_f32_e32 v33, v95, v9
	v_fmac_f32_e32 v30, v96, v7
	v_fmac_f32_e32 v31, v95, v7
	v_fmac_f32_e32 v69, v96, v28
	v_fmac_f32_e32 v66, v96, v29
	v_fmac_f32_e32 v67, v96, v26
	v_fmac_f32_e32 v64, v96, v27
	v_fmac_f32_e32 v65, v96, v24
	v_fmac_f32_e32 v62, v96, v25
	v_fmac_f32_e32 v63, v96, v22
	v_fmac_f32_e32 v46, v96, v23
	v_fmac_f32_e32 v47, v96, v20
	v_fmac_f32_e32 v44, v96, v21
	v_fmac_f32_e32 v45, v96, v18
	v_fmac_f32_e32 v42, v96, v19
	v_fmac_f32_e32 v43, v96, v16
	v_fmac_f32_e32 v40, v96, v17
	v_fmac_f32_e32 v41, v96, v14
	v_fmac_f32_e32 v38, v96, v15
	v_fmac_f32_e32 v39, v96, v12
	v_fmac_f32_e32 v36, v96, v13
	v_fmac_f32_e32 v37, v96, v10
	v_fmac_f32_e32 v34, v96, v11
	v_fmac_f32_e32 v35, v96, v8
	v_fmac_f32_e32 v32, v96, v9
	v_fmac_f32_e32 v33, v96, v6
	s_waitcnt lgkmcnt(2)
	v_fmac_f32_e32 v30, v97, v4
	v_fmac_f32_e32 v31, v96, v4
	v_fmac_f32_e32 v68, v97, v28
	v_fmac_f32_e32 v69, v97, v29
	v_fmac_f32_e32 v66, v97, v26
	v_fmac_f32_e32 v67, v97, v27
	v_fmac_f32_e32 v64, v97, v24
	v_fmac_f32_e32 v65, v97, v25
	v_fmac_f32_e32 v62, v97, v22
	v_fmac_f32_e32 v63, v97, v23
	v_fmac_f32_e32 v46, v97, v20
	v_fmac_f32_e32 v47, v97, v21
	v_fmac_f32_e32 v44, v97, v18
	v_fmac_f32_e32 v45, v97, v19
	v_fmac_f32_e32 v42, v97, v16
	v_fmac_f32_e32 v43, v97, v17
	v_fmac_f32_e32 v40, v97, v14
	v_fmac_f32_e32 v41, v97, v15
	v_fmac_f32_e32 v38, v97, v12
	v_fmac_f32_e32 v39, v97, v13
	v_fmac_f32_e32 v36, v97, v10
	v_fmac_f32_e32 v37, v97, v11
	v_fmac_f32_e32 v34, v97, v8
	v_fmac_f32_e32 v35, v97, v9
	v_fmac_f32_e32 v32, v97, v6
	v_fmac_f32_e32 v33, v97, v7
	v_fmac_f32_e32 v30, v98, v5
	v_fmac_f32_e32 v31, v97, v5
	v_fmac_f32_e32 v71, v98, v28
	v_fmac_f32_e32 v68, v98, v29
	v_fmac_f32_e32 v69, v98, v26
	v_fmac_f32_e32 v66, v98, v27
	v_fmac_f32_e32 v67, v98, v24
	v_fmac_f32_e32 v64, v98, v25
	v_fmac_f32_e32 v65, v98, v22
	v_fmac_f32_e32 v62, v98, v23
	v_fmac_f32_e32 v63, v98, v20
	v_fmac_f32_e32 v46, v98, v21
	v_fmac_f32_e32 v47, v98, v18
	v_fmac_f32_e32 v44, v98, v19
	v_fmac_f32_e32 v45, v98, v16
	v_fmac_f32_e32 v42, v98, v17
	v_fmac_f32_e32 v43, v98, v14
	v_fmac_f32_e32 v40, v98, v15
	v_fmac_f32_e32 v41, v98, v12
	v_fmac_f32_e32 v38, v98, v13
	v_fmac_f32_e32 v39, v98, v10
	v_fmac_f32_e32 v36, v98, v11
	v_fmac_f32_e32 v37, v98, v8
	v_fmac_f32_e32 v34, v98, v9
	v_fmac_f32_e32 v35, v98, v6
	v_fmac_f32_e32 v32, v98, v7
	v_fmac_f32_e32 v33, v98, v4
	s_waitcnt lgkmcnt(1)
	v_fmac_f32_e32 v30, v99, v2
	v_fmac_f32_e32 v31, v98, v2
	v_fmac_f32_e32 v70, v99, v28
	v_fmac_f32_e32 v71, v99, v29
	v_fmac_f32_e32 v68, v99, v26
	v_fmac_f32_e32 v69, v99, v27
	v_fmac_f32_e32 v66, v99, v24
	v_fmac_f32_e32 v67, v99, v25
	v_fmac_f32_e32 v64, v99, v22
	v_fmac_f32_e32 v65, v99, v23
	v_fmac_f32_e32 v62, v99, v20
	v_fmac_f32_e32 v63, v99, v21
	v_fmac_f32_e32 v46, v99, v18
	v_fmac_f32_e32 v47, v99, v19
	v_fmac_f32_e32 v44, v99, v16
	v_fmac_f32_e32 v45, v99, v17
	v_fmac_f32_e32 v42, v99, v14
	v_fmac_f32_e32 v43, v99, v15
	v_fmac_f32_e32 v40, v99, v12
	v_fmac_f32_e32 v41, v99, v13
	v_fmac_f32_e32 v38, v99, v10
	v_fmac_f32_e32 v39, v99, v11
	v_fmac_f32_e32 v36, v99, v8
	v_fmac_f32_e32 v37, v99, v9
	v_fmac_f32_e32 v34, v99, v6
	v_fmac_f32_e32 v35, v99, v7
	v_fmac_f32_e32 v32, v99, v4
	v_fmac_f32_e32 v33, v99, v5
	v_fmac_f32_e32 v30, v101, v3
	v_fmac_f32_e32 v31, v99, v3
	v_fmac_f32_e32 v120, v101, v28
	v_fmac_f32_e32 v70, v101, v29
	v_fmac_f32_e32 v71, v101, v26
	v_fmac_f32_e32 v68, v101, v27
	v_fmac_f32_e32 v69, v101, v24
	v_fmac_f32_e32 v66, v101, v25
	v_fmac_f32_e32 v67, v101, v22
	v_fmac_f32_e32 v64, v101, v23
	v_fmac_f32_e32 v65, v101, v20
	v_fmac_f32_e32 v62, v101, v21
	v_fmac_f32_e32 v63, v101, v18
	v_fmac_f32_e32 v46, v101, v19
	v_fmac_f32_e32 v47, v101, v16
	v_fmac_f32_e32 v44, v101, v17
	v_fmac_f32_e32 v45, v101, v14
	v_fmac_f32_e32 v42, v101, v15
	v_fmac_f32_e32 v43, v101, v12
	v_fmac_f32_e32 v40, v101, v13
	v_fmac_f32_e32 v41, v101, v10
	v_fmac_f32_e32 v38, v101, v11
	v_fmac_f32_e32 v39, v101, v8
	v_fmac_f32_e32 v36, v101, v9
	v_fmac_f32_e32 v37, v101, v6
	v_fmac_f32_e32 v34, v101, v7
	v_fmac_f32_e32 v35, v101, v4
	v_fmac_f32_e32 v32, v101, v5
	v_fmac_f32_e32 v33, v101, v2
	s_waitcnt lgkmcnt(0)
	v_fmac_f32_e32 v30, v102, v0
	v_fmac_f32_e32 v31, v101, v0
	v_add_u32_e32 v0, s6, v105
	v_fmac_f32_e32 v119, v102, v28
	v_fmac_f32_e32 v120, v102, v29
	v_fmac_f32_e32 v70, v102, v26
	v_fmac_f32_e32 v71, v102, v27
	v_fmac_f32_e32 v68, v102, v24
	v_fmac_f32_e32 v69, v102, v25
	v_fmac_f32_e32 v66, v102, v22
	v_fmac_f32_e32 v67, v102, v23
	v_fmac_f32_e32 v64, v102, v20
	v_fmac_f32_e32 v65, v102, v21
	v_fmac_f32_e32 v62, v102, v18
	v_fmac_f32_e32 v63, v102, v19
	v_fmac_f32_e32 v46, v102, v16
	v_fmac_f32_e32 v47, v102, v17
	v_fmac_f32_e32 v44, v102, v14
	v_fmac_f32_e32 v45, v102, v15
	v_fmac_f32_e32 v42, v102, v12
	v_fmac_f32_e32 v43, v102, v13
	v_fmac_f32_e32 v40, v102, v10
	v_fmac_f32_e32 v41, v102, v11
	v_fmac_f32_e32 v38, v102, v8
	v_fmac_f32_e32 v39, v102, v9
	v_fmac_f32_e32 v36, v102, v6
	v_fmac_f32_e32 v37, v102, v7
	v_fmac_f32_e32 v34, v102, v4
	v_fmac_f32_e32 v35, v102, v5
	v_fmac_f32_e32 v32, v102, v2
	v_fmac_f32_e32 v33, v102, v3
	v_fmac_f32_e32 v31, v102, v1
	s_barrier
	ds_write2st64_b32 v104, v117, v118 offset1:4
	ds_write2st64_b32 v104, v119, v120 offset0:8 offset1:12
	ds_write2st64_b32 v104, v70, v71 offset0:16 offset1:20
	ds_write2st64_b32 v104, v68, v69 offset0:24 offset1:28
	ds_write2st64_b32 v104, v66, v67 offset0:32 offset1:36
	ds_write2st64_b32 v104, v64, v65 offset0:40 offset1:44
	ds_write2st64_b32 v104, v62, v63 offset0:48 offset1:52
	ds_write2st64_b32 v104, v46, v47 offset0:56 offset1:60
	ds_write2st64_b32 v104, v44, v45 offset0:64 offset1:68
	ds_write2st64_b32 v104, v42, v43 offset0:72 offset1:76
	ds_write2st64_b32 v104, v40, v41 offset0:80 offset1:84
	ds_write2st64_b32 v104, v38, v39 offset0:88 offset1:92
	ds_write2st64_b32 v104, v36, v37 offset0:96 offset1:100
	ds_write2st64_b32 v104, v34, v35 offset0:104 offset1:108
	ds_write2st64_b32 v104, v32, v33 offset0:112 offset1:116
	ds_write2st64_b32 v104, v30, v31 offset0:120 offset1:124
	s_waitcnt lgkmcnt(0)
	s_barrier
	ds_read_b128 v[0:3], v0
	v_add_u32_e32 v12, s17, v105
	s_lshl_b64 s[0:1], s[2:3], 12
	s_ashr_i32 s2, s51, 31
	s_add_u32 s4, s0, s51
	s_waitcnt lgkmcnt(0)
	v_add_f32_e32 v4, v0, v1
	v_add_f32_e32 v4, v2, v4
	v_add_f32_e32 v4, v3, v4
	ds_swizzle_b32 v5, v4 offset:swizzle(SWAP,1)
	s_addc_u32 s5, s1, s2
	s_add_u32 s0, s4, s15
	s_addc_u32 s1, s5, s7
	s_lshl_b64 s[0:1], s[0:1], 11
	s_waitcnt lgkmcnt(0)
	v_add_f32_e32 v4, v4, v5
	ds_swizzle_b32 v5, v4 offset:swizzle(SWAP,2)
	s_mov_b32 s52, 0x3b800000
	s_waitcnt lgkmcnt(0)
	v_add_f32_e32 v4, v4, v5
	ds_swizzle_b32 v5, v4 offset:swizzle(SWAP,4)
	s_waitcnt lgkmcnt(0)
	v_add_f32_e32 v4, v4, v5
	ds_swizzle_b32 v5, v4 offset:swizzle(SWAP,8)
	s_waitcnt lgkmcnt(0)
	v_add_f32_e32 v4, v4, v5
	ds_swizzle_b32 v5, v4 offset:swizzle(SWAP,16)
	s_waitcnt lgkmcnt(0)
	v_add_f32_e32 v4, v4, v5
	v_mov_b32_e32 v5, v4
	s_nop 1
	v_permlane32_swap_b32_e32 v4, v5
	v_add_f32_e32 v4, v4, v5
	v_fmamk_f32 v19, v4, 0xbb800000, v1
	v_fmamk_f32 v18, v4, 0xbb800000, v0
	v_fmamk_f32 v3, v4, 0xbb800000, v3
	v_fmac_f32_e32 v2, 0xbb800000, v4
	v_mul_f32_e64 v4, v18, v18
	v_mul_f32_e64 v5, v19, v19
	v_mul_f32_e64 v0, v2, v2
	v_mul_f32_e64 v1, v3, v3
	v_add_f32_e32 v4, v4, v5
	v_add_f32_e32 v0, v0, v4
	global_load_dwordx4 v[4:7], v[56:57], off
	global_load_dwordx4 v[8:11], v[58:59], off
	ds_read_b128 v[12:15], v12
	v_add_f32_e32 v0, v1, v0
	ds_swizzle_b32 v1, v0 offset:swizzle(SWAP,1)
	s_waitcnt lgkmcnt(1)
	v_add_f32_e32 v16, v12, v13
	v_add_f32_e32 v16, v14, v16
	v_add_f32_e32 v16, v15, v16
	ds_swizzle_b32 v20, v16 offset:swizzle(SWAP,1)
	s_waitcnt lgkmcnt(1)
	v_add_f32_e32 v0, v0, v1
	ds_swizzle_b32 v1, v0 offset:swizzle(SWAP,2)
	s_waitcnt lgkmcnt(1)
	v_add_f32_e32 v16, v16, v20
	ds_swizzle_b32 v20, v16 offset:swizzle(SWAP,2)
	s_waitcnt lgkmcnt(1)
	v_add_f32_e32 v0, v0, v1
	ds_swizzle_b32 v1, v0 offset:swizzle(SWAP,4)
	s_waitcnt lgkmcnt(1)
	v_add_f32_e32 v16, v16, v20
	ds_swizzle_b32 v20, v16 offset:swizzle(SWAP,4)
	s_waitcnt lgkmcnt(1)
	v_add_f32_e32 v0, v0, v1
	ds_swizzle_b32 v1, v0 offset:swizzle(SWAP,8)
	s_waitcnt lgkmcnt(1)
	v_add_f32_e32 v16, v16, v20
	ds_swizzle_b32 v20, v16 offset:swizzle(SWAP,8)
	s_waitcnt lgkmcnt(1)
	v_add_f32_e32 v0, v0, v1
	ds_swizzle_b32 v1, v0 offset:swizzle(SWAP,16)
	s_waitcnt lgkmcnt(1)
	v_add_f32_e32 v16, v16, v20
	ds_swizzle_b32 v20, v16 offset:swizzle(SWAP,16)
	s_waitcnt lgkmcnt(1)
	v_add_f32_e32 v17, v0, v1
	v_mov_b32_e32 v21, v17
	s_nop 1
	v_permlane32_swap_b32_e32 v17, v21
	s_waitcnt lgkmcnt(0)
	v_add_f32_e32 v16, v16, v20
	v_mov_b32_e32 v20, v16
	s_nop 1
	v_permlane32_swap_b32_e32 v16, v20
	v_add_f32_e32 v16, v16, v20
	v_fmamk_f32 v13, v16, 0xbb800000, v13
	v_fmamk_f32 v12, v16, 0xbb800000, v12
	v_fmamk_f32 v15, v16, 0xbb800000, v15
	v_fmac_f32_e32 v14, 0xbb800000, v16
	v_mul_f32_e64 v24, v12, v12
	v_mul_f32_e64 v25, v13, v13
	v_mul_f32_e64 v22, v14, v14
	v_mul_f32_e64 v23, v15, v15
	v_add_f32_e32 v16, v24, v25
	v_add_f32_e32 v16, v22, v16
	v_add_f32_e32 v16, v23, v16
	ds_swizzle_b32 v20, v16 offset:swizzle(SWAP,1)
	v_lshl_add_u64 v[0:1], v[60:61], 0, s[0:1]
	s_mov_b32 s0, 0x3727c5ac
	s_waitcnt lgkmcnt(0)
	v_add_f32_e32 v16, v16, v20
	ds_swizzle_b32 v20, v16 offset:swizzle(SWAP,2)
	s_waitcnt lgkmcnt(0)
	v_add_f32_e32 v16, v16, v20
	ds_swizzle_b32 v20, v16 offset:swizzle(SWAP,4)
	s_waitcnt lgkmcnt(0)
	v_add_f32_e32 v16, v16, v20
	ds_swizzle_b32 v20, v16 offset:swizzle(SWAP,8)
	s_waitcnt lgkmcnt(0)
	v_add_f32_e32 v16, v16, v20
	ds_swizzle_b32 v20, v16 offset:swizzle(SWAP,16)
	s_waitcnt lgkmcnt(0)
	v_add_f32_e32 v16, v16, v20
	v_mov_b32_e32 v20, v16
	s_nop 1
	v_permlane32_swap_b32_e32 v16, v20
	v_add_f32_e64 v20, v16, v20
	v_add_f32_e64 v21, v17, v21
	v_mov_b64_e32 v[16:17], s[0:1]
	v_fma_f32 v20, v20, s52, v16
	v_fma_f32 v21, v21, s52, v16
	s_nop 0
	v_mul_f32_e32 v22, 0x4b800000, v21
	v_cmp_gt_f32_e64 s[2:3], s56, v21
	v_cmp_gt_f32_e64 s[0:1], s56, v20
	s_nop 0
	v_cndmask_b32_e64 v21, v21, v22, s[2:3]
	v_rsq_f32_e32 v21, v21
	s_nop 0
	v_mul_f32_e32 v22, 0x45800000, v21
	v_cndmask_b32_e64 v22, v21, v22, s[2:3]
	v_mul_f32_e64 v18, v18, v22
	v_mul_f32_e64 v19, v19, v22
	v_mul_f32_e64 v2, v2, v22
	v_mul_f32_e64 v3, v3, v22
	s_waitcnt vmcnt(0)
	v_fma_f32 v4, v4, v18, v8
	v_fma_f32 v5, v5, v19, v9
	v_fma_f32 v2, v6, v2, v10
	v_fma_f32 v3, v7, v3, v11
	v_mul_f32_e32 v6, 0xbfb8aa3b, v4
	v_mul_f32_e32 v7, 0xbfb8aa3b, v5
	v_exp_f32_e32 v6, v6
	v_exp_f32_e32 v7, v7
	v_add_f32_e32 v6, 1.0, v6
	v_add_f32_e32 v7, 1.0, v7
	v_rcp_f32_e32 v6, v6
	v_rcp_f32_e32 v7, v7
	s_nop 0
	v_mul_f32_e64 v4, v4, v6
	v_mul_f32_e64 v5, v5, v7
	s_nop 0
	v_cvt_pk_bf16_f32 v4, v4, v5
	v_mul_f32_e32 v5, 0xbfb8aa3b, v2
	v_exp_f32_e32 v5, v5
	s_nop 0
	v_add_f32_e32 v5, 1.0, v5
	v_rcp_f32_e32 v6, v5
	v_mul_f32_e32 v5, 0xbfb8aa3b, v3
	v_exp_f32_e32 v5, v5
	s_nop 0
	v_add_f32_e32 v5, 1.0, v5
	v_rcp_f32_e32 v7, v5
	s_nop 0
	v_mul_f32_e64 v2, v2, v6
	v_mul_f32_e64 v3, v3, v7
	s_nop 0
	v_cvt_pk_bf16_f32 v5, v2, v3
	global_store_dwordx2 v[0:1], v[4:5], off
	v_mul_f32_e32 v0, 0x4b800000, v20
	v_cndmask_b32_e64 v0, v20, v0, s[0:1]
	v_rsq_f32_e32 v0, v0
	s_nop 0
	v_mul_f32_e32 v1, 0x45800000, v0
	v_cndmask_b32_e64 v8, v0, v1, s[0:1]
	global_load_dwordx4 v[0:3], v[56:57], off
	global_load_dwordx4 v[4:7], v[58:59], off
	v_mul_f32_e64 v10, v12, v8
	v_mul_f32_e64 v11, v13, v8
	v_mul_f32_e64 v9, v15, v8
	v_mul_f32_e64 v8, v14, v8
	s_add_u32 s0, s4, s16
	s_addc_u32 s1, s5, s18
	s_lshl_b64 s[0:1], s[0:1], 11
	v_add_u32_e32 v12, s23, v105
	s_waitcnt vmcnt(0)
	v_fma_f32 v0, v0, v10, v4
	v_fma_f32 v1, v1, v11, v5
	s_nop 0
	v_mul_f32_e32 v4, 0xbfb8aa3b, v0
	v_mul_f32_e32 v5, 0xbfb8aa3b, v1
	v_exp_f32_e32 v4, v4
	v_exp_f32_e32 v5, v5
	v_fma_f32 v2, v2, v8, v6
	v_fma_f32 v3, v3, v9, v7
	v_add_f32_e32 v4, 1.0, v4
	v_add_f32_e32 v5, 1.0, v5
	v_rcp_f32_e32 v4, v4
	v_rcp_f32_e32 v5, v5
	s_nop 0
	v_mul_f32_e64 v0, v0, v4
	v_mul_f32_e64 v1, v1, v5
	s_nop 0
	v_cvt_pk_bf16_f32 v0, v0, v1
	v_mul_f32_e32 v1, 0xbfb8aa3b, v2
	v_exp_f32_e32 v1, v1
	s_nop 0
	v_add_f32_e32 v1, 1.0, v1
	v_rcp_f32_e32 v4, v1
	v_mul_f32_e32 v1, 0xbfb8aa3b, v3
	v_exp_f32_e32 v1, v1
	s_nop 0
	v_add_f32_e32 v1, 1.0, v1
	v_rcp_f32_e32 v5, v1
	s_nop 0
	v_mul_f32_e64 v2, v2, v4
	v_mul_f32_e64 v3, v3, v5
	s_nop 0
	v_cvt_pk_bf16_f32 v1, v2, v3
	v_lshl_add_u64 v[2:3], v[60:61], 0, s[0:1]
	global_store_dwordx2 v[2:3], v[0:1], off
	v_add_u32_e32 v0, s20, v105
	ds_read_b128 v[0:3], v0
	s_add_u32 s0, s4, s19
	s_addc_u32 s1, s5, s21
	s_lshl_b64 s[0:1], s[0:1], 11
	s_waitcnt lgkmcnt(0)
	v_add_f32_e32 v4, v0, v1
	v_add_f32_e32 v4, v2, v4
	v_add_f32_e32 v4, v3, v4
	ds_swizzle_b32 v5, v4 offset:swizzle(SWAP,1)
	s_waitcnt lgkmcnt(0)
	v_add_f32_e32 v4, v4, v5
	ds_swizzle_b32 v5, v4 offset:swizzle(SWAP,2)
	s_waitcnt lgkmcnt(0)
	v_add_f32_e32 v4, v4, v5
	ds_swizzle_b32 v5, v4 offset:swizzle(SWAP,4)
	s_waitcnt lgkmcnt(0)
	v_add_f32_e32 v4, v4, v5
	ds_swizzle_b32 v5, v4 offset:swizzle(SWAP,8)
	s_waitcnt lgkmcnt(0)
	v_add_f32_e32 v4, v4, v5
	ds_swizzle_b32 v5, v4 offset:swizzle(SWAP,16)
	s_waitcnt lgkmcnt(0)
	v_add_f32_e32 v4, v4, v5
	v_mov_b32_e32 v5, v4
	s_nop 1
	v_permlane32_swap_b32_e32 v4, v5
	v_add_f32_e32 v4, v4, v5
	v_fmamk_f32 v19, v4, 0xbb800000, v1
	v_fmamk_f32 v18, v4, 0xbb800000, v0
	v_fmamk_f32 v3, v4, 0xbb800000, v3
	v_fmac_f32_e32 v2, 0xbb800000, v4
	v_mul_f32_e64 v4, v18, v18
	v_mul_f32_e64 v5, v19, v19
	v_mul_f32_e64 v0, v2, v2
	v_mul_f32_e64 v1, v3, v3
	v_add_f32_e32 v4, v4, v5
	v_add_f32_e32 v0, v0, v4
	global_load_dwordx4 v[4:7], v[56:57], off
	global_load_dwordx4 v[8:11], v[58:59], off
	ds_read_b128 v[12:15], v12
	v_add_f32_e32 v0, v1, v0
	ds_swizzle_b32 v1, v0 offset:swizzle(SWAP,1)
	s_waitcnt lgkmcnt(1)
	v_add_f32_e32 v20, v12, v13
	v_add_f32_e32 v20, v14, v20
	v_add_f32_e32 v20, v15, v20
	ds_swizzle_b32 v22, v20 offset:swizzle(SWAP,1)
	s_waitcnt lgkmcnt(1)
	v_add_f32_e32 v0, v0, v1
	ds_swizzle_b32 v1, v0 offset:swizzle(SWAP,2)
	s_waitcnt lgkmcnt(1)
	v_add_f32_e32 v20, v20, v22
	ds_swizzle_b32 v22, v20 offset:swizzle(SWAP,2)
	s_waitcnt lgkmcnt(1)
	v_add_f32_e32 v0, v0, v1
	ds_swizzle_b32 v1, v0 offset:swizzle(SWAP,4)
	s_waitcnt lgkmcnt(1)
	v_add_f32_e32 v20, v20, v22
	ds_swizzle_b32 v22, v20 offset:swizzle(SWAP,4)
	s_waitcnt lgkmcnt(1)
	v_add_f32_e32 v0, v0, v1
	ds_swizzle_b32 v1, v0 offset:swizzle(SWAP,8)
	s_waitcnt lgkmcnt(1)
	v_add_f32_e32 v20, v20, v22
	ds_swizzle_b32 v22, v20 offset:swizzle(SWAP,8)
	s_waitcnt lgkmcnt(1)
	v_add_f32_e32 v0, v0, v1
	ds_swizzle_b32 v1, v0 offset:swizzle(SWAP,16)
	s_waitcnt lgkmcnt(1)
	v_add_f32_e32 v20, v20, v22
	ds_swizzle_b32 v22, v20 offset:swizzle(SWAP,16)
	s_waitcnt lgkmcnt(1)
	v_add_f32_e32 v21, v0, v1
	v_mov_b32_e32 v23, v21
	s_nop 1
	v_permlane32_swap_b32_e32 v21, v23
	s_waitcnt lgkmcnt(0)
	v_add_f32_e32 v20, v20, v22
	v_mov_b32_e32 v22, v20
	s_nop 1
	v_permlane32_swap_b32_e32 v20, v22
	v_add_f32_e32 v20, v20, v22
	v_fmamk_f32 v13, v20, 0xbb800000, v13
	v_fmamk_f32 v12, v20, 0xbb800000, v12
	v_fmamk_f32 v15, v20, 0xbb800000, v15
	v_fmac_f32_e32 v14, 0xbb800000, v20
	v_mul_f32_e64 v26, v12, v12
	v_mul_f32_e64 v27, v13, v13
	v_mul_f32_e64 v24, v14, v14
	v_mul_f32_e64 v25, v15, v15
	v_add_f32_e32 v20, v26, v27
	v_add_f32_e32 v20, v24, v20
	v_add_f32_e32 v20, v25, v20
	ds_swizzle_b32 v22, v20 offset:swizzle(SWAP,1)
	v_lshl_add_u64 v[0:1], v[60:61], 0, s[0:1]
	s_waitcnt lgkmcnt(0)
	v_add_f32_e32 v20, v20, v22
	ds_swizzle_b32 v22, v20 offset:swizzle(SWAP,2)
	s_waitcnt lgkmcnt(0)
	v_add_f32_e32 v20, v20, v22
	ds_swizzle_b32 v22, v20 offset:swizzle(SWAP,4)
	s_waitcnt lgkmcnt(0)
	v_add_f32_e32 v20, v20, v22
	ds_swizzle_b32 v22, v20 offset:swizzle(SWAP,8)
	s_waitcnt lgkmcnt(0)
	v_add_f32_e32 v20, v20, v22
	ds_swizzle_b32 v22, v20 offset:swizzle(SWAP,16)
	s_waitcnt lgkmcnt(0)
	v_add_f32_e32 v20, v20, v22
	v_mov_b32_e32 v22, v20
	s_nop 1
	v_permlane32_swap_b32_e32 v20, v22
	v_add_f32_e64 v20, v20, v22
	v_add_f32_e64 v21, v21, v23
	s_nop 0
	v_fma_f32 v20, v20, s52, v16
	v_fma_f32 v21, v21, s52, v16
	s_nop 0
	v_mul_f32_e32 v22, 0x4b800000, v21
	v_cmp_gt_f32_e64 s[2:3], s56, v21
	v_cmp_gt_f32_e64 s[0:1], s56, v20
	s_nop 0
	v_cndmask_b32_e64 v21, v21, v22, s[2:3]
	v_rsq_f32_e32 v21, v21
	s_nop 0
	v_mul_f32_e32 v22, 0x45800000, v21
	v_cndmask_b32_e64 v22, v21, v22, s[2:3]
	v_mul_f32_e64 v18, v18, v22
	v_mul_f32_e64 v19, v19, v22
	v_mul_f32_e64 v2, v2, v22
	v_mul_f32_e64 v3, v3, v22
	s_waitcnt vmcnt(0)
	v_fma_f32 v4, v4, v18, v8
	v_fma_f32 v5, v5, v19, v9
	v_fma_f32 v2, v6, v2, v10
	v_fma_f32 v3, v7, v3, v11
	v_mul_f32_e32 v6, 0xbfb8aa3b, v4
	v_mul_f32_e32 v7, 0xbfb8aa3b, v5
	v_exp_f32_e32 v6, v6
	v_exp_f32_e32 v7, v7
	v_add_f32_e32 v6, 1.0, v6
	v_add_f32_e32 v7, 1.0, v7
	v_rcp_f32_e32 v6, v6
	v_rcp_f32_e32 v7, v7
	s_nop 0
	v_mul_f32_e64 v4, v4, v6
	v_mul_f32_e64 v5, v5, v7
	s_nop 0
	v_cvt_pk_bf16_f32 v4, v4, v5
	v_mul_f32_e32 v5, 0xbfb8aa3b, v2
	v_exp_f32_e32 v5, v5
	s_nop 0
	v_add_f32_e32 v5, 1.0, v5
	v_rcp_f32_e32 v6, v5
	v_mul_f32_e32 v5, 0xbfb8aa3b, v3
	v_exp_f32_e32 v5, v5
	s_nop 0
	v_add_f32_e32 v5, 1.0, v5
	v_rcp_f32_e32 v7, v5
	s_nop 0
	v_mul_f32_e64 v2, v2, v6
	v_mul_f32_e64 v3, v3, v7
	s_nop 0
	v_cvt_pk_bf16_f32 v5, v2, v3
	global_store_dwordx2 v[0:1], v[4:5], off
	v_mul_f32_e32 v0, 0x4b800000, v20
	v_cndmask_b32_e64 v0, v20, v0, s[0:1]
	v_rsq_f32_e32 v0, v0
	s_nop 0
	v_mul_f32_e32 v1, 0x45800000, v0
	v_cndmask_b32_e64 v8, v0, v1, s[0:1]
	global_load_dwordx4 v[0:3], v[56:57], off
	global_load_dwordx4 v[4:7], v[58:59], off
	v_mul_f32_e64 v10, v12, v8
	v_mul_f32_e64 v11, v13, v8
	v_mul_f32_e64 v9, v15, v8
	v_mul_f32_e64 v8, v14, v8
	s_add_u32 s0, s4, s22
	s_addc_u32 s1, s5, s24
	s_lshl_b64 s[0:1], s[0:1], 11
	v_add_u32_e32 v12, s29, v105
	s_waitcnt vmcnt(0)
	v_fma_f32 v0, v0, v10, v4
	v_fma_f32 v1, v1, v11, v5
	s_nop 0
	v_mul_f32_e32 v4, 0xbfb8aa3b, v0
	v_mul_f32_e32 v5, 0xbfb8aa3b, v1
	v_exp_f32_e32 v4, v4
	v_exp_f32_e32 v5, v5
	v_fma_f32 v2, v2, v8, v6
	v_fma_f32 v3, v3, v9, v7
	v_add_f32_e32 v4, 1.0, v4
	v_add_f32_e32 v5, 1.0, v5
	v_rcp_f32_e32 v4, v4
	v_rcp_f32_e32 v5, v5
	s_nop 0
	v_mul_f32_e64 v0, v0, v4
	v_mul_f32_e64 v1, v1, v5
	s_nop 0
	v_cvt_pk_bf16_f32 v0, v0, v1
	v_mul_f32_e32 v1, 0xbfb8aa3b, v2
	v_exp_f32_e32 v1, v1
	s_nop 0
	v_add_f32_e32 v1, 1.0, v1
	v_rcp_f32_e32 v4, v1
	v_mul_f32_e32 v1, 0xbfb8aa3b, v3
	v_exp_f32_e32 v1, v1
	s_nop 0
	v_add_f32_e32 v1, 1.0, v1
	v_rcp_f32_e32 v5, v1
	s_nop 0
	v_mul_f32_e64 v2, v2, v4
	v_mul_f32_e64 v3, v3, v5
	s_nop 0
	v_cvt_pk_bf16_f32 v1, v2, v3
	v_lshl_add_u64 v[2:3], v[60:61], 0, s[0:1]
	global_store_dwordx2 v[2:3], v[0:1], off
	v_add_u32_e32 v0, s26, v105
	ds_read_b128 v[0:3], v0
	s_add_u32 s0, s4, s25
	s_addc_u32 s1, s5, s27
	s_lshl_b64 s[0:1], s[0:1], 11
	s_waitcnt lgkmcnt(0)
	v_add_f32_e32 v4, v0, v1
	v_add_f32_e32 v4, v2, v4
	v_add_f32_e32 v4, v3, v4
	ds_swizzle_b32 v5, v4 offset:swizzle(SWAP,1)
	s_waitcnt lgkmcnt(0)
	v_add_f32_e32 v4, v4, v5
	ds_swizzle_b32 v5, v4 offset:swizzle(SWAP,2)
	s_waitcnt lgkmcnt(0)
	v_add_f32_e32 v4, v4, v5
	ds_swizzle_b32 v5, v4 offset:swizzle(SWAP,4)
	s_waitcnt lgkmcnt(0)
	v_add_f32_e32 v4, v4, v5
	ds_swizzle_b32 v5, v4 offset:swizzle(SWAP,8)
	s_waitcnt lgkmcnt(0)
	v_add_f32_e32 v4, v4, v5
	ds_swizzle_b32 v5, v4 offset:swizzle(SWAP,16)
	s_waitcnt lgkmcnt(0)
	v_add_f32_e32 v4, v4, v5
	v_mov_b32_e32 v5, v4
	s_nop 1
	v_permlane32_swap_b32_e32 v4, v5
	v_add_f32_e32 v4, v4, v5
	v_fmamk_f32 v19, v4, 0xbb800000, v1
	v_fmamk_f32 v18, v4, 0xbb800000, v0
	v_fmamk_f32 v3, v4, 0xbb800000, v3
	v_fmac_f32_e32 v2, 0xbb800000, v4
	v_mul_f32_e64 v4, v18, v18
	v_mul_f32_e64 v5, v19, v19
	v_mul_f32_e64 v0, v2, v2
	v_mul_f32_e64 v1, v3, v3
	v_add_f32_e32 v4, v4, v5
	v_add_f32_e32 v0, v0, v4
	global_load_dwordx4 v[4:7], v[56:57], off
	global_load_dwordx4 v[8:11], v[58:59], off
	ds_read_b128 v[12:15], v12
	v_add_f32_e32 v0, v1, v0
	ds_swizzle_b32 v1, v0 offset:swizzle(SWAP,1)
	s_waitcnt lgkmcnt(1)
	v_add_f32_e32 v20, v12, v13
	v_add_f32_e32 v20, v14, v20
	v_add_f32_e32 v20, v15, v20
	ds_swizzle_b32 v22, v20 offset:swizzle(SWAP,1)
	s_waitcnt lgkmcnt(1)
	v_add_f32_e32 v0, v0, v1
	ds_swizzle_b32 v1, v0 offset:swizzle(SWAP,2)
	s_waitcnt lgkmcnt(1)
	v_add_f32_e32 v20, v20, v22
	ds_swizzle_b32 v22, v20 offset:swizzle(SWAP,2)
	s_waitcnt lgkmcnt(1)
	v_add_f32_e32 v0, v0, v1
	ds_swizzle_b32 v1, v0 offset:swizzle(SWAP,4)
	s_waitcnt lgkmcnt(1)
	v_add_f32_e32 v20, v20, v22
	ds_swizzle_b32 v22, v20 offset:swizzle(SWAP,4)
	s_waitcnt lgkmcnt(1)
	v_add_f32_e32 v0, v0, v1
	ds_swizzle_b32 v1, v0 offset:swizzle(SWAP,8)
	s_waitcnt lgkmcnt(1)
	v_add_f32_e32 v20, v20, v22
	ds_swizzle_b32 v22, v20 offset:swizzle(SWAP,8)
	s_waitcnt lgkmcnt(1)
	v_add_f32_e32 v0, v0, v1
	ds_swizzle_b32 v1, v0 offset:swizzle(SWAP,16)
	s_waitcnt lgkmcnt(1)
	v_add_f32_e32 v20, v20, v22
	ds_swizzle_b32 v22, v20 offset:swizzle(SWAP,16)
	s_waitcnt lgkmcnt(1)
	v_add_f32_e32 v21, v0, v1
	v_mov_b32_e32 v23, v21
	s_nop 1
	v_permlane32_swap_b32_e32 v21, v23
	s_waitcnt lgkmcnt(0)
	v_add_f32_e32 v20, v20, v22
	v_mov_b32_e32 v22, v20
	s_nop 1
	v_permlane32_swap_b32_e32 v20, v22
	v_add_f32_e32 v20, v20, v22
	v_fmamk_f32 v13, v20, 0xbb800000, v13
	v_fmamk_f32 v12, v20, 0xbb800000, v12
	v_fmamk_f32 v15, v20, 0xbb800000, v15
	v_fmac_f32_e32 v14, 0xbb800000, v20
	v_mul_f32_e64 v26, v12, v12
	v_mul_f32_e64 v27, v13, v13
	v_mul_f32_e64 v24, v14, v14
	v_mul_f32_e64 v25, v15, v15
	v_add_f32_e32 v20, v26, v27
	v_add_f32_e32 v20, v24, v20
	v_add_f32_e32 v20, v25, v20
	ds_swizzle_b32 v22, v20 offset:swizzle(SWAP,1)
	v_lshl_add_u64 v[0:1], v[60:61], 0, s[0:1]
	s_waitcnt lgkmcnt(0)
	v_add_f32_e32 v20, v20, v22
	ds_swizzle_b32 v22, v20 offset:swizzle(SWAP,2)
	s_waitcnt lgkmcnt(0)
	v_add_f32_e32 v20, v20, v22
	ds_swizzle_b32 v22, v20 offset:swizzle(SWAP,4)
	s_waitcnt lgkmcnt(0)
	v_add_f32_e32 v20, v20, v22
	ds_swizzle_b32 v22, v20 offset:swizzle(SWAP,8)
	s_waitcnt lgkmcnt(0)
	v_add_f32_e32 v20, v20, v22
	ds_swizzle_b32 v22, v20 offset:swizzle(SWAP,16)
	s_waitcnt lgkmcnt(0)
	v_add_f32_e32 v20, v20, v22
	v_mov_b32_e32 v22, v20
	s_nop 1
	v_permlane32_swap_b32_e32 v20, v22
	v_add_f32_e64 v20, v20, v22
	v_add_f32_e64 v21, v21, v23
	s_nop 0
	v_fma_f32 v20, v20, s52, v16
	v_fma_f32 v21, v21, s52, v16
	s_nop 0
	v_mul_f32_e32 v22, 0x4b800000, v21
	v_cmp_gt_f32_e64 s[2:3], s56, v21
	v_cmp_gt_f32_e64 s[0:1], s56, v20
	s_nop 0
	v_cndmask_b32_e64 v21, v21, v22, s[2:3]
	v_rsq_f32_e32 v21, v21
	s_nop 0
	v_mul_f32_e32 v22, 0x45800000, v21
	v_cndmask_b32_e64 v22, v21, v22, s[2:3]
	v_mul_f32_e64 v18, v18, v22
	v_mul_f32_e64 v19, v19, v22
	v_mul_f32_e64 v2, v2, v22
	v_mul_f32_e64 v3, v3, v22
	s_waitcnt vmcnt(0)
	v_fma_f32 v4, v4, v18, v8
	v_fma_f32 v5, v5, v19, v9
	v_fma_f32 v2, v6, v2, v10
	v_fma_f32 v3, v7, v3, v11
	v_mul_f32_e32 v6, 0xbfb8aa3b, v4
	v_mul_f32_e32 v7, 0xbfb8aa3b, v5
	v_exp_f32_e32 v6, v6
	v_exp_f32_e32 v7, v7
	v_add_f32_e32 v6, 1.0, v6
	v_add_f32_e32 v7, 1.0, v7
	v_rcp_f32_e32 v6, v6
	v_rcp_f32_e32 v7, v7
	s_nop 0
	v_mul_f32_e64 v4, v4, v6
	v_mul_f32_e64 v5, v5, v7
	s_nop 0
	v_cvt_pk_bf16_f32 v4, v4, v5
	v_mul_f32_e32 v5, 0xbfb8aa3b, v2
	v_exp_f32_e32 v5, v5
	s_nop 0
	v_add_f32_e32 v5, 1.0, v5
	v_rcp_f32_e32 v6, v5
	v_mul_f32_e32 v5, 0xbfb8aa3b, v3
	v_exp_f32_e32 v5, v5
	s_nop 0
	v_add_f32_e32 v5, 1.0, v5
	v_rcp_f32_e32 v7, v5
	s_nop 0
	v_mul_f32_e64 v2, v2, v6
	v_mul_f32_e64 v3, v3, v7
	s_nop 0
	v_cvt_pk_bf16_f32 v5, v2, v3
	global_store_dwordx2 v[0:1], v[4:5], off
	v_mul_f32_e32 v0, 0x4b800000, v20
	v_cndmask_b32_e64 v0, v20, v0, s[0:1]
	v_rsq_f32_e32 v0, v0
	s_nop 0
	v_mul_f32_e32 v1, 0x45800000, v0
	v_cndmask_b32_e64 v8, v0, v1, s[0:1]
	global_load_dwordx4 v[0:3], v[56:57], off
	global_load_dwordx4 v[4:7], v[58:59], off
	v_mul_f32_e64 v10, v12, v8
	v_mul_f32_e64 v11, v13, v8
	v_mul_f32_e64 v9, v15, v8
	v_mul_f32_e64 v8, v14, v8
	s_add_u32 s0, s4, s28
	s_addc_u32 s1, s5, s30
	s_lshl_b64 s[0:1], s[0:1], 11
	v_add_u32_e32 v12, s47, v105
	s_waitcnt vmcnt(0)
	v_fma_f32 v0, v0, v10, v4
	v_fma_f32 v1, v1, v11, v5
	s_nop 0
	v_mul_f32_e32 v4, 0xbfb8aa3b, v0
	v_mul_f32_e32 v5, 0xbfb8aa3b, v1
	v_exp_f32_e32 v4, v4
	v_exp_f32_e32 v5, v5
	v_fma_f32 v2, v2, v8, v6
	v_fma_f32 v3, v3, v9, v7
	v_add_f32_e32 v4, 1.0, v4
	v_add_f32_e32 v5, 1.0, v5
	v_rcp_f32_e32 v4, v4
	v_rcp_f32_e32 v5, v5
	s_nop 0
	v_mul_f32_e64 v0, v0, v4
	v_mul_f32_e64 v1, v1, v5
	s_nop 0
	v_cvt_pk_bf16_f32 v0, v0, v1
	v_mul_f32_e32 v1, 0xbfb8aa3b, v2
	v_exp_f32_e32 v1, v1
	s_nop 0
	v_add_f32_e32 v1, 1.0, v1
	v_rcp_f32_e32 v4, v1
	v_mul_f32_e32 v1, 0xbfb8aa3b, v3
	v_exp_f32_e32 v1, v1
	s_nop 0
	v_add_f32_e32 v1, 1.0, v1
	v_rcp_f32_e32 v5, v1
	s_nop 0
	v_mul_f32_e64 v2, v2, v4
	v_mul_f32_e64 v3, v3, v5
	s_nop 0
	v_cvt_pk_bf16_f32 v1, v2, v3
	v_lshl_add_u64 v[2:3], v[60:61], 0, s[0:1]
	global_store_dwordx2 v[2:3], v[0:1], off
	v_add_u32_e32 v0, s34, v105
	ds_read_b128 v[0:3], v0
	s_add_u32 s0, s4, s31
	s_addc_u32 s1, s5, s35
	s_lshl_b64 s[0:1], s[0:1], 11
	s_waitcnt lgkmcnt(0)
	v_add_f32_e32 v4, v0, v1
	v_add_f32_e32 v4, v2, v4
	v_add_f32_e32 v4, v3, v4
	ds_swizzle_b32 v5, v4 offset:swizzle(SWAP,1)
	s_waitcnt lgkmcnt(0)
	v_add_f32_e32 v4, v4, v5
	ds_swizzle_b32 v5, v4 offset:swizzle(SWAP,2)
	s_waitcnt lgkmcnt(0)
	v_add_f32_e32 v4, v4, v5
	ds_swizzle_b32 v5, v4 offset:swizzle(SWAP,4)
	s_waitcnt lgkmcnt(0)
	v_add_f32_e32 v4, v4, v5
	ds_swizzle_b32 v5, v4 offset:swizzle(SWAP,8)
	s_waitcnt lgkmcnt(0)
	v_add_f32_e32 v4, v4, v5
	ds_swizzle_b32 v5, v4 offset:swizzle(SWAP,16)
	s_waitcnt lgkmcnt(0)
	v_add_f32_e32 v4, v4, v5
	v_mov_b32_e32 v5, v4
	s_nop 1
	v_permlane32_swap_b32_e32 v4, v5
	v_add_f32_e32 v4, v4, v5
	v_fmamk_f32 v19, v4, 0xbb800000, v1
	v_fmamk_f32 v18, v4, 0xbb800000, v0
	v_fmamk_f32 v3, v4, 0xbb800000, v3
	v_fmac_f32_e32 v2, 0xbb800000, v4
	v_mul_f32_e64 v4, v18, v18
	v_mul_f32_e64 v5, v19, v19
	v_mul_f32_e64 v0, v2, v2
	v_mul_f32_e64 v1, v3, v3
	v_add_f32_e32 v4, v4, v5
	v_add_f32_e32 v0, v0, v4
	global_load_dwordx4 v[4:7], v[56:57], off
	global_load_dwordx4 v[8:11], v[58:59], off
	ds_read_b128 v[12:15], v12
	v_add_f32_e32 v0, v1, v0
	ds_swizzle_b32 v1, v0 offset:swizzle(SWAP,1)
	s_waitcnt lgkmcnt(1)
	v_add_f32_e32 v20, v12, v13
	v_add_f32_e32 v20, v14, v20
	v_add_f32_e32 v20, v15, v20
	ds_swizzle_b32 v22, v20 offset:swizzle(SWAP,1)
	s_waitcnt lgkmcnt(1)
	v_add_f32_e32 v0, v0, v1
	ds_swizzle_b32 v1, v0 offset:swizzle(SWAP,2)
	s_waitcnt lgkmcnt(1)
	v_add_f32_e32 v20, v20, v22
	ds_swizzle_b32 v22, v20 offset:swizzle(SWAP,2)
	s_waitcnt lgkmcnt(1)
	v_add_f32_e32 v0, v0, v1
	ds_swizzle_b32 v1, v0 offset:swizzle(SWAP,4)
	s_waitcnt lgkmcnt(1)
	v_add_f32_e32 v20, v20, v22
	ds_swizzle_b32 v22, v20 offset:swizzle(SWAP,4)
	s_waitcnt lgkmcnt(1)
	v_add_f32_e32 v0, v0, v1
	ds_swizzle_b32 v1, v0 offset:swizzle(SWAP,8)
	s_waitcnt lgkmcnt(1)
	v_add_f32_e32 v20, v20, v22
	ds_swizzle_b32 v22, v20 offset:swizzle(SWAP,8)
	s_waitcnt lgkmcnt(1)
	v_add_f32_e32 v0, v0, v1
	ds_swizzle_b32 v1, v0 offset:swizzle(SWAP,16)
	s_waitcnt lgkmcnt(1)
	v_add_f32_e32 v20, v20, v22
	ds_swizzle_b32 v22, v20 offset:swizzle(SWAP,16)
	s_waitcnt lgkmcnt(1)
	v_add_f32_e32 v21, v0, v1
	v_mov_b32_e32 v23, v21
	s_nop 1
	v_permlane32_swap_b32_e32 v21, v23
	s_waitcnt lgkmcnt(0)
	v_add_f32_e32 v20, v20, v22
	v_mov_b32_e32 v22, v20
	s_nop 1
	v_permlane32_swap_b32_e32 v20, v22
	v_add_f32_e32 v20, v20, v22
	v_fmamk_f32 v13, v20, 0xbb800000, v13
	v_fmamk_f32 v12, v20, 0xbb800000, v12
	v_fmamk_f32 v15, v20, 0xbb800000, v15
	v_fmac_f32_e32 v14, 0xbb800000, v20
	v_mul_f32_e64 v26, v12, v12
	v_mul_f32_e64 v27, v13, v13
	v_mul_f32_e64 v24, v14, v14
	v_mul_f32_e64 v25, v15, v15
	v_add_f32_e32 v20, v26, v27
	v_add_f32_e32 v20, v24, v20
	v_add_f32_e32 v20, v25, v20
	ds_swizzle_b32 v22, v20 offset:swizzle(SWAP,1)
	v_lshl_add_u64 v[0:1], v[60:61], 0, s[0:1]
	s_waitcnt lgkmcnt(0)
	v_add_f32_e32 v20, v20, v22
	ds_swizzle_b32 v22, v20 offset:swizzle(SWAP,2)
	s_waitcnt lgkmcnt(0)
	v_add_f32_e32 v20, v20, v22
	ds_swizzle_b32 v22, v20 offset:swizzle(SWAP,4)
	s_waitcnt lgkmcnt(0)
	v_add_f32_e32 v20, v20, v22
	ds_swizzle_b32 v22, v20 offset:swizzle(SWAP,8)
	s_waitcnt lgkmcnt(0)
	v_add_f32_e32 v20, v20, v22
	ds_swizzle_b32 v22, v20 offset:swizzle(SWAP,16)
	s_waitcnt lgkmcnt(0)
	v_add_f32_e32 v20, v20, v22
	v_mov_b32_e32 v22, v20
	s_nop 1
	v_permlane32_swap_b32_e32 v20, v22
	v_add_f32_e64 v20, v20, v22
	v_add_f32_e64 v21, v21, v23
	s_nop 0
	v_fma_f32 v17, v21, s52, v16
	v_fma_f32 v16, v20, s52, v16
	s_nop 0
	v_mul_f32_e32 v20, 0x4b800000, v17
	v_cmp_gt_f32_e64 s[2:3], s56, v17
	v_cmp_gt_f32_e64 s[0:1], s56, v16
	s_nop 0
	v_cndmask_b32_e64 v17, v17, v20, s[2:3]
	v_rsq_f32_e32 v17, v17
	s_nop 0
	v_mul_f32_e32 v20, 0x45800000, v17
	v_cndmask_b32_e64 v20, v17, v20, s[2:3]
	v_mul_f32_e64 v18, v18, v20
	v_mul_f32_e64 v19, v19, v20
	v_mul_f32_e64 v2, v2, v20
	v_mul_f32_e64 v3, v3, v20
	s_waitcnt vmcnt(0)
	v_fma_f32 v4, v4, v18, v8
	v_fma_f32 v5, v5, v19, v9
	v_fma_f32 v2, v6, v2, v10
	v_fma_f32 v3, v7, v3, v11
	v_mul_f32_e32 v6, 0xbfb8aa3b, v4
	v_mul_f32_e32 v7, 0xbfb8aa3b, v5
	v_exp_f32_e32 v6, v6
	v_exp_f32_e32 v7, v7
	v_add_f32_e32 v6, 1.0, v6
	v_add_f32_e32 v7, 1.0, v7
	v_rcp_f32_e32 v6, v6
	v_rcp_f32_e32 v7, v7
	s_nop 0
	v_mul_f32_e64 v4, v4, v6
	v_mul_f32_e64 v5, v5, v7
	s_nop 0
	v_cvt_pk_bf16_f32 v4, v4, v5
	v_mul_f32_e32 v5, 0xbfb8aa3b, v2
	v_exp_f32_e32 v5, v5
	s_nop 0
	v_add_f32_e32 v5, 1.0, v5
	v_rcp_f32_e32 v6, v5
	v_mul_f32_e32 v5, 0xbfb8aa3b, v3
	v_exp_f32_e32 v5, v5
	s_nop 0
	v_add_f32_e32 v5, 1.0, v5
	v_rcp_f32_e32 v7, v5
	s_nop 0
	v_mul_f32_e64 v2, v2, v6
	v_mul_f32_e64 v3, v3, v7
	s_nop 0
	v_cvt_pk_bf16_f32 v5, v2, v3
	global_store_dwordx2 v[0:1], v[4:5], off
	v_mul_f32_e32 v0, 0x4b800000, v16
	v_cndmask_b32_e64 v0, v16, v0, s[0:1]
	v_rsq_f32_e32 v0, v0
	s_nop 0
	v_mul_f32_e32 v1, 0x45800000, v0
	v_cndmask_b32_e64 v8, v0, v1, s[0:1]
	global_load_dwordx4 v[0:3], v[56:57], off
	global_load_dwordx4 v[4:7], v[58:59], off
	v_mul_f32_e64 v10, v12, v8
	v_mul_f32_e64 v11, v13, v8
	v_mul_f32_e64 v9, v15, v8
	v_mul_f32_e64 v8, v14, v8
	s_add_u32 s0, s4, s46
	s_addc_u32 s1, s5, s48
	s_lshl_b64 s[0:1], s[0:1], 11
	s_add_i32 s50, s50, s93
	s_waitcnt vmcnt(0)
	v_fma_f32 v0, v0, v10, v4
	v_fma_f32 v1, v1, v11, v5
	s_nop 0
	v_mul_f32_e32 v4, 0xbfb8aa3b, v0
	v_mul_f32_e32 v5, 0xbfb8aa3b, v1
	v_exp_f32_e32 v4, v4
	v_exp_f32_e32 v5, v5
	v_fma_f32 v2, v2, v8, v6
	v_fma_f32 v3, v3, v9, v7
	v_add_f32_e32 v4, 1.0, v4
	v_add_f32_e32 v5, 1.0, v5
	v_rcp_f32_e32 v4, v4
	v_rcp_f32_e32 v5, v5
	s_nop 0
	v_mul_f32_e64 v0, v0, v4
	v_mul_f32_e64 v1, v1, v5
	s_nop 0
	v_cvt_pk_bf16_f32 v0, v0, v1
	v_mul_f32_e32 v1, 0xbfb8aa3b, v2
	v_exp_f32_e32 v1, v1
	s_nop 0
	v_add_f32_e32 v1, 1.0, v1
	v_rcp_f32_e32 v4, v1
	v_mul_f32_e32 v1, 0xbfb8aa3b, v3
	v_exp_f32_e32 v1, v1
	s_nop 0
	v_add_f32_e32 v1, 1.0, v1
	v_rcp_f32_e32 v5, v1
	s_nop 0
	v_mul_f32_e64 v2, v2, v4
	v_mul_f32_e64 v3, v3, v5
	s_nop 0
	v_cvt_pk_bf16_f32 v1, v2, v3
	v_lshl_add_u64 v[2:3], v[60:61], 0, s[0:1]
	v_readlane_b32 s0, v252, 59
	s_add_i32 s49, s49, s0
	s_cmpk_lt_i32 s50, 0x100
	global_store_dwordx2 v[2:3], v[0:1], off
	s_cbranch_scc0 .LBB0_517

.LBB0_505:
	s_waitcnt vmcnt(0)
	v_lshlrev_b32_e32 v36, 16, v40
	v_and_b32_e32 v37, 0xffff0000, v40
	v_mul_f32_e32 v36, 0xbfb8aa3b, v36
	v_mul_f32_e32 v37, 0xbfb8aa3b, v37
	v_exp_f32_e32 v36, v36
	v_exp_f32_e32 v37, v37
	v_lshlrev_b32_e32 v40, 16, v41
	v_lshlrev_b32_e32 v38, 16, v32
	v_and_b32_e32 v39, 0xffff0000, v32
	v_mul_f32_e32 v32, 0xbfb8aa3b, v40
	v_add_f32_e32 v36, 1.0, v36
	v_add_f32_e32 v37, 1.0, v37
	v_exp_f32_e32 v32, v32
	v_rcp_f32_e32 v36, v36
	v_rcp_f32_e32 v37, v37
	v_and_b32_e32 v41, 0xffff0000, v41
	v_add_f32_e32 v32, 1.0, v32
	v_lshlrev_b32_e32 v44, 16, v42
	v_mul_f32_e64 v36, v36, v38
	v_mul_f32_e64 v37, v37, v39
	v_rcp_f32_e32 v38, v32
	v_mul_f32_e32 v32, 0xbfb8aa3b, v41
	v_exp_f32_e32 v32, v32
	v_and_b32_e32 v42, 0xffff0000, v42
	v_lshlrev_b32_e32 v45, 16, v43
	v_lshlrev_b32_e32 v40, 16, v34
	v_add_f32_e32 v32, 1.0, v32
	v_rcp_f32_e32 v39, v32
	v_lshlrev_b32_e32 v32, 16, v33
	v_and_b32_e32 v33, 0xffff0000, v33
	v_and_b32_e32 v41, 0xffff0000, v34
	v_mul_f32_e64 v38, v38, v32
	v_mul_f32_e64 v39, v39, v33
	v_mul_f32_e32 v32, 0xbfb8aa3b, v44
	v_mul_f32_e32 v33, 0xbfb8aa3b, v42
	v_exp_f32_e32 v32, v32
	v_exp_f32_e32 v33, v33
	v_mul_f32_e32 v34, 0xbfb8aa3b, v45
	v_exp_f32_e32 v34, v34
	v_add_f32_e32 v32, 1.0, v32
	v_add_f32_e32 v33, 1.0, v33
	v_rcp_f32_e32 v32, v32
	v_rcp_f32_e32 v33, v33
	v_and_b32_e32 v43, 0xffff0000, v43
	v_add_f32_e32 v34, 1.0, v34
	v_mul_f32_e64 v32, v32, v40
	v_mul_f32_e64 v33, v33, v41
	v_rcp_f32_e32 v40, v34
	v_mul_f32_e32 v34, 0xbfb8aa3b, v43
	v_exp_f32_e32 v34, v34
	s_nop 0
	v_add_f32_e32 v34, 1.0, v34
	v_rcp_f32_e32 v41, v34
	v_lshlrev_b32_e32 v34, 16, v35
	v_and_b32_e32 v35, 0xffff0000, v35
	v_mul_f32_e64 v34, v40, v34
	v_mul_f32_e64 v35, v41, v35
	ds_write_b128 v55, v[36:39]
	ds_write_b128 v55, v[32:35] offset:16
	s_or_b64 exec, exec, s[0:1]
	s_and_saveexec_b64 s[0:1], s[38:39]
	s_cbranch_execnz .LBB0_512

.LBB0_507:
	s_waitcnt vmcnt(0)
	v_lshlrev_b32_e32 v20, 16, v24
	v_and_b32_e32 v21, 0xffff0000, v24
	v_mul_f32_e32 v20, 0xbfb8aa3b, v20
	v_mul_f32_e32 v21, 0xbfb8aa3b, v21
	v_exp_f32_e32 v20, v20
	v_exp_f32_e32 v21, v21
	v_lshlrev_b32_e32 v24, 16, v25
	v_lshlrev_b32_e32 v22, 16, v16
	v_and_b32_e32 v23, 0xffff0000, v16
	v_mul_f32_e32 v16, 0xbfb8aa3b, v24
	v_add_f32_e32 v20, 1.0, v20
	v_add_f32_e32 v21, 1.0, v21
	v_exp_f32_e32 v16, v16
	v_rcp_f32_e32 v20, v20
	v_rcp_f32_e32 v21, v21
	v_and_b32_e32 v25, 0xffff0000, v25
	v_add_f32_e32 v16, 1.0, v16
	v_lshlrev_b32_e32 v28, 16, v26
	v_mul_f32_e64 v20, v20, v22
	v_mul_f32_e64 v21, v21, v23
	v_rcp_f32_e32 v22, v16
	v_mul_f32_e32 v16, 0xbfb8aa3b, v25
	v_exp_f32_e32 v16, v16
	v_and_b32_e32 v26, 0xffff0000, v26
	v_lshlrev_b32_e32 v29, 16, v27
	v_lshlrev_b32_e32 v24, 16, v18
	v_add_f32_e32 v16, 1.0, v16
	v_rcp_f32_e32 v23, v16
	v_lshlrev_b32_e32 v16, 16, v17
	v_and_b32_e32 v17, 0xffff0000, v17
	v_and_b32_e32 v25, 0xffff0000, v18
	v_mul_f32_e64 v22, v22, v16
	v_mul_f32_e64 v23, v23, v17
	v_mul_f32_e32 v16, 0xbfb8aa3b, v28
	v_mul_f32_e32 v17, 0xbfb8aa3b, v26
	v_exp_f32_e32 v16, v16
	v_exp_f32_e32 v17, v17
	v_mul_f32_e32 v18, 0xbfb8aa3b, v29
	v_exp_f32_e32 v18, v18
	v_add_f32_e32 v16, 1.0, v16
	v_add_f32_e32 v17, 1.0, v17
	v_rcp_f32_e32 v16, v16
	v_rcp_f32_e32 v17, v17
	v_and_b32_e32 v27, 0xffff0000, v27
	v_add_f32_e32 v18, 1.0, v18
	v_mul_f32_e64 v16, v16, v24
	v_mul_f32_e64 v17, v17, v25
	v_rcp_f32_e32 v24, v18
	v_mul_f32_e32 v18, 0xbfb8aa3b, v27
	v_exp_f32_e32 v18, v18
	s_nop 0
	v_add_f32_e32 v18, 1.0, v18
	v_rcp_f32_e32 v25, v18
	v_lshlrev_b32_e32 v18, 16, v19
	v_and_b32_e32 v19, 0xffff0000, v19
	v_mul_f32_e64 v18, v24, v18
	v_mul_f32_e64 v19, v25, v19
	ds_write_b128 v108, v[20:23]
	ds_write_b128 v108, v[16:19] offset:16
	s_or_b64 exec, exec, s[0:1]
	s_and_saveexec_b64 s[0:1], s[42:43]
	s_cbranch_execnz .LBB0_514

.LBB0_510:
	s_waitcnt vmcnt(0)
	v_lshlrev_b32_e32 v62, 16, v44
	v_and_b32_e32 v63, 0xffff0000, v44
	v_lshlrev_b32_e32 v64, 16, v45
	v_and_b32_e32 v65, 0xffff0000, v45
	v_mul_f32_e32 v44, 0xbfb8aa3b, v62
	v_mul_f32_e32 v45, 0xbfb8aa3b, v63
	v_exp_f32_e32 v44, v44
	v_exp_f32_e32 v45, v45
	v_lshlrev_b32_e32 v66, 16, v46
	v_and_b32_e32 v67, 0xffff0000, v46
	v_lshlrev_b32_e32 v68, 16, v47
	v_and_b32_e32 v69, 0xffff0000, v47
	v_lshlrev_b32_e32 v46, 16, v36
	v_and_b32_e32 v47, 0xffff0000, v36
	v_mul_f32_e32 v36, 0xbfb8aa3b, v64
	v_add_f32_e32 v44, 1.0, v44
	v_add_f32_e32 v45, 1.0, v45
	v_exp_f32_e32 v36, v36
	v_rcp_f32_e32 v44, v44
	v_rcp_f32_e32 v45, v45
	v_lshlrev_b32_e32 v62, 16, v38
	v_add_f32_e32 v36, 1.0, v36
	v_and_b32_e32 v63, 0xffff0000, v38
	v_mul_f32_e64 v44, v44, v46
	v_mul_f32_e64 v45, v45, v47
	v_rcp_f32_e32 v46, v36
	v_mul_f32_e32 v36, 0xbfb8aa3b, v65
	v_exp_f32_e32 v36, v36
	v_mul_f32_e32 v38, 0xbfb8aa3b, v68
	v_exp_f32_e32 v38, v38
	v_add_f32_e32 v36, 1.0, v36
	v_rcp_f32_e32 v47, v36
	v_lshlrev_b32_e32 v36, 16, v37
	v_and_b32_e32 v37, 0xffff0000, v37
	v_add_f32_e32 v38, 1.0, v38
	v_mul_f32_e64 v46, v46, v36
	v_mul_f32_e64 v47, v47, v37
	v_mul_f32_e32 v36, 0xbfb8aa3b, v66
	v_mul_f32_e32 v37, 0xbfb8aa3b, v67
	v_exp_f32_e32 v36, v36
	v_exp_f32_e32 v37, v37
	v_add_f32_e32 v36, 1.0, v36
	v_add_f32_e32 v37, 1.0, v37
	v_rcp_f32_e32 v36, v36
	v_rcp_f32_e32 v37, v37
	s_nop 0
	v_mul_f32_e64 v36, v36, v62
	v_mul_f32_e64 v37, v37, v63
	v_rcp_f32_e32 v62, v38
	v_mul_f32_e32 v38, 0xbfb8aa3b, v69
	v_exp_f32_e32 v38, v38
	s_nop 0
	v_add_f32_e32 v38, 1.0, v38
	v_rcp_f32_e32 v63, v38
	v_lshlrev_b32_e32 v38, 16, v39
	v_and_b32_e32 v39, 0xffff0000, v39
	v_mul_f32_e64 v38, v62, v38
	v_mul_f32_e64 v39, v63, v39
	ds_write_b128 v49, v[44:47]
	ds_write_b128 v49, v[36:39] offset:16
	s_or_b64 exec, exec, s[0:1]
	s_and_saveexec_b64 s[0:1], s[36:37]
	s_cbranch_execnz .LBB0_505

.LBB0_512:
	s_waitcnt vmcnt(0)
	v_lshlrev_b32_e32 v32, 16, v28
	v_and_b32_e32 v33, 0xffff0000, v28
	v_lshlrev_b32_e32 v34, 16, v29
	v_and_b32_e32 v35, 0xffff0000, v29
	v_mul_f32_e32 v28, 0xbfb8aa3b, v32
	v_mul_f32_e32 v29, 0xbfb8aa3b, v33
	v_exp_f32_e32 v28, v28
	v_exp_f32_e32 v29, v29
	v_lshlrev_b32_e32 v36, 16, v30
	v_and_b32_e32 v37, 0xffff0000, v30
	v_lshlrev_b32_e32 v38, 16, v31
	v_and_b32_e32 v39, 0xffff0000, v31
	v_lshlrev_b32_e32 v30, 16, v20
	v_and_b32_e32 v31, 0xffff0000, v20
	v_mul_f32_e32 v20, 0xbfb8aa3b, v34
	v_add_f32_e32 v28, 1.0, v28
	v_add_f32_e32 v29, 1.0, v29
	v_exp_f32_e32 v20, v20
	v_rcp_f32_e32 v28, v28
	v_rcp_f32_e32 v29, v29
	v_lshlrev_b32_e32 v32, 16, v22
	v_add_f32_e32 v20, 1.0, v20
	v_and_b32_e32 v33, 0xffff0000, v22
	v_mul_f32_e64 v28, v28, v30
	v_mul_f32_e64 v29, v29, v31
	v_rcp_f32_e32 v30, v20
	v_mul_f32_e32 v20, 0xbfb8aa3b, v35
	v_exp_f32_e32 v20, v20
	v_mul_f32_e32 v22, 0xbfb8aa3b, v38
	v_exp_f32_e32 v22, v22
	v_add_f32_e32 v20, 1.0, v20
	v_rcp_f32_e32 v31, v20
	v_lshlrev_b32_e32 v20, 16, v21
	v_and_b32_e32 v21, 0xffff0000, v21
	v_add_f32_e32 v22, 1.0, v22
	v_mul_f32_e64 v30, v30, v20
	v_mul_f32_e64 v31, v31, v21
	v_mul_f32_e32 v20, 0xbfb8aa3b, v36
	v_mul_f32_e32 v21, 0xbfb8aa3b, v37
	v_exp_f32_e32 v20, v20
	v_exp_f32_e32 v21, v21
	v_add_f32_e32 v20, 1.0, v20
	v_add_f32_e32 v21, 1.0, v21
	v_rcp_f32_e32 v20, v20
	v_rcp_f32_e32 v21, v21
	s_nop 0
	v_mul_f32_e64 v20, v20, v32
	v_mul_f32_e64 v21, v21, v33
	v_rcp_f32_e32 v32, v22
	v_mul_f32_e32 v22, 0xbfb8aa3b, v39
	v_exp_f32_e32 v22, v22
	s_nop 0
	v_add_f32_e32 v22, 1.0, v22
	v_rcp_f32_e32 v33, v22
	v_lshlrev_b32_e32 v22, 16, v23
	v_and_b32_e32 v23, 0xffff0000, v23
	v_mul_f32_e64 v22, v32, v22
	v_mul_f32_e64 v23, v33, v23
	ds_write_b128 v107, v[28:31]
	ds_write_b128 v107, v[20:23] offset:16
	s_or_b64 exec, exec, s[0:1]
	s_and_saveexec_b64 s[0:1], s[40:41]
	s_cbranch_execnz .LBB0_507

.LBB0_514:
	s_waitcnt vmcnt(0)
	v_lshlrev_b32_e32 v16, 16, v12
	v_and_b32_e32 v17, 0xffff0000, v12
	v_lshlrev_b32_e32 v18, 16, v13
	v_and_b32_e32 v19, 0xffff0000, v13
	v_mul_f32_e32 v12, 0xbfb8aa3b, v16
	v_mul_f32_e32 v13, 0xbfb8aa3b, v17
	v_exp_f32_e32 v12, v12
	v_exp_f32_e32 v13, v13
	v_lshlrev_b32_e32 v20, 16, v14
	v_and_b32_e32 v21, 0xffff0000, v14
	v_lshlrev_b32_e32 v22, 16, v15
	v_and_b32_e32 v23, 0xffff0000, v15
	v_lshlrev_b32_e32 v14, 16, v4
	v_and_b32_e32 v15, 0xffff0000, v4
	v_mul_f32_e32 v4, 0xbfb8aa3b, v18
	v_add_f32_e32 v12, 1.0, v12
	v_add_f32_e32 v13, 1.0, v13
	v_exp_f32_e32 v4, v4
	v_rcp_f32_e32 v12, v12
	v_rcp_f32_e32 v13, v13
	v_lshlrev_b32_e32 v16, 16, v6
	v_add_f32_e32 v4, 1.0, v4
	v_and_b32_e32 v17, 0xffff0000, v6
	v_mul_f32_e64 v12, v12, v14
	v_mul_f32_e64 v13, v13, v15
	v_rcp_f32_e32 v14, v4
	v_mul_f32_e32 v4, 0xbfb8aa3b, v19
	v_exp_f32_e32 v4, v4
	v_mul_f32_e32 v6, 0xbfb8aa3b, v22
	v_exp_f32_e32 v6, v6
	v_add_f32_e32 v4, 1.0, v4
	v_rcp_f32_e32 v15, v4
	v_lshlrev_b32_e32 v4, 16, v5
	v_and_b32_e32 v5, 0xffff0000, v5
	v_add_f32_e32 v6, 1.0, v6
	v_mul_f32_e64 v14, v14, v4
	v_mul_f32_e64 v15, v15, v5
	v_mul_f32_e32 v4, 0xbfb8aa3b, v20
	v_mul_f32_e32 v5, 0xbfb8aa3b, v21
	v_exp_f32_e32 v4, v4
	v_exp_f32_e32 v5, v5
	v_add_f32_e32 v4, 1.0, v4
	v_add_f32_e32 v5, 1.0, v5
	v_rcp_f32_e32 v4, v4
	v_rcp_f32_e32 v5, v5
	s_nop 0
	v_mul_f32_e64 v4, v4, v16
	v_mul_f32_e64 v5, v5, v17
	v_rcp_f32_e32 v16, v6
	v_mul_f32_e32 v6, 0xbfb8aa3b, v23
	v_exp_f32_e32 v6, v6
	s_nop 0
	v_add_f32_e32 v6, 1.0, v6
	v_rcp_f32_e32 v17, v6
	v_lshlrev_b32_e32 v6, 16, v7
	v_and_b32_e32 v7, 0xffff0000, v7
	v_mul_f32_e64 v6, v16, v6
	v_mul_f32_e64 v7, v17, v7
	ds_write_b128 v109, v[12:15]
	ds_write_b128 v109, v[4:7] offset:16
	s_or_b64 exec, exec, s[0:1]
	s_and_saveexec_b64 s[0:1], s[44:45]
	s_cbranch_execz .LBB0_491
.LBB0_515:
	s_waitcnt vmcnt(0)
	v_lshlrev_b32_e32 v4, 16, v8
	v_and_b32_e32 v5, 0xffff0000, v8
	v_mul_f32_e32 v4, 0xbfb8aa3b, v4
	v_mul_f32_e32 v5, 0xbfb8aa3b, v5
	v_exp_f32_e32 v4, v4
	v_exp_f32_e32 v5, v5
	v_lshlrev_b32_e32 v8, 16, v9
	v_lshlrev_b32_e32 v6, 16, v0
	v_and_b32_e32 v7, 0xffff0000, v0
	v_mul_f32_e32 v0, 0xbfb8aa3b, v8
	v_add_f32_e32 v4, 1.0, v4
	v_add_f32_e32 v5, 1.0, v5
	v_exp_f32_e32 v0, v0
	v_rcp_f32_e32 v4, v4
	v_rcp_f32_e32 v5, v5
	v_and_b32_e32 v9, 0xffff0000, v9
	v_add_f32_e32 v0, 1.0, v0
	v_lshlrev_b32_e32 v12, 16, v10
	v_mul_f32_e64 v4, v4, v6
	v_mul_f32_e64 v5, v5, v7
	v_rcp_f32_e32 v6, v0
	v_mul_f32_e32 v0, 0xbfb8aa3b, v9
	v_exp_f32_e32 v0, v0
	v_and_b32_e32 v10, 0xffff0000, v10
	v_lshlrev_b32_e32 v13, 16, v11
	v_lshlrev_b32_e32 v8, 16, v2
	v_add_f32_e32 v0, 1.0, v0
	v_rcp_f32_e32 v7, v0
	v_lshlrev_b32_e32 v0, 16, v1
	v_and_b32_e32 v1, 0xffff0000, v1
	v_and_b32_e32 v9, 0xffff0000, v2
	v_mul_f32_e64 v6, v6, v0
	v_mul_f32_e64 v7, v7, v1
	v_mul_f32_e32 v0, 0xbfb8aa3b, v12
	v_mul_f32_e32 v1, 0xbfb8aa3b, v10
	v_exp_f32_e32 v0, v0
	v_exp_f32_e32 v1, v1
	v_mul_f32_e32 v2, 0xbfb8aa3b, v13
	v_exp_f32_e32 v2, v2
	v_add_f32_e32 v0, 1.0, v0
	v_add_f32_e32 v1, 1.0, v1
	v_rcp_f32_e32 v0, v0
	v_rcp_f32_e32 v1, v1
	v_and_b32_e32 v11, 0xffff0000, v11
	v_add_f32_e32 v2, 1.0, v2
	v_mul_f32_e64 v0, v0, v8
	v_mul_f32_e64 v1, v1, v9
	v_rcp_f32_e32 v8, v2
	v_mul_f32_e32 v2, 0xbfb8aa3b, v11
	v_exp_f32_e32 v2, v2
	s_nop 0
	v_add_f32_e32 v2, 1.0, v2
	v_rcp_f32_e32 v9, v2
	v_lshlrev_b32_e32 v2, 16, v3
	v_and_b32_e32 v3, 0xffff0000, v3
	v_mul_f32_e64 v2, v8, v2
	v_mul_f32_e64 v3, v9, v3
	ds_write_b128 v110, v[4:7]
	ds_write_b128 v110, v[0:3] offset:16
	s_branch .LBB0_491

.LBB0_538:
	v_lshlrev_b32_e32 v66, 16, v50
	v_and_b32_e32 v67, 0xffff0000, v50
	v_lshlrev_b32_e32 v70, 16, v51
	v_and_b32_e32 v71, 0xffff0000, v51
	v_lshlrev_b32_e32 v50, 16, v98
	v_and_b32_e32 v51, 0xffff0000, v98
	v_lshlrev_b32_e32 v72, 16, v44
	v_and_b32_e32 v73, 0xffff0000, v44
	v_lshlrev_b32_e32 v64, 16, v46
	v_and_b32_e32 v65, 0xffff0000, v46
	v_lshlrev_b32_e32 v60, 16, v47
	v_and_b32_e32 v61, 0xffff0000, v47
	v_and_b32_e32 v44, 0x7c, v100
	v_lshlrev_b32_e32 v46, 16, v99
	v_and_b32_e32 v47, 0xffff0000, v99
	v_mul_f32_e64 v98, v50, v50
	v_mul_f32_e64 v99, v51, v51
	v_lshlrev_b32_e32 v58, 16, v48
	v_and_b32_e32 v59, 0xffff0000, v48
	v_lshlrev_b32_e32 v62, 16, v49
	v_and_b32_e32 v63, 0xffff0000, v49
	v_lshlrev_b32_e32 v68, 16, v45
	v_and_b32_e32 v69, 0xffff0000, v45
	v_cmp_eq_u32_e64 s[4:5], 52, v44
	v_lshlrev_b32_e32 v44, 16, v55
	v_and_b32_e32 v45, 0xffff0000, v55
	v_mul_f32_e64 v48, v46, v46
	v_mul_f32_e64 v49, v47, v47
	v_add_f32_e32 v55, v98, v99
	v_add_f32_e32 v48, v48, v55
	v_add_f32_e32 v48, v49, v48
	ds_swizzle_b32 v49, v48 offset:swizzle(SWAP,1)
	v_lshl_add_u64 v[96:97], s[2:3], 0, v[208:209]
	v_cmp_lt_i32_e64 s[2:3], 47, v100
	v_cmp_gt_i32_e32 vcc, 52, v100
	v_mul_f32_e64 v100, v44, v44
	v_mul_f32_e64 v101, v45, v45
	s_waitcnt lgkmcnt(0)
	v_add_f32_e32 v48, v48, v49
	ds_swizzle_b32 v49, v48 offset:swizzle(SWAP,2)
	v_readlane_b32 s16, v253, 28
	s_mov_b32 s6, 0x3b800000
	v_readlane_b32 s17, v253, 29
	s_mov_b32 s17, s6
	s_waitcnt lgkmcnt(0)
	v_add_f32_e32 v48, v48, v49
	ds_swizzle_b32 v49, v48 offset:swizzle(SWAP,4)
	s_mov_b32 s6, s16
	v_writelane_b32 v253, s6, 28
	v_cndmask_b32_e64 v107, 1.0, 2.0, vcc
	v_cndmask_b32_e64 v108, 0, -1.0, vcc
	s_waitcnt lgkmcnt(0)
	v_add_f32_e32 v48, v48, v49
	ds_swizzle_b32 v49, v48 offset:swizzle(SWAP,8)
	v_writelane_b32 v253, s7, 29
	v_add_f32_e64 v80, v80, -v68
	v_add_f32_e64 v81, v81, -v69
	v_add_f32_e64 v82, v82, -v64
	v_add_f32_e64 v83, v83, -v65
	v_add_f32_e64 v84, v84, -v60
	v_add_f32_e64 v85, v85, -v61
	s_waitcnt lgkmcnt(0)
	v_add_f32_e32 v48, v48, v49
	ds_swizzle_b32 v49, v48 offset:swizzle(SWAP,16)
	s_waitcnt lgkmcnt(0)
	v_add_f32_e32 v49, v48, v49
	v_add_f32_e32 v48, v100, v101
	ds_swizzle_b32 v55, v48 offset:swizzle(SWAP,1)
	v_mov_b32_e32 v99, v49
	s_nop 1
	v_permlane32_swap_b32_e32 v49, v99
	v_fma_f32 v100, v2, v84, v60
	v_fma_f32 v101, v3, v85, v61
	s_waitcnt lgkmcnt(0)
	v_add_f32_e32 v48, v48, v55
	ds_swizzle_b32 v55, v48 offset:swizzle(SWAP,2)
	v_mul_f32_e64 v84, v18, v100
	v_mul_f32_e64 v85, v19, v101
	s_waitcnt lgkmcnt(0)
	v_add_f32_e32 v48, v48, v55
	ds_swizzle_b32 v55, v48 offset:swizzle(SWAP,4)
	v_mul_f32_e64 v124, v84, v84
	v_mul_f32_e64 v125, v85, v85
	s_waitcnt lgkmcnt(0)
	v_add_f32_e32 v48, v48, v55
	ds_swizzle_b32 v55, v48 offset:swizzle(SWAP,8)
	s_waitcnt lgkmcnt(0)
	v_add_f32_e32 v48, v48, v55
	ds_swizzle_b32 v55, v48 offset:swizzle(SWAP,16)
	s_waitcnt lgkmcnt(0)
	v_add_f32_e32 v48, v48, v55
	v_mov_b32_e32 v98, v48
	s_nop 1
	v_permlane32_swap_b32_e32 v48, v98
	v_add_f32_e64 v48, v48, v98
	v_add_f32_e64 v49, v49, v99
	s_nop 0
	v_fma_f32 v48, v48, s16, v210
	v_fma_f32 v49, v49, s17, v210
	s_nop 0
	v_mul_f32_e32 v55, 0x4b800000, v49
	v_cmp_gt_f32_e64 s[6:7], s56, v49
	v_cmp_gt_f32_e32 vcc, s56, v48
	s_nop 0
	v_cndmask_b32_e64 v49, v49, v55, s[6:7]
	v_rsq_f32_e32 v49, v49
	s_nop 0
	v_mul_f32_e32 v55, 0x45800000, v49
	v_cndmask_b32_e64 v98, v49, v55, s[6:7]
	v_mul_f32_e64 v50, v98, v50
	v_mul_f32_e64 v51, v98, v51
	v_mul_f32_e64 v46, v98, v46
	v_mul_f32_e64 v47, v98, v47
	v_mul_f32_e64 v50, v32, v50
	v_mul_f32_e64 v51, v33, v51
	v_mul_f32_e64 v46, v34, v46
	v_mul_f32_e64 v47, v35, v47
	v_cvt_pk_bf16_f32 v50, v50, v51
	v_cvt_pk_bf16_f32 v51, v46, v47
	v_mul_f32_e32 v46, 0x4b800000, v48
	v_cndmask_b32_e32 v46, v48, v46, vcc
	v_rsq_f32_e32 v46, v46
	global_store_dwordx2 v[78:79], v[50:51], off offset:1024
	v_add_f32_e64 v48, v90, -v66
	v_add_f32_e64 v49, v91, -v67
	v_add_f32_e64 v50, v92, -v70
	v_add_f32_e64 v51, v93, -v71
	v_mul_f32_e32 v47, 0x45800000, v46
	v_cndmask_b32_e32 v46, v46, v47, vcc
	v_mul_f32_e64 v44, v46, v44
	v_mul_f32_e64 v45, v46, v45
	v_mul_f32_e64 v44, v56, v44
	v_mul_f32_e64 v45, v57, v45
	v_add_f32_e64 v46, v88, -v62
	v_add_f32_e64 v47, v89, -v63
	v_cvt_pk_bf16_f32 v44, v44, v45
	global_store_dword v[96:97], v44, off offset:1536
	v_add_f32_e64 v44, v86, -v58
	v_add_f32_e64 v45, v87, -v59
	v_fma_f32 v88, v14, v46, v62
	v_fma_f32 v89, v15, v47, v63
	v_fma_f32 v86, v12, v44, v58
	v_fma_f32 v87, v13, v45, v59
	v_mul_f32_e64 v46, v30, v88
	v_mul_f32_e64 v47, v31, v89
	v_mul_f32_e64 v44, v28, v86
	v_mul_f32_e64 v45, v29, v87
	v_mul_f32_e64 v112, v46, v46
	v_mul_f32_e64 v113, v47, v47
	v_mul_f32_e64 v110, v44, v44
	v_mul_f32_e64 v111, v45, v45
	v_fma_f32 v90, v8, v48, v66
	v_fma_f32 v91, v9, v49, v67
	v_add_f32_e32 v55, v110, v111
	v_mul_f32_e64 v48, v24, v90
	v_mul_f32_e64 v49, v25, v91
	v_add_f32_e32 v55, v55, v112
	v_mul_f32_e64 v114, v48, v48
	v_mul_f32_e64 v115, v49, v49
	v_fma_f32 v92, v10, v50, v70
	v_fma_f32 v93, v11, v51, v71
	v_add_f32_e32 v55, v55, v113
	v_mul_f32_e64 v50, v26, v92
	v_mul_f32_e64 v51, v27, v93
	v_add_f32_e64 v78, v94, -v72
	v_add_f32_e64 v79, v95, -v73
	v_add_f32_e32 v55, v55, v114
	v_mul_f32_e64 v116, v50, v50
	v_mul_f32_e64 v117, v51, v51
	v_fma_f32 v94, v4, v78, v72
	v_fma_f32 v95, v5, v79, v73
	v_add_f32_e32 v55, v55, v115
	v_mul_f32_e64 v78, v20, v94
	v_mul_f32_e64 v79, v21, v95
	v_add_f32_e32 v55, v55, v116
	v_mul_f32_e64 v118, v78, v78
	v_mul_f32_e64 v119, v79, v79
	v_fma_f32 v96, v6, v80, v68
	v_fma_f32 v97, v7, v81, v69
	v_add_f32_e32 v55, v55, v117
	v_mul_f32_e64 v80, v22, v96
	v_mul_f32_e64 v81, v23, v97
	v_add_f32_e32 v55, v55, v118
	v_mul_f32_e64 v120, v80, v80
	v_mul_f32_e64 v121, v81, v81
	v_fma_f32 v98, v0, v82, v64
	v_fma_f32 v99, v1, v83, v65
	v_add_f32_e32 v55, v55, v119
	v_mul_f32_e64 v82, v16, v98
	v_mul_f32_e64 v83, v17, v99
	v_add_f32_e32 v55, v55, v120
	v_mul_f32_e64 v122, v82, v82
	v_mul_f32_e64 v123, v83, v83
	v_add_f32_e32 v55, v55, v121
	v_add_f32_e32 v55, v55, v122
	v_add_f32_e32 v55, v55, v123
	v_add_f32_e32 v55, v55, v124
	v_add_f32_e32 v55, v55, v125
	ds_swizzle_b32 v103, v55 offset:swizzle(SWAP,1)
	s_waitcnt lgkmcnt(0)
	v_add_f32_e32 v55, v55, v103
	ds_swizzle_b32 v103, v55 offset:swizzle(SWAP,2)
	s_and_saveexec_b64 s[6:7], s[2:3]
	s_cbranch_execz .LBB0_540
	v_mul_f32_e64 v105, v86, -v107
	v_mul_f32_e32 v105, 0x3fb8aa3b, v105
	v_exp_f32_e32 v105, v105
	s_nop 0
	v_add_f32_e32 v105, 1.0, v105
	v_rcp_f32_e32 v105, v105
	s_nop 0
	v_fma_f32 v105, v107, v105, v108
	v_cndmask_b32_e64 v86, v105, v86, s[4:5]
	v_mul_f32_e64 v105, v87, -v107
	v_mul_f32_e32 v105, 0x3fb8aa3b, v105
	v_exp_f32_e32 v105, v105
	s_nop 0
	v_add_f32_e32 v105, 1.0, v105
	v_rcp_f32_e32 v105, v105
	s_nop 0
	v_fma_f32 v105, v107, v105, v108
	v_cndmask_b32_e64 v87, v105, v87, s[4:5]
	v_mul_f32_e64 v105, v88, -v107
	v_mul_f32_e32 v105, 0x3fb8aa3b, v105
	v_exp_f32_e32 v105, v105
	s_nop 0
	v_add_f32_e32 v105, 1.0, v105
	v_rcp_f32_e32 v105, v105
	s_nop 0
	v_fma_f32 v105, v107, v105, v108
	v_cndmask_b32_e64 v88, v105, v88, s[4:5]
	v_mul_f32_e64 v105, v89, -v107
	v_mul_f32_e32 v105, 0x3fb8aa3b, v105
	v_exp_f32_e32 v105, v105
	s_nop 0
	v_add_f32_e32 v105, 1.0, v105
	v_rcp_f32_e32 v105, v105
	s_nop 0
	v_fma_f32 v105, v107, v105, v108
	v_cndmask_b32_e64 v89, v105, v89, s[4:5]
	v_mul_f32_e64 v105, v90, -v107
	v_mul_f32_e32 v105, 0x3fb8aa3b, v105
	v_exp_f32_e32 v105, v105
	s_nop 0
	v_add_f32_e32 v105, 1.0, v105
	v_rcp_f32_e32 v105, v105
	s_nop 0
	v_fma_f32 v105, v107, v105, v108
	v_cndmask_b32_e64 v90, v105, v90, s[4:5]
	v_mul_f32_e64 v105, v91, -v107
	v_mul_f32_e32 v105, 0x3fb8aa3b, v105
	v_exp_f32_e32 v105, v105
	s_nop 0
	v_add_f32_e32 v105, 1.0, v105
	v_rcp_f32_e32 v105, v105
	s_nop 0
	v_fma_f32 v105, v107, v105, v108
	v_cndmask_b32_e64 v91, v105, v91, s[4:5]
	v_mul_f32_e64 v105, v92, -v107
	v_mul_f32_e32 v105, 0x3fb8aa3b, v105
	v_exp_f32_e32 v105, v105
	s_nop 0
	v_add_f32_e32 v105, 1.0, v105
	v_rcp_f32_e32 v105, v105
	s_nop 0
	v_fma_f32 v105, v107, v105, v108
	v_cndmask_b32_e64 v92, v105, v92, s[4:5]
	v_mul_f32_e64 v105, v93, -v107
	v_mul_f32_e32 v105, 0x3fb8aa3b, v105
	v_exp_f32_e32 v105, v105
	s_nop 0
	v_add_f32_e32 v105, 1.0, v105
	v_rcp_f32_e32 v105, v105
	s_nop 0
	v_fma_f32 v105, v107, v105, v108
	v_cndmask_b32_e64 v93, v105, v93, s[4:5]
	v_mul_f32_e64 v105, v94, -v107
	v_mul_f32_e32 v105, 0x3fb8aa3b, v105
	v_exp_f32_e32 v105, v105
	s_nop 0
	v_add_f32_e32 v105, 1.0, v105
	v_rcp_f32_e32 v105, v105
	s_nop 0
	v_fma_f32 v105, v107, v105, v108
	v_cndmask_b32_e64 v94, v105, v94, s[4:5]
	v_mul_f32_e64 v105, v95, -v107
	v_mul_f32_e32 v105, 0x3fb8aa3b, v105
	v_exp_f32_e32 v105, v105
	s_nop 0
	v_add_f32_e32 v105, 1.0, v105
	v_rcp_f32_e32 v105, v105
	s_nop 0
	v_fma_f32 v105, v107, v105, v108
	v_cndmask_b32_e64 v95, v105, v95, s[4:5]
	v_mul_f32_e64 v105, v96, -v107
	v_mul_f32_e32 v105, 0x3fb8aa3b, v105
	v_exp_f32_e32 v105, v105
	s_nop 0
	v_add_f32_e32 v105, 1.0, v105
	v_rcp_f32_e32 v105, v105
	s_nop 0
	v_fma_f32 v105, v107, v105, v108
	v_cndmask_b32_e64 v96, v105, v96, s[4:5]
	v_mul_f32_e64 v105, v97, -v107
	v_mul_f32_e32 v105, 0x3fb8aa3b, v105
	v_exp_f32_e32 v105, v105
	s_nop 0
	v_add_f32_e32 v105, 1.0, v105
	v_rcp_f32_e32 v105, v105
	s_nop 0
	v_fma_f32 v105, v107, v105, v108
	v_cndmask_b32_e64 v97, v105, v97, s[4:5]
	v_mul_f32_e64 v105, v98, -v107
	v_mul_f32_e32 v105, 0x3fb8aa3b, v105
	v_exp_f32_e32 v105, v105
	s_nop 0
	v_add_f32_e32 v105, 1.0, v105
	v_rcp_f32_e32 v105, v105
	s_nop 0
	v_fma_f32 v105, v107, v105, v108
	v_cndmask_b32_e64 v98, v105, v98, s[4:5]
	v_mul_f32_e64 v105, v99, -v107
	v_mul_f32_e32 v105, 0x3fb8aa3b, v105
	v_exp_f32_e32 v105, v105
	s_nop 0
	v_add_f32_e32 v105, 1.0, v105
	v_rcp_f32_e32 v105, v105
	s_nop 0
	v_fma_f32 v105, v107, v105, v108
	v_cndmask_b32_e64 v99, v105, v99, s[4:5]
	v_mul_f32_e64 v105, v100, -v107
	v_mul_f32_e32 v105, 0x3fb8aa3b, v105
	v_exp_f32_e32 v105, v105
	s_nop 0
	v_add_f32_e32 v105, 1.0, v105
	v_rcp_f32_e32 v105, v105
	s_nop 0
	v_fma_f32 v105, v107, v105, v108
	v_cndmask_b32_e64 v100, v105, v100, s[4:5]
	v_mul_f32_e64 v105, v101, -v107
	v_mul_f32_e32 v105, 0x3fb8aa3b, v105
	v_exp_f32_e32 v105, v105
	s_nop 0
	v_add_f32_e32 v105, 1.0, v105
	v_rcp_f32_e32 v105, v105
	s_nop 0
	v_fma_f32 v105, v107, v105, v108
	v_cndmask_b32_e64 v101, v105, v101, s[4:5]
.LBB0_540:
	s_or_b64 exec, exec, s[6:7]
	s_lshl_b64 s[6:7], s[14:15], 9
	v_cvt_pk_bf16_f32 v86, v86, v87
	v_cvt_pk_bf16_f32 v87, v88, v89
	v_cvt_pk_bf16_f32 v88, v90, v91
	v_cvt_pk_bf16_f32 v89, v92, v93
	v_lshl_add_u64 v[90:91], v[76:77], 0, s[6:7]
	global_store_dwordx4 v[90:91], v[86:89], off
	v_lshlrev_b32_e32 v208, 1, v54
	s_nop 0
	v_cvt_pk_bf16_f32 v86, v94, v95
	v_cvt_pk_bf16_f32 v87, v96, v97
	v_cvt_pk_bf16_f32 v88, v98, v99
	v_cvt_pk_bf16_f32 v89, v100, v101
	global_store_dwordx4 v[90:91], v[86:89], off offset:16
	s_and_saveexec_b64 s[16:17], s[0:1]
	s_cbranch_execz .LBB0_542
	s_waitcnt lgkmcnt(0)
	v_add_f32_e32 v55, v55, v103
	v_mul_f32_e32 v86, 0x4f800000, v55
	v_cmp_gt_f32_e32 vcc, s94, v55
	s_nop 1
	v_cndmask_b32_e32 v55, v55, v86, vcc
	v_sqrt_f32_e32 v86, v55
	s_nop 0
	v_add_u32_e32 v87, -1, v86
	v_fma_f32 v89, -v87, v86, v55
	v_add_u32_e32 v88, 1, v86
	v_cmp_ge_f32_e64 s[6:7], 0, v89
	s_nop 1
	v_cndmask_b32_e64 v87, v86, v87, s[6:7]
	v_fma_f32 v86, -v88, v86, v55
	v_cmp_lt_f32_e64 s[6:7], 0, v86
	s_nop 1
	v_cndmask_b32_e64 v86, v87, v88, s[6:7]
	v_mul_f32_e32 v87, 0x37800000, v86
	v_cndmask_b32_e32 v86, v86, v87, vcc
	v_mov_b32_e32 v87, 0x260
	v_cmp_class_f32_e32 vcc, v55, v87
	s_nop 1
	v_cndmask_b32_e32 v55, v86, v55, vcc
	v_max_f32_e32 v55, 0x2b8cbccc, v55
	v_div_scale_f32 v86, s[6:7], v55, v55, 1.0
	v_rcp_f32_e32 v87, v86
	s_lshl_b64 s[6:7], s[14:15], 8
	v_fma_f32 v88, -v86, v87, 1.0
	v_fmac_f32_e32 v87, v88, v87
	v_div_scale_f32 v88, vcc, 1.0, v55, 1.0
	v_mul_f32_e32 v89, v88, v87
	v_fma_f32 v90, -v86, v89, v88
	v_fmac_f32_e32 v89, v90, v87
	v_fma_f32 v86, -v86, v89, v88
	v_div_fmas_f32 v86, v86, v87, v89
	v_div_fixup_f32 v86, v86, v55, 1.0
	v_lshl_add_u64 v[88:89], s[8:9], 0, v[208:209]
	v_mul_f32_e64 v44, v44, v86
	v_mul_f32_e64 v45, v45, v86
	v_mul_f32_e64 v46, v46, v86
	v_mul_f32_e64 v47, v47, v86
	v_mul_f32_e64 v48, v48, v86
	v_mul_f32_e64 v49, v49, v86
	v_cvt_pk_bf16_f32 v44, v44, v45
	v_cvt_pk_bf16_f32 v45, v46, v47
	v_cvt_pk_bf16_f32 v46, v48, v49
	v_lshl_add_u64 v[48:49], s[6:7], 1, v[88:89]
	s_mov_b32 s6, 0x2ebff000
	v_mul_f32_e64 v50, v50, v86
	v_mul_f32_e64 v51, v51, v86
	v_add_co_u32_e32 v48, vcc, s6, v48
	v_mul_f32_e64 v78, v78, v86
	v_mul_f32_e64 v79, v79, v86
	v_mul_f32_e64 v80, v80, v86
	v_mul_f32_e64 v81, v81, v86
	v_mul_f32_e64 v82, v82, v86
	v_mul_f32_e64 v83, v83, v86
	v_mul_f32_e64 v84, v84, v86
	v_mul_f32_e64 v85, v85, v86
	v_cvt_pk_bf16_f32 v47, v50, v51
	v_addc_co_u32_e32 v49, vcc, 0, v49, vcc
	global_store_dwordx4 v[48:49], v[44:47], off offset:3584
	s_nop 1
	v_cvt_pk_bf16_f32 v44, v78, v79
	v_cvt_pk_bf16_f32 v45, v80, v81
	v_cvt_pk_bf16_f32 v46, v82, v83
	v_cvt_pk_bf16_f32 v47, v84, v85
	global_store_dwordx4 v[48:49], v[44:47], off offset:3600

.LBB0_549:
	v_lshlrev_b32_e32 v88, 16, v42
	v_and_b32_e32 v89, 0xffff0000, v42
	v_lshlrev_b32_e32 v90, 16, v43
	v_and_b32_e32 v91, 0xffff0000, v43
	v_lshlrev_b32_e32 v42, 16, v74
	v_and_b32_e32 v43, 0xffff0000, v74
	v_lshlrev_b32_e32 v96, 16, v38
	v_and_b32_e32 v97, 0xffff0000, v38
	v_lshlrev_b32_e32 v98, 16, v39
	v_and_b32_e32 v99, 0xffff0000, v39
	v_lshlrev_b32_e32 v38, 16, v75
	v_and_b32_e32 v39, 0xffff0000, v75
	v_mul_f32_e64 v74, v42, v42
	v_mul_f32_e64 v75, v43, v43
	v_lshlrev_b32_e32 v84, 16, v40
	v_and_b32_e32 v85, 0xffff0000, v40
	v_lshlrev_b32_e32 v86, 16, v41
	v_and_b32_e32 v87, 0xffff0000, v41
	v_mul_f32_e64 v40, v38, v38
	v_mul_f32_e64 v41, v39, v39
	v_add_f32_e32 v74, v74, v75
	v_add_f32_e32 v40, v40, v74
	v_add_f32_e32 v40, v41, v40
	ds_swizzle_b32 v41, v40 offset:swizzle(SWAP,1)
	v_lshlrev_b32_e32 v92, 16, v36
	v_and_b32_e32 v93, 0xffff0000, v36
	v_lshlrev_b32_e32 v94, 16, v37
	v_and_b32_e32 v95, 0xffff0000, v37
	s_waitcnt lgkmcnt(0)
	v_add_f32_e32 v40, v40, v41
	ds_swizzle_b32 v41, v40 offset:swizzle(SWAP,2)
	v_lshlrev_b32_e32 v36, 16, v104
	v_and_b32_e32 v37, 0xffff0000, v104
	v_mul_f32_e64 v104, v36, v36
	v_mul_f32_e64 v105, v37, v37
	v_readlane_b32 s10, v253, 28
	s_waitcnt lgkmcnt(0)
	v_add_f32_e32 v40, v40, v41
	ds_swizzle_b32 v41, v40 offset:swizzle(SWAP,4)
	s_mov_b32 s6, 0x3b800000
	v_readlane_b32 s11, v253, 29
	s_mov_b32 s11, s6
	s_mov_b32 s6, s10
	s_waitcnt lgkmcnt(0)
	v_add_f32_e32 v40, v40, v41
	ds_swizzle_b32 v41, v40 offset:swizzle(SWAP,8)
	v_writelane_b32 v253, s6, 28
	v_add_f32_e64 v64, v64, -v96
	v_add_f32_e64 v65, v65, -v97
	s_waitcnt lgkmcnt(0)
	v_add_f32_e32 v40, v40, v41
	ds_swizzle_b32 v41, v40 offset:swizzle(SWAP,16)
	v_writelane_b32 v253, s7, 29
	s_waitcnt lgkmcnt(0)
	v_add_f32_e32 v41, v40, v41
	v_add_f32_e32 v40, v104, v105
	ds_swizzle_b32 v74, v40 offset:swizzle(SWAP,1)
	v_mov_b32_e32 v75, v41
	s_nop 1
	v_permlane32_swap_b32_e32 v41, v75
	v_add_f32_e64 v104, v60, -v98
	v_add_f32_e64 v105, v61, -v99
	s_waitcnt lgkmcnt(0)
	v_add_f32_e32 v40, v40, v74
	ds_swizzle_b32 v74, v40 offset:swizzle(SWAP,2)
	v_fma_f32 v104, v2, v104, v98
	v_fma_f32 v105, v3, v105, v99
	s_waitcnt lgkmcnt(0)
	v_add_f32_e32 v40, v40, v74
	ds_swizzle_b32 v74, v40 offset:swizzle(SWAP,4)
	s_waitcnt lgkmcnt(0)
	v_add_f32_e32 v40, v40, v74
	ds_swizzle_b32 v74, v40 offset:swizzle(SWAP,8)
	s_waitcnt lgkmcnt(0)
	v_add_f32_e32 v40, v40, v74
	ds_swizzle_b32 v74, v40 offset:swizzle(SWAP,16)
	s_waitcnt lgkmcnt(0)
	v_add_f32_e32 v40, v40, v74
	v_mov_b32_e32 v74, v40
	s_nop 1
	v_permlane32_swap_b32_e32 v40, v74
	v_add_f32_e64 v40, v40, v74
	v_add_f32_e64 v41, v41, v75
	s_nop 0
	v_fma_f32 v40, v40, s10, v210
	v_fma_f32 v41, v41, s11, v210
	s_mov_b32 s10, 0x1fc00000
	v_mul_f32_e32 v74, 0x4b800000, v41
	v_cmp_gt_f32_e64 s[6:7], s56, v41
	v_cmp_gt_f32_e32 vcc, s56, v40
	s_nop 0
	v_cndmask_b32_e64 v41, v41, v74, s[6:7]
	v_rsq_f32_e32 v41, v41
	s_nop 0
	v_mul_f32_e32 v74, 0x45800000, v41
	v_cndmask_b32_e64 v74, v41, v74, s[6:7]
	v_mul_f32_e64 v42, v74, v42
	v_mul_f32_e64 v43, v74, v43
	v_mul_f32_e64 v38, v74, v38
	v_mul_f32_e64 v39, v74, v39
	v_mul_f32_e64 v42, v32, v42
	v_mul_f32_e64 v43, v33, v43
	v_mul_f32_e64 v38, v34, v38
	v_mul_f32_e64 v39, v35, v39
	v_cvt_pk_bf16_f32 v42, v42, v43
	v_cvt_pk_bf16_f32 v43, v38, v39
	v_add_co_u32_e64 v38, s[6:7], s10, v102
	s_nop 1
	v_addc_co_u32_e64 v39, s[6:7], 0, v103, s[6:7]
	global_store_dwordx2 v[38:39], v[42:43], off offset:1024
	v_mul_f32_e32 v38, 0x4b800000, v40
	v_cndmask_b32_e32 v38, v40, v38, vcc
	v_rsq_f32_e32 v38, v38
	v_add_f32_e64 v40, v66, -v88
	v_add_f32_e64 v41, v67, -v89
	v_add_f32_e64 v42, v70, -v90
	v_add_f32_e64 v43, v71, -v91
	v_fma_f32 v102, v0, v64, v96
	v_fma_f32 v103, v1, v65, v97
	v_mul_f32_e32 v39, 0x45800000, v38
	v_cndmask_b32_e32 v38, v38, v39, vcc
	v_mul_f32_e64 v36, v38, v36
	v_mul_f32_e64 v37, v38, v37
	v_mul_f32_e64 v36, v56, v36
	v_mul_f32_e64 v37, v57, v37
	v_mul_f32_e64 v64, v18, v104
	v_mul_f32_e64 v65, v19, v105
	v_cvt_pk_bf16_f32 v38, v36, v37
	v_add_co_u32_e32 v36, vcc, s10, v100
	v_mul_f32_e64 v124, v64, v64
	v_mul_f32_e64 v125, v65, v65
	s_nop 0
	v_addc_co_u32_e32 v37, vcc, 0, v101, vcc
	global_store_dword v[36:37], v38, off offset:1536
	v_add_f32_e64 v36, v58, -v84
	v_add_f32_e64 v37, v59, -v85
	v_add_f32_e64 v38, v62, -v86
	v_add_f32_e64 v39, v63, -v87
	v_fma_f32 v66, v12, v36, v84
	v_fma_f32 v67, v13, v37, v85
	v_add_f32_e64 v62, v68, -v94
	v_add_f32_e64 v63, v69, -v95
	v_mul_f32_e64 v36, v28, v66
	v_mul_f32_e64 v37, v29, v67
	v_fma_f32 v68, v14, v38, v86
	v_fma_f32 v69, v15, v39, v87
	v_mul_f32_e64 v110, v36, v36
	v_mul_f32_e64 v111, v37, v37
	v_mul_f32_e64 v38, v30, v68
	v_mul_f32_e64 v39, v31, v69
	v_add_f32_e64 v58, v72, -v92
	v_add_f32_e64 v59, v73, -v93
	v_mul_f32_e64 v112, v38, v38
	v_mul_f32_e64 v113, v39, v39
	v_fma_f32 v72, v8, v40, v88
	v_fma_f32 v73, v9, v41, v89
	v_add_f32_e32 v110, v110, v111
	v_mul_f32_e64 v40, v24, v72
	v_mul_f32_e64 v41, v25, v73
	v_add_f32_e32 v110, v110, v112
	v_mul_f32_e64 v114, v40, v40
	v_mul_f32_e64 v115, v41, v41
	v_fma_f32 v100, v10, v42, v90
	v_fma_f32 v101, v11, v43, v91
	v_add_f32_e32 v110, v110, v113
	v_mul_f32_e64 v42, v26, v100
	v_mul_f32_e64 v43, v27, v101
	v_add_f32_e32 v110, v110, v114
	v_mul_f32_e64 v116, v42, v42
	v_mul_f32_e64 v117, v43, v43
	v_fma_f32 v70, v4, v58, v92
	v_fma_f32 v71, v5, v59, v93
	v_add_f32_e32 v110, v110, v115
	v_mul_f32_e64 v58, v20, v70
	v_mul_f32_e64 v59, v21, v71
	v_add_f32_e32 v110, v110, v116
	v_mul_f32_e64 v118, v58, v58
	v_mul_f32_e64 v119, v59, v59
	v_fma_f32 v74, v6, v62, v94
	v_fma_f32 v75, v7, v63, v95
	v_add_f32_e32 v110, v110, v117
	v_mul_f32_e64 v60, v22, v74
	v_mul_f32_e64 v61, v23, v75
	v_add_f32_e32 v110, v110, v118
	v_mul_f32_e64 v120, v60, v60
	v_mul_f32_e64 v121, v61, v61
	v_add_f32_e32 v110, v110, v119
	v_mul_f32_e64 v62, v16, v102
	v_mul_f32_e64 v63, v17, v103
	v_add_f32_e32 v110, v110, v120
	v_mul_f32_e64 v122, v62, v62
	v_mul_f32_e64 v123, v63, v63
	v_add_f32_e32 v110, v110, v121
	v_add_f32_e32 v110, v110, v122
	v_add_f32_e32 v110, v110, v123
	v_add_f32_e32 v110, v110, v124
	v_add_f32_e32 v110, v110, v125
	ds_swizzle_b32 v111, v110 offset:swizzle(SWAP,1)
	s_waitcnt lgkmcnt(0)
	v_add_f32_e32 v110, v110, v111
	ds_swizzle_b32 v111, v110 offset:swizzle(SWAP,2)
	s_and_saveexec_b64 s[6:7], s[2:3]
	s_cbranch_execz .LBB0_551
	v_mul_f32_e64 v112, v66, -v107
	v_mul_f32_e32 v112, 0x3fb8aa3b, v112
	v_exp_f32_e32 v112, v112
	s_nop 0
	v_add_f32_e32 v112, 1.0, v112
	v_rcp_f32_e32 v112, v112
	s_nop 0
	v_fma_f32 v112, v107, v112, v108
	v_cndmask_b32_e64 v66, v112, v66, s[4:5]
	v_mul_f32_e64 v112, v67, -v107
	v_mul_f32_e32 v112, 0x3fb8aa3b, v112
	v_exp_f32_e32 v112, v112
	s_nop 0
	v_add_f32_e32 v112, 1.0, v112
	v_rcp_f32_e32 v112, v112
	s_nop 0
	v_fma_f32 v112, v107, v112, v108
	v_cndmask_b32_e64 v67, v112, v67, s[4:5]
	v_mul_f32_e64 v112, v68, -v107
	v_mul_f32_e32 v112, 0x3fb8aa3b, v112
	v_exp_f32_e32 v112, v112
	s_nop 0
	v_add_f32_e32 v112, 1.0, v112
	v_rcp_f32_e32 v112, v112
	s_nop 0
	v_fma_f32 v112, v107, v112, v108
	v_cndmask_b32_e64 v68, v112, v68, s[4:5]
	v_mul_f32_e64 v112, v69, -v107
	v_mul_f32_e32 v112, 0x3fb8aa3b, v112
	v_exp_f32_e32 v112, v112
	s_nop 0
	v_add_f32_e32 v112, 1.0, v112
	v_rcp_f32_e32 v112, v112
	s_nop 0
	v_fma_f32 v112, v107, v112, v108
	v_cndmask_b32_e64 v69, v112, v69, s[4:5]
	v_mul_f32_e64 v112, v72, -v107
	v_mul_f32_e32 v112, 0x3fb8aa3b, v112
	v_exp_f32_e32 v112, v112
	s_nop 0
	v_add_f32_e32 v112, 1.0, v112
	v_rcp_f32_e32 v112, v112
	s_nop 0
	v_fma_f32 v112, v107, v112, v108
	v_cndmask_b32_e64 v72, v112, v72, s[4:5]
	v_mul_f32_e64 v112, v73, -v107
	v_mul_f32_e32 v112, 0x3fb8aa3b, v112
	v_exp_f32_e32 v112, v112
	s_nop 0
	v_add_f32_e32 v112, 1.0, v112
	v_rcp_f32_e32 v112, v112
	s_nop 0
	v_fma_f32 v112, v107, v112, v108
	v_cndmask_b32_e64 v73, v112, v73, s[4:5]
	v_mul_f32_e64 v112, v100, -v107
	v_mul_f32_e32 v112, 0x3fb8aa3b, v112
	v_exp_f32_e32 v112, v112
	s_nop 0
	v_add_f32_e32 v112, 1.0, v112
	v_rcp_f32_e32 v112, v112
	s_nop 0
	v_fma_f32 v112, v107, v112, v108
	v_cndmask_b32_e64 v100, v112, v100, s[4:5]
	v_mul_f32_e64 v112, v101, -v107
	v_mul_f32_e32 v112, 0x3fb8aa3b, v112
	v_exp_f32_e32 v112, v112
	s_nop 0
	v_add_f32_e32 v112, 1.0, v112
	v_rcp_f32_e32 v112, v112
	s_nop 0
	v_fma_f32 v112, v107, v112, v108
	v_cndmask_b32_e64 v101, v112, v101, s[4:5]
	v_mul_f32_e64 v112, v70, -v107
	v_mul_f32_e32 v112, 0x3fb8aa3b, v112
	v_exp_f32_e32 v112, v112
	s_nop 0
	v_add_f32_e32 v112, 1.0, v112
	v_rcp_f32_e32 v112, v112
	s_nop 0
	v_fma_f32 v112, v107, v112, v108
	v_cndmask_b32_e64 v70, v112, v70, s[4:5]
	v_mul_f32_e64 v112, v71, -v107
	v_mul_f32_e32 v112, 0x3fb8aa3b, v112
	v_exp_f32_e32 v112, v112
	s_nop 0
	v_add_f32_e32 v112, 1.0, v112
	v_rcp_f32_e32 v112, v112
	s_nop 0
	v_fma_f32 v112, v107, v112, v108
	v_cndmask_b32_e64 v71, v112, v71, s[4:5]
	v_mul_f32_e64 v112, v74, -v107
	v_mul_f32_e32 v112, 0x3fb8aa3b, v112
	v_exp_f32_e32 v112, v112
	s_nop 0
	v_add_f32_e32 v112, 1.0, v112
	v_rcp_f32_e32 v112, v112
	s_nop 0
	v_fma_f32 v112, v107, v112, v108
	v_cndmask_b32_e64 v74, v112, v74, s[4:5]
	v_mul_f32_e64 v112, v75, -v107
	v_mul_f32_e32 v112, 0x3fb8aa3b, v112
	v_exp_f32_e32 v112, v112
	s_nop 0
	v_add_f32_e32 v112, 1.0, v112
	v_rcp_f32_e32 v112, v112
	s_nop 0
	v_fma_f32 v112, v107, v112, v108
	v_cndmask_b32_e64 v75, v112, v75, s[4:5]
	v_mul_f32_e64 v112, v102, -v107
	v_mul_f32_e32 v112, 0x3fb8aa3b, v112
	v_exp_f32_e32 v112, v112
	s_nop 0
	v_add_f32_e32 v112, 1.0, v112
	v_rcp_f32_e32 v112, v112
	s_nop 0
	v_fma_f32 v112, v107, v112, v108
	v_cndmask_b32_e64 v102, v112, v102, s[4:5]
	v_mul_f32_e64 v112, v103, -v107
	v_mul_f32_e32 v112, 0x3fb8aa3b, v112
	v_exp_f32_e32 v112, v112
	s_nop 0
	v_add_f32_e32 v112, 1.0, v112
	v_rcp_f32_e32 v112, v112
	s_nop 0
	v_fma_f32 v112, v107, v112, v108
	v_cndmask_b32_e64 v103, v112, v103, s[4:5]
	v_mul_f32_e64 v112, v104, -v107
	v_mul_f32_e32 v112, 0x3fb8aa3b, v112
	v_exp_f32_e32 v112, v112
	s_nop 0
	v_add_f32_e32 v112, 1.0, v112
	v_rcp_f32_e32 v112, v112
	s_nop 0
	v_fma_f32 v112, v107, v112, v108
	v_cndmask_b32_e64 v104, v112, v104, s[4:5]
	v_mul_f32_e64 v112, v105, -v107
	v_mul_f32_e32 v112, 0x3fb8aa3b, v112
	v_exp_f32_e32 v112, v112
	s_nop 0
	v_add_f32_e32 v112, 1.0, v112
	v_rcp_f32_e32 v112, v112
	s_nop 0
	v_fma_f32 v112, v107, v112, v108
	v_cndmask_b32_e64 v105, v112, v105, s[4:5]
.LBB0_551:
	s_or_b64 exec, exec, s[6:7]
	v_cvt_pk_bf16_f32 v66, v66, v67
	v_cvt_pk_bf16_f32 v67, v68, v69
	v_cvt_pk_bf16_f32 v68, v72, v73
	v_cvt_pk_bf16_f32 v69, v100, v101
	global_store_dwordx4 v[76:77], v[66:69], off offset:-16
	s_nop 1
	v_cvt_pk_bf16_f32 v66, v70, v71
	v_cvt_pk_bf16_f32 v67, v74, v75
	v_cvt_pk_bf16_f32 v68, v102, v103
	v_cvt_pk_bf16_f32 v69, v104, v105
	global_store_dwordx4 v[76:77], v[66:69], off
	s_and_saveexec_b64 s[10:11], s[0:1]
	s_cbranch_execz .LBB0_544
	s_waitcnt lgkmcnt(0)
	v_add_f32_e32 v66, v110, v111
	v_mul_f32_e32 v67, 0x4f800000, v66
	v_cmp_gt_f32_e32 vcc, s94, v66
	s_nop 1
	v_cndmask_b32_e32 v66, v66, v67, vcc
	v_sqrt_f32_e32 v67, v66
	s_nop 0
	v_add_u32_e32 v68, -1, v67
	v_fma_f32 v70, -v68, v67, v66
	v_add_u32_e32 v69, 1, v67
	v_cmp_ge_f32_e64 s[6:7], 0, v70
	s_nop 1
	v_cndmask_b32_e64 v68, v67, v68, s[6:7]
	v_fma_f32 v67, -v69, v67, v66
	v_cmp_lt_f32_e64 s[6:7], 0, v67
	s_nop 1
	v_cndmask_b32_e64 v67, v68, v69, s[6:7]
	v_mul_f32_e32 v68, 0x37800000, v67
	v_cndmask_b32_e32 v67, v67, v68, vcc
	v_mov_b32_e32 v68, 0x260
	v_cmp_class_f32_e32 vcc, v66, v68
	s_nop 1
	v_cndmask_b32_e32 v66, v67, v66, vcc
	v_max_f32_e32 v66, 0x2b8cbccc, v66
	v_div_scale_f32 v67, s[6:7], v66, v66, 1.0
	v_rcp_f32_e32 v68, v67
	s_mov_b32 s6, 0x2ebff000
	v_fma_f32 v69, -v67, v68, 1.0
	v_fmac_f32_e32 v68, v69, v68
	v_div_scale_f32 v69, vcc, 1.0, v66, 1.0
	v_mul_f32_e32 v70, v69, v68
	v_fma_f32 v71, -v67, v70, v69
	v_fmac_f32_e32 v70, v71, v68
	v_fma_f32 v67, -v67, v70, v69
	v_div_fmas_f32 v67, v67, v68, v70
	v_div_fixup_f32 v66, v67, v66, 1.0
	v_mul_f32_e64 v36, v36, v66
	v_mul_f32_e64 v37, v37, v66
	v_mul_f32_e64 v38, v38, v66
	v_mul_f32_e64 v39, v39, v66
	v_mul_f32_e64 v40, v40, v66
	v_mul_f32_e64 v41, v41, v66
	v_cvt_pk_bf16_f32 v36, v36, v37
	v_cvt_pk_bf16_f32 v37, v38, v39
	v_cvt_pk_bf16_f32 v38, v40, v41
	v_lshl_add_u64 v[40:41], s[8:9], 0, v[78:79]
	v_mul_f32_e64 v42, v42, v66
	v_mul_f32_e64 v43, v43, v66
	v_add_co_u32_e32 v40, vcc, s6, v40
	v_mul_f32_e64 v58, v58, v66
	v_mul_f32_e64 v59, v59, v66
	v_mul_f32_e64 v60, v60, v66
	v_mul_f32_e64 v61, v61, v66
	v_mul_f32_e64 v62, v62, v66
	v_mul_f32_e64 v63, v63, v66
	v_mul_f32_e64 v64, v64, v66
	v_mul_f32_e64 v65, v65, v66
	v_cvt_pk_bf16_f32 v39, v42, v43
	v_addc_co_u32_e32 v41, vcc, 0, v41, vcc
	global_store_dwordx4 v[40:41], v[36:39], off offset:3584
	s_nop 1
	v_cvt_pk_bf16_f32 v36, v58, v59
	v_cvt_pk_bf16_f32 v37, v60, v61
	v_cvt_pk_bf16_f32 v38, v62, v63
	v_cvt_pk_bf16_f32 v39, v64, v65
	global_store_dwordx4 v[40:41], v[36:39], off offset:3600
	s_branch .LBB0_544

.LBB0_764:
	s_ashr_i32 s11, s14, 31
	s_lshr_b32 s11, s11, 20
	s_add_i32 s11, s14, s11
	s_ashr_i32 s15, s11, 12
	s_and_b32 s11, s11, 0xfffff000
	s_sub_i32 s14, s14, s11
	s_ashr_i32 s11, s10, 31
	s_lshl_b64 s[16:17], s[10:11], 2
	v_lshlrev_b32_e32 v48, 16, v24
	v_and_b32_e32 v49, 0xffff0000, v24
	v_lshlrev_b32_e32 v50, 16, v25
	v_and_b32_e32 v51, 0xffff0000, v25
	v_lshl_add_u64 v[24:25], v[28:29], 0, s[16:17]
	global_load_dwordx4 v[52:55], v[24:25], off
	v_lshl_add_u64 v[24:25], v[30:31], 0, s[16:17]
	global_load_dwordx4 v[58:61], v[24:25], off
	v_mul_f32_e64 v24, v48, v48
	v_mul_f32_e64 v25, v49, v49
	v_lshlrev_b32_e32 v62, 16, v26
	v_and_b32_e32 v63, 0xffff0000, v26
	v_lshlrev_b32_e32 v64, 16, v27
	v_and_b32_e32 v65, 0xffff0000, v27
	v_mul_f32_e64 v26, v50, v50
	v_mul_f32_e64 v27, v51, v51
	v_add_f32_e32 v24, v24, v25
	v_add_f32_e32 v24, v26, v24
	v_lshlrev_b32_e32 v66, 16, v46
	v_and_b32_e32 v67, 0xffff0000, v46
	v_lshlrev_b32_e32 v68, 16, v47
	v_and_b32_e32 v69, 0xffff0000, v47
	v_mul_f32_e64 v46, v62, v62
	v_mul_f32_e64 v47, v63, v63
	v_add_f32_e32 v24, v27, v24
	v_add_f32_e32 v24, v46, v24
	v_mul_f32_e64 v70, v64, v64
	v_mul_f32_e64 v71, v65, v65
	v_add_f32_e32 v24, v47, v24
	v_add_f32_e32 v24, v70, v24
	v_mul_f32_e64 v72, v66, v66
	v_mul_f32_e64 v73, v67, v67
	v_add_f32_e32 v24, v71, v24
	v_add_f32_e32 v24, v72, v24
	v_mul_f32_e64 v74, v68, v68
	v_mul_f32_e64 v75, v69, v69
	v_add_f32_e32 v24, v73, v24
	v_add_f32_e32 v24, v74, v24
	v_add_f32_e32 v24, v75, v24
	ds_swizzle_b32 v25, v24 offset:swizzle(SWAP,1)
	v_lshl_add_u32 v44, s15, 3, v56
	v_ashrrev_i32_e32 v45, 31, v44
	s_ashr_i32 s15, s14, 31
	v_readlane_b32 s22, v252, 38
	s_waitcnt lgkmcnt(0)
	v_add_f32_e32 v24, v24, v25
	ds_swizzle_b32 v25, v24 offset:swizzle(SWAP,2)
	v_mov_b32_e32 v39, v209
	v_readlane_b32 s23, v252, 39
	s_waitcnt lgkmcnt(0)
	v_add_f32_e32 v24, v24, v25
	ds_swizzle_b32 v25, v24 offset:swizzle(SWAP,4)
	s_waitcnt lgkmcnt(0)
	v_add_f32_e32 v24, v24, v25
	v_fmamk_f32 v24, v24, 0x3c2aaaab, v210
	v_cmp_gt_f32_e32 vcc, s56, v24
	v_mul_f32_e32 v25, 0x4b800000, v24
	s_nop 0
	v_cndmask_b32_e32 v24, v24, v25, vcc
	v_rsq_f32_e32 v24, v24
	s_nop 0
	v_mul_f32_e32 v25, 0x45800000, v24
	v_cndmask_b32_e32 v70, v24, v25, vcc
	v_mul_f32_e64 v24, v4, v70
	v_mul_f32_e64 v25, v5, v70
	v_mul_f32_e64 v26, v6, v70
	v_mul_f32_e64 v27, v7, v70
	v_mul_f32_e64 v24, v24, v48
	v_mul_f32_e64 v25, v25, v49
	v_mul_f32_e64 v48, v2, v70
	v_mul_f32_e64 v49, v3, v70
	v_mul_f32_e64 v26, v26, v50
	v_mul_f32_e64 v27, v27, v51
	v_mul_f32_e64 v50, v48, v64
	v_mul_f32_e64 v51, v49, v65
	v_mul_f32_e64 v48, v70, v66
	v_mul_f32_e64 v49, v70, v67
	v_mul_f32_e64 v46, v0, v70
	v_mul_f32_e64 v47, v1, v70
	v_mul_f32_e64 v48, v8, v48
	v_mul_f32_e64 v49, v9, v49
	v_mul_f32_e64 v46, v46, v62
	v_mul_f32_e64 v47, v47, v63
	ds_swizzle_b32 v62, v48 offset:swizzle(SWAP,4)
	ds_swizzle_b32 v63, v49 offset:swizzle(SWAP,4)
	v_cvt_pk_bf16_f32 v24, v24, v25
	v_cvt_pk_bf16_f32 v25, v26, v27
	v_cvt_pk_bf16_f32 v26, v46, v47
	v_cvt_pk_bf16_f32 v27, v50, v51
	s_andn2_b64 vcc, exec, s[22:23]
	s_waitcnt vmcnt(0) lgkmcnt(0)
	v_mul_f32_e64 v58, v58, v62
	v_mul_f32_e64 v59, v59, v63
	s_nop 0
	v_cndmask_b32_e64 v59, v59, -v59, s[0:1]
	v_cndmask_b32_e64 v58, v58, -v58, s[0:1]
	v_fma_f32 v48, v52, v48, v58
	v_fma_f32 v49, v53, v49, v59
	v_mul_f32_e64 v52, v70, v68
	v_mul_f32_e64 v53, v70, v69
	v_mul_f32_e64 v52, v10, v52
	v_mul_f32_e64 v53, v11, v53
	ds_swizzle_b32 v58, v52 offset:swizzle(SWAP,4)
	ds_swizzle_b32 v59, v53 offset:swizzle(SWAP,4)
	s_waitcnt lgkmcnt(0)
	v_mul_f32_e64 v58, v60, v58
	v_mul_f32_e64 v59, v61, v59
	s_nop 0
	v_cndmask_b32_e64 v59, v59, -v59, s[0:1]
	v_cndmask_b32_e64 v58, v58, -v58, s[0:1]
	v_fma_f32 v52, v54, v52, v58
	v_fma_f32 v53, v55, v53, v59
	v_lshlrev_b64 v[54:55], 12, v[44:45]
	v_lshl_add_u64 v[54:55], v[54:55], 0, s[14:15]
	v_mov_b64_e32 v[58:59], s[8:9]
	v_mad_u64_u32 v[58:59], s[16:17], v54, s88, v[58:59]
	v_mad_i32_i24 v59, v55, s88, v59
	v_lshl_add_u64 v[46:47], v[58:59], 0, v[208:209]
	global_store_dwordx4 v[46:47], v[24:27], off
	s_mov_b64 s[16:17], -1
	s_nop 0
	v_cvt_pk_bf16_f32 v24, v48, v49
	v_cvt_pk_bf16_f32 v25, v52, v53
	v_lshl_add_u64 v[26:27], v[58:59], 0, v[38:39]
	global_store_dwordx2 v[26:27], v[24:25], off offset:128
	s_cbranch_vccnz .LBB0_766
	s_lshl_b64 s[14:15], s[14:15], 1
	s_add_u32 s14, s6, s14
	s_addc_u32 s15, s7, s15
	v_lshlrev_b64 v[24:25], 19, v[44:45]
	v_lshl_add_u64 v[24:25], s[14:15], 0, v[24:25]
	v_lshl_add_u64 v[24:25], v[24:25], 0, v[32:33]
	s_movk_i32 s11, 0x2000
	v_add_co_u32_e32 v26, vcc, s11, v24
	s_movk_i32 s11, 0x4000
	s_nop 0
	v_addc_co_u32_e32 v27, vcc, 0, v25, vcc
	global_store_short_d16_hi v[26:27], v12, off
	v_add_co_u32_e32 v26, vcc, s11, v24
	global_store_short v[24:25], v12, off
	s_nop 0
	v_addc_co_u32_e32 v27, vcc, 0, v25, vcc
	global_store_short v[26:27], v13, off
	v_add_co_u32_e32 v26, vcc, s82, v24
	s_mov_b64 s[16:17], 0
	s_nop 0
	v_addc_co_u32_e32 v27, vcc, 0, v25, vcc
	global_store_short_d16_hi v[26:27], v13, off
	v_add_co_u32_e32 v26, vcc, s83, v24
	s_nop 1
	v_addc_co_u32_e32 v27, vcc, 0, v25, vcc
	global_store_short v[26:27], v14, off
	v_add_co_u32_e32 v26, vcc, 0xa000, v24
	s_nop 1
	v_addc_co_u32_e32 v27, vcc, 0, v25, vcc
	global_store_short_d16_hi v[26:27], v14, off
	v_add_co_u32_e32 v26, vcc, 0xc000, v24
	s_nop 1
	v_addc_co_u32_e32 v27, vcc, 0, v25, vcc
	v_add_co_u32_e32 v24, vcc, 0xe000, v24
	global_store_short v[26:27], v15, off
	s_nop 0
	v_addc_co_u32_e32 v25, vcc, 0, v25, vcc
	global_store_short_d16_hi v[24:25], v15, off

.LBB0_787:
	s_or_b64 exec, exec, s[82:83]
	v_lshlrev_b32_e32 v54, 16, v36
	v_and_b32_e32 v55, 0xffff0000, v36
	v_add_f32_e64 v54, v0, v54
	v_add_f32_e64 v55, v1, v55
	v_lshlrev_b32_e32 v0, 16, v37
	v_and_b32_e32 v1, 0xffff0000, v37
	v_add_f32_e64 v36, v2, v0
	v_add_f32_e64 v37, v3, v1
	v_lshlrev_b32_e32 v0, 16, v38
	v_and_b32_e32 v1, 0xffff0000, v38
	v_add_f32_e64 v4, v4, v0
	v_add_f32_e64 v5, v5, v1
	v_lshlrev_b32_e32 v0, 16, v39
	v_and_b32_e32 v1, 0xffff0000, v39
	v_add_f32_e64 v6, v6, v0
	v_add_f32_e64 v7, v7, v1
	v_lshlrev_b32_e32 v0, 16, v32
	v_and_b32_e32 v1, 0xffff0000, v32
	v_add_f32_e64 v8, v8, v0
	v_add_f32_e64 v9, v9, v1
	v_lshlrev_b32_e32 v0, 16, v33
	v_and_b32_e32 v1, 0xffff0000, v33
	v_add_f32_e64 v10, v10, v0
	v_add_f32_e64 v11, v11, v1
	v_lshlrev_b32_e32 v0, 16, v34
	v_and_b32_e32 v1, 0xffff0000, v34
	v_add_f32_e64 v12, v12, v0
	v_add_f32_e64 v13, v13, v1
	v_lshlrev_b32_e32 v0, 16, v35
	v_and_b32_e32 v1, 0xffff0000, v35
	s_add_u32 s82, s58, 0x2000
	v_add_f32_e64 v14, v14, v0
	v_add_f32_e64 v15, v15, v1
	s_addc_u32 s83, s59, 0
	v_cvt_pk_bf16_f32 v0, v16, v17
	v_cvt_pk_bf16_f32 v1, v18, v19
	v_cvt_pk_bf16_f32 v2, v20, v21
	v_cvt_pk_bf16_f32 v3, v22, v23
	v_lshl_add_u64 v[16:17], s[58:59], 0, v[48:49]
	global_store_dwordx4 v[16:17], v[0:3], off
	s_mov_b64 s[84:85], 0x4000
	s_nop 0
	v_cvt_pk_bf16_f32 v0, v54, v55
	v_cvt_pk_bf16_f32 v1, v36, v37
	v_cvt_pk_bf16_f32 v2, v4, v5
	v_cvt_pk_bf16_f32 v3, v6, v7
	v_lshl_add_u64 v[4:5], s[82:83], 0, v[48:49]
	global_store_dwordx4 v[4:5], v[0:3], off
	v_lshl_add_u64 v[4:5], s[82:83], 0, v[50:51]
	v_readlane_b32 s82, v253, 12
	v_cvt_pk_bf16_f32 v0, v24, v25
	v_cvt_pk_bf16_f32 v1, v26, v27
	v_cvt_pk_bf16_f32 v2, v28, v29
	v_cvt_pk_bf16_f32 v3, v30, v31
	global_store_dwordx4 v[16:17], v[0:3], off offset:1024
	s_nop 1
	v_cvt_pk_bf16_f32 v0, v8, v9
	v_cvt_pk_bf16_f32 v1, v10, v11
	v_cvt_pk_bf16_f32 v2, v12, v13
	v_cvt_pk_bf16_f32 v3, v14, v15
	global_store_dwordx4 v[4:5], v[0:3], off

.LBB0_791:
	v_lshlrev_b32_e32 v0, 16, v90
	s_waitcnt vmcnt(1)
	v_add_f32_e32 v0, v3, v0
	v_lshlrev_b32_e32 v4, 16, v95
	v_mul_f32_e32 v0, 0xbfb8aa3b, v0
	v_add_f32_e32 v4, v3, v4
	v_exp_f32_e32 v0, v0
	v_mul_f32_e32 v4, 0xbfb8aa3b, v4
	v_exp_f32_e32 v5, v4
	v_lshlrev_b32_e32 v29, 16, v102
	v_add_f32_e32 v0, 1.0, v0
	v_rcp_f32_e32 v4, v0
	v_add_f32_e32 v0, 1.0, v5
	v_lshlrev_b32_e32 v5, 16, v98
	v_add_f32_e32 v5, v3, v5
	v_mul_f32_e32 v5, 0xbfb8aa3b, v5
	v_add_f32_e32 v29, v3, v29
	v_exp_f32_e32 v5, v5
	v_mul_f32_e32 v29, 0xbfb8aa3b, v29
	v_exp_f32_e32 v29, v29
	v_rcp_f32_e32 v31, v0
	v_add_f32_e32 v0, 1.0, v5
	v_lshlrev_b32_e32 v5, 16, v106
	v_rcp_f32_e32 v32, v0
	v_add_f32_e32 v0, 1.0, v29
	v_add_f32_e32 v5, v3, v5
	v_lshlrev_b32_e32 v29, 16, v116
	v_mul_f32_e32 v5, 0xbfb8aa3b, v5
	v_add_f32_e32 v29, v3, v29
	v_exp_f32_e32 v5, v5
	v_mul_f32_e32 v29, 0xbfb8aa3b, v29
	v_exp_f32_e32 v29, v29
	v_rcp_f32_e32 v35, v0
	v_add_f32_e32 v0, 1.0, v5
	v_lshlrev_b32_e32 v5, 16, v141
	v_rcp_f32_e32 v36, v0
	v_add_f32_e32 v0, 1.0, v29
	v_add_f32_e32 v5, v3, v5
	v_lshlrev_b32_e32 v29, 16, v161
	v_mul_f32_e32 v5, 0xbfb8aa3b, v5
	v_add_f32_e32 v3, v3, v29
	v_exp_f32_e32 v5, v5
	v_mul_f32_e32 v3, 0xbfb8aa3b, v3
	v_exp_f32_e32 v3, v3
	v_rcp_f32_e32 v39, v0
	v_add_f32_e32 v0, 1.0, v5
	v_rcp_f32_e32 v54, v0
	v_add_f32_e32 v0, 1.0, v3
	v_rcp_f32_e32 v3, v0
	v_add_f32_e32 v0, -1.0, v4
	s_waitcnt vmcnt(0)
	v_fma_f32 v5, v2, v0, 1.0
	v_add_f32_e32 v0, -1.0, v31
	v_fma_f32 v30, v2, v0, 1.0
	v_add_f32_e32 v0, -1.0, v32
	v_fma_f32 v33, v2, v0, 1.0
	v_add_f32_e32 v0, -1.0, v35
	v_and_b32_e32 v65, 0xffff0000, v164
	v_lshlrev_b32_e32 v64, 16, v164
	v_fma_f32 v34, v2, v0, 1.0
	v_add_f32_e32 v0, -1.0, v36
	v_mul_f32_e64 v66, v32, v64
	v_mul_f32_e64 v67, v33, v65
	v_and_b32_e32 v33, 0xffff0000, v165
	v_lshlrev_b32_e32 v32, 16, v165
	v_fma_f32 v37, v2, v0, 1.0
	v_add_f32_e32 v0, -1.0, v39
	v_and_b32_e32 v57, 0xffff0000, v162
	v_lshlrev_b32_e32 v56, 16, v162
	v_mul_f32_e64 v34, v34, v32
	v_mul_f32_e64 v35, v35, v33
	v_fma_f32 v38, v2, v0, 1.0
	v_add_f32_e32 v0, -1.0, v54
	v_add_f32_e32 v32, -1.0, v3
	v_readlane_b32 s66, v254, 5
	v_mul_f32_e64 v58, v4, v56
	v_mul_f32_e64 v59, v5, v57
	v_fma_f32 v55, v2, v0, 1.0
	v_and_b32_e32 v5, 0xffff0000, v170
	v_lshlrev_b32_e32 v4, 16, v170
	v_fma_f32 v2, v2, v32, 1.0
	v_readlane_b32 s67, v254, 6
	v_mul_f32_e64 v2, v2, v4
	v_mul_f32_e64 v3, v3, v5
	v_lshlrev_b32_e32 v29, 16, v87
	v_cndmask_b32_e64 v4, 0, v28, s[66:67]
	v_readlane_b32 s66, v254, 7
	v_readlane_b32 s67, v254, 8
	v_and_b32_e32 v63, 0xffff0000, v163
	v_lshlrev_b32_e32 v62, 16, v163
	v_cndmask_b32_e64 v1, 0, v1, s[66:67]
	v_readlane_b32 s66, v254, 9
	v_readlane_b32 s67, v254, 10
	v_add_f32_e32 v1, v4, v1
	v_mul_f32_e64 v30, v30, v62
	v_mul_f32_e64 v31, v31, v63
	v_cndmask_b32_e64 v4, 0, v6, s[66:67]
	v_readlane_b32 s66, v254, 11
	v_add_f32_e32 v1, v1, v4
	v_cndmask_b32_e64 v4, 0, v7, s[36:37]
	v_readlane_b32 s67, v254, 12
	v_add_f32_e32 v1, v1, v4
	v_lshlrev_b32_e32 v60, 16, v91
	v_cndmask_b32_e64 v4, 0, v8, s[66:67]
	v_readlane_b32 s66, v254, 13
	v_readlane_b32 s67, v254, 14
	v_add_f32_e32 v1, v1, v4
	v_lshlrev_b32_e32 v76, 16, v94
	v_cndmask_b32_e64 v4, 0, v9, s[66:67]
	v_readlane_b32 s66, v254, 15
	v_readlane_b32 s67, v254, 16
	v_add_f32_e32 v1, v1, v4
	v_lshlrev_b32_e32 v62, 16, v99
	v_cndmask_b32_e64 v4, 0, v10, s[66:67]
	v_readlane_b32 s66, v254, 17
	v_readlane_b32 s67, v254, 18
	v_add_f32_e32 v1, v1, v4
	v_and_b32_e32 v69, 0xffff0000, v166
	v_cndmask_b32_e64 v4, 0, v11, s[66:67]
	v_add_f32_e32 v1, v1, v4
	v_sub_f32_e32 v8, v1, v12
	v_add_f32_e32 v4, v12, v8
	v_mul_f32_e32 v6, 0x3fb8aa3b, v8
	v_mul_f32_e32 v4, 0x3fb8aa3b, v4
	v_exp_f32_e32 v7, v6
	v_exp_f32_e32 v6, v4
	v_mul_f32_e32 v4, 0xbfb8aa3b, v8
	v_exp_f32_e32 v4, v4
	v_add_f32_e64 v10, -v56, neg(0)
	v_add_f32_e64 v11, -v57, neg(0)
	v_sub_f32_e32 v8, v22, v8
	v_mov_b32_e32 v11, v29
	v_mul_f32_e64 v6, v6, v10
	v_mul_f32_e64 v7, v7, v11
	v_mul_f32_e64 v10, v58, v4
	v_mul_f32_e64 v11, v59, v4
	v_cvt_pk_bf16_f32 v4, v6, s0
	ds_write_b16 v143, v4 offset:64512
	v_cvt_pk_bf16_f32 v4, v7, s0
	ds_write_b16 v143, v4
	v_cvt_pk_bf16_f32 v4, v10, s0
	ds_write_b16 v144, v4
	v_cvt_pk_bf16_f32 v4, v11, s0
	ds_write_b16 v145, v4
	v_add_f32_e32 v4, v27, v1
	v_mul_f32_e32 v10, 0x3fb8aa3b, v4
	v_mul_f32_e32 v11, 0xbfb8aa3b, v4
	v_add_f32_e32 v7, v13, v4
	v_exp_f32_e32 v10, v10
	v_exp_f32_e32 v61, v11
	v_sub_f32_e32 v4, v22, v4
	v_mul_f32_e32 v8, 0x3fb8aa3b, v8
	v_mul_f32_e32 v7, 0x3fb8aa3b, v7
	v_mul_f32_e32 v4, 0x3fb8aa3b, v4
	v_exp_f32_e32 v8, v8
	v_exp_f32_e32 v7, v7
	v_exp_f32_e32 v13, v4
	v_mov_b32_e32 v11, v31
	v_mul_f32_e64 v10, v10, v60
	v_mul_f32_e64 v11, v11, v61
	v_mov_b32_e32 v12, v61
	v_cvt_pk_bf16_f32 v10, v10, s0
	v_mul_f32_e64 v9, v59, v8
	v_mul_f32_e64 v8, v58, v8
	v_mul_f32_e64 v4, v7, -v63
	v_mul_f32_e64 v28, v30, v12
	v_mul_f32_e64 v29, v31, v13
	v_mul_f32_e32 v7, v30, v13
	ds_write_b16 v143, v10 offset:144
	v_cvt_pk_bf16_f32 v10, v11, s0
	ds_write_b16 v146, v10
	v_cvt_pk_bf16_f32 v10, v28, s0
	v_cvt_pk_bf16_f32 v28, v9, v7
	v_add_f32_e32 v7, v26, v1
	v_cvt_pk_bf16_f32 v12, v4, s0
	v_cvt_pk_bf16_f32 v6, v6, v4
	v_add_f32_e32 v4, v14, v7
	ds_write_b16 v147, v10
	v_cvt_pk_bf16_f32 v10, v8, v29
	v_mul_f32_e32 v8, 0x3fb8aa3b, v7
	v_mul_f32_e32 v4, 0x3fb8aa3b, v4
	v_exp_f32_e32 v9, v8
	v_exp_f32_e32 v8, v4
	v_mul_f32_e32 v4, 0xbfb8aa3b, v7
	v_exp_f32_e32 v4, v4
	v_add_f32_e64 v26, -v64, neg(0)
	v_add_f32_e64 v27, -v65, neg(0)
	v_sub_f32_e32 v7, v22, v7
	v_mov_b32_e32 v27, v76
	v_mul_f32_e64 v8, v8, v26
	v_mul_f32_e64 v9, v9, v27
	v_mul_f32_e64 v26, v66, v4
	v_mul_f32_e64 v27, v67, v4
	v_cvt_pk_bf16_f32 v4, v8, s0
	ds_write_b16 v143, v4 offset:64800
	v_cvt_pk_bf16_f32 v4, v9, s0
	ds_write_b16 v143, v4 offset:288
	v_cvt_pk_bf16_f32 v4, v26, s0
	ds_write_b16 v148, v4
	v_cvt_pk_bf16_f32 v4, v27, s0
	v_mul_f32_e32 v7, 0x3fb8aa3b, v7
	ds_write_b16 v149, v4
	v_add_f32_e32 v4, v25, v1
	ds_write_b16 v143, v12 offset:64656
	v_exp_f32_e32 v12, v7
	v_add_f32_e32 v7, v15, v4
	v_mul_f32_e32 v9, 0x3fb8aa3b, v4
	v_mul_f32_e32 v7, 0x3fb8aa3b, v7
	v_exp_f32_e32 v14, v9
	v_exp_f32_e32 v7, v7
	v_mul_f32_e32 v9, 0xbfb8aa3b, v4
	v_exp_f32_e32 v63, v9
	v_sub_f32_e32 v4, v22, v4
	v_mul_f32_e32 v4, 0x3fb8aa3b, v4
	v_exp_f32_e32 v27, v4
	v_mul_f32_e64 v4, v7, -v33
	v_mov_b32_e32 v15, v35
	v_mul_f32_e64 v14, v14, v62
	v_mul_f32_e64 v15, v15, v63
	v_cvt_pk_bf16_f32 v7, v4, s0
	v_mov_b32_e32 v26, v63
	ds_write_b16 v143, v7 offset:64944
	v_cvt_pk_bf16_f32 v7, v14, s0
	v_mul_f32_e64 v13, v67, v12
	v_mul_f32_e64 v12, v66, v12
	v_mul_f32_e64 v30, v34, v26
	v_mul_f32_e64 v31, v35, v27
	ds_write_b16 v143, v7 offset:432
	v_cvt_pk_bf16_f32 v7, v15, s0
	ds_write_b16 v150, v7
	v_cvt_pk_bf16_f32 v7, v30, s0
	v_cvt_pk_bf16_f32 v11, v12, v31
	v_add_f32_e32 v12, v24, v1
	ds_write_b16 v151, v7
	v_cvt_pk_bf16_f32 v7, v8, v4
	v_add_f32_e32 v4, v16, v12
	v_mul_f32_e32 v9, v34, v27
	v_mul_f32_e32 v8, 0x3fb8aa3b, v12
	v_mul_f32_e32 v4, 0x3fb8aa3b, v4
	v_cvt_pk_bf16_f32 v29, v13, v9
	v_exp_f32_e32 v9, v8
	v_exp_f32_e32 v8, v4
	v_mul_f32_e32 v4, 0xbfb8aa3b, v12
	v_lshlrev_b32_e32 v68, 16, v166
	v_exp_f32_e32 v4, v4
	v_lshlrev_b32_e32 v79, 16, v103
	v_add_f32_e64 v14, -v68, neg(0)
	v_add_f32_e64 v15, -v69, neg(0)
	v_mul_f32_e64 v36, v36, v68
	v_mul_f32_e64 v37, v37, v69
	v_mov_b32_e32 v15, v79
	v_mul_f32_e64 v8, v8, v14
	v_mul_f32_e64 v9, v9, v15
	v_mul_f32_e64 v14, v36, v4
	v_mul_f32_e64 v15, v37, v4
	v_cvt_pk_bf16_f32 v4, v8, s0
	ds_write_b16 v143, v4 offset:65088
	v_cvt_pk_bf16_f32 v4, v9, s0
	ds_write_b16 v143, v4 offset:576
	v_cvt_pk_bf16_f32 v4, v14, s0
	ds_write_b16 v152, v4
	v_cvt_pk_bf16_f32 v4, v15, s0
	ds_write_b16 v153, v4
	v_add_f32_e32 v4, v23, v1
	v_sub_f32_e32 v12, v22, v12
	v_add_f32_e32 v9, v17, v4
	v_mul_f32_e32 v14, 0x3fb8aa3b, v4
	v_mul_f32_e32 v15, 0xbfb8aa3b, v4
	v_sub_f32_e32 v4, v22, v4
	v_lshlrev_b32_e32 v45, 16, v88
	v_lshlrev_b32_e32 v71, 16, v92
	v_mul_f32_e32 v12, 0x3fb8aa3b, v12
	v_mul_f32_e32 v9, 0x3fb8aa3b, v9
	v_mul_f32_e32 v4, 0x3fb8aa3b, v4
	v_cvt_pk_bf16_f32 v32, v45, v71
	v_exp_f32_e32 v12, v12
	v_exp_f32_e32 v14, v14
	v_exp_f32_e32 v9, v9
	v_exp_f32_e32 v71, v15
	v_exp_f32_e32 v17, v4
	v_and_b32_e32 v73, 0xffff0000, v167
	v_lshlrev_b32_e32 v72, 16, v167
	v_mul_f32_e64 v38, v38, v72
	v_mul_f32_e64 v39, v39, v73
	v_lshlrev_b32_e32 v70, 16, v107
	v_mov_b32_e32 v15, v39
	v_mul_f32_e64 v13, v37, v12
	v_mul_f32_e64 v12, v36, v12
	v_mul_f32_e64 v4, v9, -v73
	v_mul_f32_e64 v14, v14, v70
	v_mul_f32_e64 v15, v15, v71
	v_mul_f32_e32 v9, v38, v17
	v_mov_b32_e32 v16, v71
	v_cvt_pk_bf16_f32 v14, v14, s0
	v_cvt_pk_bf16_f32 v30, v13, v9
	v_add_f32_e32 v9, v1, v21
	v_mul_f32_e64 v24, v38, v16
	v_mul_f32_e64 v25, v39, v17
	v_cvt_pk_bf16_f32 v16, v4, s0
	ds_write_b16 v143, v14 offset:720
	v_cvt_pk_bf16_f32 v14, v15, s0
	v_cvt_pk_bf16_f32 v8, v8, v4
	v_add_f32_e32 v4, v18, v9
	ds_write_b16 v154, v14
	v_cvt_pk_bf16_f32 v14, v24, s0
	v_mul_f32_e32 v13, 0x3fb8aa3b, v9
	v_mul_f32_e32 v4, 0x3fb8aa3b, v4
	ds_write_b16 v155, v14
	v_exp_f32_e32 v15, v13
	v_exp_f32_e32 v14, v4
	v_mul_f32_e32 v4, 0xbfb8aa3b, v9
	v_and_b32_e32 v75, 0xffff0000, v169
	v_lshlrev_b32_e32 v74, 16, v169
	v_exp_f32_e32 v4, v4
	v_lshlrev_b32_e32 v72, 16, v114
	v_cvt_pk_bf16_f32 v12, v12, v25
	v_add_f32_e64 v24, -v74, neg(0)
	v_add_f32_e64 v25, -v75, neg(0)
	v_mul_f32_e64 v54, v54, v74
	v_mul_f32_e64 v55, v55, v75
	v_mov_b32_e32 v25, v72
	v_sub_f32_e32 v9, v22, v9
	v_mul_f32_e64 v14, v14, v24
	v_mul_f32_e64 v15, v15, v25
	v_mul_f32_e32 v9, 0x3fb8aa3b, v9
	v_mul_f32_e64 v24, v54, v4
	v_mul_f32_e64 v25, v55, v4
	v_cvt_pk_bf16_f32 v4, v14, s0
	ds_write_b16 v143, v16 offset:65232
	v_exp_f32_e32 v16, v9
	ds_write_b16 v143, v4 offset:65376
	v_cvt_pk_bf16_f32 v4, v15, s0
	v_add_f32_e32 v9, v1, v20
	ds_write_b16 v143, v4 offset:864
	v_cvt_pk_bf16_f32 v4, v24, s0
	v_add_f32_e32 v1, v19, v9
	ds_write_b16 v156, v4
	v_cvt_pk_bf16_f32 v4, v25, s0
	v_mul_f32_e32 v1, 0x3fb8aa3b, v1
	ds_write_b16 v157, v4
	v_mul_f32_e32 v4, 0x3fb8aa3b, v9
	v_exp_f32_e32 v13, v1
	v_mul_f32_e32 v1, 0xbfb8aa3b, v9
	v_sub_f32_e32 v9, v22, v9
	v_exp_f32_e32 v1, v1
	v_mul_f32_e32 v9, 0x3fb8aa3b, v9
	v_exp_f32_e32 v4, v4
	v_exp_f32_e32 v19, v9
	v_lshlrev_b32_e32 v0, 16, v139
	v_mul_f32_e64 v9, v13, -v5
	v_mov_b32_e32 v5, v3
	v_mov_b32_e32 v18, v1
	v_mul_f32_e64 v4, v4, v0
	v_mul_f32_e64 v5, v5, v1
	v_mul_f32_e64 v0, v2, v18
	v_mul_f32_e64 v1, v3, v19
	v_cvt_pk_bf16_f32 v3, v9, s0
	v_mul_f32_e64 v17, v55, v16
	v_mul_f32_e64 v16, v54, v16
	v_mul_f32_e32 v2, v2, v19
	ds_write_b16 v143, v3 offset:65520
	v_cvt_pk_bf16_f32 v3, v4, s0
	v_lshlrev_b32_e32 v77, 16, v96
	v_lshlrev_b32_e32 v78, 16, v100
	v_lshlrev_b32_e32 v80, 16, v104
	v_lshlrev_b32_e32 v81, 16, v108
	v_lshlrev_b32_e32 v82, 16, v120
	v_lshlrev_b32_e32 v83, 16, v142
	ds_write_b16 v143, v3 offset:1008
	v_cvt_pk_bf16_f32 v3, v5, s0
	v_cvt_pk_bf16_f32 v0, v0, s0
	v_cvt_pk_bf16_f32 v9, v14, v9
	v_cvt_pk_bf16_f32 v31, v17, v2
	v_mov_b32_e32 v2, v209
	v_mov_b32_e32 v4, v209
	v_cvt_pk_bf16_f32 v33, v77, v78
	v_cvt_pk_bf16_f32 v34, v80, v81
	ds_write_b16 v158, v3
	ds_write_b16 v159, v0
	v_cvt_pk_bf16_f32 v13, v16, v1
	v_cvt_pk_bf16_f32 v35, v82, v83
	ds_write_b128 v115, v[6:9] offset:9216
	ds_write_b128 v115, v[10:13] offset:18432
	ds_write_b128 v115, v[28:31] offset:27648
	ds_write_b128 v115, v[32:35] offset:36864
	s_waitcnt lgkmcnt(0)
	s_barrier
	ds_read_b128 v[20:23], v119
	ds_read_b128 v[24:27], v121 offset:64512
	v_mov_b32_e32 v5, v4
	v_mov_b32_e32 v6, v4
	v_mov_b32_e32 v7, v4
	v_mov_b32_e32 v8, v4
	v_mov_b32_e32 v9, v4
	v_mov_b32_e32 v10, v4
	v_mov_b32_e32 v11, v4
	v_mov_b32_e32 v12, v4
	v_mov_b32_e32 v13, v4
	v_mov_b32_e32 v14, v4
	v_mov_b32_e32 v15, v4
	v_mov_b32_e32 v16, v4
	v_mov_b32_e32 v17, v4
	v_mov_b32_e32 v18, v4
	v_mov_b32_e32 v19, v4
	ds_read_b128 v[28:31], v119 offset:32
	ds_read_b128 v[32:35], v121 offset:64544
	s_waitcnt lgkmcnt(2)
	v_mfma_f32_32x32x16_bf16 v[4:19], v[20:23], v[24:27], v[4:19]
	v_readlane_b32 s66, v254, 19
	v_readlane_b32 s67, v254, 20
	s_or_b64 vcc, s[56:57], s[52:53]
	s_waitcnt lgkmcnt(0)
	v_mfma_f32_32x32x16_bf16 v[4:19], v[28:31], v[32:35], v[4:19]
	ds_read_b128 v[20:23], v119 offset:64
	ds_read_b128 v[24:27], v121 offset:64576
	ds_read_b128 v[28:31], v119 offset:96
	ds_read_b128 v[32:35], v121 offset:64608
	s_waitcnt lgkmcnt(2)
	v_mfma_f32_32x32x16_bf16 v[4:19], v[20:23], v[24:27], v[4:19]
	v_mov_b32_e32 v20, v209
	ds_read_b128 v[36:39], v119
	ds_read_b128 v[54:57], v121
	v_mov_b32_e32 v21, v20
	v_mov_b32_e32 v22, v20
	v_mov_b32_e32 v23, v20
	s_waitcnt lgkmcnt(2)
	v_mfma_f32_32x32x16_bf16 v[4:19], v[28:31], v[32:35], v[4:19]
	v_mov_b32_e32 v24, v20
	v_mov_b32_e32 v25, v20
	v_mov_b32_e32 v26, v20
	v_mov_b32_e32 v27, v20
	v_mov_b32_e32 v28, v20
	v_mov_b32_e32 v29, v20
	v_mov_b32_e32 v30, v20
	v_mov_b32_e32 v31, v20
	v_mov_b32_e32 v32, v20
	v_mov_b32_e32 v33, v20
	v_mov_b32_e32 v34, v20
	v_mov_b32_e32 v35, v20
	ds_read_b128 v[58:61], v119 offset:32
	ds_read_b128 v[62:65], v121 offset:32
	s_waitcnt lgkmcnt(2)
	v_mfma_f32_32x32x16_bf16 v[20:35], v[36:39], v[54:57], v[20:35]
	v_cndmask_b32_e64 v19, 0, v19, s[16:17]
	v_cndmask_b32_e64 v18, 0, v18, s[96:97]
	v_cndmask_b32_e64 v17, 0, v17, s[4:5]
	v_cndmask_b32_e64 v16, 0, v16, s[6:7]
	v_cndmask_b32_e64 v15, 0, v15, s[8:9]
	v_cndmask_b32_e64 v14, 0, v14, s[10:11]
	v_cndmask_b32_e64 v13, 0, v13, s[38:39]
	s_waitcnt lgkmcnt(0)
	v_mfma_f32_32x32x16_bf16 v[20:35], v[58:61], v[62:65], v[20:35]
	ds_read_b128 v[36:39], v119 offset:64
	ds_read_b128 v[54:57], v121 offset:64
	ds_read_b128 v[58:61], v119 offset:96
	ds_read_b128 v[62:65], v121 offset:96
	v_cndmask_b32_e64 v12, 0, v12, s[40:41]
	v_cndmask_b32_e64 v11, 0, v11, s[42:43]
	v_cndmask_b32_e64 v10, 0, v10, s[44:45]
	v_cndmask_b32_e64 v9, 0, v9, s[46:47]
	v_cndmask_b32_e64 v8, 0, v8, s[48:49]
	v_cndmask_b32_e64 v7, 0, v7, s[50:51]
	s_waitcnt lgkmcnt(2)
	v_mfma_f32_32x32x16_bf16 v[20:35], v[36:39], v[54:57], v[20:35]
	v_cndmask_b32_e64 v6, 0, v6, s[54:55]
	v_cndmask_b32_e64 v5, 0, v5, s[56:57]
	v_cndmask_b32_e32 v4, 0, v4, vcc
	s_and_b64 vcc, exec, s[36:37]
	s_waitcnt lgkmcnt(0)
	v_mfma_f32_32x32x16_bf16 v[20:35], v[58:61], v[62:65], v[20:35]
	s_nop 11
	v_cndmask_b32_e64 v0, v20, 0, s[66:67]
	v_readlane_b32 s66, v254, 21
	v_readlane_b32 s67, v254, 22
	v_cndmask_b32_e64 v0, v0, v20, s[52:53]
	v_cndmask_b32_e64 v221, 0, v21, s[52:53]
	v_cndmask_b32_e64 v219, v22, 0, s[66:67]
	v_readlane_b32 s66, v254, 23
	v_readlane_b32 s67, v254, 24
	s_nop 1
	v_cndmask_b32_e64 v220, v23, 0, s[66:67]
	v_readlane_b32 s66, v254, 25
	v_readlane_b32 s67, v254, 26
	s_nop 1
	v_cndmask_b32_e64 v217, v24, 0, s[66:67]
	v_readlane_b32 s66, v254, 27
	v_readlane_b32 s67, v254, 28
	s_nop 1
	v_cndmask_b32_e64 v218, v25, 0, s[66:67]
	v_readlane_b32 s66, v254, 29
	v_readlane_b32 s67, v254, 30
	s_nop 1
	v_cndmask_b32_e64 v207, v26, 0, s[66:67]
	v_readlane_b32 s66, v254, 31
	v_readlane_b32 s67, v254, 32
	s_nop 1
	v_cndmask_b32_e64 v216, v27, 0, s[66:67]
	v_readlane_b32 s66, v254, 33
	v_readlane_b32 s67, v254, 34
	s_nop 1
	v_cndmask_b32_e64 v203, v28, 0, s[66:67]
	v_readlane_b32 s66, v254, 35
	v_readlane_b32 s67, v254, 36
	s_nop 1
	v_cndmask_b32_e64 v205, v29, 0, s[66:67]
	v_readlane_b32 s66, v254, 37
	v_readlane_b32 s67, v254, 38
	s_nop 1
	v_cndmask_b32_e64 v204, v30, 0, s[66:67]
	v_readlane_b32 s66, v254, 39
	v_readlane_b32 s67, v254, 40
	s_nop 1
	v_cndmask_b32_e64 v206, v31, 0, s[66:67]
	v_readlane_b32 s66, v254, 41
	v_readlane_b32 s67, v254, 42
	s_nop 1
	v_cndmask_b32_e64 v202, v32, 0, s[66:67]
	v_readlane_b32 s66, v254, 43
	v_readlane_b32 s67, v254, 44
	s_nop 1
	v_cndmask_b32_e64 v201, v33, 0, s[66:67]
	v_readlane_b32 s66, v254, 45
	v_readlane_b32 s67, v254, 46
	s_nop 1
	v_cndmask_b32_e64 v200, v34, 0, s[66:67]
	v_readlane_b32 s66, v254, 47
	v_readlane_b32 s67, v254, 48
	s_nop 1
	v_cndmask_b32_e64 v222, v35, 0, s[66:67]
	s_mov_b64 s[66:67], -1
	s_cbranch_vccz .LBB0_793
	v_cvt_pk_bf16_f32 v1, v4, s0
	ds_write_b16 v123, v1 offset:55296
	v_cvt_pk_bf16_f32 v1, v5, s0
	ds_write_b16 v123, v1 offset:55440
	v_cvt_pk_bf16_f32 v1, v6, s0
	ds_write_b16 v123, v1 offset:55584
	v_cvt_pk_bf16_f32 v1, v7, s0
	ds_write_b16 v123, v1 offset:55728
	v_cvt_pk_bf16_f32 v1, v8, s0
	ds_write_b16 v123, v1 offset:56448
	v_cvt_pk_bf16_f32 v1, v9, s0
	ds_write_b16 v123, v1 offset:56592
	v_cvt_pk_bf16_f32 v1, v10, s0
	ds_write_b16 v123, v1 offset:56736
	v_cvt_pk_bf16_f32 v1, v11, s0
	ds_write_b16 v123, v1 offset:56880
	v_cvt_pk_bf16_f32 v1, v12, s0
	ds_write_b16 v123, v1 offset:57600
	v_cvt_pk_bf16_f32 v1, v13, s0
	ds_write_b16 v123, v1 offset:57744
	v_cvt_pk_bf16_f32 v1, v14, s0
	ds_write_b16 v123, v1 offset:57888
	v_cvt_pk_bf16_f32 v1, v15, s0
	ds_write_b16 v123, v1 offset:58032
	v_cvt_pk_bf16_f32 v1, v16, s0
	ds_write_b16 v123, v1 offset:58752
	v_cvt_pk_bf16_f32 v1, v17, s0
	ds_write_b16 v123, v1 offset:58896
	v_cvt_pk_bf16_f32 v1, v18, s0
	ds_write_b16 v123, v1 offset:59040
	v_cvt_pk_bf16_f32 v1, v19, s0
	ds_write_b16 v123, v1 offset:59184
	s_mov_b64 s[66:67], 0

.LBB0_827:
	s_and_b64 vcc, exec, s[58:59]
	s_waitcnt lgkmcnt(0)
	s_barrier
	s_cbranch_vccnz .LBB0_829
	ds_read_b32 v5, v181 offset:64
	ds_read2_b64 v[10:13], v181 offset0:16 offset1:50
	ds_read_b96 v[2:4], v181 offset:192
	ds_read_b128 v[24:27], v181 offset:256
	s_mov_b32 s64, s65
	s_mov_b32 s66, s65
	s_mov_b32 s67, s65
	s_waitcnt lgkmcnt(1)
	v_mov_b32_e32 v79, v4
	v_mov_b32_e32 v4, v10
	v_fma_f32 v36, v52, v4, v46
	v_fma_f32 v37, v53, v5, v47
	v_mov_b32_e32 v78, v3
	v_mov_b32_e32 v45, v37
	v_fma_f32 v1, v44, v2, v182
	s_waitcnt lgkmcnt(0)
	v_mul_f32_e64 v2, v44, v24
	v_mul_f32_e64 v3, v45, v25
	v_fma_f32 v11, v37, v11, v36
	v_add_f32_e32 v2, v183, v2
	v_add_f32_e32 v208, v2, v3
	ds_read_b96 v[2:4], v181 offset:320
	ds_read2_b32 v[60:61], v181 offset0:83 offset1:84
	ds_read_b128 v[28:31], v181 offset:384
	v_mov_b32_e32 v10, v37
	v_mul_f32_e64 v78, v10, v78
	v_mul_f32_e64 v79, v11, v79
	s_waitcnt lgkmcnt(2)
	v_mov_b32_e32 v82, v3
	v_fma_f32 v215, v44, v2, v184
	s_waitcnt lgkmcnt(0)
	v_mul_f32_e64 v2, v44, v28
	v_mul_f32_e64 v3, v45, v29
	v_mov_b32_e32 v83, v4
	v_add_f32_e32 v2, v185, v2
	v_add_f32_e32 v223, v2, v3
	ds_read_b96 v[2:4], v181 offset:448
	ds_read2_b32 v[64:65], v181 offset0:115 offset1:116
	ds_read2_b32 v[62:63], v181 offset0:117 offset1:118
	ds_read_b128 v[32:35], v181 offset:512
	v_mul_f32_e64 v82, v10, v82
	v_mul_f32_e64 v83, v11, v83
	v_add_f32_e32 v1, v1, v78
	v_add_f32_e32 v36, v215, v82
	s_waitcnt lgkmcnt(3)
	v_mov_b32_e32 v28, v3
	v_fma_f32 v237, v44, v2, v186
	s_waitcnt lgkmcnt(0)
	v_mul_f32_e64 v2, v44, v32
	v_mul_f32_e64 v3, v45, v33
	v_mov_b32_e32 v29, v4
	v_add_f32_e32 v2, v187, v2
	v_add_f32_e32 v243, v2, v3
	ds_read_b96 v[2:4], v181 offset:576
	ds_read2_b32 v[70:71], v181 offset0:147 offset1:148
	ds_read_b128 v[14:17], v181 offset:528
	ds_read2_b32 v[68:69], v181 offset0:149 offset1:150
	ds_read2_b32 v[56:57], v181 offset0:151 offset1:152
	ds_read_b128 v[224:227], v181 offset:640
	v_mul_f32_e64 v28, v10, v28
	v_mul_f32_e64 v29, v11, v29
	v_add_f32_e32 v36, v36, v83
	v_add_f32_e32 v28, v237, v28
	s_waitcnt lgkmcnt(5)
	v_mov_b32_e32 v84, v3
	v_fma_f32 v244, v44, v2, v188
	s_waitcnt lgkmcnt(0)
	v_mul_f32_e64 v2, v44, v224
	v_mul_f32_e64 v3, v45, v225
	v_mov_b32_e32 v85, v4
	v_add_f32_e32 v2, v189, v2
	v_add_f32_e32 v245, v2, v3
	ds_read_b96 v[2:4], v181 offset:704
	s_waitcnt lgkmcnt(0)
	v_mov_b32_e32 v224, v3
	v_mov_b32_e32 v225, v4
	v_fma_f32 v246, v44, v2, v190
	ds_read2_b32 v[74:75], v181 offset0:179 offset1:180
	ds_read_b128 v[18:21], v181 offset:656
	ds_read2_b32 v[72:73], v181 offset0:181 offset1:182
	ds_read2_b32 v[58:59], v181 offset0:183 offset1:184
	ds_read2_b64 v[2:5], v181 offset0:84 offset1:118
	ds_read2_b32 v[38:39], v181 offset0:185 offset1:186
	ds_read_b128 v[228:231], v181 offset:768
	s_waitcnt lgkmcnt(0)
	v_mul_f32_e64 v6, v44, v228
	v_mul_f32_e64 v7, v45, v229
	s_nop 0
	v_add_f32_e32 v6, v191, v6
	v_add_f32_e32 v45, v6, v7
	ds_read_b96 v[6:8], v181 offset:832
	s_waitcnt lgkmcnt(0)
	v_mov_b32_e32 v228, v7
	v_mov_b32_e32 v229, v8
	v_fma_f32 v247, v44, v6, v192
	ds_read2_b32 v[80:81], v181 offset0:211 offset1:212
	ds_read_b128 v[22:25], v181 offset:784
	ds_read2_b32 v[76:77], v181 offset0:213 offset1:214
	ds_read2_b32 v[66:67], v181 offset0:215 offset1:216
	ds_read_b128 v[6:9], v181 offset:800
	ds_read2_b32 v[54:55], v181 offset0:217 offset1:218
	ds_read2_b32 v[32:33], v181 offset0:219 offset1:220
	ds_read_b128 v[232:235], v181 offset:896
	ds_read_b96 v[212:214], v181 offset:960
	s_waitcnt lgkmcnt(1)
	v_fma_f32 v232, v44, v232, v193
	s_waitcnt lgkmcnt(0)
	v_fma_f32 v212, v44, v212, v194
	v_fmac_f32_e32 v212, v37, v213
	v_add_f32_e32 v213, v28, v29
	v_mul_f32_e64 v28, v10, v84
	v_mul_f32_e64 v29, v11, v85
	v_fmac_f32_e32 v232, v37, v233
	v_add_f32_e32 v28, v244, v28
	v_add_f32_e32 v215, v28, v29
	v_mul_f32_e64 v28, v10, v224
	v_mul_f32_e64 v29, v11, v225
	v_fmac_f32_e32 v212, v11, v214
	v_add_f32_e32 v28, v246, v28
	v_add_f32_e32 v224, v28, v29
	v_mul_f32_e64 v28, v10, v228
	v_mul_f32_e64 v29, v11, v229
	s_nop 0
	v_add_f32_e32 v10, v247, v28
	v_add_f32_e32 v10, v10, v29
	v_add_f32_e32 v29, v1, v79
	v_mov_b32_e32 v28, v11
	v_mul_f32_e64 v26, v28, v26
	v_mul_f32_e64 v27, v29, v27
	v_mul_f32_e64 v30, v28, v30
	v_mul_f32_e64 v31, v29, v31
	v_add_f32_e32 v26, v208, v26
	v_add_f32_e32 v30, v223, v30
	v_add_f32_e32 v27, v26, v27
	v_mov_b32_e32 v26, v29
	v_mul_f32_e64 v78, v28, v234
	v_mul_f32_e64 v79, v29, v235
	v_mul_f32_e64 v82, v28, v230
	v_mul_f32_e64 v83, v29, v231
	v_mul_f32_e64 v84, v28, v226
	v_mul_f32_e64 v85, v29, v227
	v_mul_f32_e64 v34, v28, v34
	v_mul_f32_e64 v35, v29, v35
	v_add_f32_e32 v28, v30, v31
	v_mul_f32_e64 v30, v26, v60
	v_mul_f32_e64 v31, v27, v61
	v_mul_f32_e64 v60, v26, v64
	v_mul_f32_e64 v61, v27, v65
	v_add_f32_e32 v30, v36, v30
	v_add_f32_e32 v36, v213, v60
	v_add_f32_e32 v1, v232, v78
	v_add_f32_e32 v45, v45, v82
	v_add_f32_e32 v78, v245, v84
	v_add_f32_e32 v34, v243, v34
	v_add_f32_e32 v36, v36, v61
	v_mul_f32_e64 v60, v26, v70
	v_mul_f32_e64 v61, v27, v71
	v_add_f32_e32 v208, v34, v35
	v_add_f32_e32 v78, v78, v85
	v_add_f32_e32 v45, v45, v83
	ds_read2_b32 v[34:35], v181 offset0:243 offset1:244
	ds_read_b128 v[82:85], v181 offset:912
	v_add_f32_e32 v60, v215, v60
	v_add_f32_e32 v64, v60, v61
	v_mul_f32_e64 v60, v26, v74
	v_mul_f32_e64 v61, v27, v75
	v_add_f32_e32 v31, v30, v31
	v_mov_b32_e32 v30, v27
	v_add_f32_e32 v60, v224, v60
	v_mul_f32_e64 v12, v30, v12
	v_mul_f32_e64 v13, v31, v13
	v_add_f32_e32 v65, v60, v61
	v_mul_f32_e64 v60, v26, v80
	v_mul_f32_e64 v61, v27, v81
	v_mul_f32_e64 v22, v30, v22
	v_mul_f32_e64 v23, v31, v23
	v_mul_f32_e64 v18, v30, v18
	v_mul_f32_e64 v19, v31, v19
	v_add_f32_e32 v12, v28, v12
	v_add_f32_e32 v10, v10, v60
	s_waitcnt lgkmcnt(1)
	v_mul_f32_e64 v34, v26, v34
	v_mul_f32_e64 v35, v27, v35
	v_add_f32_e32 v22, v45, v22
	v_add_f32_e32 v18, v78, v18
	v_add_f32_e32 v13, v12, v13
	v_mov_b32_e32 v12, v31
	v_add_f32_e32 v10, v10, v61
	s_waitcnt lgkmcnt(0)
	v_mul_f32_e64 v60, v30, v82
	v_mul_f32_e64 v61, v31, v83
	v_add_f32_e32 v26, v212, v34
	v_mul_f32_e64 v14, v30, v14
	v_mul_f32_e64 v15, v31, v15
	v_add_f32_e32 v30, v18, v19
	v_add_f32_e32 v34, v22, v23
	ds_read2_b32 v[18:19], v181 offset0:245 offset1:246
	v_mul_f32_e64 v22, v12, v68
	v_mul_f32_e64 v23, v13, v69
	v_add_f32_e32 v26, v26, v35
	v_add_f32_e32 v22, v64, v22
	v_add_f32_e32 v14, v208, v14
	v_add_f32_e32 v35, v22, v23
	v_mul_f32_e64 v22, v12, v72
	v_mul_f32_e64 v23, v13, v73
	v_add_f32_e32 v28, v14, v15
	v_mul_f32_e64 v14, v12, v62
	v_mul_f32_e64 v15, v13, v63
	v_add_f32_e32 v22, v65, v22
	v_add_f32_e32 v1, v1, v79
	v_add_f32_e32 v14, v36, v14
	v_add_f32_e32 v36, v22, v23
	v_mul_f32_e64 v22, v12, v76
	v_mul_f32_e64 v23, v13, v77
	v_add_f32_e32 v1, v1, v60
	v_add_f32_e32 v10, v10, v22
	v_add_f32_e32 v15, v14, v15
	v_mov_b32_e32 v14, v13
	s_waitcnt lgkmcnt(0)
	v_mul_f32_e64 v18, v12, v18
	v_mul_f32_e64 v19, v13, v19
	v_add_f32_e32 v1, v1, v61
	v_add_f32_e32 v10, v10, v23
	v_mul_f32_e64 v22, v14, v84
	v_mul_f32_e64 v23, v15, v85
	v_add_f32_e32 v12, v26, v18
	v_mul_f32_e64 v20, v14, v20
	v_mul_f32_e64 v21, v15, v21
	v_mul_f32_e64 v16, v14, v16
	v_mul_f32_e64 v17, v15, v17
	v_add_f32_e32 v1, v1, v22
	v_add_f32_e32 v12, v12, v19
	v_mul_f32_e64 v18, v14, v24
	v_mul_f32_e64 v19, v15, v25
	v_add_f32_e32 v20, v30, v20
	v_add_f32_e32 v14, v28, v16
	v_add_f32_e32 v18, v34, v18
	v_add_f32_e32 v26, v20, v21
	v_add_f32_e32 v1, v1, v23
	ds_read2_b32 v[24:25], v181 offset0:247 offset1:248
	ds_read_b128 v[20:23], v181 offset:928
	v_add_f32_e32 v17, v14, v17
	v_mov_b32_e32 v16, v15
	v_add_f32_e32 v28, v18, v19
	v_mul_f32_e64 v18, v16, v56
	v_mul_f32_e64 v19, v17, v57
	s_waitcnt lgkmcnt(1)
	v_mul_f32_e64 v24, v16, v24
	v_mul_f32_e64 v25, v17, v25
	v_add_f32_e32 v14, v35, v18
	v_mul_f32_e64 v34, v16, v58
	v_mul_f32_e64 v35, v17, v59
	v_add_f32_e32 v19, v14, v19
	v_add_f32_e32 v18, v36, v34
	v_add_f32_e32 v30, v18, v35
	v_mov_b32_e32 v18, v17
	s_waitcnt lgkmcnt(0)
	v_mul_f32_e64 v20, v18, v20
	v_mul_f32_e64 v21, v19, v21
	v_mul_f32_e64 v2, v18, v2
	v_mul_f32_e64 v3, v19, v3
	v_add_f32_e32 v1, v1, v20
	v_add_f32_e32 v1, v1, v21
	ds_read2_b32 v[20:21], v181 offset0:249 offset1:250
	v_add_f32_e32 v2, v26, v2
	v_add_f32_e32 v12, v12, v24
	v_mul_f32_e64 v6, v18, v6
	v_mul_f32_e64 v7, v19, v7
	v_add_f32_e32 v3, v2, v3
	v_mov_b32_e32 v2, v19
	v_add_f32_e32 v12, v12, v25
	v_add_f32_e32 v6, v28, v6
	s_waitcnt lgkmcnt(0)
	v_mul_f32_e64 v20, v2, v20
	v_mul_f32_e64 v21, v3, v21
	v_add_f32_e32 v14, v6, v7
	v_mul_f32_e64 v6, v2, v38
	v_mul_f32_e64 v7, v3, v39
	v_mul_f32_e64 v24, v2, v54
	v_mul_f32_e64 v25, v3, v55
	v_add_f32_e32 v2, v12, v20
	v_add_f32_e32 v6, v30, v6
	v_add_f32_e32 v2, v2, v21
	ds_read2_b32 v[20:21], v181 offset0:251 offset1:252
	v_add_f32_e32 v7, v6, v7
	v_mov_b32_e32 v6, v3
	v_mul_f32_e64 v34, v16, v66
	v_mul_f32_e64 v35, v17, v67
	v_mul_f32_e64 v8, v6, v8
	v_mul_f32_e64 v9, v7, v9
	v_add_f32_e32 v10, v10, v34
	v_mul_f32_e64 v22, v6, v22
	v_mul_f32_e64 v23, v7, v23
	v_add_f32_e32 v6, v14, v8
	v_add_f32_e32 v10, v10, v35
	v_add_f32_e32 v9, v6, v9
	v_mov_b32_e32 v8, v7
	v_add_f32_e32 v10, v10, v24
	v_add_f32_e32 v1, v1, v22
	s_waitcnt lgkmcnt(0)
	v_mul_f32_e64 v20, v8, v20
	v_mul_f32_e64 v21, v9, v21
	v_add_f32_e32 v10, v10, v25
	v_add_f32_e32 v1, v1, v23
	v_mul_f32_e64 v22, v8, v32
	v_mul_f32_e64 v23, v9, v33
	v_add_f32_e32 v2, v2, v20
	v_add_f32_e32 v6, v10, v22
	v_add_f32_e32 v2, v2, v21
	ds_read2_b32 v[20:21], v181 offset0:253 offset1:254
	v_add_f32_e32 v25, v6, v23
	v_mov_b32_e32 v24, v9
	v_mul_f32_e64 v4, v24, v4
	v_mul_f32_e64 v5, v25, v5
	s_nop 0
	v_add_f32_e32 v1, v1, v4
	v_add_f32_e32 v5, v1, v5
	v_mov_b32_e32 v4, v25
	s_waitcnt lgkmcnt(0)
	v_mul_f32_e64 v20, v4, v20
	v_mul_f32_e64 v21, v5, v21
	s_nop 0
	v_add_f32_e32 v1, v2, v20
	v_add_f32_e32 v1, v1, v21
	v_mov_b64_e32 v[20:21], s[64:65]
	v_mov_b64_e32 v[22:23], s[66:67]
	ds_write_b128 v113, v[20:23] offset:64512
	ds_write_b128 v126, v[20:23]
	ds_write_b128 v113, v[20:23] offset:64528
	ds_write_b128 v126, v[20:23] offset:16
	ds_write_b128 v113, v[20:23] offset:64544
	ds_write_b128 v126, v[20:23] offset:32
	ds_write_b128 v113, v[20:23] offset:64560
	ds_write_b128 v126, v[20:23] offset:48
	ds_write_b128 v113, v[20:23] offset:64576
	ds_write_b128 v126, v[20:23] offset:64
	ds_write_b128 v113, v[20:23] offset:64592
	ds_write_b128 v126, v[20:23] offset:80
	ds_write_b128 v113, v[20:23] offset:64608
	ds_write_b128 v126, v[20:23] offset:96
	ds_write_b128 v113, v[20:23] offset:64624
	ds_write_b128 v126, v[20:23] offset:112
	v_cvt_pk_bf16_f32 v20, v44, v37
	v_cvt_pk_bf16_f32 v21, v11, v29
	v_cvt_pk_bf16_f32 v22, v27, v31
	v_cvt_pk_bf16_f32 v23, v13, v15
	s_waitcnt lgkmcnt(0)
	ds_write_b128 v127, v[20:23] offset:64512
	v_cvt_pk_bf16_f32 v20, v17, v19
	v_cvt_pk_bf16_f32 v21, v3, v7
	v_cvt_pk_bf16_f32 v22, v9, v25
	v_cvt_pk_bf16_f32 v23, v5, v1
	v_cvt_pk_bf16_f32 v2, v37, s0
	ds_write_b128 v127, v[20:23] offset:64528
	ds_write_b16 v196, v195
	ds_write_b16 v196, v2 offset:144
	v_cvt_pk_bf16_f32 v2, v11, s0
	ds_write_b16 v196, v2 offset:288
	v_cvt_pk_bf16_f32 v2, v29, s0
	ds_write_b16 v196, v2 offset:432
	v_cvt_pk_bf16_f32 v2, v27, s0
	ds_write_b16 v196, v2 offset:576
	v_cvt_pk_bf16_f32 v2, v31, s0
	ds_write_b16 v196, v2 offset:720
	v_cvt_pk_bf16_f32 v2, v13, s0
	ds_write_b16 v196, v2 offset:864
	v_cvt_pk_bf16_f32 v2, v15, s0
	ds_write_b16 v196, v2 offset:1008
	v_cvt_pk_bf16_f32 v2, v17, s0
	ds_write_b16 v196, v2 offset:1152
	v_cvt_pk_bf16_f32 v2, v19, s0
	ds_write_b16 v196, v2 offset:1296
	v_cvt_pk_bf16_f32 v2, v3, s0
	ds_write_b16 v196, v2 offset:1440
	v_cvt_pk_bf16_f32 v2, v7, s0
	ds_write_b16 v196, v2 offset:1584
	v_cvt_pk_bf16_f32 v2, v9, s0
	ds_write_b16 v196, v2 offset:1728
	v_cvt_pk_bf16_f32 v2, v25, s0
	ds_write_b16 v196, v2 offset:1872
	v_cvt_pk_bf16_f32 v2, v5, s0
	v_cvt_pk_bf16_f32 v1, v1, s0
	ds_write_b16 v196, v2 offset:2016
	ds_write_b16 v197, v1

.LBB0_833:
	s_and_b64 vcc, exec, s[58:59]
	s_waitcnt lgkmcnt(0)
	s_barrier
	s_cbranch_vccnz .LBB0_835
	ds_read_b128 v[34:37], v131
	ds_read_b128 v[54:57], v132
	s_waitcnt lgkmcnt(0)
	s_nop 0
	v_mfma_f32_32x32x16_bf16 v[18:33], v[34:37], v[54:57], 0
	ds_read_b128 v[34:37], v131 offset:32
	ds_read_b128 v[54:57], v132 offset:32
	s_waitcnt lgkmcnt(0)
	v_mfma_f32_32x32x16_bf16 v[18:33], v[34:37], v[54:57], v[18:33]
	ds_read_b128 v[34:37], v131 offset:64
	ds_read_b128 v[54:57], v132 offset:64
	s_waitcnt lgkmcnt(0)
	v_mfma_f32_32x32x16_bf16 v[18:33], v[34:37], v[54:57], v[18:33]
	ds_read_b128 v[34:37], v131 offset:96
	ds_read_b128 v[54:57], v132 offset:96
	s_waitcnt lgkmcnt(0)
	v_mfma_f32_32x32x16_bf16 v[18:33], v[34:37], v[54:57], v[18:33]
	s_nop 11
	v_cvt_pk_bf16_f32 v34, v18, v19
	v_cvt_pk_bf16_f32 v35, v20, v21
	v_cvt_pk_bf16_f32 v36, v22, v23
	v_cvt_pk_bf16_f32 v37, v24, v25
	v_add_f32_e64 v16, v16, v32
	v_add_f32_e64 v17, v17, v33
	v_add_f32_e64 v14, v14, v30
	v_add_f32_e64 v15, v15, v31
	v_add_f32_e64 v12, v12, v28
	v_add_f32_e64 v13, v13, v29
	v_add_f32_e64 v10, v10, v26
	v_add_f32_e64 v11, v11, v27
	v_add_f32_e64 v8, v8, v24
	v_add_f32_e64 v9, v9, v25
	v_add_f32_e64 v6, v6, v22
	v_add_f32_e64 v7, v7, v23
	v_add_f32_e64 v4, v4, v20
	v_add_f32_e64 v5, v5, v21
	v_add_f32_e64 v2, v2, v18
	v_add_f32_e64 v3, v3, v19
	v_cvt_pk_bf16_f32 v38, v26, v27
	v_cvt_pk_bf16_f32 v39, v28, v29
	v_cvt_pk_bf16_f32 v54, v30, v31
	v_cvt_pk_bf16_f32 v55, v32, v33
	ds_write2_b64 v124, v[34:35], v[36:37] offset1:2
	ds_write2_b64 v124, v[38:39], v[54:55] offset0:4 offset1:6

.LBB0_839:
	v_add3_u32 v1, s58, v117, v118
	s_waitcnt lgkmcnt(0)
	s_barrier
	ds_read_b128 v[18:21], v1
	ds_read_b128 v[22:25], v136
	s_ashr_i32 s85, s84, 31
	s_lshl_b64 s[58:59], s[84:85], 15
	s_waitcnt lgkmcnt(0)
	v_mfma_f32_32x32x16_bf16 v[2:17], v[18:21], v[22:25], 0
	ds_read_b128 v[18:21], v1 offset:32
	ds_read_b128 v[22:25], v136 offset:32
	v_readlane_b32 s83, v253, 56
	s_add_u32 s58, s83, s58
	v_readlane_b32 s83, v253, 57
	s_addc_u32 s59, s83, s59
	v_readlane_b32 s83, v254, 4
	s_add_i32 s82, s82, s83
	s_waitcnt lgkmcnt(0)
	v_mfma_f32_32x32x16_bf16 v[2:17], v[18:21], v[22:25], v[2:17]
	ds_read_b128 v[18:21], v1 offset:64
	ds_read_b128 v[22:25], v136 offset:64
	ds_read_b128 v[26:29], v1 offset:96
	v_add3_u32 v1, s82, v109, v122
	s_mov_b64 s[82:83], -1
	s_and_b64 vcc, exec, s[36:37]
	s_waitcnt lgkmcnt(1)
	v_mfma_f32_32x32x16_bf16 v[2:17], v[18:21], v[22:25], v[2:17]
	ds_read_b128 v[18:21], v136 offset:96
	s_waitcnt lgkmcnt(0)
	v_mfma_f32_32x32x16_bf16 v[2:17], v[26:29], v[18:21], v[2:17]
	s_nop 11
	v_cvt_pk_bf16_f32 v2, v2, s0
	v_cvt_pk_bf16_f32 v3, v3, s0
	v_cvt_pk_bf16_f32 v4, v4, s0
	ds_write_b16 v1, v2
	ds_write_b16 v1, v3 offset:144
	ds_write_b16 v1, v4 offset:288
	v_cvt_pk_bf16_f32 v2, v5, s0
	ds_write_b16 v1, v2 offset:432
	v_cvt_pk_bf16_f32 v2, v6, s0
	ds_write_b16 v1, v2 offset:1152
	v_cvt_pk_bf16_f32 v2, v7, s0
	ds_write_b16 v1, v2 offset:1296
	v_cvt_pk_bf16_f32 v2, v8, s0
	ds_write_b16 v1, v2 offset:1440
	v_cvt_pk_bf16_f32 v2, v9, s0
	ds_write_b16 v1, v2 offset:1584
	v_cvt_pk_bf16_f32 v2, v10, s0
	ds_write_b16 v1, v2 offset:2304
	v_cvt_pk_bf16_f32 v2, v11, s0
	ds_write_b16 v1, v2 offset:2448
	v_cvt_pk_bf16_f32 v2, v12, s0
	ds_write_b16 v1, v2 offset:2592
	v_cvt_pk_bf16_f32 v2, v13, s0
	ds_write_b16 v1, v2 offset:2736
	v_cvt_pk_bf16_f32 v2, v14, s0
	ds_write_b16 v1, v2 offset:3456
	v_cvt_pk_bf16_f32 v2, v15, s0
	ds_write_b16 v1, v2 offset:3600
	v_cvt_pk_bf16_f32 v2, v16, s0
	ds_write_b16 v1, v2 offset:3744
	v_cvt_pk_bf16_f32 v2, v17, s0
	ds_write_b16 v1, v2 offset:3888
	s_waitcnt lgkmcnt(0)
	s_barrier
	s_cbranch_vccz .LBB0_841
	ds_read_b128 v[32:35], v137
	ds_read_b128 v[36:39], v137 offset:32
	ds_read_b128 v[54:57], v121 offset:46080
	ds_read_b128 v[58:61], v121 offset:46112
	ds_read_b128 v[62:65], v137 offset:64
	ds_read_b128 v[66:69], v137 offset:96
	ds_read_b128 v[70:73], v121 offset:46144
	ds_read_b128 v[74:77], v121 offset:46176
	ds_read_b128 v[2:5], v137
	ds_read_b128 v[6:9], v121 offset:18432
	ds_read_b128 v[10:13], v137 offset:32
	ds_read_b128 v[78:81], v121 offset:18464
	s_waitcnt lgkmcnt(2)
	v_mfma_f32_32x32x16_bf16 v[16:31], v[2:5], v[6:9], 0
	ds_read_b128 v[6:9], v137 offset:64
	v_mov_b32_e32 v1, v221
	v_mov_b32_e32 v2, v219
	v_mov_b32_e32 v3, v220
	v_mov_b32_e32 v4, v217
	v_mov_b32_e32 v5, v218
	v_mov_b32_e32 v14, v200
	s_waitcnt lgkmcnt(1)
	v_mfma_f32_32x32x16_bf16 v[16:31], v[10:13], v[78:81], v[16:31]
	ds_read_b128 v[10:13], v121 offset:18496
	v_mov_b32_e32 v15, v222
	ds_read_b128 v[78:81], v137 offset:96
	ds_read_b128 v[82:85], v121 offset:18528
	v_add_u32_e32 v45, 0x6800, v199
	s_mov_b64 s[82:83], 0
	s_waitcnt lgkmcnt(2)
	v_mfma_f32_32x32x16_bf16 v[16:31], v[6:9], v[10:13], v[16:31]
	v_mov_b32_e32 v6, v207
	v_mov_b32_e32 v7, v216
	v_mov_b32_e32 v8, v203
	v_mov_b32_e32 v9, v205
	v_mov_b32_e32 v10, v204
	v_mov_b32_e32 v11, v206
	v_mov_b32_e32 v12, v202
	v_mov_b32_e32 v13, v201
	s_waitcnt lgkmcnt(0)
	v_mfma_f32_32x32x16_bf16 v[16:31], v[78:81], v[82:85], v[16:31]
	ds_read2_b64 v[78:81], v45 offset0:128 offset1:130
	ds_read2_b64 v[82:85], v45 offset0:132 offset1:134
	s_waitcnt lgkmcnt(1)
	v_lshlrev_b32_e32 v200, 16, v78
	v_and_b32_e32 v201, 0xffff0000, v78
	v_mfma_f32_32x32x16_bf16 v[0:15], v[32:35], v[54:57], v[0:15]
	v_lshlrev_b32_e32 v32, 16, v79
	v_and_b32_e32 v33, 0xffff0000, v79
	s_nop 3
	v_add_f32_e64 v18, v18, v32
	v_add_f32_e64 v19, v19, v33
	v_lshlrev_b32_e32 v32, 16, v80
	v_and_b32_e32 v33, 0xffff0000, v80
	v_add_f32_e64 v20, v20, v32
	v_add_f32_e64 v21, v21, v33
	v_lshlrev_b32_e32 v32, 16, v81
	v_mfma_f32_32x32x16_bf16 v[0:15], v[36:39], v[58:61], v[0:15]
	v_and_b32_e32 v33, 0xffff0000, v81
	v_add_f32_e64 v22, v22, v32
	v_add_f32_e64 v23, v23, v33
	s_waitcnt lgkmcnt(0)
	v_lshlrev_b32_e32 v32, 16, v82
	v_and_b32_e32 v33, 0xffff0000, v82
	v_add_f32_e64 v24, v24, v32
	v_add_f32_e64 v25, v25, v33
	v_lshlrev_b32_e32 v32, 16, v83
	v_and_b32_e32 v33, 0xffff0000, v83
	v_mfma_f32_32x32x16_bf16 v[0:15], v[62:65], v[70:73], v[0:15]
	v_add_f32_e64 v26, v26, v32
	v_add_f32_e64 v27, v27, v33
	v_lshlrev_b32_e32 v32, 16, v84
	v_and_b32_e32 v33, 0xffff0000, v84
	v_add_f32_e64 v16, v16, v200
	v_add_f32_e64 v17, v17, v201
	v_add_f32_e64 v28, v28, v32
	v_add_f32_e64 v29, v29, v33
	v_lshlrev_b32_e32 v32, 16, v85
	v_and_b32_e32 v33, 0xffff0000, v85
	v_mfma_f32_32x32x16_bf16 v[0:15], v[66:69], v[74:77], v[0:15]
	v_add_f32_e64 v30, v30, v32
	v_add_f32_e64 v31, v31, v33
	s_nop 9
	v_cvt_pk_bf16_f32 v0, v0, v1
	v_cvt_pk_bf16_f32 v1, v2, v3
	v_cvt_pk_bf16_f32 v2, v4, v5
	v_cvt_pk_bf16_f32 v3, v6, v7
	ds_write2_b64 v135, v[0:1], v[2:3] offset1:2
	v_cvt_pk_bf16_f32 v0, v8, v9
	v_cvt_pk_bf16_f32 v1, v10, v11
	v_cvt_pk_bf16_f32 v2, v12, v13
	v_cvt_pk_bf16_f32 v3, v14, v15
	ds_write2_b64 v135, v[0:1], v[2:3] offset0:4 offset1:6
	v_cvt_pk_bf16_f32 v0, v16, v17
	v_cvt_pk_bf16_f32 v1, v18, v19
	v_cvt_pk_bf16_f32 v2, v20, v21
	v_cvt_pk_bf16_f32 v3, v22, v23
	ds_write2_b64 v124, v[0:1], v[2:3] offset1:2
	v_cvt_pk_bf16_f32 v0, v24, v25
	v_cvt_pk_bf16_f32 v1, v26, v27
	v_cvt_pk_bf16_f32 v2, v28, v29
	v_cvt_pk_bf16_f32 v3, v30, v31
	ds_write2_b64 v124, v[0:1], v[2:3] offset0:4 offset1:6

.LBB0_950:
	s_waitcnt vmcnt(0)
	v_readfirstlane_b32 s38, v241
	v_mov_b32_e32 v48, v173
	s_nop 1
	v_permlane32_swap_b32_e32 v173, v48
	v_add_f32_e32 v48, v173, v48
	v_div_scale_f32 v49, s[14:15], v48, v48, 1.0
	v_rcp_f32_e32 v50, v49
	s_lshl_b32 s64, s23, 7
	v_lshlrev_b32_e32 v208, 2, v188
	s_mov_b64 s[14:15], 0x23c00200
	v_fma_f32 v51, -v49, v50, 1.0
	v_fmac_f32_e32 v50, v51, v50
	v_div_scale_f32 v51, vcc, 1.0, v48, 1.0
	v_mul_f32_e32 v52, v51, v50
	v_fma_f32 v53, -v49, v52, v51
	v_fmac_f32_e32 v52, v53, v50
	v_fma_f32 v49, -v49, v52, v51
	v_div_fmas_f32 v49, v49, v50, v52
	v_lshlrev_b64 v[50:51], 11, v[200:201]
	v_lshl_add_u64 v[50:51], s[8:9], 0, v[50:51]
	v_lshl_add_u64 v[50:51], v[50:51], 0, s[64:65]
	v_div_fixup_f32 v48, v49, v48, 1.0
	v_lshl_add_u64 v[50:51], v[50:51], 0, v[208:209]
	v_lshl_add_u64 v[52:53], v[50:51], 0, s[14:15]
	v_mul_f32_e64 v32, v32, v48
	v_mul_f32_e64 v33, v33, v48
	v_mul_f32_e64 v34, v34, v48
	v_mul_f32_e64 v35, v35, v48
	v_mul_f32_e64 v36, v36, v48
	v_mul_f32_e64 v37, v37, v48
	v_mul_f32_e64 v38, v38, v48
	v_mul_f32_e64 v39, v39, v48
	v_cvt_pk_bf16_f32 v32, v32, v33
	v_cvt_pk_bf16_f32 v33, v34, v35
	v_cvt_pk_bf16_f32 v34, v36, v37
	v_cvt_pk_bf16_f32 v35, v38, v39
	v_mul_f32_e64 v16, v16, v48
	v_mul_f32_e64 v17, v17, v48
	v_mul_f32_e64 v18, v18, v48
	v_mul_f32_e64 v19, v19, v48
	v_mul_f32_e64 v20, v20, v48
	v_mul_f32_e64 v21, v21, v48
	v_mul_f32_e64 v22, v22, v48
	v_mul_f32_e64 v23, v23, v48
	v_cvt_pk_bf16_f32 v16, v16, v17
	v_cvt_pk_bf16_f32 v17, v18, v19
	v_cvt_pk_bf16_f32 v18, v20, v21
	v_cvt_pk_bf16_f32 v19, v22, v23
	v_permlane32_swap_b32_e32 v32, v34
	v_permlane32_swap_b32_e32 v33, v35
	global_store_dwordx4 v[52:53], v[32:35], off
	v_mul_f32_e64 v40, v40, v48
	v_mul_f32_e64 v41, v41, v48
	v_mul_f32_e64 v42, v42, v48
	v_mul_f32_e64 v43, v43, v48
	v_mul_f32_e64 v44, v44, v48
	v_mul_f32_e64 v45, v45, v48
	v_mul_f32_e64 v46, v46, v48
	v_mul_f32_e64 v47, v47, v48
	v_cvt_pk_bf16_f32 v40, v40, v41
	v_cvt_pk_bf16_f32 v41, v42, v43
	v_cvt_pk_bf16_f32 v42, v44, v45
	v_cvt_pk_bf16_f32 v43, v46, v47
	v_permlane32_swap_b32_e32 v16, v18
	v_permlane32_swap_b32_e32 v17, v19
	global_store_dwordx4 v[52:53], v[16:19], off offset:64
	v_mul_f32_e64 v24, v24, v48
	v_mul_f32_e64 v25, v25, v48
	v_mul_f32_e64 v26, v26, v48
	v_mul_f32_e64 v27, v27, v48
	v_mul_f32_e64 v28, v28, v48
	v_mul_f32_e64 v29, v29, v48
	v_mul_f32_e64 v30, v30, v48
	v_mul_f32_e64 v31, v31, v48
	v_cvt_pk_bf16_f32 v24, v24, v25
	v_cvt_pk_bf16_f32 v25, v26, v27
	v_cvt_pk_bf16_f32 v26, v28, v29
	v_cvt_pk_bf16_f32 v27, v30, v31
	v_permlane32_swap_b32_e32 v40, v42
	v_permlane32_swap_b32_e32 v41, v43
	global_store_dwordx4 v[52:53], v[40:43], off offset:32
	s_mov_b64 s[14:15], 0
	s_nop 1
	v_permlane32_swap_b32_e32 v24, v26
	v_permlane32_swap_b32_e32 v25, v27
	global_store_dwordx4 v[52:53], v[24:27], off offset:96

.LBB0_961:
	s_or_b64 exec, exec, s[18:19]
	s_ashr_i32 s18, s24, 5
	s_sub_i32 s25, 15, s18
	s_and_b32 s23, s24, 7
	s_lshl_b32 s24, s25, 8
	s_add_i32 s24, s24, s22
	s_lshl_b32 s18, s26, 9
	s_and_b32 s18, s18, 0x3000
	s_ashr_i32 s19, s24, 31
	s_add_u32 s18, s24, s18
	v_or_b32_e32 v200, s18, v160
	v_mov_b64_e32 v[16:17], s[12:13]
	s_addc_u32 s26, s19, 0
	v_mad_u64_u32 v[16:17], s[18:19], v200, s54, v[16:17]
	v_mov_b32_e32 v18, 0x600
	v_mad_i32_i24 v17, s26, v18, v17
	s_mul_i32 s18, s23, 0xc0
	s_mov_b32 s19, s65
	v_lshl_add_u64 v[16:17], v[16:17], 0, s[18:19]
	v_lshlrev_b32_e32 v208, 1, v180
	v_lshl_add_u64 v[16:17], v[16:17], 0, v[208:209]
	global_load_dwordx4 v[120:123], v[16:17], off offset:128
	global_load_dwordx4 v[124:127], v[16:17], off offset:160
	global_load_dwordx4 v[130:133], v[16:17], off offset:96
	global_load_dwordx4 v[138:141], v[16:17], off offset:64
	global_load_dwordx4 v[146:149], v[16:17], off offset:32
	global_load_dwordx4 v[154:157], v[16:17], off
	s_load_dwordx2 s[18:19], s[6:7], 0x90
	v_lshlrev_b32_e32 v16, 2, v180
	v_mov_b32_e32 v17, v209
	global_load_dwordx4 v[100:103], v[198:199], off offset:128
	v_mov_b32_e32 v201, s26
	s_waitcnt lgkmcnt(0)
	v_lshl_add_u64 v[18:19], v[162:163], 2, s[18:19]
	v_lshl_add_u64 v[24:25], v[18:19], 0, v[16:17]
	global_load_dwordx4 v[76:79], v[24:25], off offset:16
	global_load_dwordx4 v[88:91], v[24:25], off
	global_load_dwordx4 v[68:71], v[24:25], off offset:80
	global_load_dwordx4 v[72:75], v[24:25], off offset:64
	global_load_dwordx4 v[60:63], v[24:25], off offset:144
	global_load_dwordx4 v[64:67], v[24:25], off offset:128
	global_load_dwordx4 v[52:55], v[24:25], off offset:208
	global_load_dwordx4 v[56:59], v[24:25], off offset:192
	global_load_dwordx4 v[16:19], v[24:25], off offset:272
	global_load_dwordx4 v[36:39], v[24:25], off offset:256
	global_load_dwordx4 v[20:23], v[24:25], off offset:336
	global_load_dwordx4 v[32:35], v[24:25], off offset:320
	v_lshlrev_b64 v[24:25], 6, v[200:201]
	v_lshl_add_u64 v[28:29], v[182:183], 0, v[24:25]
	v_lshl_add_u64 v[44:45], v[184:185], 0, v[24:25]
	global_load_dwordx4 v[24:27], v[28:29], off offset:16
	global_load_dwordx4 v[40:43], v[28:29], off
	s_nop 0
	global_load_dwordx4 v[28:31], v[44:45], off offset:16
	s_nop 0
	global_load_dwordx4 v[44:47], v[44:45], off
	s_waitcnt vmcnt(22)
	v_lshlrev_b32_e32 v108, 16, v123
	v_and_b32_e32 v109, 0xffff0000, v123
	s_waitcnt vmcnt(21)
	v_lshlrev_b32_e32 v110, 16, v127
	v_and_b32_e32 v111, 0xffff0000, v127
	v_lshlrev_b32_e32 v112, 16, v122
	s_waitcnt vmcnt(17)
	v_and_b32_e32 v153, 0xffff0000, v154
	v_lshlrev_b32_e32 v152, 16, v154
	v_mul_f32_e32 v154, v153, v153
	v_lshlrev_b32_e32 v150, 16, v155
	v_and_b32_e32 v151, 0xffff0000, v155
	v_fma_f32 v155, v153, v153, v154
	v_fma_f32 v154, v152, v152, v154
	v_and_b32_e32 v113, 0xffff0000, v122
	v_lshlrev_b32_e32 v114, 16, v126
	v_and_b32_e32 v115, 0xffff0000, v126
	v_lshlrev_b32_e32 v116, 16, v121
	v_and_b32_e32 v117, 0xffff0000, v121
	v_lshlrev_b32_e32 v118, 16, v125
	v_and_b32_e32 v119, 0xffff0000, v125
	v_lshlrev_b32_e32 v106, 16, v120
	v_and_b32_e32 v107, 0xffff0000, v120
	v_lshlrev_b32_e32 v120, 16, v124
	v_and_b32_e32 v121, 0xffff0000, v124
	v_lshlrev_b32_e32 v122, 16, v133
	v_and_b32_e32 v123, 0xffff0000, v133
	v_lshlrev_b32_e32 v124, 16, v132
	v_and_b32_e32 v125, 0xffff0000, v132
	v_lshlrev_b32_e32 v126, 16, v131
	v_and_b32_e32 v127, 0xffff0000, v131
	v_lshlrev_b32_e32 v128, 16, v130
	v_and_b32_e32 v129, 0xffff0000, v130
	v_lshlrev_b32_e32 v130, 16, v141
	v_and_b32_e32 v131, 0xffff0000, v141
	v_lshlrev_b32_e32 v132, 16, v140
	v_and_b32_e32 v133, 0xffff0000, v140
	v_lshlrev_b32_e32 v134, 16, v139
	v_and_b32_e32 v135, 0xffff0000, v139
	v_lshlrev_b32_e32 v136, 16, v138
	v_and_b32_e32 v137, 0xffff0000, v138
	v_lshlrev_b32_e32 v138, 16, v149
	v_and_b32_e32 v139, 0xffff0000, v149
	v_lshlrev_b32_e32 v140, 16, v148
	v_and_b32_e32 v141, 0xffff0000, v148
	v_lshlrev_b32_e32 v148, 16, v156
	v_and_b32_e32 v149, 0xffff0000, v156
	v_fma_f32 v154, v150, v150, v154
	v_fma_f32 v155, v151, v151, v155
	v_mul_f32_e32 v156, v151, v151
	v_add_f32_e64 v154, v156, v154
	v_add_f32_e64 v155, v156, v155
	v_fma_f32 v154, v148, v148, v154
	v_fma_f32 v155, v149, v149, v155
	v_mul_f32_e32 v156, v149, v149
	v_lshlrev_b32_e32 v142, 16, v147
	v_and_b32_e32 v143, 0xffff0000, v147
	v_lshlrev_b32_e32 v144, 16, v146
	v_and_b32_e32 v145, 0xffff0000, v146
	v_lshlrev_b32_e32 v146, 16, v157
	v_and_b32_e32 v147, 0xffff0000, v157
	v_add_f32_e64 v154, v156, v154
	v_add_f32_e64 v155, v156, v155
	v_fma_f32 v154, v146, v146, v154
	v_fma_f32 v155, v147, v147, v155
	v_mul_f32_e32 v156, v147, v147
	v_add_f32_e64 v154, v156, v154
	v_add_f32_e64 v155, v156, v155
	v_fma_f32 v154, v144, v144, v154
	v_fma_f32 v155, v145, v145, v155
	v_mul_f32_e32 v156, v145, v145
	v_add_f32_e64 v154, v156, v154
	v_add_f32_e64 v155, v156, v155
	v_fma_f32 v154, v142, v142, v154
	v_fma_f32 v155, v143, v143, v155
	v_mul_f32_e32 v156, v143, v143
	v_add_f32_e64 v154, v156, v154
	v_add_f32_e64 v155, v156, v155
	v_fma_f32 v154, v140, v140, v154
	v_fma_f32 v155, v141, v141, v155
	v_mul_f32_e32 v156, v141, v141
	v_add_f32_e64 v154, v156, v154
	v_add_f32_e64 v155, v156, v155
	v_fma_f32 v154, v138, v138, v154
	v_fma_f32 v155, v139, v139, v155
	v_mul_f32_e32 v156, v139, v139
	v_add_f32_e64 v154, v156, v154
	v_add_f32_e64 v155, v156, v155
	v_fma_f32 v154, v136, v136, v154
	v_fma_f32 v155, v137, v137, v155
	v_mul_f32_e32 v156, v137, v137
	v_add_f32_e64 v154, v156, v154
	v_add_f32_e64 v155, v156, v155
	v_fma_f32 v154, v134, v134, v154
	v_fma_f32 v155, v135, v135, v155
	v_mul_f32_e32 v156, v135, v135
	v_add_f32_e64 v154, v156, v154
	v_add_f32_e64 v155, v156, v155
	v_fma_f32 v154, v132, v132, v154
	v_fma_f32 v155, v133, v133, v155
	v_mul_f32_e32 v156, v133, v133
	v_add_f32_e64 v154, v156, v154
	v_add_f32_e64 v155, v156, v155
	v_fma_f32 v154, v130, v130, v154
	v_fma_f32 v155, v131, v131, v155
	v_mul_f32_e32 v156, v131, v131
	v_add_f32_e64 v154, v156, v154
	v_add_f32_e64 v155, v156, v155
	v_fma_f32 v154, v128, v128, v154
	v_fma_f32 v155, v129, v129, v155
	v_mul_f32_e32 v156, v129, v129
	v_add_f32_e64 v154, v156, v154
	v_add_f32_e64 v155, v156, v155
	v_fma_f32 v154, v126, v126, v154
	v_fma_f32 v155, v127, v127, v155
	v_mul_f32_e32 v156, v127, v127
	v_add_f32_e64 v154, v156, v154
	v_add_f32_e64 v155, v156, v155
	v_fma_f32 v154, v124, v124, v154
	v_fma_f32 v155, v125, v125, v155
	v_mul_f32_e32 v156, v125, v125
	v_add_f32_e64 v154, v156, v154
	v_add_f32_e64 v155, v156, v155
	v_fma_f32 v154, v122, v122, v154
	v_fma_f32 v155, v123, v123, v155
	v_mul_f32_e32 v156, v123, v123
	v_add_f32_e64 v154, v156, v154
	v_add_f32_e64 v155, v156, v155
	v_fma_f32 v154, v106, v106, v154
	v_fma_f32 v155, v107, v107, v155
	v_mul_f32_e32 v156, v107, v107
	v_add_f32_e64 v154, v156, v154
	v_add_f32_e64 v155, v156, v155
	v_fma_f32 v154, v116, v116, v154
	v_fma_f32 v155, v117, v117, v155
	v_mul_f32_e32 v156, v117, v117
	v_add_f32_e64 v154, v156, v154
	v_add_f32_e64 v155, v156, v155
	v_fma_f32 v154, v112, v112, v154
	v_fma_f32 v155, v113, v113, v155
	v_mul_f32_e32 v156, v113, v113
	v_add_f32_e64 v154, v156, v154
	v_add_f32_e64 v155, v156, v155
	v_fma_f32 v154, v108, v108, v154
	v_fma_f32 v155, v109, v109, v155
	v_mul_f32_e32 v156, v109, v109
	v_add_f32_e64 v154, v156, v154
	v_add_f32_e64 v155, v156, v155
	v_fma_f32 v154, v120, v120, v154
	v_fma_f32 v155, v121, v121, v155
	v_mul_f32_e32 v156, v121, v121
	v_add_f32_e64 v154, v156, v154
	v_add_f32_e64 v155, v156, v155
	v_fma_f32 v154, v118, v118, v154
	v_fma_f32 v155, v119, v119, v155
	v_mul_f32_e32 v156, v119, v119
	v_add_f32_e64 v154, v156, v154
	v_add_f32_e64 v155, v156, v155
	v_fma_f32 v154, v114, v114, v154
	v_fma_f32 v155, v115, v115, v155
	v_mul_f32_e32 v156, v115, v115
	v_add_f32_e64 v154, v156, v154
	v_add_f32_e64 v155, v156, v155
	v_fma_f32 v154, v110, v110, v154
	v_fma_f32 v155, v111, v111, v155
	v_mul_f32_e32 v156, v111, v111
	v_add_f32_e64 v154, v156, v154
	v_add_f32_e64 v155, v156, v155
	v_mov_b32_e32 v155, v154
	v_add_u32_e32 v156, 0, v161
	s_nop 0
	v_permlane32_swap_b32_e32 v154, v155
	ds_write_b128 v156, v[92:95]
	v_add_u32_e32 v92, 0x3400, v220
	s_and_saveexec_b64 s[18:19], s[4:5]
	s_xor_b64 s[18:19], exec, s[18:19]
	s_cbranch_execz .LBB0_963
	ds_write2_b64 v92, v[84:85], v[86:87] offset1:2
	ds_write_b128 v156, v[96:99] offset:22592

.LBB0_967:
	s_or_b64 exec, exec, s[18:19]
	v_add_f32_e32 v80, v154, v155
	v_fmamk_f32 v80, v80, 0x3c2aaaab, v210
	v_mul_f32_e32 v81, 0x4b800000, v80
	v_cmp_gt_f32_e32 vcc, s56, v80
	s_mov_b32 s18, 0x3e16c740
	s_lshl_b32 s25, s25, 2
	v_cndmask_b32_e32 v80, v80, v81, vcc
	v_rsq_f32_e32 v80, v80
	s_add_i32 s26, s25, 4
	s_mov_b32 s30, 0
	v_lshl_add_u64 v[202:203], v[166:167], 1, s[16:17]
	v_mul_f32_e32 v81, 0x45800000, v80
	v_cndmask_b32_e32 v80, v80, v81, vcc
	v_mul_f32_e32 v82, 0x3e16c740, v80
	s_waitcnt vmcnt(10)
	v_mul_f32_e64 v52, v52, v82
	v_mul_f32_e64 v53, v53, v82
	v_mul_f32_e64 v88, v88, v82
	v_mul_f32_e64 v89, v89, v82
	v_mul_f32_e64 v52, v52, v124
	v_mul_f32_e64 v53, v53, v125
	v_mul_f32_e64 v90, v90, v82
	v_mul_f32_e64 v91, v91, v82
	v_cvt_pk_bf16_f32 v102, v52, v53
	v_mul_f32_e64 v52, v80, v106
	v_mul_f32_e64 v53, v80, v107
	global_load_dwordx4 v[104:107], v[198:199], off offset:256
	s_waitcnt vmcnt(8)
	v_mul_f32_e64 v36, v36, v52
	v_mul_f32_e64 v37, v37, v53
	v_mul_f32_e64 v52, v80, v120
	v_mul_f32_e64 v53, v80, v121
	s_waitcnt vmcnt(6)
	v_mul_f32_e64 v32, v52, v32
	v_mul_f32_e64 v33, v53, v33
	v_mul_f32_e64 v76, v76, v82
	v_mul_f32_e64 v77, v77, v82
	s_waitcnt vmcnt(2)
	v_mul_f32_e64 v52, v44, v32
	v_mul_f32_e64 v53, v45, v33
	v_mul_f32_e64 v32, v40, v32
	v_mul_f32_e64 v33, v41, v33
	v_fma_f32 v52, v40, v36, -v52
	v_fma_f32 v53, v41, v37, -v53
	v_fma_f32 v32, v44, v36, v32
	v_fma_f32 v33, v45, v37, v33
	v_mul_f32_e64 v36, v80, v116
	v_mul_f32_e64 v37, v80, v117
	v_mul_f32_e64 v36, v38, v36
	v_mul_f32_e64 v37, v39, v37
	v_mul_f32_e64 v38, v80, v118
	v_mul_f32_e64 v39, v80, v119
	v_mul_f32_e64 v34, v38, v34
	v_mul_f32_e64 v35, v39, v35
	v_mul_f32_e64 v32, v32, s18
	v_mul_f32_e64 v33, v33, s18
	v_mul_f32_e64 v38, v46, v34
	v_mul_f32_e64 v39, v47, v35
	v_mul_f32_e64 v34, v42, v34
	v_mul_f32_e64 v35, v43, v35
	v_fma_f32 v38, v42, v36, -v38
	v_fma_f32 v39, v43, v37, -v39
	v_fma_f32 v34, v46, v36, v34
	v_fma_f32 v35, v47, v37, v35
	v_mul_f32_e64 v36, v80, v112
	v_mul_f32_e64 v37, v80, v113
	v_mul_f32_e64 v16, v36, v16
	v_mul_f32_e64 v17, v37, v17
	v_mul_f32_e64 v36, v80, v114
	v_mul_f32_e64 v37, v80, v115
	v_mul_f32_e64 v20, v36, v20
	v_mul_f32_e64 v21, v37, v21
	v_cvt_pk_bf16_f32 v112, v32, v33
	v_mul_f32_e64 v36, v28, v20
	v_mul_f32_e64 v37, v29, v21
	v_mul_f32_e64 v20, v24, v20
	v_mul_f32_e64 v21, v25, v21
	v_fma_f32 v36, v24, v16, -v36
	v_fma_f32 v37, v25, v17, -v37
	v_fma_f32 v16, v28, v16, v20
	v_fma_f32 v17, v29, v17, v21
	v_mul_f32_e64 v20, v80, v108
	v_mul_f32_e64 v21, v80, v109
	v_mul_f32_e64 v18, v20, v18
	v_mul_f32_e64 v19, v21, v19
	v_mul_f32_e64 v20, v80, v110
	v_mul_f32_e64 v21, v80, v111
	v_mul_f32_e64 v20, v20, v22
	v_mul_f32_e64 v21, v21, v23
	v_mov_b32_e32 v32, v209
	v_mul_f32_e64 v22, v30, v20
	v_mul_f32_e64 v23, v31, v21
	v_mul_f32_e64 v20, v26, v20
	v_mul_f32_e64 v21, v27, v21
	v_fma_f32 v22, v26, v18, -v22
	v_fma_f32 v23, v27, v19, -v23
	v_fma_f32 v18, v30, v18, v20
	v_fma_f32 v19, v31, v19, v21
	v_mul_f32_e64 v78, v78, v82
	v_mul_f32_e64 v79, v79, v82
	v_mul_f32_e64 v72, v72, v82
	v_mul_f32_e64 v73, v73, v82
	v_mul_f32_e64 v74, v74, v82
	v_mul_f32_e64 v75, v75, v82
	v_mul_f32_e64 v68, v68, v82
	v_mul_f32_e64 v69, v69, v82
	v_mul_f32_e64 v70, v70, v82
	v_mul_f32_e64 v71, v71, v82
	v_mul_f32_e64 v64, v64, v82
	v_mul_f32_e64 v65, v65, v82
	v_mul_f32_e64 v66, v66, v82
	v_mul_f32_e64 v67, v67, v82
	v_mul_f32_e64 v60, v60, v82
	v_mul_f32_e64 v61, v61, v82
	v_mul_f32_e64 v62, v62, v82
	v_mul_f32_e64 v63, v63, v82
	v_mul_f32_e64 v56, v56, v82
	v_mul_f32_e64 v57, v57, v82
	v_mul_f32_e64 v58, v58, v82
	v_mul_f32_e64 v59, v59, v82
	v_mul_f32_e64 v54, v54, v82
	v_mul_f32_e64 v55, v55, v82
	v_mul_f32_e64 v38, v38, s18
	v_mul_f32_e64 v39, v39, s18
	v_mul_f32_e64 v34, v34, s18
	v_mul_f32_e64 v35, v35, s18
	v_mul_f32_e64 v36, v36, s18
	v_mul_f32_e64 v37, v37, s18
	v_mul_f32_e64 v16, v16, s18
	v_mul_f32_e64 v17, v17, s18
	v_mul_f32_e64 v22, v22, s18
	v_mul_f32_e64 v23, v23, s18
	v_mul_f32_e64 v18, v18, s18
	v_mul_f32_e64 v19, v19, s18
	s_waitcnt lgkmcnt(0)
	s_barrier
	v_mul_f32_e64 v88, v88, v152
	v_mul_f32_e64 v89, v89, v153
	v_mov_b32_e32 v33, v32
	v_mul_f32_e64 v90, v90, v150
	v_mul_f32_e64 v91, v91, v151
	v_mul_f32_e64 v76, v76, v148
	v_mul_f32_e64 v77, v77, v149
	v_mul_f32_e64 v78, v78, v146
	v_mul_f32_e64 v79, v79, v147
	v_mul_f32_e64 v72, v72, v144
	v_mul_f32_e64 v73, v73, v145
	v_mul_f32_e64 v74, v74, v142
	v_mul_f32_e64 v75, v75, v143
	v_mul_f32_e64 v68, v68, v140
	v_mul_f32_e64 v69, v69, v141
	v_mul_f32_e64 v70, v70, v138
	v_mul_f32_e64 v71, v71, v139
	v_mul_f32_e64 v64, v64, v136
	v_mul_f32_e64 v65, v65, v137
	v_mul_f32_e64 v66, v66, v134
	v_mul_f32_e64 v67, v67, v135
	v_mul_f32_e64 v60, v60, v132
	v_mul_f32_e64 v61, v61, v133
	v_mul_f32_e64 v62, v62, v130
	v_mul_f32_e64 v63, v63, v131
	v_mul_f32_e64 v56, v56, v128
	v_mul_f32_e64 v57, v57, v129
	v_mul_f32_e64 v58, v58, v126
	v_mul_f32_e64 v59, v59, v127
	v_mul_f32_e64 v54, v54, v122
	v_mul_f32_e64 v55, v55, v123
	v_mul_f32_e64 v52, v52, s18
	v_mul_f32_e64 v53, v53, s18
	v_cvt_pk_bf16_f32 v109, v38, v39
	v_cvt_pk_bf16_f32 v110, v36, v37
	v_cvt_pk_bf16_f32 v111, v22, v23
	v_cvt_pk_bf16_f32 v113, v34, v35
	v_cvt_pk_bf16_f32 v114, v16, v17
	v_cvt_pk_bf16_f32 v115, v18, v19
	v_mov_b32_e32 v34, v32
	v_mov_b32_e32 v35, v32
	v_mov_b32_e32 v36, v32
	v_mov_b32_e32 v37, v32
	v_mov_b32_e32 v38, v32
	v_mov_b32_e32 v39, v32
	v_mov_b32_e32 v40, v32
	v_mov_b32_e32 v41, v32
	v_mov_b32_e32 v42, v32
	v_mov_b32_e32 v43, v32
	v_mov_b32_e32 v44, v32
	v_mov_b32_e32 v45, v32
	v_mov_b32_e32 v46, v32
	v_mov_b32_e32 v47, v32
	v_mov_b64_e32 v[16:17], v[32:33]
	s_waitcnt vmcnt(1)
	v_mov_b64_e32 v[82:83], v[50:51]
	v_cvt_pk_bf16_f32 v88, v88, v89
	v_cvt_pk_bf16_f32 v89, v90, v91
	v_cvt_pk_bf16_f32 v90, v76, v77
	v_cvt_pk_bf16_f32 v91, v78, v79
	v_cvt_pk_bf16_f32 v92, v72, v73
	v_cvt_pk_bf16_f32 v93, v74, v75
	v_cvt_pk_bf16_f32 v94, v68, v69
	v_cvt_pk_bf16_f32 v95, v70, v71
	v_cvt_pk_bf16_f32 v96, v64, v65
	v_cvt_pk_bf16_f32 v97, v66, v67
	v_cvt_pk_bf16_f32 v98, v60, v61
	v_cvt_pk_bf16_f32 v99, v62, v63
	v_cvt_pk_bf16_f32 v100, v56, v57
	v_cvt_pk_bf16_f32 v101, v58, v59
	v_cvt_pk_bf16_f32 v103, v54, v55
	v_cvt_pk_bf16_f32 v108, v52, v53
	s_or_b32 s27, s24, 31
	v_lshl_add_u64 v[204:205], v[170:171], 1, s[16:17]
	v_or_b32_e32 v223, s24, v160
	v_lshl_add_u64 v[206:207], v[192:193], 0, s[64:65]
	v_lshl_add_u64 v[216:217], v[194:195], 0, s[14:15]
	v_lshl_add_u64 v[218:219], v[196:197], 0, s[14:15]
	v_mov_b32_e32 v173, 0
	s_movk_i32 s28, 0x7f
	v_mov_b64_e32 v[18:19], v[34:35]
	v_mov_b64_e32 v[20:21], v[36:37]
	v_mov_b64_e32 v[22:23], v[38:39]
	v_mov_b64_e32 v[24:25], v[40:41]
	v_mov_b64_e32 v[26:27], v[42:43]
	v_mov_b64_e32 v[28:29], v[44:45]
	v_mov_b64_e32 v[30:31], v[46:47]
	v_mov_b64_e32 v[80:81], v[48:49]
	s_mov_b64 s[34:35], 0x3000

.LBB0_1060:
	v_lshlrev_b32_e32 v63, 16, v60
	v_and_b32_e32 v64, 0xffff0000, v60
	v_lshlrev_b32_e32 v66, 16, v61
	v_and_b32_e32 v67, 0xffff0000, v61
	v_add_f32_e32 v60, v12, v63
	v_add_f32_e32 v61, v13, v64
	v_mul_f32_e32 v60, 0xbfb8aa3b, v60
	v_mul_f32_e32 v61, 0xbfb8aa3b, v61
	v_exp_f32_e32 v60, v60
	v_exp_f32_e32 v61, v61
	v_lshlrev_b32_e32 v64, 16, v54
	v_and_b32_e32 v65, 0xffff0000, v54
	v_lshlrev_b32_e32 v56, 16, v46
	v_add_f32_e64 v60, v60, 1.0
	v_add_f32_e64 v61, v61, 1.0
	v_and_b32_e32 v57, 0xffff0000, v46
	v_div_scale_f32 v54, s[20:21], v61, v61, 1.0
	v_rcp_f32_e32 v63, v54
	v_lshlrev_b32_e32 v58, 16, v47
	v_and_b32_e32 v59, 0xffff0000, v47
	v_lshlrev_b32_e32 v52, 16, v48
	v_fma_f32 v68, -v54, v63, 1.0
	v_fmac_f32_e32 v63, v68, v63
	v_div_scale_f32 v68, vcc, 1.0, v61, 1.0
	v_mul_f32_e32 v69, v68, v63
	v_fma_f32 v70, -v54, v69, v68
	v_fmac_f32_e32 v69, v70, v63
	v_fma_f32 v54, -v54, v69, v68
	v_div_fmas_f32 v54, v54, v63, v69
	v_div_fixup_f32 v61, v54, v61, 1.0
	v_div_scale_f32 v54, s[20:21], v60, v60, 1.0
	v_rcp_f32_e32 v63, v54
	v_and_b32_e32 v53, 0xffff0000, v48
	v_lshlrev_b32_e32 v48, 16, v49
	v_and_b32_e32 v49, 0xffff0000, v49
	v_fma_f32 v68, -v54, v63, 1.0
	v_fmac_f32_e32 v63, v68, v63
	v_div_scale_f32 v68, vcc, 1.0, v60, 1.0
	v_mul_f32_e32 v69, v68, v63
	v_fma_f32 v70, -v54, v69, v68
	v_fmac_f32_e32 v69, v70, v63
	v_fma_f32 v54, -v54, v69, v68
	v_div_fmas_f32 v54, v54, v63, v69
	v_div_fixup_f32 v60, v54, v60, 1.0
	v_add_f32_e64 v60, v60, -1.0
	v_add_f32_e64 v61, v61, -1.0
	v_add_f32_e32 v54, v14, v66
	v_fma_f32 v60, v16, v60, 1.0
	v_fma_f32 v61, v17, v61, 1.0
	v_mul_f32_e32 v54, 0xbfb8aa3b, v54
	v_mul_f32_e64 v60, v60, v64
	v_mul_f32_e64 v61, v61, v65
	v_exp_f32_e32 v64, v54
	v_add_f32_e32 v54, v15, v67
	v_mul_f32_e32 v54, 0xbfb8aa3b, v54
	v_exp_f32_e32 v65, v54
	v_lshlrev_b32_e32 v54, 16, v55
	v_and_b32_e32 v55, 0xffff0000, v55
	v_mul_f32_e64 v56, v60, v56
	v_mul_f32_e64 v57, v61, v57
	v_add_f32_e64 v64, v64, 1.0
	v_add_f32_e64 v65, v65, 1.0
	v_mul_f32_e64 v56, v8, v56
	v_mul_f32_e64 v57, v9, v57
	v_div_scale_f32 v63, s[20:21], v65, v65, 1.0
	v_rcp_f32_e32 v66, v63
	v_add_f32_e32 v56, v56, v57
	v_lshlrev_b32_e32 v46, 16, v50
	v_and_b32_e32 v47, 0xffff0000, v50
	v_fma_f32 v67, -v63, v66, 1.0
	v_fmac_f32_e32 v66, v67, v66
	v_div_scale_f32 v67, vcc, 1.0, v65, 1.0
	v_mul_f32_e32 v68, v67, v66
	v_fma_f32 v69, -v63, v68, v67
	v_fmac_f32_e32 v68, v69, v66
	v_fma_f32 v63, -v63, v68, v67
	v_div_fmas_f32 v63, v63, v66, v68
	v_div_fixup_f32 v65, v63, v65, 1.0
	v_div_scale_f32 v63, s[20:21], v64, v64, 1.0
	v_rcp_f32_e32 v66, v63
	v_lshlrev_b32_e32 v50, 16, v51
	v_and_b32_e32 v51, 0xffff0000, v51
	v_fma_f32 v67, -v63, v66, 1.0
	v_fmac_f32_e32 v66, v67, v66
	v_div_scale_f32 v67, vcc, 1.0, v64, 1.0
	v_mul_f32_e32 v68, v67, v66
	v_fma_f32 v69, -v63, v68, v67
	v_fmac_f32_e32 v68, v69, v66
	v_fma_f32 v63, -v63, v68, v67
	v_div_fmas_f32 v63, v63, v66, v68
	v_div_fixup_f32 v64, v63, v64, 1.0
	v_add_f32_e64 v64, v64, -1.0
	v_add_f32_e64 v65, v65, -1.0
	v_add_f32_e32 v63, v20, v21
	v_fma_f32 v64, v18, v64, 1.0
	v_fma_f32 v65, v19, v65, 1.0
	v_add_f32_e32 v63, v22, v63
	v_mul_f32_e64 v54, v64, v54
	v_mul_f32_e64 v55, v65, v55
	v_add_f32_e32 v63, v23, v63
	v_mul_f32_e64 v54, v54, v58
	v_mul_f32_e64 v55, v55, v59
	s_nop 0
	v_mul_f32_e64 v54, v10, v54
	v_mul_f32_e64 v55, v11, v55
	s_nop 0
	v_add_f32_e32 v54, v54, v56
	v_add_f32_e32 v54, v55, v54
	ds_swizzle_b32 v55, v63 offset:swizzle(SWAP,1)
	ds_swizzle_b32 v56, v54 offset:swizzle(SWAP,1)
	s_waitcnt lgkmcnt(1)
	v_add_f32_e32 v55, v63, v55
	s_waitcnt lgkmcnt(0)
	v_add_f32_e32 v54, v54, v56
	ds_swizzle_b32 v56, v55 offset:swizzle(SWAP,2)
	s_waitcnt lgkmcnt(0)
	v_add_f32_e32 v55, v55, v56
	ds_swizzle_b32 v56, v54 offset:swizzle(SWAP,2)
	s_waitcnt lgkmcnt(0)
	v_add_f32_e32 v54, v54, v56
	ds_swizzle_b32 v56, v55 offset:swizzle(SWAP,4)
	s_waitcnt lgkmcnt(0)
	v_add_f32_e32 v55, v55, v56
	ds_swizzle_b32 v56, v54 offset:swizzle(SWAP,4)
	s_waitcnt lgkmcnt(0)
	v_add_f32_e32 v54, v54, v56
	ds_swizzle_b32 v56, v55 offset:swizzle(SWAP,8)
	s_waitcnt lgkmcnt(0)
	v_add_f32_e32 v55, v55, v56
	ds_swizzle_b32 v56, v54 offset:swizzle(SWAP,8)
	v_fmamk_f32 v21, v55, 0xbc800000, v21
	v_fmamk_f32 v20, v55, 0xbc800000, v20
	v_fmamk_f32 v23, v55, 0xbc800000, v23
	v_fmac_f32_e32 v22, 0xbc800000, v55
	v_mul_f32_e64 v58, v20, v20
	v_mul_f32_e64 v59, v21, v21
	s_waitcnt lgkmcnt(0)
	v_add_f32_e32 v54, v54, v56
	v_mul_f32_e64 v56, v22, v22
	v_mul_f32_e64 v57, v23, v23
	v_add_f32_e32 v55, v58, v59
	v_add_f32_e32 v55, v56, v55
	v_add_f32_e32 v55, v57, v55
	ds_swizzle_b32 v56, v55 offset:swizzle(SWAP,1)
	s_waitcnt lgkmcnt(0)
	v_add_f32_e32 v55, v55, v56
	ds_swizzle_b32 v56, v55 offset:swizzle(SWAP,2)
	s_waitcnt lgkmcnt(0)
	v_add_f32_e32 v55, v55, v56
	ds_swizzle_b32 v56, v55 offset:swizzle(SWAP,4)
	s_waitcnt lgkmcnt(0)
	v_add_f32_e32 v55, v55, v56
	ds_swizzle_b32 v56, v55 offset:swizzle(SWAP,8)
	s_waitcnt lgkmcnt(0)
	v_add_f32_e32 v55, v55, v56
	v_mov_b32_e32 v56, 0x3a27c5ac
	v_fmamk_f32 v55, v55, 0x3c800000, v56
	v_cmp_gt_f32_e32 vcc, s56, v55
	v_mul_f32_e32 v56, 0x4b800000, v55
	s_nop 0
	v_cndmask_b32_e32 v55, v55, v56, vcc
	v_rsq_f32_e32 v55, v55
	s_nop 0
	v_mul_f32_e32 v56, 0x45800000, v55
	v_cndmask_b32_e32 v56, v55, v56, vcc
	v_mul_f32_e64 v20, v20, v56
	v_mul_f32_e64 v21, v21, v56
	v_mul_f32_e64 v22, v22, v56
	v_mul_f32_e64 v23, v23, v56
	v_fma_f32 v20, v0, v20, v4
	v_fma_f32 v21, v1, v21, v5
	v_fma_f32 v22, v2, v22, v6
	v_fma_f32 v23, v3, v23, v7
	v_fma_f32 v20, v54, v52, v20
	v_fma_f32 v21, v54, v53, v21
	v_fma_f32 v22, v54, v48, v22
	v_fma_f32 v23, v54, v49, v23
	v_mul_f32_e64 v22, v22, v50
	v_mul_f32_e64 v23, v23, v51
	v_mul_f32_e64 v20, v20, v46
	v_mul_f32_e64 v21, v21, v47
	s_andn2_b64 vcc, exec, s[10:11]
	v_cvt_pk_bf16_f32 v20, v20, v21
	v_cvt_pk_bf16_f32 v21, v22, v23
	s_cbranch_vccnz .LBB0_1062
	buffer_store_dwordx2 v[20:21], v62, s[60:63], 0 offen sc1
	s_cbranch_execnz .LBB0_1057
	s_branch .LBB0_1056

.LBB0_1164:
	s_ashr_i32 s10, s54, 31
	s_lshr_b32 s10, s10, 20
	v_mov_b32_e32 v128, v243
	s_add_i32 s10, s54, s10
	s_ashr_i32 s10, s10, 12
	v_and_b32_e32 v153, 15, v128
	s_lshl_b32 s11, s55, 8
	v_lshrrev_b32_e32 v128, 2, v128
	s_mulk_i32 s10, 0x1800
	v_and_or_b32 v128, v128, 12, s11
	s_ashr_i32 s11, s10, 31
	v_or_b32_e32 v146, s45, v128
	s_lshl_b64 s[10:11], s[10:11], 2
	s_add_u32 s10, s36, s10
	v_ashrrev_i32_e32 v147, 31, v146
	s_addc_u32 s11, s37, s11
	v_lshlrev_b64 v[132:133], 2, v[146:147]
	v_lshl_add_u64 v[158:159], s[10:11], 0, v[132:133]
	v_lshl_add_u64 v[134:135], s[20:21], 0, v[132:133]
	global_load_dwordx4 v[128:131], v[158:159], off
	s_add_i32 s10, s54, s44
	global_load_dwordx4 v[134:137], v[134:135], off
	v_readlane_b32 s66, v253, 44
	s_andn2_b64 vcc, exec, s[0:1]
	v_readlane_b32 s67, v253, 45
	s_waitcnt vmcnt(0)
	v_add_f32_e64 v140, v128, v134
	v_add_f32_e64 v141, v129, v135
	v_or_b32_e32 v134, 16, v146
	v_ashrrev_i32_e32 v135, 31, v134
	v_lshl_add_u64 v[134:135], v[134:135], 2, s[20:21]
	v_add_f32_e64 v138, v130, v136
	v_add_f32_e64 v139, v131, v137
	global_load_dwordx4 v[128:131], v[158:159], off offset:64
	s_nop 0
	global_load_dwordx4 v[134:137], v[134:135], off
	s_waitcnt vmcnt(0)
	v_add_f32_e64 v144, v128, v134
	v_add_f32_e64 v145, v129, v135
	v_or_b32_e32 v134, 0x80, v146
	v_ashrrev_i32_e32 v135, 31, v134
	v_lshl_add_u64 v[134:135], v[134:135], 2, s[20:21]
	v_add_f32_e64 v142, v130, v136
	v_add_f32_e64 v143, v131, v137
	global_load_dwordx4 v[128:131], v[158:159], off offset:512
	global_load_dwordx4 v[154:157], v[134:135], off
	s_waitcnt vmcnt(0)
	v_add_f32_e64 v136, v128, v154
	v_add_f32_e64 v137, v129, v155
	v_or_b32_e32 v128, 0x90, v146
	v_ashrrev_i32_e32 v129, 31, v128
	v_lshl_add_u64 v[128:129], v[128:129], 2, s[20:21]
	v_add_f32_e64 v134, v130, v156
	v_add_f32_e64 v135, v131, v157
	global_load_dwordx4 v[154:157], v[158:159], off offset:576
	v_add_u32_e32 v146, s10, v153
	global_load_dwordx4 v[158:161], v[128:129], off
	v_ashrrev_i32_e32 v147, 31, v146
	s_mov_b64 s[10:11], -1
	s_waitcnt vmcnt(0)
	v_add_f32_e64 v130, v154, v158
	v_add_f32_e64 v131, v155, v159
	v_lshlrev_b64 v[154:155], 12, v[146:147]
	v_lshl_add_u64 v[154:155], s[2:3], 0, v[154:155]
	v_lshl_add_u64 v[158:159], v[154:155], 0, v[132:133]
	v_add_f32_e64 v128, v156, v160
	v_add_f32_e64 v129, v157, v161
	global_load_dwordx4 v[154:157], v[158:159], off
	s_waitcnt vmcnt(0)
	v_fma_f32 v126, v126, v138, v156
	v_fma_f32 v127, v127, v139, v157
	v_fma_f32 v124, v124, v140, v154
	v_fma_f32 v125, v125, v141, v155
	global_store_dwordx4 v[158:159], v[124:127], off
	global_load_dwordx4 v[124:127], v[158:159], off offset:64
	s_waitcnt vmcnt(0)
	v_fma_f32 v122, v122, v142, v126
	v_fma_f32 v123, v123, v143, v127
	v_fma_f32 v120, v120, v144, v124
	v_fma_f32 v121, v121, v145, v125
	global_store_dwordx4 v[158:159], v[120:123], off offset:64
	global_load_dwordx4 v[120:123], v[158:159], off offset:512
	s_waitcnt vmcnt(0)
	v_fma_f32 v118, v118, v134, v122
	v_fma_f32 v119, v119, v135, v123
	v_fma_f32 v116, v116, v136, v120
	v_fma_f32 v117, v117, v137, v121
	global_store_dwordx4 v[158:159], v[116:119], off offset:512
	global_load_dwordx4 v[116:119], v[158:159], off offset:576
	s_waitcnt vmcnt(0)
	v_fma_f32 v114, v114, v128, v118
	v_fma_f32 v115, v115, v129, v119
	v_fma_f32 v112, v112, v130, v116
	v_fma_f32 v113, v113, v131, v117
	global_store_dwordx4 v[158:159], v[112:115], off offset:576
	s_nop 1
	v_add_u32_e32 v112, 16, v146
	v_ashrrev_i32_e32 v113, 31, v112
	v_lshlrev_b64 v[112:113], 12, v[112:113]
	v_lshl_add_u64 v[112:113], s[2:3], 0, v[112:113]
	v_lshl_add_u64 v[116:117], v[112:113], 0, v[132:133]
	global_load_dwordx4 v[112:115], v[116:117], off
	s_waitcnt vmcnt(0)
	v_fma_f32 v110, v110, v138, v114
	v_fma_f32 v111, v111, v139, v115
	v_fma_f32 v108, v108, v140, v112
	v_fma_f32 v109, v109, v141, v113
	global_store_dwordx4 v[116:117], v[108:111], off
	global_load_dwordx4 v[108:111], v[116:117], off offset:64
	s_waitcnt vmcnt(0)
	v_fma_f32 v106, v106, v142, v110
	v_fma_f32 v107, v107, v143, v111
	v_fma_f32 v104, v104, v144, v108
	v_fma_f32 v105, v105, v145, v109
	global_store_dwordx4 v[116:117], v[104:107], off offset:64
	global_load_dwordx4 v[104:107], v[116:117], off offset:512
	s_waitcnt vmcnt(0)
	v_fma_f32 v102, v102, v134, v106
	v_fma_f32 v103, v103, v135, v107
	v_fma_f32 v100, v100, v136, v104
	v_fma_f32 v101, v101, v137, v105
	global_store_dwordx4 v[116:117], v[100:103], off offset:512
	global_load_dwordx4 v[100:103], v[116:117], off offset:576
	s_waitcnt vmcnt(0)
	v_fma_f32 v98, v98, v128, v102
	v_fma_f32 v99, v99, v129, v103
	v_fma_f32 v96, v96, v130, v100
	v_fma_f32 v97, v97, v131, v101
	global_store_dwordx4 v[116:117], v[96:99], off offset:576
	s_nop 1
	v_add_u32_e32 v96, 32, v146
	v_ashrrev_i32_e32 v97, 31, v96
	v_lshlrev_b64 v[96:97], 12, v[96:97]
	v_lshl_add_u64 v[96:97], s[2:3], 0, v[96:97]
	v_lshl_add_u64 v[100:101], v[96:97], 0, v[132:133]
	global_load_dwordx4 v[96:99], v[100:101], off
	s_waitcnt vmcnt(0)
	v_fma_f32 v94, v94, v138, v98
	v_fma_f32 v95, v95, v139, v99
	v_fma_f32 v92, v92, v140, v96
	v_fma_f32 v93, v93, v141, v97
	global_store_dwordx4 v[100:101], v[92:95], off
	global_load_dwordx4 v[92:95], v[100:101], off offset:64
	s_waitcnt vmcnt(0)
	v_fma_f32 v90, v90, v142, v94
	v_fma_f32 v91, v91, v143, v95
	v_fma_f32 v88, v88, v144, v92
	v_fma_f32 v89, v89, v145, v93
	global_store_dwordx4 v[100:101], v[88:91], off offset:64
	global_load_dwordx4 v[88:91], v[100:101], off offset:512
	s_waitcnt vmcnt(0)
	v_fma_f32 v86, v86, v134, v90
	v_fma_f32 v87, v87, v135, v91
	v_fma_f32 v84, v84, v136, v88
	v_fma_f32 v85, v85, v137, v89
	global_store_dwordx4 v[100:101], v[84:87], off offset:512
	global_load_dwordx4 v[84:87], v[100:101], off offset:576
	s_waitcnt vmcnt(0)
	v_fma_f32 v82, v82, v128, v86
	v_fma_f32 v83, v83, v129, v87
	v_fma_f32 v80, v80, v130, v84
	v_fma_f32 v81, v81, v131, v85
	global_store_dwordx4 v[100:101], v[80:83], off offset:576
	s_nop 1
	v_add_u32_e32 v80, 48, v146
	v_ashrrev_i32_e32 v81, 31, v80
	v_lshlrev_b64 v[80:81], 12, v[80:81]
	v_lshl_add_u64 v[80:81], s[2:3], 0, v[80:81]
	v_lshl_add_u64 v[84:85], v[80:81], 0, v[132:133]
	global_load_dwordx4 v[80:83], v[84:85], off
	s_waitcnt vmcnt(0)
	v_fma_f32 v78, v78, v138, v82
	v_fma_f32 v79, v79, v139, v83
	v_fma_f32 v76, v76, v140, v80
	v_fma_f32 v77, v77, v141, v81
	global_store_dwordx4 v[84:85], v[76:79], off
	global_load_dwordx4 v[76:79], v[84:85], off offset:64
	s_waitcnt vmcnt(0)
	v_fma_f32 v74, v74, v142, v78
	v_fma_f32 v75, v75, v143, v79
	v_fma_f32 v72, v72, v144, v76
	v_fma_f32 v73, v73, v145, v77
	global_store_dwordx4 v[84:85], v[72:75], off offset:64
	global_load_dwordx4 v[72:75], v[84:85], off offset:512
	s_waitcnt vmcnt(0)
	v_fma_f32 v70, v70, v134, v74
	v_fma_f32 v71, v71, v135, v75
	v_fma_f32 v68, v68, v136, v72
	v_fma_f32 v69, v69, v137, v73
	global_store_dwordx4 v[84:85], v[68:71], off offset:512
	global_load_dwordx4 v[68:71], v[84:85], off offset:576
	s_waitcnt vmcnt(0)
	v_fma_f32 v66, v66, v128, v70
	v_fma_f32 v67, v67, v129, v71
	v_fma_f32 v64, v64, v130, v68
	v_fma_f32 v65, v65, v131, v69
	global_store_dwordx4 v[84:85], v[64:67], off offset:576
	s_nop 1
	v_add_u32_e32 v64, 0x80, v146
	v_ashrrev_i32_e32 v65, 31, v64
	v_lshlrev_b64 v[64:65], 12, v[64:65]
	v_lshl_add_u64 v[64:65], s[2:3], 0, v[64:65]
	v_lshl_add_u64 v[68:69], v[64:65], 0, v[132:133]
	global_load_dwordx4 v[64:67], v[68:69], off
	s_waitcnt vmcnt(0)
	v_fma_f32 v62, v62, v138, v66
	v_fma_f32 v63, v63, v139, v67
	v_fma_f32 v60, v60, v140, v64
	v_fma_f32 v61, v61, v141, v65
	global_store_dwordx4 v[68:69], v[60:63], off
	global_load_dwordx4 v[60:63], v[68:69], off offset:64
	s_waitcnt vmcnt(0)
	v_fma_f32 v58, v58, v142, v62
	v_fma_f32 v59, v59, v143, v63
	v_fma_f32 v56, v56, v144, v60
	v_fma_f32 v57, v57, v145, v61
	global_store_dwordx4 v[68:69], v[56:59], off offset:64
	global_load_dwordx4 v[56:59], v[68:69], off offset:512
	s_waitcnt vmcnt(0)
	v_fma_f32 v54, v54, v134, v58
	v_fma_f32 v55, v55, v135, v59
	v_fma_f32 v52, v52, v136, v56
	v_fma_f32 v53, v53, v137, v57
	global_store_dwordx4 v[68:69], v[52:55], off offset:512
	global_load_dwordx4 v[52:55], v[68:69], off offset:576
	s_waitcnt vmcnt(0)
	v_fma_f32 v50, v50, v128, v54
	v_fma_f32 v51, v51, v129, v55
	v_fma_f32 v48, v48, v130, v52
	v_fma_f32 v49, v49, v131, v53
	global_store_dwordx4 v[68:69], v[48:51], off offset:576
	s_nop 1
	v_add_u32_e32 v48, 0x90, v146
	v_ashrrev_i32_e32 v49, 31, v48
	v_lshlrev_b64 v[48:49], 12, v[48:49]
	v_lshl_add_u64 v[48:49], s[2:3], 0, v[48:49]
	v_lshl_add_u64 v[52:53], v[48:49], 0, v[132:133]
	global_load_dwordx4 v[48:51], v[52:53], off
	s_waitcnt vmcnt(0)
	v_fma_f32 v46, v46, v138, v50
	v_fma_f32 v47, v47, v139, v51
	v_fma_f32 v44, v44, v140, v48
	v_fma_f32 v45, v45, v141, v49
	global_store_dwordx4 v[52:53], v[44:47], off
	global_load_dwordx4 v[44:47], v[52:53], off offset:64
	s_waitcnt vmcnt(0)
	v_fma_f32 v42, v42, v142, v46
	v_fma_f32 v43, v43, v143, v47
	v_fma_f32 v40, v40, v144, v44
	v_fma_f32 v41, v41, v145, v45
	global_store_dwordx4 v[52:53], v[40:43], off offset:64
	global_load_dwordx4 v[40:43], v[52:53], off offset:512
	s_waitcnt vmcnt(0)
	v_fma_f32 v38, v38, v134, v42
	v_fma_f32 v39, v39, v135, v43
	v_fma_f32 v36, v36, v136, v40
	v_fma_f32 v37, v37, v137, v41
	global_store_dwordx4 v[52:53], v[36:39], off offset:512
	global_load_dwordx4 v[36:39], v[52:53], off offset:576
	s_waitcnt vmcnt(0)
	v_fma_f32 v34, v34, v128, v38
	v_fma_f32 v35, v35, v129, v39
	v_fma_f32 v32, v32, v130, v36
	v_fma_f32 v33, v33, v131, v37
	global_store_dwordx4 v[52:53], v[32:35], off offset:576
	s_nop 1
	v_add_u32_e32 v32, 0xa0, v146
	v_ashrrev_i32_e32 v33, 31, v32
	v_lshlrev_b64 v[32:33], 12, v[32:33]
	v_lshl_add_u64 v[32:33], s[2:3], 0, v[32:33]
	v_lshl_add_u64 v[36:37], v[32:33], 0, v[132:133]
	global_load_dwordx4 v[32:35], v[36:37], off
	s_waitcnt vmcnt(0)
	v_fma_f32 v30, v30, v138, v34
	v_fma_f32 v31, v31, v139, v35
	v_fma_f32 v28, v28, v140, v32
	v_fma_f32 v29, v29, v141, v33
	global_store_dwordx4 v[36:37], v[28:31], off
	global_load_dwordx4 v[28:31], v[36:37], off offset:64
	s_waitcnt vmcnt(0)
	v_fma_f32 v26, v26, v142, v30
	v_fma_f32 v27, v27, v143, v31
	v_fma_f32 v24, v24, v144, v28
	v_fma_f32 v25, v25, v145, v29
	global_store_dwordx4 v[36:37], v[24:27], off offset:64
	global_load_dwordx4 v[24:27], v[36:37], off offset:512
	s_waitcnt vmcnt(0)
	v_fma_f32 v22, v22, v134, v26
	v_fma_f32 v23, v23, v135, v27
	v_fma_f32 v20, v20, v136, v24
	v_fma_f32 v21, v21, v137, v25
	global_store_dwordx4 v[36:37], v[20:23], off offset:512
	global_load_dwordx4 v[20:23], v[36:37], off offset:576
	s_waitcnt vmcnt(0)
	v_fma_f32 v18, v18, v128, v22
	v_fma_f32 v19, v19, v129, v23
	v_fma_f32 v16, v16, v130, v20
	v_fma_f32 v17, v17, v131, v21
	global_store_dwordx4 v[36:37], v[16:19], off offset:576
	s_nop 1
	v_add_u32_e32 v16, 0xb0, v146
	v_ashrrev_i32_e32 v17, 31, v16
	v_lshlrev_b64 v[16:17], 12, v[16:17]
	v_lshl_add_u64 v[16:17], s[2:3], 0, v[16:17]
	v_lshl_add_u64 v[16:17], v[16:17], 0, v[132:133]
	global_load_dwordx4 v[18:21], v[16:17], off
	s_waitcnt vmcnt(0)
	v_fma_f32 v14, v14, v138, v20
	v_fma_f32 v15, v15, v139, v21
	v_fma_f32 v12, v12, v140, v18
	v_fma_f32 v13, v13, v141, v19
	global_store_dwordx4 v[16:17], v[12:15], off
	global_load_dwordx4 v[12:15], v[16:17], off offset:64
	s_waitcnt vmcnt(0)
	v_fma_f32 v10, v10, v142, v14
	v_fma_f32 v11, v11, v143, v15
	v_fma_f32 v8, v8, v144, v12
	v_fma_f32 v9, v9, v145, v13
	global_store_dwordx4 v[16:17], v[8:11], off offset:64
	global_load_dwordx4 v[8:11], v[16:17], off offset:512
	s_waitcnt vmcnt(0)
	v_fma_f32 v6, v6, v134, v10
	v_fma_f32 v7, v7, v135, v11
	v_fma_f32 v4, v4, v136, v8
	v_fma_f32 v5, v5, v137, v9
	global_store_dwordx4 v[16:17], v[4:7], off offset:512
	global_load_dwordx4 v[4:7], v[16:17], off offset:576
	s_waitcnt vmcnt(0)
	v_fma_f32 v2, v2, v128, v6
	v_fma_f32 v3, v3, v129, v7
	v_fma_f32 v0, v0, v130, v4
	v_fma_f32 v1, v1, v131, v5
	global_store_dwordx4 v[16:17], v[0:3], off offset:576
	s_cbranch_vccnz .LBB0_1153
	s_andn2_b64 vcc, exec, s[18:19]
	s_cbranch_vccnz .LBB0_1152
	s_barrier
	s_branch .LBB0_1152

.LBB0_1186:
	v_mov_b32_e32 v128, v243
	s_mov_b64 s[34:35], s[12:13]
	s_mov_b64 s[10:11], s[14:15]
	s_load_dwordx2 s[30:31], s[34:35], 0x28
	s_and_b64 s[2:3], s[20:21], exec
	s_cselect_b32 s2, 0, 0x130
	s_add_u32 s2, s34, s2
	s_addc_u32 s3, s35, 0
	s_load_dwordx2 s[2:3], s[2:3], 0x0
	s_waitcnt lgkmcnt(0)
	s_add_u32 s78, s30, s26
	s_addc_u32 s79, s31, s27
	s_add_u32 s38, s78, 0x2000
	s_addc_u32 s39, s79, 0
	s_ashr_i32 s30, s60, 31
	s_lshr_b32 s30, s30, 20
	s_add_i32 s30, s60, s30
	s_ashr_i32 s30, s30, 12
	s_lshl_b32 s31, s77, 8
	v_bfe_u32 v153, v128, 4, 2
	s_or_b32 s31, s31, s56
	s_mulk_i32 s30, 0x1800
	v_lshl_or_b32 v218, v153, 2, s31
	s_ashr_i32 s31, s30, 31
	s_lshl_b64 s[30:31], s[30:31], 2
	s_add_u32 s36, s10, s30
	v_ashrrev_i32_e32 v219, 31, v218
	s_addc_u32 s37, s11, s31
	v_lshlrev_b64 v[140:141], 2, v[218:219]
	v_and_b32_e32 v152, 15, v128
	v_lshl_add_u64 v[142:143], s[36:37], 0, v[140:141]
	s_mov_b32 s36, 0x102000
	v_add_co_u32_e32 v128, vcc, s36, v142
	v_or_b32_e32 v237, s55, v152
	s_nop 0
	v_addc_co_u32_e32 v129, vcc, 0, v143, vcc
	v_add_u32_e32 v216, s60, v237
	flat_load_dwordx4 v[132:135], v[128:129]
	v_lshl_add_u64 v[128:129], s[38:39], 0, v[140:141]
	v_ashrrev_i32_e32 v217, 31, v216
	global_load_dwordx4 v[136:139], v[128:129], off
	v_lshlrev_b64 v[128:129], 10, v[216:217]
	v_lshl_add_u64 v[128:129], v[128:129], 0, v[218:219]
	v_lshlrev_b64 v[144:145], 2, v[128:129]
	v_lshl_add_u64 v[146:147], s[2:3], 0, v[144:145]
	global_load_dwordx4 v[128:131], v[146:147], off
	s_load_dwordx2 s[36:37], s[34:35], 0x130
	s_nop 0
	s_load_dwordx2 s[34:35], s[34:35], 0x38
	v_or_b32_e32 v148, 16, v218
	v_or_b32_e32 v158, 0x80, v218
	v_or_b32_e32 v156, 0x90, v218
	v_ashrrev_i32_e32 v149, 31, v148
	v_ashrrev_i32_e32 v159, 31, v158
	v_ashrrev_i32_e32 v157, 31, v156
	v_lshl_add_u64 v[150:151], v[148:149], 2, s[38:39]
	v_lshl_add_u64 v[154:155], v[158:159], 2, s[38:39]
	v_lshl_add_u64 v[168:169], v[156:157], 2, s[38:39]
	s_mov_b64 s[38:39], 0x102000
	global_load_dwordx4 v[160:163], v[150:151], off
	global_load_dwordx4 v[164:167], v[154:155], off
	s_nop 0
	global_load_dwordx4 v[168:171], v[168:169], off
	s_waitcnt lgkmcnt(0)
	v_lshl_add_u64 v[150:151], s[36:37], 0, v[144:145]
	v_lshl_add_u64 v[154:155], v[142:143], 0, s[38:39]
	flat_load_dwordx4 v[142:145], v[154:155] offset:64
	flat_load_dwordx4 v[172:175], v[154:155] offset:512
	flat_load_dwordx4 v[176:179], v[154:155] offset:576
	v_cmp_eq_u32_e32 vcc, 0, v153
	s_waitcnt vmcnt(0)
	v_add_f32_e64 v134, v134, v138
	v_add_f32_e64 v135, v135, v139
	v_add_f32_e64 v132, v132, v136
	v_add_f32_e64 v133, v133, v137
	v_fma_f32 v74, v74, v134, v130
	v_fma_f32 v75, v75, v135, v131
	v_fma_f32 v72, v72, v132, v128
	v_fma_f32 v73, v73, v133, v129
	global_store_dwordx4 v[150:151], v[72:75], off
	global_load_dwordx4 v[180:183], v[146:147], off offset:64
	s_waitcnt lgkmcnt(0)
	v_add_f32_e64 v130, v144, v162
	v_add_f32_e64 v131, v145, v163
	v_add_f32_e64 v138, v142, v160
	v_add_f32_e64 v139, v143, v161
	v_add_f32_e64 v142, v174, v166
	v_add_f32_e64 v143, v175, v167
	v_add_f32_e64 v144, v172, v164
	v_add_f32_e64 v145, v173, v165
	v_add_f32_e64 v136, v176, v168
	v_add_f32_e64 v137, v177, v169
	v_add_f32_e64 v128, v178, v170
	v_add_f32_e64 v129, v179, v171
	s_waitcnt vmcnt(0)
	v_fma_f32 v82, v82, v130, v182
	v_fma_f32 v83, v83, v131, v183
	v_fma_f32 v80, v80, v138, v180
	v_fma_f32 v81, v81, v139, v181
	global_store_dwordx4 v[150:151], v[80:83], off offset:64
	global_load_dwordx4 v[160:163], v[146:147], off offset:512
	s_waitcnt vmcnt(0)
	v_fma_f32 v90, v90, v142, v162
	v_fma_f32 v91, v91, v143, v163
	v_fma_f32 v88, v88, v144, v160
	v_fma_f32 v89, v89, v145, v161
	global_store_dwordx4 v[150:151], v[88:91], off offset:512
	global_load_dwordx4 v[160:163], v[146:147], off offset:576
	v_mul_f32_e32 v146, v73, v73
	v_mul_f32_e32 v147, v81, v81
	v_fmac_f32_e32 v146, v72, v72
	v_fmac_f32_e32 v147, v80, v80
	v_fmac_f32_e32 v146, v74, v74
	v_fmac_f32_e32 v147, v82, v82
	v_fmac_f32_e32 v146, v75, v75
	v_fmac_f32_e32 v147, v83, v83
	v_add_f32_e32 v146, v146, v147
	v_mul_f32_e32 v147, v89, v89
	v_fmac_f32_e32 v147, v88, v88
	v_fmac_f32_e32 v147, v90, v90
	v_fmac_f32_e32 v147, v91, v91
	v_add_f32_e32 v146, v146, v147
	s_waitcnt vmcnt(0)
	v_fma_f32 v96, v96, v136, v160
	v_fma_f32 v97, v97, v137, v161
	s_nop 0
	v_mul_f32_e32 v147, v97, v97
	v_fma_f32 v98, v98, v128, v162
	v_fma_f32 v99, v99, v129, v163
	v_fmac_f32_e32 v147, v96, v96
	v_fmac_f32_e32 v147, v98, v98
	v_fmac_f32_e32 v147, v99, v99
	v_add_f32_e32 v147, v146, v147
	ds_swizzle_b32 v154, v147 offset:swizzle(SWAP,16)
	global_store_dwordx4 v[150:151], v[96:99], off offset:576
	v_lshl_add_u32 v146, v152, 2, s67
	s_waitcnt lgkmcnt(0)
	v_add_f32_e32 v147, v147, v154
	v_mov_b32_e32 v150, v147
	s_nop 1
	v_permlane32_swap_b32_e32 v147, v150
	s_and_saveexec_b64 s[38:39], vcc
	v_add_f32_e32 v147, v147, v150
	ds_write_b32 v146, v147
	s_or_b64 exec, exec, s[38:39]
	v_or_b32_e32 v247, 16, v237
	v_add_u32_e32 v220, s60, v247
	v_ashrrev_i32_e32 v221, 31, v220
	v_lshlrev_b64 v[150:151], 10, v[220:221]
	v_lshl_add_u64 v[150:151], v[150:151], 0, v[218:219]
	v_lshlrev_b64 v[150:151], 2, v[150:151]
	v_lshl_add_u64 v[154:155], s[2:3], 0, v[150:151]
	global_load_dwordx4 v[160:163], v[154:155], off
	v_lshl_add_u64 v[150:151], s[36:37], 0, v[150:151]
	s_waitcnt vmcnt(0)
	v_fma_f32 v106, v106, v134, v162
	v_fma_f32 v107, v107, v135, v163
	v_fma_f32 v104, v104, v132, v160
	v_fma_f32 v105, v105, v133, v161
	global_store_dwordx4 v[150:151], v[104:107], off
	global_load_dwordx4 v[160:163], v[154:155], off offset:64
	v_mul_f32_e32 v147, v105, v105
	v_fmac_f32_e32 v147, v104, v104
	v_fmac_f32_e32 v147, v106, v106
	v_fmac_f32_e32 v147, v107, v107
	s_waitcnt vmcnt(0)
	v_fma_f32 v110, v110, v130, v162
	v_fma_f32 v111, v111, v131, v163
	v_fma_f32 v108, v108, v138, v160
	v_fma_f32 v109, v109, v139, v161
	global_store_dwordx4 v[150:151], v[108:111], off offset:64
	global_load_dwordx4 v[160:163], v[154:155], off offset:512
	s_waitcnt vmcnt(0)
	v_fma_f32 v118, v118, v142, v162
	v_fma_f32 v119, v119, v143, v163
	v_fma_f32 v116, v116, v144, v160
	v_fma_f32 v117, v117, v145, v161
	global_store_dwordx4 v[150:151], v[116:119], off offset:512
	global_load_dwordx4 v[160:163], v[154:155], off offset:576
	v_mul_f32_e32 v154, v109, v109
	v_fmac_f32_e32 v154, v108, v108
	v_fmac_f32_e32 v154, v110, v110
	v_fmac_f32_e32 v154, v111, v111
	v_add_f32_e32 v147, v147, v154
	v_mul_f32_e32 v154, v117, v117
	v_fmac_f32_e32 v154, v116, v116
	v_fmac_f32_e32 v154, v118, v118
	v_fmac_f32_e32 v154, v119, v119
	v_add_f32_e32 v147, v147, v154
	s_waitcnt vmcnt(0)
	v_fma_f32 v124, v124, v136, v160
	v_fma_f32 v125, v125, v137, v161
	s_nop 0
	v_mul_f32_e32 v154, v125, v125
	v_fma_f32 v126, v126, v128, v162
	v_fma_f32 v127, v127, v129, v163
	v_fmac_f32_e32 v154, v124, v124
	v_fmac_f32_e32 v154, v126, v126
	v_fmac_f32_e32 v154, v127, v127
	v_add_f32_e32 v147, v147, v154
	ds_swizzle_b32 v154, v147 offset:swizzle(SWAP,16)
	global_store_dwordx4 v[150:151], v[124:127], off offset:576
	s_waitcnt lgkmcnt(0)
	v_add_f32_e32 v147, v147, v154
	v_mov_b32_e32 v150, v147
	s_nop 1
	v_permlane32_swap_b32_e32 v147, v150
	s_and_saveexec_b64 s[38:39], vcc
	v_add_f32_e32 v147, v147, v150
	ds_write_b32 v146, v147 offset:64
	s_or_b64 exec, exec, s[38:39]
	v_or_b32_e32 v248, 32, v237
	v_add_u32_e32 v222, s60, v248
	v_ashrrev_i32_e32 v223, 31, v222
	v_lshlrev_b64 v[150:151], 10, v[222:223]
	v_lshl_add_u64 v[150:151], v[150:151], 0, v[218:219]
	v_lshlrev_b64 v[150:151], 2, v[150:151]
	v_lshl_add_u64 v[154:155], s[2:3], 0, v[150:151]
	global_load_dwordx4 v[160:163], v[154:155], off
	v_lshl_add_u64 v[150:151], s[36:37], 0, v[150:151]
	s_waitcnt vmcnt(0)
	v_fma_f32 v122, v122, v134, v162
	v_fma_f32 v123, v123, v135, v163
	v_fma_f32 v120, v120, v132, v160
	v_fma_f32 v121, v121, v133, v161
	global_store_dwordx4 v[150:151], v[120:123], off
	global_load_dwordx4 v[160:163], v[154:155], off offset:64
	v_mul_f32_e32 v147, v121, v121
	v_fmac_f32_e32 v147, v120, v120
	v_fmac_f32_e32 v147, v122, v122
	v_fmac_f32_e32 v147, v123, v123
	s_waitcnt vmcnt(0)
	v_fma_f32 v114, v114, v130, v162
	v_fma_f32 v115, v115, v131, v163
	v_fma_f32 v112, v112, v138, v160
	v_fma_f32 v113, v113, v139, v161
	global_store_dwordx4 v[150:151], v[112:115], off offset:64
	global_load_dwordx4 v[160:163], v[154:155], off offset:512
	s_waitcnt vmcnt(0)
	v_fma_f32 v102, v102, v142, v162
	v_fma_f32 v103, v103, v143, v163
	v_fma_f32 v100, v100, v144, v160
	v_fma_f32 v101, v101, v145, v161
	global_store_dwordx4 v[150:151], v[100:103], off offset:512
	global_load_dwordx4 v[160:163], v[154:155], off offset:576
	v_mul_f32_e32 v154, v113, v113
	v_fmac_f32_e32 v154, v112, v112
	v_fmac_f32_e32 v154, v114, v114
	v_fmac_f32_e32 v154, v115, v115
	v_add_f32_e32 v147, v147, v154
	v_mul_f32_e32 v154, v101, v101
	v_fmac_f32_e32 v154, v100, v100
	v_fmac_f32_e32 v154, v102, v102
	v_fmac_f32_e32 v154, v103, v103
	v_add_f32_e32 v147, v147, v154
	s_waitcnt vmcnt(0)
	v_fma_f32 v92, v92, v136, v160
	v_fma_f32 v93, v93, v137, v161
	s_nop 0
	v_mul_f32_e32 v154, v93, v93
	v_fma_f32 v94, v94, v128, v162
	v_fma_f32 v95, v95, v129, v163
	v_fmac_f32_e32 v154, v92, v92
	v_fmac_f32_e32 v154, v94, v94
	v_fmac_f32_e32 v154, v95, v95
	v_add_f32_e32 v147, v147, v154
	ds_swizzle_b32 v154, v147 offset:swizzle(SWAP,16)
	global_store_dwordx4 v[150:151], v[92:95], off offset:576
	s_waitcnt lgkmcnt(0)
	v_add_f32_e32 v147, v147, v154
	v_mov_b32_e32 v150, v147
	s_nop 1
	v_permlane32_swap_b32_e32 v147, v150
	s_and_saveexec_b64 s[38:39], vcc
	v_add_f32_e32 v147, v147, v150
	ds_write_b32 v146, v147 offset:128
	s_or_b64 exec, exec, s[38:39]
	v_or_b32_e32 v249, 48, v237
	v_add_u32_e32 v224, s60, v249
	v_ashrrev_i32_e32 v225, 31, v224
	v_lshlrev_b64 v[150:151], 10, v[224:225]
	v_lshl_add_u64 v[150:151], v[150:151], 0, v[218:219]
	v_lshlrev_b64 v[150:151], 2, v[150:151]
	v_lshl_add_u64 v[154:155], s[2:3], 0, v[150:151]
	global_load_dwordx4 v[160:163], v[154:155], off
	v_lshl_add_u64 v[150:151], s[36:37], 0, v[150:151]
	s_waitcnt vmcnt(0)
	v_fma_f32 v86, v86, v134, v162
	v_fma_f32 v87, v87, v135, v163
	v_fma_f32 v84, v84, v132, v160
	v_fma_f32 v85, v85, v133, v161
	global_store_dwordx4 v[150:151], v[84:87], off
	global_load_dwordx4 v[160:163], v[154:155], off offset:64
	v_mul_f32_e32 v147, v85, v85
	v_fmac_f32_e32 v147, v84, v84
	v_fmac_f32_e32 v147, v86, v86
	v_fmac_f32_e32 v147, v87, v87
	s_waitcnt vmcnt(0)
	v_fma_f32 v78, v78, v130, v162
	v_fma_f32 v79, v79, v131, v163
	v_fma_f32 v76, v76, v138, v160
	v_fma_f32 v77, v77, v139, v161
	global_store_dwordx4 v[150:151], v[76:79], off offset:64
	global_load_dwordx4 v[160:163], v[154:155], off offset:512
	s_waitcnt vmcnt(0)
	v_fma_f32 v70, v70, v142, v162
	v_fma_f32 v71, v71, v143, v163
	v_fma_f32 v68, v68, v144, v160
	v_fma_f32 v69, v69, v145, v161
	global_store_dwordx4 v[150:151], v[68:71], off offset:512
	global_load_dwordx4 v[160:163], v[154:155], off offset:576
	v_mul_f32_e32 v154, v77, v77
	v_fmac_f32_e32 v154, v76, v76
	v_fmac_f32_e32 v154, v78, v78
	v_fmac_f32_e32 v154, v79, v79
	v_add_f32_e32 v147, v147, v154
	v_mul_f32_e32 v154, v69, v69
	v_fmac_f32_e32 v154, v68, v68
	v_fmac_f32_e32 v154, v70, v70
	v_fmac_f32_e32 v154, v71, v71
	v_add_f32_e32 v147, v147, v154
	s_waitcnt vmcnt(0)
	v_fma_f32 v64, v64, v136, v160
	v_fma_f32 v65, v65, v137, v161
	s_nop 0
	v_mul_f32_e32 v154, v65, v65
	v_fma_f32 v66, v66, v128, v162
	v_fma_f32 v67, v67, v129, v163
	v_fmac_f32_e32 v154, v64, v64
	v_fmac_f32_e32 v154, v66, v66
	v_fmac_f32_e32 v154, v67, v67
	v_add_f32_e32 v147, v147, v154
	ds_swizzle_b32 v154, v147 offset:swizzle(SWAP,16)
	global_store_dwordx4 v[150:151], v[64:67], off offset:576
	s_waitcnt lgkmcnt(0)
	v_add_f32_e32 v147, v147, v154
	v_mov_b32_e32 v150, v147
	s_nop 1
	v_permlane32_swap_b32_e32 v147, v150
	s_and_saveexec_b64 s[38:39], vcc
	v_add_f32_e32 v147, v147, v150
	ds_write_b32 v146, v147 offset:192
	s_or_b64 exec, exec, s[38:39]
	v_add_u32_e32 v226, 0x80, v216
	v_ashrrev_i32_e32 v227, 31, v226
	v_lshlrev_b64 v[150:151], 10, v[226:227]
	v_lshl_add_u64 v[150:151], v[150:151], 0, v[218:219]
	v_lshlrev_b64 v[150:151], 2, v[150:151]
	v_lshl_add_u64 v[154:155], s[2:3], 0, v[150:151]
	global_load_dwordx4 v[160:163], v[154:155], off
	v_lshl_add_u64 v[150:151], s[36:37], 0, v[150:151]
	s_waitcnt vmcnt(0)
	v_fma_f32 v62, v62, v134, v162
	v_fma_f32 v63, v63, v135, v163
	v_fma_f32 v60, v60, v132, v160
	v_fma_f32 v61, v61, v133, v161
	global_store_dwordx4 v[150:151], v[60:63], off
	global_load_dwordx4 v[160:163], v[154:155], off offset:64
	v_mul_f32_e32 v147, v61, v61
	v_fmac_f32_e32 v147, v60, v60
	v_fmac_f32_e32 v147, v62, v62
	v_fmac_f32_e32 v147, v63, v63
	s_waitcnt vmcnt(0)
	v_fma_f32 v58, v58, v130, v162
	v_fma_f32 v59, v59, v131, v163
	v_fma_f32 v56, v56, v138, v160
	v_fma_f32 v57, v57, v139, v161
	global_store_dwordx4 v[150:151], v[56:59], off offset:64
	global_load_dwordx4 v[160:163], v[154:155], off offset:512
	s_waitcnt vmcnt(0)
	v_fma_f32 v54, v54, v142, v162
	v_fma_f32 v55, v55, v143, v163
	v_fma_f32 v52, v52, v144, v160
	v_fma_f32 v53, v53, v145, v161
	global_store_dwordx4 v[150:151], v[52:55], off offset:512
	global_load_dwordx4 v[160:163], v[154:155], off offset:576
	v_mul_f32_e32 v154, v57, v57
	v_fmac_f32_e32 v154, v56, v56
	v_fmac_f32_e32 v154, v58, v58
	v_fmac_f32_e32 v154, v59, v59
	v_add_f32_e32 v147, v147, v154
	v_mul_f32_e32 v154, v53, v53
	v_fmac_f32_e32 v154, v52, v52
	v_fmac_f32_e32 v154, v54, v54
	v_fmac_f32_e32 v154, v55, v55
	v_add_f32_e32 v147, v147, v154
	s_waitcnt vmcnt(0)
	v_fma_f32 v48, v48, v136, v160
	v_fma_f32 v49, v49, v137, v161
	s_nop 0
	v_mul_f32_e32 v154, v49, v49
	v_fma_f32 v50, v50, v128, v162
	v_fma_f32 v51, v51, v129, v163
	v_fmac_f32_e32 v154, v48, v48
	v_fmac_f32_e32 v154, v50, v50
	v_fmac_f32_e32 v154, v51, v51
	v_add_f32_e32 v147, v147, v154
	ds_swizzle_b32 v154, v147 offset:swizzle(SWAP,16)
	global_store_dwordx4 v[150:151], v[48:51], off offset:576
	s_waitcnt lgkmcnt(0)
	v_add_f32_e32 v147, v147, v154
	v_mov_b32_e32 v150, v147
	s_nop 1
	v_permlane32_swap_b32_e32 v147, v150
	s_and_saveexec_b64 s[38:39], vcc
	v_add_f32_e32 v147, v147, v150
	ds_write_b32 v146, v147 offset:512
	s_or_b64 exec, exec, s[38:39]
	v_add_u32_e32 v228, 0x90, v216
	v_ashrrev_i32_e32 v229, 31, v228
	v_lshlrev_b64 v[150:151], 10, v[228:229]
	v_lshl_add_u64 v[150:151], v[150:151], 0, v[218:219]
	v_lshlrev_b64 v[150:151], 2, v[150:151]
	v_lshl_add_u64 v[154:155], s[2:3], 0, v[150:151]
	global_load_dwordx4 v[160:163], v[154:155], off
	v_lshl_add_u64 v[150:151], s[36:37], 0, v[150:151]
	s_waitcnt vmcnt(0)
	v_fma_f32 v46, v46, v134, v162
	v_fma_f32 v47, v47, v135, v163
	v_fma_f32 v44, v44, v132, v160
	v_fma_f32 v45, v45, v133, v161
	global_store_dwordx4 v[150:151], v[44:47], off
	global_load_dwordx4 v[160:163], v[154:155], off offset:64
	v_mul_f32_e32 v147, v45, v45
	v_fmac_f32_e32 v147, v44, v44
	v_fmac_f32_e32 v147, v46, v46
	v_fmac_f32_e32 v147, v47, v47
	s_waitcnt vmcnt(0)
	v_fma_f32 v42, v42, v130, v162
	v_fma_f32 v43, v43, v131, v163
	v_fma_f32 v40, v40, v138, v160
	v_fma_f32 v41, v41, v139, v161
	global_store_dwordx4 v[150:151], v[40:43], off offset:64
	global_load_dwordx4 v[160:163], v[154:155], off offset:512
	s_waitcnt vmcnt(0)
	v_fma_f32 v38, v38, v142, v162
	v_fma_f32 v39, v39, v143, v163
	v_fma_f32 v36, v36, v144, v160
	v_fma_f32 v37, v37, v145, v161
	global_store_dwordx4 v[150:151], v[36:39], off offset:512
	global_load_dwordx4 v[160:163], v[154:155], off offset:576
	v_mul_f32_e32 v154, v41, v41
	v_fmac_f32_e32 v154, v40, v40
	v_fmac_f32_e32 v154, v42, v42
	v_fmac_f32_e32 v154, v43, v43
	v_add_f32_e32 v147, v147, v154
	v_mul_f32_e32 v154, v37, v37
	v_fmac_f32_e32 v154, v36, v36
	v_fmac_f32_e32 v154, v38, v38
	v_fmac_f32_e32 v154, v39, v39
	v_add_f32_e32 v147, v147, v154
	s_waitcnt vmcnt(0)
	v_fma_f32 v32, v32, v136, v160
	v_fma_f32 v33, v33, v137, v161
	s_nop 0
	v_mul_f32_e32 v154, v33, v33
	v_fma_f32 v34, v34, v128, v162
	v_fma_f32 v35, v35, v129, v163
	v_fmac_f32_e32 v154, v32, v32
	v_fmac_f32_e32 v154, v34, v34
	v_fmac_f32_e32 v154, v35, v35
	v_add_f32_e32 v147, v147, v154
	ds_swizzle_b32 v154, v147 offset:swizzle(SWAP,16)
	global_store_dwordx4 v[150:151], v[32:35], off offset:576
	s_waitcnt lgkmcnt(0)
	v_add_f32_e32 v147, v147, v154
	v_mov_b32_e32 v150, v147
	s_nop 1
	v_permlane32_swap_b32_e32 v147, v150
	s_and_saveexec_b64 s[38:39], vcc
	v_add_f32_e32 v147, v147, v150
	ds_write_b32 v146, v147 offset:576
	s_or_b64 exec, exec, s[38:39]
	v_add_u32_e32 v230, 0xa0, v216
	v_ashrrev_i32_e32 v231, 31, v230
	v_lshlrev_b64 v[150:151], 10, v[230:231]
	v_lshl_add_u64 v[150:151], v[150:151], 0, v[218:219]
	v_lshlrev_b64 v[150:151], 2, v[150:151]
	v_lshl_add_u64 v[154:155], s[2:3], 0, v[150:151]
	global_load_dwordx4 v[160:163], v[154:155], off
	v_lshl_add_u64 v[150:151], s[36:37], 0, v[150:151]
	s_waitcnt vmcnt(0)
	v_fma_f32 v30, v30, v134, v162
	v_fma_f32 v31, v31, v135, v163
	v_fma_f32 v28, v28, v132, v160
	v_fma_f32 v29, v29, v133, v161
	global_store_dwordx4 v[150:151], v[28:31], off
	global_load_dwordx4 v[160:163], v[154:155], off offset:64
	v_mul_f32_e32 v147, v29, v29
	v_fmac_f32_e32 v147, v28, v28
	v_fmac_f32_e32 v147, v30, v30
	v_fmac_f32_e32 v147, v31, v31
	s_waitcnt vmcnt(0)
	v_fma_f32 v26, v26, v130, v162
	v_fma_f32 v27, v27, v131, v163
	v_fma_f32 v24, v24, v138, v160
	v_fma_f32 v25, v25, v139, v161
	global_store_dwordx4 v[150:151], v[24:27], off offset:64
	global_load_dwordx4 v[160:163], v[154:155], off offset:512
	s_waitcnt vmcnt(0)
	v_fma_f32 v22, v22, v142, v162
	v_fma_f32 v23, v23, v143, v163
	v_fma_f32 v20, v20, v144, v160
	v_fma_f32 v21, v21, v145, v161
	global_store_dwordx4 v[150:151], v[20:23], off offset:512
	global_load_dwordx4 v[160:163], v[154:155], off offset:576
	v_mul_f32_e32 v154, v25, v25
	v_fmac_f32_e32 v154, v24, v24
	v_fmac_f32_e32 v154, v26, v26
	v_fmac_f32_e32 v154, v27, v27
	v_add_f32_e32 v147, v147, v154
	v_mul_f32_e32 v154, v21, v21
	v_fmac_f32_e32 v154, v20, v20
	v_fmac_f32_e32 v154, v22, v22
	v_fmac_f32_e32 v154, v23, v23
	v_add_f32_e32 v147, v147, v154
	s_waitcnt vmcnt(0)
	v_fma_f32 v16, v16, v136, v160
	v_fma_f32 v17, v17, v137, v161
	s_nop 0
	v_mul_f32_e32 v154, v17, v17
	v_fma_f32 v18, v18, v128, v162
	v_fma_f32 v19, v19, v129, v163
	v_fmac_f32_e32 v154, v16, v16
	v_fmac_f32_e32 v154, v18, v18
	v_fmac_f32_e32 v154, v19, v19
	v_add_f32_e32 v147, v147, v154
	ds_swizzle_b32 v154, v147 offset:swizzle(SWAP,16)
	global_store_dwordx4 v[150:151], v[16:19], off offset:576
	s_waitcnt lgkmcnt(0)
	v_add_f32_e32 v147, v147, v154
	v_mov_b32_e32 v150, v147
	s_nop 1
	v_permlane32_swap_b32_e32 v147, v150
	s_and_saveexec_b64 s[38:39], vcc
	v_add_f32_e32 v147, v147, v150
	ds_write_b32 v146, v147 offset:640
	s_or_b64 exec, exec, s[38:39]
	v_add_u32_e32 v232, 0xb0, v216
	v_ashrrev_i32_e32 v233, 31, v232
	v_lshlrev_b64 v[150:151], 10, v[232:233]
	v_lshl_add_u64 v[150:151], v[150:151], 0, v[218:219]
	v_lshlrev_b64 v[150:151], 2, v[150:151]
	v_lshl_add_u64 v[154:155], s[2:3], 0, v[150:151]
	global_load_dwordx4 v[160:163], v[154:155], off
	v_lshl_add_u64 v[150:151], s[36:37], 0, v[150:151]
	s_waitcnt vmcnt(0)
	v_fma_f32 v14, v14, v134, v162
	v_fma_f32 v15, v15, v135, v163
	v_fma_f32 v12, v12, v132, v160
	v_fma_f32 v13, v13, v133, v161
	global_store_dwordx4 v[150:151], v[12:15], off
	global_load_dwordx4 v[132:135], v[154:155], off offset:64
	s_waitcnt vmcnt(0)
	v_fma_f32 v10, v10, v130, v134
	v_fma_f32 v11, v11, v131, v135
	v_fma_f32 v8, v8, v138, v132
	v_fma_f32 v9, v9, v139, v133
	global_store_dwordx4 v[150:151], v[8:11], off offset:64
	global_load_dwordx4 v[130:133], v[154:155], off offset:512
	v_mul_f32_e32 v134, v13, v13
	v_mul_f32_e32 v135, v9, v9
	v_fmac_f32_e32 v134, v12, v12
	v_fmac_f32_e32 v135, v8, v8
	v_fmac_f32_e32 v134, v14, v14
	v_fmac_f32_e32 v135, v10, v10
	v_fmac_f32_e32 v134, v15, v15
	v_fmac_f32_e32 v135, v11, v11
	v_add_f32_e32 v134, v134, v135
	s_waitcnt vmcnt(0)
	v_fma_f32 v6, v6, v142, v132
	v_fma_f32 v7, v7, v143, v133
	v_fma_f32 v4, v4, v144, v130
	v_fma_f32 v5, v5, v145, v131
	global_store_dwordx4 v[150:151], v[4:7], off offset:512
	global_load_dwordx4 v[130:133], v[154:155], off offset:576
	v_mul_f32_e32 v135, v5, v5
	v_fmac_f32_e32 v135, v4, v4
	v_fmac_f32_e32 v135, v6, v6
	v_fmac_f32_e32 v135, v7, v7
	v_add_f32_e32 v134, v134, v135
	s_waitcnt vmcnt(0)
	v_fma_f32 v0, v0, v136, v130
	v_fma_f32 v1, v1, v137, v131
	v_fma_f32 v2, v2, v128, v132
	v_fma_f32 v3, v3, v129, v133
	v_mul_f32_e32 v128, v1, v1
	v_fmac_f32_e32 v128, v0, v0
	v_fmac_f32_e32 v128, v2, v2
	v_fmac_f32_e32 v128, v3, v3
	v_add_f32_e32 v128, v134, v128
	ds_swizzle_b32 v129, v128 offset:swizzle(SWAP,16)
	global_store_dwordx4 v[150:151], v[0:3], off offset:576
	s_waitcnt lgkmcnt(0)
	v_add_f32_e32 v128, v128, v129
	v_mov_b32_e32 v129, v128
	s_nop 1
	v_permlane32_swap_b32_e32 v128, v129
	s_and_saveexec_b64 s[2:3], vcc
	v_add_f32_e32 v128, v128, v129
	ds_write_b32 v146, v128 offset:704
	s_or_b64 exec, exec, s[2:3]
	s_add_u32 s36, s10, s16
	s_addc_u32 s37, s11, s17
	s_add_u32 s2, s10, s66
	s_addc_u32 s3, s11, 0
	s_add_u32 s60, s2, 0x1fa00000
	s_addc_u32 s80, s3, 0
	s_lshl_b32 s2, s76, 6
	s_ashr_i32 s3, s2, 31
	s_lshl_b64 s[2:3], s[2:3], 2
	s_add_u32 s2, s36, s2
	v_lshlrev_b32_e32 v128, 4, v153
	s_waitcnt lgkmcnt(0)
	s_barrier
	s_addc_u32 s3, s37, s3
	v_or3_b32 v234, v128, s59, v152
	s_add_u32 s36, s2, 0x30000
	s_movk_i32 s2, 0x100
	s_addc_u32 s37, s3, 0
	v_cmp_gt_i32_e64 s[2:3], s2, v234
	s_and_saveexec_b64 s[38:39], s[2:3]
	s_cbranch_execz .LBB0_1205
	v_lshlrev_b32_e32 v130, 2, v234
	v_add_u32_e32 v128, 0, v130
	v_add_u32_e32 v131, 0x21000, v128
	ds_read2st64_b32 v[128:129], v131 offset1:4
	s_lshl_b32 s81, s76, 12
	s_lshl_b32 s77, s77, 10
	s_and_b32 s61, s80, 0xffff
	s_add_i32 s81, s81, s77
	s_waitcnt lgkmcnt(0)
	v_add_f32_e32 v132, v128, v129
	ds_read2st64_b32 v[128:129], v131 offset0:8 offset1:12
	s_waitcnt lgkmcnt(0)
	v_add_f32_e32 v128, v132, v128
	v_add_f32_e32 v128, v128, v129
	buffer_store_dword v128, v130, s[60:63], s81 offen sc1
	s_waitcnt vmcnt(0)
	v_and_b32_e32 v128, 63, v234
	v_cmp_eq_u32_e32 vcc, 0, v128
	s_and_b64 exec, exec, vcc
	s_cbranch_execz .LBB0_1205
	v_mov_b64_e32 v[128:129], s[36:37]
	flat_atomic_add v[128:129], v211

.LBB0_1221:
	s_or_b64 exec, exec, s[30:31]
	s_waitcnt vmcnt(0) lgkmcnt(0)
	v_add_f32_e64 v134, v134, 1.0
	v_add_f32_e64 v135, v135, 1.0
	v_add_f32_e64 v132, v132, 1.0
	v_add_f32_e64 v133, v133, 1.0
	v_add_f32_e64 v130, v134, v130
	v_add_f32_e64 v131, v135, v131
	v_add_f32_e64 v132, v132, v128
	v_add_f32_e64 v133, v133, v129
	v_mul_f32_e64 v128, v138, v130
	v_mul_f32_e64 v129, v139, v131
	v_mul_f32_e64 v130, v136, v132
	v_mul_f32_e64 v131, v137, v133
	v_lshl_add_u64 v[132:133], v[218:219], 1, s[10:11]
	s_mov_b64 s[2:3], 0x19400000
	v_lshl_add_u64 v[132:133], v[132:133], 0, s[2:3]
	s_add_i32 s2, 0, 0x22000
	s_waitcnt lgkmcnt(0)
	s_barrier
	v_lshl_add_u32 v135, v237, 2, s2
	ds_read_b32 v134, v135
	v_add_f32_e64 v142, v158, v142
	v_add_f32_e64 v143, v159, v143
	v_add_f32_e64 v140, v156, v140
	v_add_f32_e64 v141, v157, v141
	v_add_f32_e64 v150, v150, 1.0
	v_add_f32_e64 v151, v151, 1.0
	v_add_f32_e64 v148, v148, 1.0
	v_add_f32_e64 v149, v149, 1.0
	s_waitcnt lgkmcnt(0)
	v_mul_f32_e64 v74, v74, v134
	v_mul_f32_e64 v75, v75, v134
	v_mul_f32_e64 v72, v72, v134
	v_mul_f32_e64 v73, v73, v134
	v_lshlrev_b64 v[136:137], 11, v[216:217]
	v_fma_f32 v74, v128, v74, v142
	v_fma_f32 v75, v129, v75, v143
	v_fma_f32 v72, v130, v72, v140
	v_fma_f32 v73, v131, v73, v141
	v_add_f32_e64 v150, v150, v154
	v_add_f32_e64 v151, v151, v155
	v_add_f32_e64 v148, v148, v152
	v_add_f32_e64 v149, v149, v153
	v_lshl_add_u64 v[136:137], v[132:133], 0, v[136:137]
	v_cvt_pk_bf16_f32 v72, v72, v73
	v_cvt_pk_bf16_f32 v73, v74, v75
	v_add_f32_e64 v162, v166, v162
	v_add_f32_e64 v163, v167, v163
	v_add_f32_e64 v160, v164, v160
	v_add_f32_e64 v161, v165, v161
	v_mul_f32_e64 v146, v146, v150
	v_mul_f32_e64 v147, v147, v151
	v_mul_f32_e64 v144, v144, v148
	v_mul_f32_e64 v145, v145, v149
	flat_store_dwordx2 v[136:137], v[72:73]
	v_mul_f32_e64 v72, v82, v134
	v_mul_f32_e64 v73, v83, v134
	v_mul_f32_e64 v74, v80, v134
	v_mul_f32_e64 v75, v81, v134
	v_add_f32_e64 v174, v174, 1.0
	v_add_f32_e64 v175, v175, 1.0
	v_add_f32_e64 v172, v172, 1.0
	v_add_f32_e64 v173, v173, 1.0
	v_fma_f32 v72, v146, v72, v162
	v_fma_f32 v73, v147, v73, v163
	v_fma_f32 v74, v144, v74, v160
	v_fma_f32 v75, v145, v75, v161
	v_add_f32_e64 v174, v174, v178
	v_add_f32_e64 v175, v175, v179
	v_add_f32_e64 v172, v172, v176
	v_add_f32_e64 v173, v173, v177
	v_cvt_pk_bf16_f32 v74, v74, v75
	v_cvt_pk_bf16_f32 v75, v72, v73
	v_add_f32_e64 v182, v182, v186
	v_add_f32_e64 v183, v183, v187
	v_add_f32_e64 v180, v180, v184
	v_add_f32_e64 v181, v181, v185
	v_mul_f32_e64 v170, v170, v174
	v_mul_f32_e64 v171, v171, v175
	v_mul_f32_e64 v168, v168, v172
	v_mul_f32_e64 v169, v169, v173
	flat_store_dwordx2 v[136:137], v[74:75] offset:32
	v_mul_f32_e64 v72, v90, v134
	v_mul_f32_e64 v73, v91, v134
	v_mul_f32_e64 v74, v88, v134
	v_mul_f32_e64 v75, v89, v134
	v_add_f32_e64 v194, v194, 1.0
	v_add_f32_e64 v195, v195, 1.0
	v_add_f32_e64 v192, v192, 1.0
	v_add_f32_e64 v193, v193, 1.0
	v_fma_f32 v72, v170, v72, v182
	v_fma_f32 v73, v171, v73, v183
	v_fma_f32 v74, v168, v74, v180
	v_fma_f32 v75, v169, v75, v181
	v_add_f32_e64 v194, v194, v198
	v_add_f32_e64 v195, v195, v199
	v_add_f32_e64 v192, v192, v196
	v_add_f32_e64 v193, v193, v197
	v_cvt_pk_bf16_f32 v74, v74, v75
	v_cvt_pk_bf16_f32 v75, v72, v73
	v_add_f32_e64 v202, v202, v206
	v_add_f32_e64 v203, v203, v207
	v_add_f32_e64 v200, v200, v204
	v_add_f32_e64 v201, v201, v205
	v_mul_f32_e64 v190, v190, v194
	v_mul_f32_e64 v191, v191, v195
	v_mul_f32_e64 v188, v188, v192
	v_mul_f32_e64 v189, v189, v193
	flat_store_dwordx2 v[136:137], v[74:75] offset:256
	v_mul_f32_e64 v72, v98, v134
	v_mul_f32_e64 v73, v99, v134
	v_mul_f32_e64 v74, v96, v134
	v_mul_f32_e64 v75, v97, v134
	v_fma_f32 v72, v190, v72, v202
	v_fma_f32 v73, v191, v73, v203
	v_fma_f32 v74, v188, v74, v200
	v_fma_f32 v75, v189, v75, v201
	v_readlane_b32 s78, v253, 40
	v_cvt_pk_bf16_f32 v74, v74, v75
	v_cvt_pk_bf16_f32 v75, v72, v73
	flat_store_dwordx2 v[136:137], v[74:75] offset:288
	v_lshl_add_u32 v72, v247, 2, s2
	ds_read_b32 v72, v72
	v_lshlrev_b64 v[74:75], 11, v[220:221]
	v_lshl_add_u64 v[74:75], v[132:133], 0, v[74:75]
	v_readlane_b32 s80, v253, 42
	s_andn2_b64 vcc, exec, s[0:1]
	s_waitcnt lgkmcnt(0)
	v_mul_f32_e64 v80, v106, v72
	v_mul_f32_e64 v81, v107, v72
	v_mul_f32_e64 v82, v104, v72
	v_mul_f32_e64 v83, v105, v72
	v_fma_f32 v80, v128, v80, v142
	v_fma_f32 v81, v129, v81, v143
	v_fma_f32 v82, v130, v82, v140
	v_fma_f32 v83, v131, v83, v141
	v_readlane_b32 s79, v253, 41
	v_cvt_pk_bf16_f32 v82, v82, v83
	v_cvt_pk_bf16_f32 v83, v80, v81
	flat_store_dwordx2 v[74:75], v[82:83]
	v_mul_f32_e64 v80, v110, v72
	v_mul_f32_e64 v81, v111, v72
	v_mul_f32_e64 v82, v108, v72
	v_mul_f32_e64 v83, v109, v72
	v_fma_f32 v80, v146, v80, v162
	v_fma_f32 v81, v147, v81, v163
	v_fma_f32 v82, v144, v82, v160
	v_fma_f32 v83, v145, v83, v161
	v_readlane_b32 s81, v253, 43
	v_cvt_pk_bf16_f32 v82, v82, v83
	v_cvt_pk_bf16_f32 v83, v80, v81
	flat_store_dwordx2 v[74:75], v[82:83] offset:32
	v_mul_f32_e64 v80, v118, v72
	v_mul_f32_e64 v81, v119, v72
	v_mul_f32_e64 v82, v116, v72
	v_mul_f32_e64 v83, v117, v72
	v_fma_f32 v80, v170, v80, v182
	v_fma_f32 v81, v171, v81, v183
	v_fma_f32 v82, v168, v82, v180
	v_fma_f32 v83, v169, v83, v181
	s_nop 0
	v_cvt_pk_bf16_f32 v82, v82, v83
	v_cvt_pk_bf16_f32 v83, v80, v81
	v_mul_f32_e64 v80, v126, v72
	v_mul_f32_e64 v81, v127, v72
	v_mul_f32_e64 v73, v125, v72
	v_mul_f32_e64 v72, v124, v72
	v_fma_f32 v80, v190, v80, v202
	v_fma_f32 v81, v191, v81, v203
	v_fma_f32 v72, v188, v72, v200
	v_fma_f32 v73, v189, v73, v201
	flat_store_dwordx2 v[74:75], v[82:83] offset:256
	v_cvt_pk_bf16_f32 v72, v72, v73
	v_cvt_pk_bf16_f32 v73, v80, v81
	flat_store_dwordx2 v[74:75], v[72:73] offset:288
	v_lshl_add_u32 v72, v248, 2, s2
	ds_read_b32 v72, v72
	v_lshlrev_b64 v[74:75], 11, v[222:223]
	v_lshl_add_u64 v[74:75], v[132:133], 0, v[74:75]
	s_waitcnt lgkmcnt(0)
	v_mul_f32_e64 v80, v122, v72
	v_mul_f32_e64 v81, v123, v72
	v_mul_f32_e64 v82, v120, v72
	v_mul_f32_e64 v83, v121, v72
	v_fma_f32 v80, v128, v80, v142
	v_fma_f32 v81, v129, v81, v143
	v_fma_f32 v82, v130, v82, v140
	v_fma_f32 v83, v131, v83, v141
	s_nop 0
	v_cvt_pk_bf16_f32 v82, v82, v83
	v_cvt_pk_bf16_f32 v83, v80, v81
	flat_store_dwordx2 v[74:75], v[82:83]
	v_mul_f32_e64 v80, v114, v72
	v_mul_f32_e64 v81, v115, v72
	v_mul_f32_e64 v82, v112, v72
	v_mul_f32_e64 v83, v113, v72
	v_fma_f32 v80, v146, v80, v162
	v_fma_f32 v81, v147, v81, v163
	v_fma_f32 v82, v144, v82, v160
	v_fma_f32 v83, v145, v83, v161
	s_nop 0
	v_cvt_pk_bf16_f32 v82, v82, v83
	v_cvt_pk_bf16_f32 v83, v80, v81
	flat_store_dwordx2 v[74:75], v[82:83] offset:32
	v_mul_f32_e64 v80, v102, v72
	v_mul_f32_e64 v81, v103, v72
	v_mul_f32_e64 v82, v100, v72
	v_mul_f32_e64 v83, v101, v72
	v_fma_f32 v80, v170, v80, v182
	v_fma_f32 v81, v171, v81, v183
	v_fma_f32 v82, v168, v82, v180
	v_fma_f32 v83, v169, v83, v181
	s_nop 0
	v_cvt_pk_bf16_f32 v82, v82, v83
	v_cvt_pk_bf16_f32 v83, v80, v81
	v_mul_f32_e64 v80, v94, v72
	v_mul_f32_e64 v81, v95, v72
	v_mul_f32_e64 v73, v93, v72
	v_mul_f32_e64 v72, v92, v72
	v_fma_f32 v80, v190, v80, v202
	v_fma_f32 v81, v191, v81, v203
	v_fma_f32 v72, v188, v72, v200
	v_fma_f32 v73, v189, v73, v201
	flat_store_dwordx2 v[74:75], v[82:83] offset:256
	v_cvt_pk_bf16_f32 v72, v72, v73
	v_cvt_pk_bf16_f32 v73, v80, v81
	flat_store_dwordx2 v[74:75], v[72:73] offset:288
	v_lshl_add_u32 v72, v249, 2, s2
	ds_read_b32 v72, v72
	v_lshlrev_b64 v[74:75], 11, v[224:225]
	v_lshl_add_u64 v[74:75], v[132:133], 0, v[74:75]
	s_mov_b64 s[2:3], -1
	s_waitcnt lgkmcnt(0)
	v_mul_f32_e64 v80, v86, v72
	v_mul_f32_e64 v81, v87, v72
	v_mul_f32_e64 v82, v84, v72
	v_mul_f32_e64 v83, v85, v72
	v_mul_f32_e64 v78, v78, v72
	v_mul_f32_e64 v79, v79, v72
	v_mul_f32_e64 v76, v76, v72
	v_mul_f32_e64 v77, v77, v72
	v_mul_f32_e64 v70, v70, v72
	v_mul_f32_e64 v71, v71, v72
	v_mul_f32_e64 v68, v68, v72
	v_mul_f32_e64 v69, v69, v72
	v_mul_f32_e64 v66, v66, v72
	v_mul_f32_e64 v67, v67, v72
	v_mul_f32_e64 v64, v64, v72
	v_mul_f32_e64 v65, v65, v72
	v_fma_f32 v80, v128, v80, v142
	v_fma_f32 v81, v129, v81, v143
	v_fma_f32 v82, v130, v82, v140
	v_fma_f32 v83, v131, v83, v141
	v_fma_f32 v78, v146, v78, v162
	v_fma_f32 v79, v147, v79, v163
	v_fma_f32 v76, v144, v76, v160
	v_fma_f32 v77, v145, v77, v161
	v_fma_f32 v70, v170, v70, v182
	v_fma_f32 v71, v171, v71, v183
	v_fma_f32 v68, v168, v68, v180
	v_fma_f32 v69, v169, v69, v181
	v_fma_f32 v66, v190, v66, v202
	v_fma_f32 v67, v191, v67, v203
	v_fma_f32 v64, v188, v64, v200
	v_fma_f32 v65, v189, v65, v201
	v_cvt_pk_bf16_f32 v82, v82, v83
	v_cvt_pk_bf16_f32 v83, v80, v81
	v_cvt_pk_bf16_f32 v76, v76, v77
	v_cvt_pk_bf16_f32 v77, v78, v79
	v_cvt_pk_bf16_f32 v68, v68, v69
	v_cvt_pk_bf16_f32 v69, v70, v71
	v_cvt_pk_bf16_f32 v64, v64, v65
	v_cvt_pk_bf16_f32 v65, v66, v67
	flat_store_dwordx2 v[74:75], v[82:83]
	flat_store_dwordx2 v[74:75], v[76:77] offset:32
	flat_store_dwordx2 v[74:75], v[68:69] offset:256
	flat_store_dwordx2 v[74:75], v[64:65] offset:288
	ds_read_b32 v64, v135 offset:512
	v_lshlrev_b64 v[66:67], 11, v[226:227]
	v_lshl_add_u64 v[66:67], v[132:133], 0, v[66:67]
	s_waitcnt lgkmcnt(0)
	v_mul_f32_e64 v62, v62, v64
	v_mul_f32_e64 v63, v63, v64
	v_mul_f32_e64 v60, v60, v64
	v_mul_f32_e64 v61, v61, v64
	v_mul_f32_e64 v58, v58, v64
	v_mul_f32_e64 v59, v59, v64
	v_mul_f32_e64 v56, v56, v64
	v_mul_f32_e64 v57, v57, v64
	v_mul_f32_e64 v54, v54, v64
	v_mul_f32_e64 v55, v55, v64
	v_mul_f32_e64 v52, v52, v64
	v_mul_f32_e64 v53, v53, v64
	v_mul_f32_e64 v50, v50, v64
	v_mul_f32_e64 v51, v51, v64
	v_mul_f32_e64 v48, v48, v64
	v_mul_f32_e64 v49, v49, v64
	v_fma_f32 v62, v128, v62, v142
	v_fma_f32 v63, v129, v63, v143
	v_fma_f32 v60, v130, v60, v140
	v_fma_f32 v61, v131, v61, v141
	v_fma_f32 v58, v146, v58, v162
	v_fma_f32 v59, v147, v59, v163
	v_fma_f32 v56, v144, v56, v160
	v_fma_f32 v57, v145, v57, v161
	v_fma_f32 v54, v170, v54, v182
	v_fma_f32 v55, v171, v55, v183
	v_fma_f32 v52, v168, v52, v180
	v_fma_f32 v53, v169, v53, v181
	v_fma_f32 v50, v190, v50, v202
	v_fma_f32 v51, v191, v51, v203
	v_fma_f32 v48, v188, v48, v200
	v_fma_f32 v49, v189, v49, v201
	v_cvt_pk_bf16_f32 v60, v60, v61
	v_cvt_pk_bf16_f32 v61, v62, v63
	v_cvt_pk_bf16_f32 v56, v56, v57
	v_cvt_pk_bf16_f32 v57, v58, v59
	v_cvt_pk_bf16_f32 v52, v52, v53
	v_cvt_pk_bf16_f32 v53, v54, v55
	v_cvt_pk_bf16_f32 v48, v48, v49
	v_cvt_pk_bf16_f32 v49, v50, v51
	flat_store_dwordx2 v[66:67], v[60:61]
	flat_store_dwordx2 v[66:67], v[56:57] offset:32
	flat_store_dwordx2 v[66:67], v[52:53] offset:256
	flat_store_dwordx2 v[66:67], v[48:49] offset:288
	ds_read_b32 v48, v135 offset:576
	v_lshlrev_b64 v[50:51], 11, v[228:229]
	v_lshl_add_u64 v[50:51], v[132:133], 0, v[50:51]
	s_waitcnt lgkmcnt(0)
	v_mul_f32_e64 v46, v46, v48
	v_mul_f32_e64 v47, v47, v48
	v_mul_f32_e64 v44, v44, v48
	v_mul_f32_e64 v45, v45, v48
	v_mul_f32_e64 v42, v42, v48
	v_mul_f32_e64 v43, v43, v48
	v_mul_f32_e64 v40, v40, v48
	v_mul_f32_e64 v41, v41, v48
	v_mul_f32_e64 v38, v38, v48
	v_mul_f32_e64 v39, v39, v48
	v_mul_f32_e64 v36, v36, v48
	v_mul_f32_e64 v37, v37, v48
	v_mul_f32_e64 v34, v34, v48
	v_mul_f32_e64 v35, v35, v48
	v_mul_f32_e64 v32, v32, v48
	v_mul_f32_e64 v33, v33, v48
	v_fma_f32 v46, v128, v46, v142
	v_fma_f32 v47, v129, v47, v143
	v_fma_f32 v44, v130, v44, v140
	v_fma_f32 v45, v131, v45, v141
	v_fma_f32 v42, v146, v42, v162
	v_fma_f32 v43, v147, v43, v163
	v_fma_f32 v40, v144, v40, v160
	v_fma_f32 v41, v145, v41, v161
	v_fma_f32 v38, v170, v38, v182
	v_fma_f32 v39, v171, v39, v183
	v_fma_f32 v36, v168, v36, v180
	v_fma_f32 v37, v169, v37, v181
	v_fma_f32 v34, v190, v34, v202
	v_fma_f32 v35, v191, v35, v203
	v_fma_f32 v32, v188, v32, v200
	v_fma_f32 v33, v189, v33, v201
	v_cvt_pk_bf16_f32 v44, v44, v45
	v_cvt_pk_bf16_f32 v45, v46, v47
	v_cvt_pk_bf16_f32 v40, v40, v41
	v_cvt_pk_bf16_f32 v41, v42, v43
	v_cvt_pk_bf16_f32 v36, v36, v37
	v_cvt_pk_bf16_f32 v37, v38, v39
	v_cvt_pk_bf16_f32 v32, v32, v33
	v_cvt_pk_bf16_f32 v33, v34, v35
	flat_store_dwordx2 v[50:51], v[44:45]
	flat_store_dwordx2 v[50:51], v[40:41] offset:32
	flat_store_dwordx2 v[50:51], v[36:37] offset:256
	flat_store_dwordx2 v[50:51], v[32:33] offset:288
	ds_read_b32 v32, v135 offset:640
	v_lshlrev_b64 v[34:35], 11, v[230:231]
	v_lshl_add_u64 v[34:35], v[132:133], 0, v[34:35]
	s_waitcnt lgkmcnt(0)
	v_mul_f32_e64 v30, v30, v32
	v_mul_f32_e64 v31, v31, v32
	v_mul_f32_e64 v28, v28, v32
	v_mul_f32_e64 v29, v29, v32
	v_mul_f32_e64 v26, v26, v32
	v_mul_f32_e64 v27, v27, v32
	v_mul_f32_e64 v24, v24, v32
	v_mul_f32_e64 v25, v25, v32
	v_mul_f32_e64 v22, v22, v32
	v_mul_f32_e64 v23, v23, v32
	v_mul_f32_e64 v20, v20, v32
	v_mul_f32_e64 v21, v21, v32
	v_mul_f32_e64 v18, v18, v32
	v_mul_f32_e64 v19, v19, v32
	v_mul_f32_e64 v16, v16, v32
	v_mul_f32_e64 v17, v17, v32
	v_fma_f32 v30, v128, v30, v142
	v_fma_f32 v31, v129, v31, v143
	v_fma_f32 v28, v130, v28, v140
	v_fma_f32 v29, v131, v29, v141
	v_fma_f32 v26, v146, v26, v162
	v_fma_f32 v27, v147, v27, v163
	v_fma_f32 v24, v144, v24, v160
	v_fma_f32 v25, v145, v25, v161
	v_fma_f32 v22, v170, v22, v182
	v_fma_f32 v23, v171, v23, v183
	v_fma_f32 v20, v168, v20, v180
	v_fma_f32 v21, v169, v21, v181
	v_fma_f32 v18, v190, v18, v202
	v_fma_f32 v19, v191, v19, v203
	v_fma_f32 v16, v188, v16, v200
	v_fma_f32 v17, v189, v17, v201
	v_cvt_pk_bf16_f32 v28, v28, v29
	v_cvt_pk_bf16_f32 v29, v30, v31
	v_cvt_pk_bf16_f32 v24, v24, v25
	v_cvt_pk_bf16_f32 v25, v26, v27
	v_cvt_pk_bf16_f32 v20, v20, v21
	v_cvt_pk_bf16_f32 v21, v22, v23
	v_cvt_pk_bf16_f32 v16, v16, v17
	v_cvt_pk_bf16_f32 v17, v18, v19
	flat_store_dwordx2 v[34:35], v[28:29]
	flat_store_dwordx2 v[34:35], v[24:25] offset:32
	flat_store_dwordx2 v[34:35], v[20:21] offset:256
	flat_store_dwordx2 v[34:35], v[16:17] offset:288
	ds_read_b32 v16, v135 offset:704
	v_lshlrev_b64 v[18:19], 11, v[232:233]
	v_lshl_add_u64 v[18:19], v[132:133], 0, v[18:19]
	s_waitcnt lgkmcnt(0)
	v_mul_f32_e64 v14, v14, v16
	v_mul_f32_e64 v15, v15, v16
	v_mul_f32_e64 v12, v12, v16
	v_mul_f32_e64 v13, v13, v16
	v_mul_f32_e64 v10, v10, v16
	v_mul_f32_e64 v11, v11, v16
	v_mul_f32_e64 v8, v8, v16
	v_mul_f32_e64 v9, v9, v16
	v_mul_f32_e64 v6, v6, v16
	v_mul_f32_e64 v7, v7, v16
	v_mul_f32_e64 v4, v4, v16
	v_mul_f32_e64 v5, v5, v16
	v_mul_f32_e64 v2, v2, v16
	v_mul_f32_e64 v3, v3, v16
	v_mul_f32_e64 v0, v0, v16
	v_mul_f32_e64 v1, v1, v16
	v_fma_f32 v14, v128, v14, v142
	v_fma_f32 v15, v129, v15, v143
	v_fma_f32 v12, v130, v12, v140
	v_fma_f32 v13, v131, v13, v141
	v_fma_f32 v10, v146, v10, v162
	v_fma_f32 v11, v147, v11, v163
	v_fma_f32 v8, v144, v8, v160
	v_fma_f32 v9, v145, v9, v161
	v_fma_f32 v6, v170, v6, v182
	v_fma_f32 v7, v171, v7, v183
	v_fma_f32 v4, v168, v4, v180
	v_fma_f32 v5, v169, v5, v181
	v_fma_f32 v2, v190, v2, v202
	v_fma_f32 v3, v191, v3, v203
	v_fma_f32 v0, v188, v0, v200
	v_fma_f32 v1, v189, v1, v201
	v_cvt_pk_bf16_f32 v12, v12, v13
	v_cvt_pk_bf16_f32 v13, v14, v15
	v_cvt_pk_bf16_f32 v8, v8, v9
	v_cvt_pk_bf16_f32 v9, v10, v11
	v_cvt_pk_bf16_f32 v4, v4, v5
	v_cvt_pk_bf16_f32 v5, v6, v7
	v_cvt_pk_bf16_f32 v0, v0, v1
	v_cvt_pk_bf16_f32 v1, v2, v3
	flat_store_dwordx2 v[18:19], v[12:13]
	flat_store_dwordx2 v[18:19], v[8:9] offset:32
	flat_store_dwordx2 v[18:19], v[4:5] offset:256
	flat_store_dwordx2 v[18:19], v[0:1] offset:288
	s_cbranch_vccnz .LBB0_1175
	s_andn2_b64 vcc, exec, s[18:19]
	s_cbranch_vccnz .LBB0_1174
	s_barrier
	s_branch .LBB0_1174

.LBB0_1287:
	s_ashr_i32 s8, s26, 31
	s_lshr_b32 s8, s8, 20
	s_add_i32 s8, s26, s8
	s_ashr_i32 s10, s8, 12
	s_cmp_eq_u32 s10, s40
	s_cbranch_scc1 .LBB0_1289
	s_waitcnt vmcnt(5)
	v_mov_b64_e32 v[126:127], v[122:123]
	v_mov_b64_e32 v[124:125], v[120:121]
	v_mov_b64_e32 v[122:123], v[118:119]
	v_mov_b64_e32 v[120:121], v[116:117]
	v_mov_b64_e32 v[118:119], v[114:115]
	v_mov_b64_e32 v[116:117], v[112:113]
	v_mov_b64_e32 v[114:115], v[110:111]
	v_mov_b64_e32 v[112:113], v[108:109]
	v_mov_b64_e32 v[110:111], v[106:107]
	v_mov_b64_e32 v[108:109], v[104:105]
	v_mov_b64_e32 v[106:107], v[102:103]
	v_mov_b64_e32 v[104:105], v[100:101]
	v_mov_b64_e32 v[102:103], v[98:99]
	v_mov_b64_e32 v[100:101], v[96:97]
	v_mov_b64_e32 v[98:99], v[94:95]
	v_mov_b64_e32 v[96:97], v[92:93]
	v_mov_b64_e32 v[94:95], v[90:91]
	v_mov_b64_e32 v[92:93], v[88:89]
	v_mov_b64_e32 v[90:91], v[86:87]
	v_mov_b64_e32 v[88:89], v[84:85]
	v_mov_b64_e32 v[86:87], v[82:83]
	v_mov_b64_e32 v[84:85], v[80:81]
	v_mov_b64_e32 v[82:83], v[78:79]
	v_mov_b64_e32 v[80:81], v[76:77]
	v_mov_b64_e32 v[78:79], v[74:75]
	v_mov_b64_e32 v[76:77], v[72:73]
	v_mov_b64_e32 v[74:75], v[70:71]
	v_mov_b64_e32 v[72:73], v[68:69]
	v_mov_b64_e32 v[70:71], v[66:67]
	v_mov_b64_e32 v[68:69], v[64:65]
	v_mov_b64_e32 v[66:67], v[62:63]
	v_mov_b64_e32 v[64:65], v[60:61]
	v_mov_b64_e32 v[62:63], v[58:59]
	v_mov_b64_e32 v[60:61], v[56:57]
	v_mov_b64_e32 v[58:59], v[54:55]
	v_mov_b64_e32 v[56:57], v[52:53]
	v_mov_b64_e32 v[54:55], v[50:51]
	v_mov_b64_e32 v[52:53], v[48:49]
	v_mov_b64_e32 v[50:51], v[46:47]
	s_mul_i32 s8, s10, 0x1800
	v_mov_b64_e32 v[48:49], v[44:45]
	v_mov_b64_e32 v[46:47], v[42:43]
	s_ashr_i32 s9, s8, 31
	v_mov_b64_e32 v[44:45], v[40:41]
	v_mov_b64_e32 v[42:43], v[38:39]
	s_lshl_b64 s[8:9], s[8:9], 2
	v_mov_b64_e32 v[40:41], v[36:37]
	v_mov_b64_e32 v[38:39], v[34:35]
	s_add_u32 s8, s38, s8
	v_mov_b64_e32 v[36:37], v[32:33]
	v_mov_b64_e32 v[34:35], v[30:31]
	s_addc_u32 s9, s39, s9
	v_mov_b64_e32 v[32:33], v[28:29]
	v_mov_b64_e32 v[30:31], v[26:27]
	v_lshl_add_u64 v[130:131], s[8:9], 0, v[208:209]
	s_mov_b64 s[8:9], 0x4000
	v_mov_b64_e32 v[28:29], v[24:25]
	v_mov_b64_e32 v[26:27], v[22:23]
	v_lshl_add_u64 v[128:129], v[130:131], 0, s[8:9]
	s_movk_i32 s8, 0x4000
	v_mov_b64_e32 v[24:25], v[20:21]
	v_mov_b64_e32 v[22:23], v[18:19]
	v_add_co_u32_e32 v132, vcc, s8, v130
	s_mov_b64 s[8:9], 0x3000
	v_mov_b64_e32 v[20:21], v[16:17]
	v_mov_b64_e32 v[18:19], v[14:15]
	v_lshl_add_u64 v[0:1], v[130:131], 0, s[8:9]
	s_movk_i32 s8, 0x3000
	v_mov_b64_e32 v[16:17], v[12:13]
	v_mov_b64_e32 v[14:15], v[10:11]
	v_add_co_u32_e64 v2, s[8:9], s8, v130
	v_mov_b64_e32 v[12:13], v[8:9]
	v_mov_b64_e32 v[10:11], v[6:7]
	v_addc_co_u32_e64 v3, s[8:9], 0, v131, s[8:9]
	v_addc_co_u32_e32 v133, vcc, 0, v131, vcc
	v_mov_b64_e32 v[8:9], v[4:5]
	v_mov_b64_e32 v[4:5], v[202:203]
	global_load_dwordx4 v[134:137], v[2:3], off
	global_load_dwordx4 v[138:141], v[248:249], off
	global_load_dwordx4 v[142:145], v[248:249], off offset:1024
	global_load_dwordx4 v[146:149], v[128:129], off offset:1024
	global_load_dwordx4 v[150:153], v[128:129], off offset:2048
	global_load_dwordx4 v[154:157], v[0:1], off offset:1024
	global_load_dwordx4 v[158:161], v[0:1], off offset:2048
	global_load_dwordx4 v[162:165], v[0:1], off offset:3072
	global_load_dwordx4 v[166:169], v[248:249], off offset:2048
	global_load_dwordx4 v[170:173], v[248:249], off offset:3072
	v_mov_b64_e32 v[6:7], v[204:205]
	global_load_dwordx4 v[202:205], v[132:133], off
	global_load_dwordx4 v[216:219], v[206:207], off offset:1024
	s_load_dwordx2 s[8:9], s[24:25], 0x38
	global_load_dwordx4 v[220:223], v[206:207], off offset:2048
	global_load_dwordx4 v[224:227], v[128:129], off offset:3072
	global_load_dwordx4 v[228:231], v[206:207], off
	s_mov_b32 s40, s10
	s_waitcnt lgkmcnt(0)
	s_add_u32 s8, s8, s28
	s_addc_u32 s9, s9, s29
	global_load_dwordx4 v[232:235], v208, s[8:9] offset:1024
	global_load_dwordx4 v[244:247], v208, s[8:9] offset:2048
	global_load_dwordx4 v[212:215], v[206:207], off offset:3072
	global_load_dwordx4 v[194:197], v208, s[8:9]
	global_load_dwordx4 v[0:3], v208, s[8:9] offset:3072
	s_waitcnt vmcnt(18)
	v_add_f32_e64 v128, v134, v138
	v_add_f32_e64 v129, v135, v139
	v_add_f32_e64 v130, v136, v140
	v_add_f32_e64 v131, v137, v141
	s_waitcnt vmcnt(16)
	v_add_f32_e64 v148, v148, 1.0
	v_add_f32_e64 v149, v149, 1.0
	s_waitcnt vmcnt(15)
	v_add_f32_e64 v150, v150, 1.0
	v_add_f32_e64 v151, v151, 1.0
	s_waitcnt vmcnt(14)
	v_add_f32_e64 v134, v156, v144
	v_add_f32_e64 v135, v157, v145
	v_add_f32_e64 v132, v154, v142
	v_add_f32_e64 v133, v155, v143
	v_add_f32_e64 v144, v152, 1.0
	v_add_f32_e64 v145, v153, 1.0
	v_add_f32_e64 v146, v146, 1.0
	v_add_f32_e64 v147, v147, 1.0
	s_waitcnt vmcnt(11)
	v_add_f32_e64 v138, v160, v168
	v_add_f32_e64 v139, v161, v169
	s_waitcnt vmcnt(9)
	v_add_f32_e64 v152, v204, 1.0
	v_add_f32_e64 v153, v205, 1.0
	v_add_f32_e64 v154, v202, 1.0
	v_add_f32_e64 v155, v203, 1.0
	v_mov_b64_e32 v[204:205], v[6:7]
	v_mov_b64_e32 v[202:203], v[4:5]
	v_mov_b64_e32 v[4:5], v[8:9]
	v_mov_b64_e32 v[6:7], v[10:11]
	v_mov_b64_e32 v[8:9], v[12:13]
	v_mov_b64_e32 v[10:11], v[14:15]
	v_mov_b64_e32 v[12:13], v[16:17]
	v_mov_b64_e32 v[14:15], v[18:19]
	v_mov_b64_e32 v[16:17], v[20:21]
	v_mov_b64_e32 v[18:19], v[22:23]
	v_mov_b64_e32 v[20:21], v[24:25]
	v_mov_b64_e32 v[22:23], v[26:27]
	v_mov_b64_e32 v[24:25], v[28:29]
	v_mov_b64_e32 v[26:27], v[30:31]
	v_mov_b64_e32 v[28:29], v[32:33]
	v_mov_b64_e32 v[30:31], v[34:35]
	v_mov_b64_e32 v[32:33], v[36:37]
	v_mov_b64_e32 v[34:35], v[38:39]
	v_mov_b64_e32 v[36:37], v[40:41]
	v_mov_b64_e32 v[38:39], v[42:43]
	v_mov_b64_e32 v[40:41], v[44:45]
	v_mov_b64_e32 v[42:43], v[46:47]
	v_mov_b64_e32 v[44:45], v[48:49]
	v_mov_b64_e32 v[46:47], v[50:51]
	v_mov_b64_e32 v[48:49], v[52:53]
	v_mov_b64_e32 v[50:51], v[54:55]
	v_mov_b64_e32 v[52:53], v[56:57]
	v_mov_b64_e32 v[54:55], v[58:59]
	v_mov_b64_e32 v[56:57], v[60:61]
	v_mov_b64_e32 v[58:59], v[62:63]
	v_mov_b64_e32 v[60:61], v[64:65]
	v_mov_b64_e32 v[62:63], v[66:67]
	v_mov_b64_e32 v[64:65], v[68:69]
	v_mov_b64_e32 v[66:67], v[70:71]
	v_mov_b64_e32 v[68:69], v[72:73]
	v_mov_b64_e32 v[70:71], v[74:75]
	v_mov_b64_e32 v[72:73], v[76:77]
	v_mov_b64_e32 v[74:75], v[78:79]
	v_mov_b64_e32 v[76:77], v[80:81]
	v_mov_b64_e32 v[78:79], v[82:83]
	v_mov_b64_e32 v[80:81], v[84:85]
	v_mov_b64_e32 v[82:83], v[86:87]
	v_mov_b64_e32 v[84:85], v[88:89]
	v_mov_b64_e32 v[86:87], v[90:91]
	v_mov_b64_e32 v[88:89], v[92:93]
	v_mov_b64_e32 v[90:91], v[94:95]
	v_mov_b64_e32 v[92:93], v[96:97]
	v_mov_b64_e32 v[94:95], v[98:99]
	v_mov_b64_e32 v[96:97], v[100:101]
	v_mov_b64_e32 v[98:99], v[102:103]
	v_mov_b64_e32 v[100:101], v[104:105]
	v_mov_b64_e32 v[102:103], v[106:107]
	v_mov_b64_e32 v[104:105], v[108:109]
	v_mov_b64_e32 v[106:107], v[110:111]
	v_mov_b64_e32 v[108:109], v[112:113]
	v_mov_b64_e32 v[110:111], v[114:115]
	v_mov_b64_e32 v[112:113], v[116:117]
	v_add_f32_e64 v142, v164, v172
	v_add_f32_e64 v143, v165, v173
	v_add_f32_e64 v140, v162, v170
	v_add_f32_e64 v141, v163, v171
	v_mov_b64_e32 v[114:115], v[118:119]
	v_mov_b64_e32 v[116:117], v[120:121]
	s_waitcnt vmcnt(8)
	v_add_f32_e64 v148, v148, v218
	v_add_f32_e64 v149, v149, v219
	s_waitcnt vmcnt(7)
	v_add_f32_e64 v160, v150, v220
	v_add_f32_e64 v161, v151, v221
	s_waitcnt vmcnt(6)
	v_add_f32_e64 v162, v226, 1.0
	v_add_f32_e64 v163, v227, 1.0
	v_add_f32_e64 v164, v224, 1.0
	v_add_f32_e64 v165, v225, 1.0
	v_add_f32_e64 v136, v158, v166
	v_add_f32_e64 v137, v159, v167
	v_mov_b64_e32 v[118:119], v[122:123]
	v_mov_b64_e32 v[120:121], v[124:125]
	v_add_f32_e64 v156, v146, v216
	v_add_f32_e64 v157, v147, v217
	v_add_f32_e64 v158, v144, v222
	v_add_f32_e64 v159, v145, v223
	s_waitcnt vmcnt(5)
	v_add_f32_e64 v152, v152, v230
	v_add_f32_e64 v153, v153, v231
	v_add_f32_e64 v154, v154, v228
	v_add_f32_e64 v155, v155, v229
	s_waitcnt vmcnt(4)
	v_mul_f32_e64 v146, v234, v148
	v_mul_f32_e64 v147, v235, v149
	s_waitcnt vmcnt(3)
	v_mul_f32_e64 v148, v244, v160
	v_mul_f32_e64 v149, v245, v161
	s_waitcnt vmcnt(2)
	v_add_f32_e64 v160, v162, v214
	v_add_f32_e64 v161, v163, v215
	v_add_f32_e64 v162, v164, v212
	v_add_f32_e64 v163, v165, v213
	v_mov_b64_e32 v[122:123], v[126:127]
	v_mul_f32_e64 v144, v232, v156
	v_mul_f32_e64 v145, v233, v157
	v_mul_f32_e64 v150, v246, v158
	v_mul_f32_e64 v151, v247, v159
	s_waitcnt vmcnt(1)
	v_mul_f32_e64 v158, v196, v152
	v_mul_f32_e64 v159, v197, v153
	v_mul_f32_e64 v156, v194, v154
	v_mul_f32_e64 v157, v195, v155
	s_waitcnt vmcnt(0)
	v_mul_f32_e64 v154, v2, v160
	v_mul_f32_e64 v155, v3, v161
	v_mul_f32_e64 v152, v0, v162
	v_mul_f32_e64 v153, v1, v163

.LBB0_1291:
	v_mul_f32_e32 v0, v189, v189
	v_mul_f32_e32 v1, v185, v185
	v_fmac_f32_e32 v0, v188, v188
	v_fmac_f32_e32 v1, v184, v184
	v_fmac_f32_e32 v0, v190, v190
	v_fmac_f32_e32 v1, v186, v186
	v_fmac_f32_e32 v0, v191, v191
	v_fmac_f32_e32 v1, v187, v187
	v_add_f32_e32 v0, v1, v0
	v_mul_f32_e32 v1, v181, v181
	v_fmac_f32_e32 v1, v180, v180
	v_fmac_f32_e32 v1, v182, v182
	v_fmac_f32_e32 v1, v183, v183
	v_add_f32_e32 v0, v1, v0
	v_mul_f32_e32 v1, v177, v177
	v_fmac_f32_e32 v1, v176, v176
	v_fmac_f32_e32 v1, v178, v178
	v_fmac_f32_e32 v1, v179, v179
	v_add_f32_e32 v0, v1, v0
	ds_swizzle_b32 v1, v0 offset:swizzle(SWAP,1)
	v_add_u32_e32 v194, 0, v193
	s_mov_b32 s8, s62
	s_waitcnt lgkmcnt(0)
	v_add_f32_e32 v0, v0, v1
	ds_swizzle_b32 v1, v0 offset:swizzle(SWAP,2)
	s_waitcnt lgkmcnt(0)
	v_add_f32_e32 v0, v0, v1
	ds_swizzle_b32 v1, v0 offset:swizzle(SWAP,4)
	s_waitcnt lgkmcnt(0)
	v_add_f32_e32 v0, v0, v1
	ds_swizzle_b32 v1, v0 offset:swizzle(SWAP,8)
	s_waitcnt lgkmcnt(0)
	v_add_f32_e32 v0, v0, v1
	ds_swizzle_b32 v1, v0 offset:swizzle(SWAP,16)
	s_waitcnt lgkmcnt(0)
	v_add_f32_e32 v0, v0, v1
	v_mov_b32_e32 v1, v0
	s_nop 1
	v_permlane32_swap_b32_e32 v0, v1
	v_add_f32_e32 v0, v0, v1
	v_fmamk_f32 v0, v0, 0x3a800000, v210
	v_cmp_gt_f32_e32 vcc, s56, v0
	v_mul_f32_e32 v1, 0x4b800000, v0
	s_nop 0
	v_cndmask_b32_e32 v0, v0, v1, vcc
	v_rsq_f32_e32 v0, v0
	s_nop 0
	v_mul_f32_e32 v1, 0x45800000, v0
	v_cndmask_b32_e32 v0, v0, v1, vcc
	v_add_u32_e32 v1, 0x10000, v194
	v_mul_f32_e64 v2, v188, v0
	v_mul_f32_e64 v3, v189, v0
	v_mul_f32_e64 v188, v190, v0
	v_mul_f32_e64 v189, v191, v0
	v_fma_f32 v190, v156, v2, v128
	v_fma_f32 v191, v157, v3, v129
	v_fma_f32 v188, v158, v188, v130
	v_fma_f32 v189, v159, v189, v131
	v_cvt_pk_fp8_f32 v2, v190, v191
	v_fma_f32 v195, v9, v190, 0
	v_fma_f32 v196, v10, v190, 0
	v_fmac_f32_e32 v195, v203, v191
	v_cvt_pk_fp8_f32 v2, v188, v189 op_sel:[0,0,1]
	v_fmac_f32_e32 v196, v204, v191
	v_fmac_f32_e32 v195, v25, v188
	v_fmac_f32_e32 v196, v26, v188
	ds_write_b32 v1, v2
	v_mul_f32_e64 v2, v184, v0
	v_mul_f32_e64 v3, v185, v0
	v_mul_f32_e64 v184, v186, v0
	v_mul_f32_e64 v185, v187, v0
	v_fma_f32 v186, v144, v2, v132
	v_fma_f32 v187, v145, v3, v133
	v_fma_f32 v184, v146, v184, v134
	v_fma_f32 v185, v147, v185, v135
	v_cvt_pk_fp8_f32 v1, v186, v187
	v_add_u32_e32 v2, 0x10100, v194
	v_fmac_f32_e32 v195, v17, v189
	v_fmac_f32_e32 v196, v18, v189
	v_cvt_pk_fp8_f32 v1, v184, v185 op_sel:[0,0,1]
	v_fmac_f32_e32 v195, v45, v186
	v_fmac_f32_e32 v196, v46, v186
	v_fmac_f32_e32 v195, v37, v187
	ds_write_b32 v2, v1
	v_mul_f32_e64 v2, v180, v0
	v_mul_f32_e64 v3, v181, v0
	v_mul_f32_e64 v180, v182, v0
	v_mul_f32_e64 v181, v183, v0
	v_fma_f32 v182, v148, v2, v136
	v_fma_f32 v183, v149, v3, v137
	v_fma_f32 v180, v150, v180, v138
	v_fma_f32 v181, v151, v181, v139
	v_cvt_pk_fp8_f32 v1, v182, v183
	v_add_u32_e32 v2, 0x10200, v194
	v_fmac_f32_e32 v196, v38, v187
	v_fmac_f32_e32 v195, v61, v184
	v_cvt_pk_fp8_f32 v1, v180, v181 op_sel:[0,0,1]
	v_fmac_f32_e32 v196, v62, v184
	v_fmac_f32_e32 v195, v49, v185
	v_fmac_f32_e32 v196, v50, v185
	ds_write_b32 v2, v1
	v_mul_f32_e64 v2, v176, v0
	v_mul_f32_e64 v3, v177, v0
	v_mul_f32_e64 v1, v179, v0
	v_mul_f32_e64 v0, v178, v0
	v_fma_f32 v178, v152, v2, v140
	v_fma_f32 v179, v153, v3, v141
	v_fma_f32 v176, v154, v0, v142
	v_fma_f32 v177, v155, v1, v143
	v_add_u32_e32 v1, 0x10300, v194
	v_cvt_pk_fp8_f32 v0, v178, v179
	v_fma_f32 v194, v8, v190, 0
	v_fmac_f32_e32 v194, v202, v191
	v_fma_f32 v2, v14, v190, 0
	v_cvt_pk_fp8_f32 v0, v176, v177 op_sel:[0,0,1]
	v_fma_f32 v3, v15, v190, 0
	v_fmac_f32_e32 v194, v24, v188
	v_fmac_f32_e32 v2, v6, v191
	ds_write_b32 v1, v0
	v_fma_f32 v0, v12, v190, 0
	v_fmac_f32_e32 v0, v4, v191
	v_fma_f32 v1, v13, v190, 0
	v_fma_f32 v190, v11, v190, 0
	v_fmac_f32_e32 v0, v28, v188
	v_fmac_f32_e32 v1, v5, v191
	v_fmac_f32_e32 v3, v7, v191
	v_fmac_f32_e32 v190, v205, v191
	v_fmac_f32_e32 v0, v20, v189
	v_fmac_f32_e32 v194, v16, v189
	v_fmac_f32_e32 v1, v29, v188
	v_fmac_f32_e32 v2, v30, v188
	v_fmac_f32_e32 v3, v31, v188
	v_fmac_f32_e32 v190, v27, v188
	v_fmac_f32_e32 v0, v32, v186
	v_fmac_f32_e32 v194, v44, v186
	v_fmac_f32_e32 v1, v21, v189
	v_fmac_f32_e32 v2, v22, v189
	v_fmac_f32_e32 v3, v23, v189
	v_fmac_f32_e32 v190, v19, v189
	v_fmac_f32_e32 v0, v40, v187
	v_fmac_f32_e32 v194, v36, v187
	v_fmac_f32_e32 v1, v33, v186
	v_fmac_f32_e32 v2, v34, v186
	v_fmac_f32_e32 v3, v35, v186
	v_fmac_f32_e32 v190, v47, v186
	v_fmac_f32_e32 v0, v56, v184
	v_fmac_f32_e32 v194, v60, v184
	v_fmac_f32_e32 v1, v41, v187
	v_fmac_f32_e32 v2, v42, v187
	v_fmac_f32_e32 v3, v43, v187
	v_fmac_f32_e32 v190, v39, v187
	v_fmac_f32_e32 v0, v52, v185
	v_fmac_f32_e32 v194, v48, v185
	v_fmac_f32_e32 v1, v57, v184
	v_fmac_f32_e32 v2, v58, v184
	v_fmac_f32_e32 v3, v59, v184
	v_fmac_f32_e32 v190, v63, v184
	v_fmac_f32_e32 v0, v76, v182
	v_fmac_f32_e32 v194, v72, v182
	v_fmac_f32_e32 v1, v53, v185
	v_fmac_f32_e32 v2, v54, v185
	v_fmac_f32_e32 v3, v55, v185
	v_fmac_f32_e32 v190, v51, v185
	v_fmac_f32_e32 v0, v68, v183
	v_fmac_f32_e32 v194, v64, v183
	v_fmac_f32_e32 v1, v77, v182
	v_fmac_f32_e32 v2, v78, v182
	v_fmac_f32_e32 v3, v79, v182
	v_fmac_f32_e32 v195, v73, v182
	v_fmac_f32_e32 v196, v74, v182
	v_fmac_f32_e32 v190, v75, v182
	v_fmac_f32_e32 v0, v92, v180
	v_fmac_f32_e32 v194, v88, v180
	v_fmac_f32_e32 v1, v69, v183
	v_fmac_f32_e32 v2, v70, v183
	v_fmac_f32_e32 v3, v71, v183
	v_fmac_f32_e32 v195, v65, v183
	v_fmac_f32_e32 v196, v66, v183
	v_fmac_f32_e32 v190, v67, v183
	v_fmac_f32_e32 v0, v84, v181
	v_fmac_f32_e32 v194, v80, v181
	v_fmac_f32_e32 v1, v93, v180
	v_fmac_f32_e32 v2, v94, v180
	v_fmac_f32_e32 v3, v95, v180
	v_fmac_f32_e32 v195, v89, v180
	v_fmac_f32_e32 v196, v90, v180
	v_fmac_f32_e32 v190, v91, v180
	v_fmac_f32_e32 v0, v96, v178
	v_fmac_f32_e32 v194, v108, v178
	v_fmac_f32_e32 v1, v85, v181
	v_fmac_f32_e32 v2, v86, v181
	v_fmac_f32_e32 v3, v87, v181
	v_fmac_f32_e32 v195, v81, v181
	v_fmac_f32_e32 v196, v82, v181
	v_fmac_f32_e32 v190, v83, v181
	v_fmac_f32_e32 v0, v104, v179
	v_fmac_f32_e32 v194, v100, v179
	v_fmac_f32_e32 v1, v97, v178
	v_fmac_f32_e32 v2, v98, v178
	v_fmac_f32_e32 v3, v99, v178
	v_fmac_f32_e32 v195, v109, v178
	v_fmac_f32_e32 v196, v110, v178
	v_fmac_f32_e32 v190, v111, v178
	v_fmac_f32_e32 v0, v120, v176
	v_fmac_f32_e32 v194, v198, v176
	v_fmac_f32_e32 v1, v105, v179
	v_fmac_f32_e32 v2, v106, v179
	v_fmac_f32_e32 v3, v107, v179
	v_fmac_f32_e32 v195, v101, v179
	v_fmac_f32_e32 v196, v102, v179
	v_fmac_f32_e32 v190, v103, v179
	v_fmac_f32_e32 v0, v116, v177
	v_fmac_f32_e32 v194, v112, v177
	v_fmac_f32_e32 v1, v121, v176
	v_fmac_f32_e32 v2, v122, v176
	v_fmac_f32_e32 v3, v123, v176
	v_fmac_f32_e32 v195, v199, v176
	v_fmac_f32_e32 v196, v200, v176
	v_fmac_f32_e32 v190, v201, v176
	v_cndmask_b32_e64 v176, v194, v0, s[0:1]
	v_cndmask_b32_e64 v0, v0, v194, s[0:1]
	v_fmac_f32_e32 v1, v117, v177
	v_mbcnt_lo_u32_b32 v178, s8, 0
	v_fmac_f32_e32 v2, v118, v177
	v_fmac_f32_e32 v3, v119, v177
	v_fmac_f32_e32 v195, v113, v177
	v_fmac_f32_e32 v196, v114, v177
	v_fmac_f32_e32 v190, v115, v177
	v_mov_b32_e32 v177, v0
	v_mbcnt_hi_u32_b32 v178, s8, v178
	s_nop 0
	v_permlane32_swap_b32_e32 v0, v177
	v_cmp_gt_u32_e32 vcc, 32, v178
	s_mov_b32 s8, s62
	s_nop 0
	v_cndmask_b32_e32 v0, v0, v177, vcc
	v_add_f32_e32 v0, v176, v0
	v_cndmask_b32_e64 v176, v195, v1, s[0:1]
	v_cndmask_b32_e64 v1, v1, v195, s[0:1]
	v_mbcnt_lo_u32_b32 v178, s8, 0
	v_mov_b32_e32 v177, v1
	v_mbcnt_hi_u32_b32 v178, s8, v178
	s_nop 0
	v_permlane32_swap_b32_e32 v1, v177
	v_cmp_gt_u32_e32 vcc, 32, v178
	s_mov_b32 s8, s62
	s_nop 0
	v_cndmask_b32_e32 v1, v1, v177, vcc
	v_add_f32_e32 v1, v176, v1
	v_cndmask_b32_e64 v176, v196, v2, s[0:1]
	v_cndmask_b32_e64 v2, v2, v196, s[0:1]
	v_mbcnt_lo_u32_b32 v178, s8, 0
	v_mov_b32_e32 v177, v2
	v_mbcnt_hi_u32_b32 v178, s8, v178
	s_nop 0
	v_permlane32_swap_b32_e32 v2, v177
	v_cmp_gt_u32_e32 vcc, 32, v178
	s_mov_b32 s8, s62
	s_nop 0
	v_cndmask_b32_e32 v2, v2, v177, vcc
	v_add_f32_e32 v2, v176, v2
	v_cndmask_b32_e64 v176, v190, v3, s[0:1]
	v_cndmask_b32_e64 v3, v3, v190, s[0:1]
	v_mbcnt_lo_u32_b32 v178, s8, 0
	v_mov_b32_e32 v177, v3
	v_mbcnt_hi_u32_b32 v178, s8, v178
	s_nop 0
	v_permlane32_swap_b32_e32 v3, v177
	v_cmp_gt_u32_e32 vcc, 32, v178
	s_nop 1
	v_cndmask_b32_e32 v3, v3, v177, vcc
	v_add_f32_e32 v3, v176, v3
	v_cndmask_b32_e64 v176, v2, v0, s[2:3]
	v_cndmask_b32_e64 v0, v0, v2, s[2:3]
	v_cndmask_b32_e64 v2, v3, v1, s[2:3]
	v_cndmask_b32_e64 v1, v1, v3, s[2:3]
	ds_swizzle_b32 v0, v0 offset:swizzle(SWAP,16)
	ds_swizzle_b32 v1, v1 offset:swizzle(SWAP,16)
	s_waitcnt lgkmcnt(1)
	v_add_f32_e32 v0, v176, v0
	s_waitcnt lgkmcnt(0)
	v_add_f32_e32 v1, v2, v1
	v_cndmask_b32_e64 v2, v1, v0, s[4:5]
	v_cndmask_b32_e64 v0, v0, v1, s[4:5]
	ds_swizzle_b32 v0, v0 offset:swizzle(SWAP,8)
	s_waitcnt lgkmcnt(0)
	v_add_f32_e32 v0, v2, v0
	ds_swizzle_b32 v1, v0 offset:swizzle(SWAP,4)
	s_waitcnt lgkmcnt(0)
	v_add_f32_e32 v0, v0, v1
	ds_swizzle_b32 v1, v0 offset:swizzle(SWAP,2)
	s_waitcnt lgkmcnt(0)
	v_add_f32_e32 v0, v0, v1
	ds_swizzle_b32 v1, v0 offset:swizzle(SWAP,1)
	s_waitcnt lgkmcnt(0)
	v_add_f32_e32 v0, v0, v1
	s_nop 0
	v_readlane_b32 s8, v0, 0
	v_readlane_b32 s9, v0, 8
	v_readlane_b32 s10, v0, 16
	v_readlane_b32 s11, v0, 24
	v_readlane_b32 s12, v0, 32
	v_readlane_b32 s13, v0, 40
	v_readlane_b32 s14, v0, 48
	v_readlane_b32 s15, v0, 56
	s_and_saveexec_b64 s[34:35], s[6:7]
	s_cbranch_execz .LBB0_1286
	v_max_f32_e64 v0, s9, s9
	v_max_f32_e64 v1, s8, s8
	v_max_f32_e32 v0, v1, v0
	v_mov_b32_e32 v1, s11
	v_max3_f32 v0, v0, s10, v1
	v_mov_b32_e32 v1, s13
	v_max3_f32 v0, v0, s12, v1
	v_mov_b32_e32 v1, s15
	v_max3_f32 v0, v0, s14, v1
	v_sub_f32_e32 v1, s15, v0
	v_sub_f32_e32 v2, s14, v0
	v_sub_f32_e32 v3, s13, v0
	v_sub_f32_e32 v176, s12, v0
	v_sub_f32_e32 v177, s11, v0
	v_sub_f32_e32 v178, s10, v0
	v_sub_f32_e32 v179, s9, v0
	v_sub_f32_e32 v0, s8, v0
	v_mul_f32_e32 v179, 0x3fb8aa3b, v179
	v_mul_f32_e32 v0, 0x3fb8aa3b, v0
	v_exp_f32_e32 v179, v179
	v_exp_f32_e32 v180, v0
	v_mul_f32_e32 v0, 0x3fb8aa3b, v178
	v_exp_f32_e32 v178, v0
	v_mul_f32_e32 v177, 0x3fb8aa3b, v177
	v_exp_f32_e32 v177, v177
	v_cmp_gt_f32_e64 s[8:9], v179, v180
	v_mul_f32_e32 v176, 0x3fb8aa3b, v176
	v_exp_f32_e32 v176, v176
	v_cndmask_b32_e64 v0, v180, v179, s[8:9]
	v_cmp_gt_f32_e64 s[10:11], v178, v0
	v_mul_f32_e32 v3, 0x3fb8aa3b, v3
	v_exp_f32_e32 v3, v3
	v_cndmask_b32_e64 v0, v0, v178, s[10:11]
	v_cmp_gt_f32_e64 s[12:13], v177, v0
	v_mul_f32_e32 v2, 0x3fb8aa3b, v2
	v_exp_f32_e32 v2, v2
	v_cndmask_b32_e64 v0, v0, v177, s[12:13]
	v_cmp_gt_f32_e64 s[14:15], v176, v0
	v_mul_f32_e32 v1, 0x3fb8aa3b, v1
	v_exp_f32_e32 v1, v1
	v_cndmask_b32_e64 v0, v0, v176, s[14:15]
	v_cmp_gt_f32_e64 s[16:17], v3, v0
	v_cndmask_b32_e64 v181, 0, 1, s[8:9]
	s_nop 0
	v_cndmask_b32_e64 v0, v0, v3, s[16:17]
	v_cmp_gt_f32_e64 s[18:19], v2, v0
	s_nop 1
	v_cndmask_b32_e64 v0, v0, v2, s[18:19]
	v_cmp_ngt_f32_e32 vcc, v1, v0
	s_and_b64 s[20:21], s[18:19], vcc
	s_and_b64 s[8:9], s[10:11], exec
	v_readfirstlane_b32 s8, v181
	s_cselect_b32 s10, 2, s8
	s_and_b64 s[8:9], s[12:13], exec
	s_cselect_b32 s10, 3, s10
	s_and_b64 s[8:9], s[14:15], exec
	s_cselect_b32 s10, 4, s10
	s_and_b64 s[8:9], s[16:17], exec
	s_cselect_b32 s10, 5, s10
	s_and_b64 s[8:9], s[18:19], exec
	s_cselect_b32 s10, 6, s10
	s_and_b64 s[8:9], vcc, exec
	s_cselect_b32 s41, s10, 7
	s_cmp_lg_u32 s41, 5
	s_cselect_b64 s[18:19], -1, 0
	s_cmp_lg_u32 s41, 4
	s_cselect_b64 s[16:17], -1, 0
	s_cmp_lg_u32 s41, 3
	s_cselect_b64 s[14:15], -1, 0
	s_cmp_lg_u32 s41, 2
	s_cselect_b64 s[12:13], -1, 0
	s_cmp_lg_u32 s41, 1
	s_cselect_b64 s[10:11], -1, 0
	s_cmp_eq_u32 s41, 0
	s_cselect_b64 s[42:43], -1, 0
	v_cmp_nlt_f32_e64 s[8:9], -1.0, v180
	s_or_b64 s[42:43], s[8:9], s[42:43]
	v_cndmask_b32_e64 v180, v180, -1.0, s[42:43]
	v_cmp_gt_f32_e64 s[8:9], v179, v180
	s_and_b64 s[8:9], s[10:11], s[8:9]
	v_cndmask_b32_e32 v0, v1, v0, vcc
	v_cndmask_b32_e64 v179, v180, v179, s[8:9]
	v_cmp_gt_f32_e64 s[10:11], v178, v179
	s_and_b64 s[10:11], s[12:13], s[10:11]
	s_nop 0
	v_cndmask_b32_e64 v178, v179, v178, s[10:11]
	v_cmp_gt_f32_e64 s[12:13], v177, v178
	s_and_b64 s[12:13], s[14:15], s[12:13]
	s_nop 0
	v_cndmask_b32_e64 v177, v178, v177, s[12:13]
	v_cmp_gt_f32_e64 s[14:15], v176, v177
	s_and_b64 s[14:15], s[16:17], s[14:15]
	s_nop 0
	v_cndmask_b32_e64 v176, v177, v176, s[14:15]
	v_cmp_gt_f32_e64 s[16:17], v3, v176
	s_and_b64 s[16:17], s[18:19], s[16:17]
	s_nop 0
	v_cndmask_b32_e64 v3, v176, v3, s[16:17]
	v_cmp_ngt_f32_e64 s[18:19], v2, v3
	s_or_b64 s[18:19], s[20:21], s[18:19]
	s_nop 0
	v_cndmask_b32_e64 v2, v2, v3, s[18:19]
	v_cmp_gt_f32_e64 s[20:21], v1, v2
	s_and_b64 vcc, vcc, s[20:21]
	v_cndmask_b32_e64 v3, 0, -1, s[42:43]
	s_and_b64 s[8:9], s[8:9], exec
	v_cndmask_b32_e32 v1, v2, v1, vcc
	v_readfirstlane_b32 s8, v3
	v_add_f32_e32 v176, v0, v1
	s_cselect_b32 s20, 1, s8
	v_div_scale_f32 v177, s[8:9], v176, v176, 1.0
	s_and_b64 s[8:9], s[10:11], exec
	v_rcp_f32_e32 v178, v177
	s_cselect_b32 s10, 2, s20
	s_and_b64 s[8:9], s[12:13], exec
	s_cselect_b32 s10, 3, s10
	s_and_b64 s[8:9], s[14:15], exec
	s_cselect_b32 s10, 4, s10
	s_and_b64 s[8:9], s[16:17], exec
	s_cselect_b32 s10, 5, s10
	s_and_b64 s[8:9], s[18:19], exec
	v_fma_f32 v180, -v177, v178, 1.0
	s_cselect_b32 s10, s10, 6
	s_and_b64 s[8:9], vcc, exec
	v_fmac_f32_e32 v178, v180, v178
	v_div_scale_f32 v180, vcc, 1.0, v176, 1.0
	v_mul_f32_e32 v181, v180, v178
	v_fma_f32 v182, -v177, v181, v180
	v_fmac_f32_e32 v181, v182, v178
	v_fma_f32 v177, -v177, v181, v180
	v_div_fmas_f32 v177, v177, v178, v181
	s_cselect_b32 s10, 7, s10
	s_add_i32 s11, s27, 0
	v_div_fixup_f32 v176, v177, v176, 1.0
	v_mov_b32_e32 v2, s41
	v_readlane_b32 s41, v253, 51
	v_mov_b32_e32 v3, s10
	v_mov_b32_e32 v179, s11
	v_mul_f32_e64 v0, v0, v176
	v_mul_f32_e64 v1, v1, v176
	ds_write2st64_b64 v179, v[2:3], v[0:1] offset1:8
	s_branch .LBB0_1286

.LBB0_1649:
	v_mov_b32_e32 v128, v208
	s_mov_b64 s[10:11], s[18:19]
	s_mov_b64 s[36:37], s[16:17]
	s_load_dwordx2 s[2:3], s[36:37], 0x130
	s_load_dwordx4 s[12:15], s[36:37], 0x28
	v_bfe_u32 v149, v128, 4, 2
	v_and_b32_e32 v148, 15, v128
	s_mov_b32 s41, 0x105000
	v_or_b32_e32 v247, s57, v148
	s_waitcnt lgkmcnt(0)
	s_add_u32 s36, s12, s26
	s_addc_u32 s37, s13, s27
	s_add_u32 s38, s36, 0x5000
	s_addc_u32 s39, s37, 0
	s_ashr_i32 s36, s40, 31
	s_lshr_b32 s36, s36, 20
	s_add_i32 s36, s40, s36
	s_ashr_i32 s36, s36, 12
	s_lshl_b32 s37, s80, 8
	s_or_b32 s37, s37, s58
	s_mulk_i32 s36, 0x1800
	v_lshl_or_b32 v216, v149, 2, s37
	s_ashr_i32 s37, s36, 31
	s_lshl_b64 s[36:37], s[36:37], 2
	s_add_u32 s60, s10, s36
	v_ashrrev_i32_e32 v217, 31, v216
	s_addc_u32 s61, s11, s37
	v_lshlrev_b64 v[136:137], 2, v[216:217]
	v_lshl_add_u64 v[128:129], s[60:61], 0, v[136:137]
	s_mov_b64 s[60:61], 0x105000
	v_lshl_add_u64 v[154:155], v[128:129], 0, s[60:61]
	v_add_co_u32_e32 v128, vcc, s41, v128
	v_lshl_add_u64 v[132:133], s[38:39], 0, v[136:137]
	s_nop 0
	v_addc_co_u32_e32 v129, vcc, 0, v129, vcc
	flat_load_dwordx4 v[128:131], v[128:129]
	v_or_b32_e32 v140, 16, v216
	global_load_dwordx4 v[132:135], v[132:133], off
	v_ashrrev_i32_e32 v141, 31, v140
	v_or_b32_e32 v156, 0x80, v216
	v_ashrrev_i32_e32 v157, 31, v156
	v_or_b32_e32 v158, 0x90, v216
	v_ashrrev_i32_e32 v159, 31, v158
	v_add_u32_e32 v218, s40, v247
	v_ashrrev_i32_e32 v219, 31, v218
	v_cmp_eq_u32_e32 vcc, 0, v149
	s_waitcnt vmcnt(0) lgkmcnt(0)
	v_add_f32_e64 v146, v128, v132
	v_add_f32_e64 v147, v129, v133
	v_lshl_add_u64 v[132:133], v[140:141], 2, s[38:39]
	v_add_f32_e64 v144, v130, v134
	v_add_f32_e64 v145, v131, v135
	flat_load_dwordx4 v[128:131], v[154:155] offset:64
	s_nop 0
	global_load_dwordx4 v[132:135], v[132:133], off
	s_waitcnt vmcnt(0) lgkmcnt(0)
	v_add_f32_e64 v142, v128, v132
	v_add_f32_e64 v143, v129, v133
	v_lshl_add_u64 v[132:133], v[156:157], 2, s[38:39]
	v_add_f32_e64 v138, v130, v134
	v_add_f32_e64 v139, v131, v135
	flat_load_dwordx4 v[128:131], v[154:155] offset:512
	global_load_dwordx4 v[150:153], v[132:133], off
	s_waitcnt vmcnt(0) lgkmcnt(0)
	v_add_f32_e64 v134, v128, v150
	v_add_f32_e64 v135, v129, v151
	v_lshl_add_u64 v[128:129], v[158:159], 2, s[38:39]
	v_add_f32_e64 v132, v130, v152
	v_add_f32_e64 v133, v131, v153
	flat_load_dwordx4 v[150:153], v[154:155] offset:576
	global_load_dwordx4 v[160:163], v[128:129], off
	s_waitcnt vmcnt(0) lgkmcnt(0)
	v_add_f32_e64 v128, v152, v162
	v_add_f32_e64 v129, v153, v163
	v_lshlrev_b64 v[152:153], 12, v[218:219]
	v_lshl_add_u64 v[152:153], s[2:3], 0, v[152:153]
	v_add_f32_e64 v130, v150, v160
	v_add_f32_e64 v131, v151, v161
	v_lshl_add_u64 v[160:161], v[152:153], 0, v[136:137]
	global_load_dwordx4 v[152:155], v[160:161], off
	v_lshl_add_u32 v150, v148, 2, s74
	s_waitcnt vmcnt(0)
	v_fma_f32 v30, v30, v144, v154
	v_fma_f32 v31, v31, v145, v155
	v_fma_f32 v28, v28, v146, v152
	v_fma_f32 v29, v29, v147, v153
	global_load_dwordx4 v[152:155], v[160:161], off offset:64
	v_mul_f32_e32 v151, v29, v29
	v_fmac_f32_e32 v151, v28, v28
	v_fmac_f32_e32 v151, v30, v30
	v_fmac_f32_e32 v151, v31, v31
	global_store_dwordx4 v[160:161], v[28:31], off
	s_waitcnt vmcnt(1)
	v_fma_f32 v32, v32, v142, v152
	v_fma_f32 v33, v33, v143, v153
	s_nop 0
	v_mul_f32_e32 v152, v33, v33
	v_fma_f32 v34, v34, v138, v154
	v_fma_f32 v35, v35, v139, v155
	v_fmac_f32_e32 v152, v32, v32
	v_fmac_f32_e32 v152, v34, v34
	v_fmac_f32_e32 v152, v35, v35
	v_add_f32_e32 v151, v151, v152
	global_load_dwordx4 v[152:155], v[160:161], off offset:512
	s_waitcnt vmcnt(0)
	v_fma_f32 v40, v40, v134, v152
	v_fma_f32 v41, v41, v135, v153
	s_nop 0
	v_mul_f32_e32 v152, v41, v41
	v_fma_f32 v42, v42, v132, v154
	v_fma_f32 v43, v43, v133, v155
	v_fmac_f32_e32 v152, v40, v40
	v_fmac_f32_e32 v152, v42, v42
	v_fmac_f32_e32 v152, v43, v43
	v_add_f32_e32 v151, v151, v152
	global_load_dwordx4 v[152:155], v[160:161], off offset:576
	s_waitcnt vmcnt(0)
	v_fma_f32 v48, v48, v130, v152
	v_fma_f32 v49, v49, v131, v153
	s_nop 0
	v_mul_f32_e32 v152, v49, v49
	v_fma_f32 v50, v50, v128, v154
	v_fma_f32 v51, v51, v129, v155
	v_fmac_f32_e32 v152, v48, v48
	v_fmac_f32_e32 v152, v50, v50
	v_fmac_f32_e32 v152, v51, v51
	v_add_f32_e32 v151, v151, v152
	ds_swizzle_b32 v152, v151 offset:swizzle(SWAP,16)
	global_store_dwordx4 v[160:161], v[32:35], off offset:64
	global_store_dwordx4 v[160:161], v[40:43], off offset:512
	global_store_dwordx4 v[160:161], v[48:51], off offset:576
	s_waitcnt lgkmcnt(0)
	v_add_f32_e32 v151, v151, v152
	v_mov_b32_e32 v152, v151
	s_nop 1
	v_permlane32_swap_b32_e32 v151, v152
	s_and_saveexec_b64 s[38:39], vcc
	v_add_f32_e32 v151, v151, v152
	ds_write_b32 v150, v151
	s_or_b64 exec, exec, s[38:39]
	v_or_b32_e32 v248, 16, v247
	v_add_u32_e32 v220, s40, v248
	v_ashrrev_i32_e32 v221, 31, v220
	v_lshlrev_b64 v[152:153], 12, v[220:221]
	v_lshl_add_u64 v[152:153], s[2:3], 0, v[152:153]
	v_lshl_add_u64 v[160:161], v[216:217], 2, v[152:153]
	global_load_dwordx4 v[152:155], v[160:161], off
	s_waitcnt vmcnt(0)
	v_fma_f32 v58, v58, v144, v154
	v_fma_f32 v59, v59, v145, v155
	v_fma_f32 v56, v56, v146, v152
	v_fma_f32 v57, v57, v147, v153
	global_load_dwordx4 v[152:155], v[160:161], off offset:64
	v_mul_f32_e32 v151, v57, v57
	v_fmac_f32_e32 v151, v56, v56
	v_fmac_f32_e32 v151, v58, v58
	v_fmac_f32_e32 v151, v59, v59
	global_store_dwordx4 v[160:161], v[56:59], off
	s_waitcnt vmcnt(1)
	v_fma_f32 v64, v64, v142, v152
	v_fma_f32 v65, v65, v143, v153
	s_nop 0
	v_mul_f32_e32 v152, v65, v65
	v_fma_f32 v66, v66, v138, v154
	v_fma_f32 v67, v67, v139, v155
	v_fmac_f32_e32 v152, v64, v64
	v_fmac_f32_e32 v152, v66, v66
	v_fmac_f32_e32 v152, v67, v67
	v_add_f32_e32 v151, v151, v152
	global_load_dwordx4 v[152:155], v[160:161], off offset:512
	s_waitcnt vmcnt(0)
	v_fma_f32 v72, v72, v134, v152
	v_fma_f32 v73, v73, v135, v153
	s_nop 0
	v_mul_f32_e32 v152, v73, v73
	v_fma_f32 v74, v74, v132, v154
	v_fma_f32 v75, v75, v133, v155
	v_fmac_f32_e32 v152, v72, v72
	v_fmac_f32_e32 v152, v74, v74
	v_fmac_f32_e32 v152, v75, v75
	v_add_f32_e32 v151, v151, v152
	global_load_dwordx4 v[152:155], v[160:161], off offset:576
	s_waitcnt vmcnt(0)
	v_fma_f32 v80, v80, v130, v152
	v_fma_f32 v81, v81, v131, v153
	s_nop 0
	v_mul_f32_e32 v152, v81, v81
	v_fma_f32 v82, v82, v128, v154
	v_fma_f32 v83, v83, v129, v155
	v_fmac_f32_e32 v152, v80, v80
	v_fmac_f32_e32 v152, v82, v82
	v_fmac_f32_e32 v152, v83, v83
	v_add_f32_e32 v151, v151, v152
	ds_swizzle_b32 v152, v151 offset:swizzle(SWAP,16)
	global_store_dwordx4 v[160:161], v[64:67], off offset:64
	global_store_dwordx4 v[160:161], v[72:75], off offset:512
	global_store_dwordx4 v[160:161], v[80:83], off offset:576
	s_waitcnt lgkmcnt(0)
	v_add_f32_e32 v151, v151, v152
	v_mov_b32_e32 v152, v151
	s_nop 1
	v_permlane32_swap_b32_e32 v151, v152
	s_and_saveexec_b64 s[38:39], vcc
	v_add_f32_e32 v151, v151, v152
	ds_write_b32 v150, v151 offset:64
	s_or_b64 exec, exec, s[38:39]
	v_or_b32_e32 v249, 32, v247
	v_add_u32_e32 v222, s40, v249
	v_ashrrev_i32_e32 v223, 31, v222
	v_lshlrev_b64 v[152:153], 12, v[222:223]
	v_lshl_add_u64 v[152:153], s[2:3], 0, v[152:153]
	v_lshl_add_u64 v[160:161], v[216:217], 2, v[152:153]
	global_load_dwordx4 v[152:155], v[160:161], off
	s_waitcnt vmcnt(0)
	v_fma_f32 v90, v90, v144, v154
	v_fma_f32 v91, v91, v145, v155
	v_fma_f32 v88, v88, v146, v152
	v_fma_f32 v89, v89, v147, v153
	global_load_dwordx4 v[152:155], v[160:161], off offset:64
	v_mul_f32_e32 v151, v89, v89
	v_fmac_f32_e32 v151, v88, v88
	v_fmac_f32_e32 v151, v90, v90
	v_fmac_f32_e32 v151, v91, v91
	global_store_dwordx4 v[160:161], v[88:91], off
	s_waitcnt vmcnt(1)
	v_fma_f32 v92, v92, v142, v152
	v_fma_f32 v93, v93, v143, v153
	s_nop 0
	v_mul_f32_e32 v152, v93, v93
	v_fma_f32 v94, v94, v138, v154
	v_fma_f32 v95, v95, v139, v155
	v_fmac_f32_e32 v152, v92, v92
	v_fmac_f32_e32 v152, v94, v94
	v_fmac_f32_e32 v152, v95, v95
	v_add_f32_e32 v151, v151, v152
	global_load_dwordx4 v[152:155], v[160:161], off offset:512
	s_waitcnt vmcnt(0)
	v_fma_f32 v100, v100, v134, v152
	v_fma_f32 v101, v101, v135, v153
	s_nop 0
	v_mul_f32_e32 v152, v101, v101
	v_fma_f32 v102, v102, v132, v154
	v_fma_f32 v103, v103, v133, v155
	v_fmac_f32_e32 v152, v100, v100
	v_fmac_f32_e32 v152, v102, v102
	v_fmac_f32_e32 v152, v103, v103
	v_add_f32_e32 v151, v151, v152
	global_load_dwordx4 v[152:155], v[160:161], off offset:576
	s_waitcnt vmcnt(0)
	v_fma_f32 v108, v108, v130, v152
	v_fma_f32 v109, v109, v131, v153
	s_nop 0
	v_mul_f32_e32 v152, v109, v109
	v_fma_f32 v110, v110, v128, v154
	v_fma_f32 v111, v111, v129, v155
	v_fmac_f32_e32 v152, v108, v108
	v_fmac_f32_e32 v152, v110, v110
	v_fmac_f32_e32 v152, v111, v111
	v_add_f32_e32 v151, v151, v152
	ds_swizzle_b32 v152, v151 offset:swizzle(SWAP,16)
	global_store_dwordx4 v[160:161], v[92:95], off offset:64
	global_store_dwordx4 v[160:161], v[100:103], off offset:512
	global_store_dwordx4 v[160:161], v[108:111], off offset:576
	s_waitcnt lgkmcnt(0)
	v_add_f32_e32 v151, v151, v152
	v_mov_b32_e32 v152, v151
	s_nop 1
	v_permlane32_swap_b32_e32 v151, v152
	s_and_saveexec_b64 s[38:39], vcc
	v_add_f32_e32 v151, v151, v152
	ds_write_b32 v150, v151 offset:128
	s_or_b64 exec, exec, s[38:39]
	v_or_b32_e32 v237, 48, v247
	v_add_u32_e32 v224, s40, v237
	v_ashrrev_i32_e32 v225, 31, v224
	v_lshlrev_b64 v[152:153], 12, v[224:225]
	v_lshl_add_u64 v[152:153], s[2:3], 0, v[152:153]
	v_lshl_add_u64 v[160:161], v[216:217], 2, v[152:153]
	global_load_dwordx4 v[152:155], v[160:161], off
	s_waitcnt vmcnt(0)
	v_fma_f32 v118, v118, v144, v154
	v_fma_f32 v119, v119, v145, v155
	v_fma_f32 v116, v116, v146, v152
	v_fma_f32 v117, v117, v147, v153
	global_load_dwordx4 v[152:155], v[160:161], off offset:64
	v_mul_f32_e32 v151, v117, v117
	v_fmac_f32_e32 v151, v116, v116
	v_fmac_f32_e32 v151, v118, v118
	v_fmac_f32_e32 v151, v119, v119
	global_store_dwordx4 v[160:161], v[116:119], off
	s_waitcnt vmcnt(1)
	v_fma_f32 v120, v120, v142, v152
	v_fma_f32 v121, v121, v143, v153
	s_nop 0
	v_mul_f32_e32 v152, v121, v121
	v_fma_f32 v122, v122, v138, v154
	v_fma_f32 v123, v123, v139, v155
	v_fmac_f32_e32 v152, v120, v120
	v_fmac_f32_e32 v152, v122, v122
	v_fmac_f32_e32 v152, v123, v123
	v_add_f32_e32 v151, v151, v152
	global_load_dwordx4 v[152:155], v[160:161], off offset:512
	s_waitcnt vmcnt(0)
	v_fma_f32 v124, v124, v134, v152
	v_fma_f32 v125, v125, v135, v153
	s_nop 0
	v_mul_f32_e32 v152, v125, v125
	v_fma_f32 v126, v126, v132, v154
	v_fma_f32 v127, v127, v133, v155
	v_fmac_f32_e32 v152, v124, v124
	v_fmac_f32_e32 v152, v126, v126
	v_fmac_f32_e32 v152, v127, v127
	v_add_f32_e32 v151, v151, v152
	global_load_dwordx4 v[152:155], v[160:161], off offset:576
	s_waitcnt vmcnt(0)
	v_fma_f32 v112, v112, v130, v152
	v_fma_f32 v113, v113, v131, v153
	s_nop 0
	v_mul_f32_e32 v152, v113, v113
	v_fma_f32 v114, v114, v128, v154
	v_fma_f32 v115, v115, v129, v155
	v_fmac_f32_e32 v152, v112, v112
	v_fmac_f32_e32 v152, v114, v114
	v_fmac_f32_e32 v152, v115, v115
	v_add_f32_e32 v151, v151, v152
	ds_swizzle_b32 v152, v151 offset:swizzle(SWAP,16)
	global_store_dwordx4 v[160:161], v[120:123], off offset:64
	global_store_dwordx4 v[160:161], v[124:127], off offset:512
	global_store_dwordx4 v[160:161], v[112:115], off offset:576
	s_waitcnt lgkmcnt(0)
	v_add_f32_e32 v151, v151, v152
	v_mov_b32_e32 v152, v151
	s_nop 1
	v_permlane32_swap_b32_e32 v151, v152
	s_and_saveexec_b64 s[38:39], vcc
	v_add_f32_e32 v151, v151, v152
	ds_write_b32 v150, v151 offset:192
	s_or_b64 exec, exec, s[38:39]
	v_add_u32_e32 v226, 0x80, v218
	v_ashrrev_i32_e32 v227, 31, v226
	v_lshlrev_b64 v[152:153], 12, v[226:227]
	v_lshl_add_u64 v[152:153], s[2:3], 0, v[152:153]
	v_lshl_add_u64 v[160:161], v[216:217], 2, v[152:153]
	global_load_dwordx4 v[152:155], v[160:161], off
	s_waitcnt vmcnt(0)
	v_fma_f32 v106, v106, v144, v154
	v_fma_f32 v107, v107, v145, v155
	v_fma_f32 v104, v104, v146, v152
	v_fma_f32 v105, v105, v147, v153
	global_load_dwordx4 v[152:155], v[160:161], off offset:64
	v_mul_f32_e32 v151, v105, v105
	v_fmac_f32_e32 v151, v104, v104
	v_fmac_f32_e32 v151, v106, v106
	v_fmac_f32_e32 v151, v107, v107
	global_store_dwordx4 v[160:161], v[104:107], off
	s_waitcnt vmcnt(1)
	v_fma_f32 v96, v96, v142, v152
	v_fma_f32 v97, v97, v143, v153
	s_nop 0
	v_mul_f32_e32 v152, v97, v97
	v_fma_f32 v98, v98, v138, v154
	v_fma_f32 v99, v99, v139, v155
	v_fmac_f32_e32 v152, v96, v96
	v_fmac_f32_e32 v152, v98, v98
	v_fmac_f32_e32 v152, v99, v99
	v_add_f32_e32 v151, v151, v152
	global_load_dwordx4 v[152:155], v[160:161], off offset:512
	s_waitcnt vmcnt(0)
	v_fma_f32 v84, v84, v134, v152
	v_fma_f32 v85, v85, v135, v153
	s_nop 0
	v_mul_f32_e32 v152, v85, v85
	v_fma_f32 v86, v86, v132, v154
	v_fma_f32 v87, v87, v133, v155
	v_fmac_f32_e32 v152, v84, v84
	v_fmac_f32_e32 v152, v86, v86
	v_fmac_f32_e32 v152, v87, v87
	v_add_f32_e32 v151, v151, v152
	global_load_dwordx4 v[152:155], v[160:161], off offset:576
	s_waitcnt vmcnt(0)
	v_fma_f32 v76, v76, v130, v152
	v_fma_f32 v77, v77, v131, v153
	s_nop 0
	v_mul_f32_e32 v152, v77, v77
	v_fma_f32 v78, v78, v128, v154
	v_fma_f32 v79, v79, v129, v155
	v_fmac_f32_e32 v152, v76, v76
	v_fmac_f32_e32 v152, v78, v78
	v_fmac_f32_e32 v152, v79, v79
	v_add_f32_e32 v151, v151, v152
	ds_swizzle_b32 v152, v151 offset:swizzle(SWAP,16)
	global_store_dwordx4 v[160:161], v[96:99], off offset:64
	global_store_dwordx4 v[160:161], v[84:87], off offset:512
	global_store_dwordx4 v[160:161], v[76:79], off offset:576
	s_waitcnt lgkmcnt(0)
	v_add_f32_e32 v151, v151, v152
	v_mov_b32_e32 v152, v151
	s_nop 1
	v_permlane32_swap_b32_e32 v151, v152
	s_and_saveexec_b64 s[38:39], vcc
	v_add_f32_e32 v151, v151, v152
	ds_write_b32 v150, v151 offset:512
	s_or_b64 exec, exec, s[38:39]
	v_add_u32_e32 v228, 0x90, v218
	v_ashrrev_i32_e32 v229, 31, v228
	v_lshlrev_b64 v[152:153], 12, v[228:229]
	v_lshl_add_u64 v[152:153], s[2:3], 0, v[152:153]
	v_lshl_add_u64 v[160:161], v[216:217], 2, v[152:153]
	global_load_dwordx4 v[152:155], v[160:161], off
	s_waitcnt vmcnt(0)
	v_fma_f32 v70, v70, v144, v154
	v_fma_f32 v71, v71, v145, v155
	v_fma_f32 v68, v68, v146, v152
	v_fma_f32 v69, v69, v147, v153
	global_load_dwordx4 v[152:155], v[160:161], off offset:64
	v_mul_f32_e32 v151, v69, v69
	v_fmac_f32_e32 v151, v68, v68
	v_fmac_f32_e32 v151, v70, v70
	v_fmac_f32_e32 v151, v71, v71
	global_store_dwordx4 v[160:161], v[68:71], off
	s_waitcnt vmcnt(1)
	v_fma_f32 v60, v60, v142, v152
	v_fma_f32 v61, v61, v143, v153
	s_nop 0
	v_mul_f32_e32 v152, v61, v61
	v_fma_f32 v62, v62, v138, v154
	v_fma_f32 v63, v63, v139, v155
	v_fmac_f32_e32 v152, v60, v60
	v_fmac_f32_e32 v152, v62, v62
	v_fmac_f32_e32 v152, v63, v63
	v_add_f32_e32 v151, v151, v152
	global_load_dwordx4 v[152:155], v[160:161], off offset:512
	s_waitcnt vmcnt(0)
	v_fma_f32 v52, v52, v134, v152
	v_fma_f32 v53, v53, v135, v153
	s_nop 0
	v_mul_f32_e32 v152, v53, v53
	v_fma_f32 v54, v54, v132, v154
	v_fma_f32 v55, v55, v133, v155
	v_fmac_f32_e32 v152, v52, v52
	v_fmac_f32_e32 v152, v54, v54
	v_fmac_f32_e32 v152, v55, v55
	v_add_f32_e32 v151, v151, v152
	global_load_dwordx4 v[152:155], v[160:161], off offset:576
	s_waitcnt vmcnt(0)
	v_fma_f32 v44, v44, v130, v152
	v_fma_f32 v45, v45, v131, v153
	s_nop 0
	v_mul_f32_e32 v152, v45, v45
	v_fma_f32 v46, v46, v128, v154
	v_fma_f32 v47, v47, v129, v155
	v_fmac_f32_e32 v152, v44, v44
	v_fmac_f32_e32 v152, v46, v46
	v_fmac_f32_e32 v152, v47, v47
	v_add_f32_e32 v151, v151, v152
	ds_swizzle_b32 v152, v151 offset:swizzle(SWAP,16)
	global_store_dwordx4 v[160:161], v[60:63], off offset:64
	global_store_dwordx4 v[160:161], v[52:55], off offset:512
	global_store_dwordx4 v[160:161], v[44:47], off offset:576
	s_waitcnt lgkmcnt(0)
	v_add_f32_e32 v151, v151, v152
	v_mov_b32_e32 v152, v151
	s_nop 1
	v_permlane32_swap_b32_e32 v151, v152
	s_and_saveexec_b64 s[38:39], vcc
	v_add_f32_e32 v151, v151, v152
	ds_write_b32 v150, v151 offset:576
	s_or_b64 exec, exec, s[38:39]
	v_add_u32_e32 v230, 0xa0, v218
	v_ashrrev_i32_e32 v231, 31, v230
	v_lshlrev_b64 v[152:153], 12, v[230:231]
	v_lshl_add_u64 v[152:153], s[2:3], 0, v[152:153]
	v_lshl_add_u64 v[160:161], v[216:217], 2, v[152:153]
	global_load_dwordx4 v[152:155], v[160:161], off
	s_waitcnt vmcnt(0)
	v_fma_f32 v38, v38, v144, v154
	v_fma_f32 v39, v39, v145, v155
	v_fma_f32 v36, v36, v146, v152
	v_fma_f32 v37, v37, v147, v153
	global_load_dwordx4 v[152:155], v[160:161], off offset:64
	v_mul_f32_e32 v151, v37, v37
	v_fmac_f32_e32 v151, v36, v36
	v_fmac_f32_e32 v151, v38, v38
	v_fmac_f32_e32 v151, v39, v39
	global_store_dwordx4 v[160:161], v[36:39], off
	s_waitcnt vmcnt(1)
	v_fma_f32 v24, v24, v142, v152
	v_fma_f32 v25, v25, v143, v153
	s_nop 0
	v_mul_f32_e32 v152, v25, v25
	v_fma_f32 v26, v26, v138, v154
	v_fma_f32 v27, v27, v139, v155
	v_fmac_f32_e32 v152, v24, v24
	v_fmac_f32_e32 v152, v26, v26
	v_fmac_f32_e32 v152, v27, v27
	v_add_f32_e32 v151, v151, v152
	global_load_dwordx4 v[152:155], v[160:161], off offset:512
	s_waitcnt vmcnt(0)
	v_fma_f32 v20, v20, v134, v152
	v_fma_f32 v21, v21, v135, v153
	s_nop 0
	v_mul_f32_e32 v152, v21, v21
	v_fma_f32 v22, v22, v132, v154
	v_fma_f32 v23, v23, v133, v155
	v_fmac_f32_e32 v152, v20, v20
	v_fmac_f32_e32 v152, v22, v22
	v_fmac_f32_e32 v152, v23, v23
	v_add_f32_e32 v151, v151, v152
	global_load_dwordx4 v[152:155], v[160:161], off offset:576
	s_waitcnt vmcnt(0)
	v_fma_f32 v16, v16, v130, v152
	v_fma_f32 v17, v17, v131, v153
	s_nop 0
	v_mul_f32_e32 v152, v17, v17
	v_fma_f32 v18, v18, v128, v154
	v_fma_f32 v19, v19, v129, v155
	v_fmac_f32_e32 v152, v16, v16
	v_fmac_f32_e32 v152, v18, v18
	v_fmac_f32_e32 v152, v19, v19
	v_add_f32_e32 v151, v151, v152
	ds_swizzle_b32 v152, v151 offset:swizzle(SWAP,16)
	global_store_dwordx4 v[160:161], v[24:27], off offset:64
	global_store_dwordx4 v[160:161], v[20:23], off offset:512
	global_store_dwordx4 v[160:161], v[16:19], off offset:576
	s_waitcnt lgkmcnt(0)
	v_add_f32_e32 v151, v151, v152
	v_mov_b32_e32 v152, v151
	s_nop 1
	v_permlane32_swap_b32_e32 v151, v152
	s_and_saveexec_b64 s[38:39], vcc
	v_add_f32_e32 v151, v151, v152
	ds_write_b32 v150, v151 offset:640
	s_or_b64 exec, exec, s[38:39]
	v_add_u32_e32 v232, 0xb0, v218
	v_ashrrev_i32_e32 v233, 31, v232
	v_lshlrev_b64 v[152:153], 12, v[232:233]
	v_lshl_add_u64 v[152:153], s[2:3], 0, v[152:153]
	v_lshl_add_u64 v[160:161], v[216:217], 2, v[152:153]
	global_load_dwordx4 v[152:155], v[160:161], off
	s_waitcnt vmcnt(0)
	v_fma_f32 v14, v14, v144, v154
	v_fma_f32 v15, v15, v145, v155
	v_fma_f32 v12, v12, v146, v152
	v_fma_f32 v13, v13, v147, v153
	global_load_dwordx4 v[144:147], v[160:161], off offset:64
	v_mul_f32_e32 v151, v13, v13
	v_fmac_f32_e32 v151, v12, v12
	v_fmac_f32_e32 v151, v14, v14
	v_fmac_f32_e32 v151, v15, v15
	global_store_dwordx4 v[160:161], v[12:15], off
	s_waitcnt vmcnt(1)
	v_fma_f32 v8, v8, v142, v144
	v_fma_f32 v9, v9, v143, v145
	global_load_dwordx4 v[142:145], v[160:161], off offset:512
	v_fma_f32 v10, v10, v138, v146
	v_fma_f32 v11, v11, v139, v147
	v_mul_f32_e32 v138, v9, v9
	v_fmac_f32_e32 v138, v8, v8
	v_fmac_f32_e32 v138, v10, v10
	v_fmac_f32_e32 v138, v11, v11
	v_add_f32_e32 v138, v151, v138
	global_store_dwordx4 v[160:161], v[8:11], off offset:64
	s_waitcnt vmcnt(1)
	v_fma_f32 v4, v4, v134, v142
	v_fma_f32 v5, v5, v135, v143
	v_fma_f32 v6, v6, v132, v144
	v_fma_f32 v7, v7, v133, v145
	v_mul_f32_e32 v132, v5, v5
	v_fmac_f32_e32 v132, v4, v4
	v_fmac_f32_e32 v132, v6, v6
	v_fmac_f32_e32 v132, v7, v7
	v_add_f32_e32 v138, v138, v132
	global_load_dwordx4 v[132:135], v[160:161], off offset:576
	s_waitcnt vmcnt(0)
	v_fma_f32 v0, v0, v130, v132
	v_fma_f32 v1, v1, v131, v133
	v_fma_f32 v2, v2, v128, v134
	v_fma_f32 v3, v3, v129, v135
	v_mul_f32_e32 v128, v1, v1
	v_fmac_f32_e32 v128, v0, v0
	v_fmac_f32_e32 v128, v2, v2
	v_fmac_f32_e32 v128, v3, v3
	v_add_f32_e32 v128, v138, v128
	ds_swizzle_b32 v129, v128 offset:swizzle(SWAP,16)
	global_store_dwordx4 v[160:161], v[4:7], off offset:512
	global_store_dwordx4 v[160:161], v[0:3], off offset:576
	s_waitcnt lgkmcnt(0)
	v_add_f32_e32 v128, v128, v129
	v_mov_b32_e32 v129, v128
	s_nop 1
	v_permlane32_swap_b32_e32 v128, v129
	s_and_saveexec_b64 s[2:3], vcc
	v_add_f32_e32 v128, v128, v129
	ds_write_b32 v150, v128 offset:704
	s_or_b64 exec, exec, s[2:3]
	s_add_u32 s38, s10, s28
	s_addc_u32 s39, s11, s29
	s_add_u32 s2, s10, s73
	s_addc_u32 s3, s11, 0
	s_add_u32 s60, s2, 0x1fa00000
	s_addc_u32 s46, s3, 0
	s_lshl_b32 s2, s79, 6
	s_ashr_i32 s3, s2, 31
	s_lshl_b64 s[2:3], s[2:3], 2
	s_add_u32 s2, s38, s2
	v_lshlrev_b32_e32 v128, 4, v149
	s_waitcnt lgkmcnt(0)
	s_barrier
	s_addc_u32 s3, s39, s3
	v_or3_b32 v234, v128, s67, v148
	s_add_u32 s38, s2, 0x30000
	s_movk_i32 s2, 0x100
	s_addc_u32 s39, s3, 0
	v_cmp_gt_i32_e64 s[2:3], s2, v234
	s_and_saveexec_b64 s[40:41], s[2:3]
	s_cbranch_execz .LBB0_1668
	v_lshlrev_b32_e32 v130, 2, v234
	v_add_u32_e32 v128, 0, v130
	v_add_u32_e32 v131, 0x21000, v128
	ds_read2st64_b32 v[128:129], v131 offset1:4
	s_lshl_b32 s81, s79, 12
	s_lshl_b32 s80, s80, 10
	s_and_b32 s61, s46, 0xffff
	s_add_i32 s81, s81, s80
	s_waitcnt lgkmcnt(0)
	v_add_f32_e32 v132, v128, v129
	ds_read2st64_b32 v[128:129], v131 offset0:8 offset1:12
	s_waitcnt lgkmcnt(0)
	v_add_f32_e32 v128, v132, v128
	v_add_f32_e32 v128, v128, v129
	buffer_store_dword v128, v130, s[60:63], s81 offen sc1
	s_waitcnt vmcnt(0)
	v_and_b32_e32 v128, 63, v234
	v_cmp_eq_u32_e32 vcc, 0, v128
	s_and_b64 exec, exec, vcc
	s_cbranch_execz .LBB0_1668
	v_mov_b64_e32 v[128:129], s[38:39]
	flat_atomic_add v[128:129], v211

.LBB0_1684:
	s_or_b64 exec, exec, s[12:13]
	s_waitcnt vmcnt(0) lgkmcnt(0)
	v_add_f32_e64 v134, v134, 1.0
	v_add_f32_e64 v135, v135, 1.0
	v_add_f32_e64 v132, v132, 1.0
	v_add_f32_e64 v133, v133, 1.0
	v_add_f32_e64 v130, v134, v130
	v_add_f32_e64 v131, v135, v131
	v_add_f32_e64 v132, v132, v128
	v_add_f32_e64 v133, v133, v129
	v_mul_f32_e64 v128, v138, v130
	v_mul_f32_e64 v129, v139, v131
	v_mul_f32_e64 v130, v136, v132
	v_mul_f32_e64 v131, v137, v133
	v_lshl_add_u64 v[132:133], v[216:217], 1, s[10:11]
	s_mov_b64 s[2:3], 0x19400000
	v_lshl_add_u64 v[132:133], v[132:133], 0, s[2:3]
	s_add_i32 s2, 0, 0x22000
	s_waitcnt lgkmcnt(0)
	s_barrier
	v_lshl_add_u32 v135, v247, 2, s2
	ds_read_b32 v134, v135
	v_add_f32_e64 v142, v158, v142
	v_add_f32_e64 v143, v159, v143
	v_add_f32_e64 v140, v156, v140
	v_add_f32_e64 v141, v157, v141
	v_add_f32_e64 v154, v154, 1.0
	v_add_f32_e64 v155, v155, 1.0
	v_add_f32_e64 v152, v152, 1.0
	v_add_f32_e64 v153, v153, 1.0
	s_waitcnt lgkmcnt(0)
	v_mul_f32_e64 v30, v30, v134
	v_mul_f32_e64 v31, v31, v134
	v_mul_f32_e64 v28, v28, v134
	v_mul_f32_e64 v29, v29, v134
	v_lshlrev_b64 v[136:137], 11, v[218:219]
	v_fma_f32 v30, v128, v30, v142
	v_fma_f32 v31, v129, v31, v143
	v_fma_f32 v28, v130, v28, v140
	v_fma_f32 v29, v131, v29, v141
	v_add_f32_e64 v150, v154, v150
	v_add_f32_e64 v151, v155, v151
	v_add_f32_e64 v148, v152, v148
	v_add_f32_e64 v149, v153, v149
	v_lshl_add_u64 v[136:137], v[132:133], 0, v[136:137]
	v_cvt_pk_bf16_f32 v28, v28, v29
	v_cvt_pk_bf16_f32 v29, v30, v31
	v_add_f32_e64 v162, v166, v162
	v_add_f32_e64 v163, v167, v163
	v_add_f32_e64 v160, v164, v160
	v_add_f32_e64 v161, v165, v161
	v_mul_f32_e64 v146, v146, v150
	v_mul_f32_e64 v147, v147, v151
	v_mul_f32_e64 v144, v144, v148
	v_mul_f32_e64 v145, v145, v149
	flat_store_dwordx2 v[136:137], v[28:29]
	v_mul_f32_e64 v28, v34, v134
	v_mul_f32_e64 v29, v35, v134
	v_mul_f32_e64 v30, v32, v134
	v_mul_f32_e64 v31, v33, v134
	v_add_f32_e64 v178, v178, 1.0
	v_add_f32_e64 v179, v179, 1.0
	v_add_f32_e64 v176, v176, 1.0
	v_add_f32_e64 v177, v177, 1.0
	v_fma_f32 v28, v146, v28, v162
	v_fma_f32 v29, v147, v29, v163
	v_fma_f32 v30, v144, v30, v160
	v_fma_f32 v31, v145, v31, v161
	v_add_f32_e64 v174, v178, v174
	v_add_f32_e64 v175, v179, v175
	v_add_f32_e64 v172, v176, v172
	v_add_f32_e64 v173, v177, v173
	v_cvt_pk_bf16_f32 v30, v30, v31
	v_cvt_pk_bf16_f32 v31, v28, v29
	v_add_f32_e64 v182, v182, v190
	v_add_f32_e64 v183, v183, v191
	v_add_f32_e64 v180, v180, v188
	v_add_f32_e64 v181, v181, v189
	v_mul_f32_e64 v170, v170, v174
	v_mul_f32_e64 v171, v171, v175
	v_mul_f32_e64 v168, v168, v172
	v_mul_f32_e64 v169, v169, v173
	flat_store_dwordx2 v[136:137], v[30:31] offset:32
	v_mul_f32_e64 v28, v42, v134
	v_mul_f32_e64 v29, v43, v134
	v_mul_f32_e64 v30, v40, v134
	v_mul_f32_e64 v31, v41, v134
	v_add_f32_e64 v198, v198, 1.0
	v_add_f32_e64 v199, v199, 1.0
	v_add_f32_e64 v196, v196, 1.0
	v_add_f32_e64 v197, v197, 1.0
	v_fma_f32 v28, v170, v28, v182
	v_fma_f32 v29, v171, v29, v183
	v_fma_f32 v30, v168, v30, v180
	v_fma_f32 v31, v169, v31, v181
	v_add_f32_e64 v194, v198, v194
	v_add_f32_e64 v195, v199, v195
	v_add_f32_e64 v192, v196, v192
	v_add_f32_e64 v193, v197, v193
	v_cvt_pk_bf16_f32 v30, v30, v31
	v_cvt_pk_bf16_f32 v31, v28, v29
	v_add_f32_e64 v202, v202, v206
	v_add_f32_e64 v203, v203, v207
	v_add_f32_e64 v200, v200, v204
	v_add_f32_e64 v201, v201, v205
	v_mul_f32_e64 v186, v186, v194
	v_mul_f32_e64 v187, v187, v195
	v_mul_f32_e64 v184, v184, v192
	v_mul_f32_e64 v185, v185, v193
	flat_store_dwordx2 v[136:137], v[30:31] offset:256
	v_mul_f32_e64 v28, v50, v134
	v_mul_f32_e64 v29, v51, v134
	v_mul_f32_e64 v30, v48, v134
	v_mul_f32_e64 v31, v49, v134
	v_fma_f32 v28, v186, v28, v202
	v_fma_f32 v29, v187, v29, v203
	v_fma_f32 v30, v184, v30, v200
	v_fma_f32 v31, v185, v31, v201
	s_andn2_b64 vcc, exec, s[0:1]
	v_cvt_pk_bf16_f32 v30, v30, v31
	v_cvt_pk_bf16_f32 v31, v28, v29
	flat_store_dwordx2 v[136:137], v[30:31] offset:288
	v_lshl_add_u32 v28, v248, 2, s2
	ds_read_b32 v28, v28
	v_lshlrev_b64 v[30:31], 11, v[220:221]
	v_lshl_add_u64 v[30:31], v[132:133], 0, v[30:31]
	s_waitcnt lgkmcnt(0)
	v_mul_f32_e64 v32, v58, v28
	v_mul_f32_e64 v33, v59, v28
	v_mul_f32_e64 v34, v56, v28
	v_mul_f32_e64 v35, v57, v28
	v_fma_f32 v32, v128, v32, v142
	v_fma_f32 v33, v129, v33, v143
	v_fma_f32 v34, v130, v34, v140
	v_fma_f32 v35, v131, v35, v141
	s_nop 0
	v_cvt_pk_bf16_f32 v34, v34, v35
	v_cvt_pk_bf16_f32 v35, v32, v33
	flat_store_dwordx2 v[30:31], v[34:35]
	v_mul_f32_e64 v32, v66, v28
	v_mul_f32_e64 v33, v67, v28
	v_mul_f32_e64 v34, v64, v28
	v_mul_f32_e64 v35, v65, v28
	v_fma_f32 v32, v146, v32, v162
	v_fma_f32 v33, v147, v33, v163
	v_fma_f32 v34, v144, v34, v160
	v_fma_f32 v35, v145, v35, v161
	s_nop 0
	v_cvt_pk_bf16_f32 v34, v34, v35
	v_cvt_pk_bf16_f32 v35, v32, v33
	flat_store_dwordx2 v[30:31], v[34:35] offset:32
	v_mul_f32_e64 v32, v74, v28
	v_mul_f32_e64 v33, v75, v28
	v_mul_f32_e64 v34, v72, v28
	v_mul_f32_e64 v35, v73, v28
	v_fma_f32 v32, v170, v32, v182
	v_fma_f32 v33, v171, v33, v183
	v_fma_f32 v34, v168, v34, v180
	v_fma_f32 v35, v169, v35, v181
	s_nop 0
	v_cvt_pk_bf16_f32 v34, v34, v35
	v_cvt_pk_bf16_f32 v35, v32, v33
	v_mul_f32_e64 v32, v82, v28
	v_mul_f32_e64 v33, v83, v28
	v_mul_f32_e64 v29, v81, v28
	v_mul_f32_e64 v28, v80, v28
	v_fma_f32 v32, v186, v32, v202
	v_fma_f32 v33, v187, v33, v203
	v_fma_f32 v28, v184, v28, v200
	v_fma_f32 v29, v185, v29, v201
	flat_store_dwordx2 v[30:31], v[34:35] offset:256
	v_cvt_pk_bf16_f32 v28, v28, v29
	v_cvt_pk_bf16_f32 v29, v32, v33
	flat_store_dwordx2 v[30:31], v[28:29] offset:288
	v_lshl_add_u32 v28, v249, 2, s2
	ds_read_b32 v28, v28
	v_lshlrev_b64 v[30:31], 11, v[222:223]
	v_lshl_add_u64 v[30:31], v[132:133], 0, v[30:31]
	s_waitcnt lgkmcnt(0)
	v_mul_f32_e64 v32, v90, v28
	v_mul_f32_e64 v33, v91, v28
	v_mul_f32_e64 v34, v88, v28
	v_mul_f32_e64 v35, v89, v28
	v_fma_f32 v32, v128, v32, v142
	v_fma_f32 v33, v129, v33, v143
	v_fma_f32 v34, v130, v34, v140
	v_fma_f32 v35, v131, v35, v141
	s_nop 0
	v_cvt_pk_bf16_f32 v34, v34, v35
	v_cvt_pk_bf16_f32 v35, v32, v33
	flat_store_dwordx2 v[30:31], v[34:35]
	v_mul_f32_e64 v32, v94, v28
	v_mul_f32_e64 v33, v95, v28
	v_mul_f32_e64 v34, v92, v28
	v_mul_f32_e64 v35, v93, v28
	v_fma_f32 v32, v146, v32, v162
	v_fma_f32 v33, v147, v33, v163
	v_fma_f32 v34, v144, v34, v160
	v_fma_f32 v35, v145, v35, v161
	s_nop 0
	v_cvt_pk_bf16_f32 v34, v34, v35
	v_cvt_pk_bf16_f32 v35, v32, v33
	flat_store_dwordx2 v[30:31], v[34:35] offset:32
	v_mul_f32_e64 v32, v102, v28
	v_mul_f32_e64 v33, v103, v28
	v_mul_f32_e64 v34, v100, v28
	v_mul_f32_e64 v35, v101, v28
	v_fma_f32 v32, v170, v32, v182
	v_fma_f32 v33, v171, v33, v183
	v_fma_f32 v34, v168, v34, v180
	v_fma_f32 v35, v169, v35, v181
	s_nop 0
	v_cvt_pk_bf16_f32 v34, v34, v35
	v_cvt_pk_bf16_f32 v35, v32, v33
	v_mul_f32_e64 v32, v110, v28
	v_mul_f32_e64 v33, v111, v28
	v_mul_f32_e64 v29, v109, v28
	v_mul_f32_e64 v28, v108, v28
	v_fma_f32 v32, v186, v32, v202
	v_fma_f32 v33, v187, v33, v203
	v_fma_f32 v28, v184, v28, v200
	v_fma_f32 v29, v185, v29, v201
	flat_store_dwordx2 v[30:31], v[34:35] offset:256
	v_cvt_pk_bf16_f32 v28, v28, v29
	v_cvt_pk_bf16_f32 v29, v32, v33
	flat_store_dwordx2 v[30:31], v[28:29] offset:288
	v_lshl_add_u32 v28, v237, 2, s2
	ds_read_b32 v28, v28
	v_lshlrev_b64 v[30:31], 11, v[224:225]
	v_lshl_add_u64 v[30:31], v[132:133], 0, v[30:31]
	s_mov_b64 s[2:3], -1
	s_waitcnt lgkmcnt(0)
	v_mul_f32_e64 v32, v118, v28
	v_mul_f32_e64 v33, v119, v28
	v_mul_f32_e64 v34, v116, v28
	v_mul_f32_e64 v35, v117, v28
	v_fma_f32 v32, v128, v32, v142
	v_fma_f32 v33, v129, v33, v143
	v_fma_f32 v34, v130, v34, v140
	v_fma_f32 v35, v131, v35, v141
	s_nop 0
	v_cvt_pk_bf16_f32 v34, v34, v35
	v_cvt_pk_bf16_f32 v35, v32, v33
	flat_store_dwordx2 v[30:31], v[34:35]
	v_mul_f32_e64 v32, v122, v28
	v_mul_f32_e64 v33, v123, v28
	v_mul_f32_e64 v34, v120, v28
	v_mul_f32_e64 v35, v121, v28
	v_fma_f32 v32, v146, v32, v162
	v_fma_f32 v33, v147, v33, v163
	v_fma_f32 v34, v144, v34, v160
	v_fma_f32 v35, v145, v35, v161
	s_nop 0
	v_cvt_pk_bf16_f32 v34, v34, v35
	v_cvt_pk_bf16_f32 v35, v32, v33
	flat_store_dwordx2 v[30:31], v[34:35] offset:32
	v_mul_f32_e64 v32, v126, v28
	v_mul_f32_e64 v33, v127, v28
	v_mul_f32_e64 v34, v124, v28
	v_mul_f32_e64 v35, v125, v28
	v_fma_f32 v32, v170, v32, v182
	v_fma_f32 v33, v171, v33, v183
	v_fma_f32 v34, v168, v34, v180
	v_fma_f32 v35, v169, v35, v181
	s_nop 0
	v_cvt_pk_bf16_f32 v34, v34, v35
	v_cvt_pk_bf16_f32 v35, v32, v33
	v_mul_f32_e64 v32, v114, v28
	v_mul_f32_e64 v33, v115, v28
	v_mul_f32_e64 v29, v113, v28
	v_mul_f32_e64 v28, v112, v28
	v_fma_f32 v32, v186, v32, v202
	v_fma_f32 v33, v187, v33, v203
	v_fma_f32 v28, v184, v28, v200
	v_fma_f32 v29, v185, v29, v201
	flat_store_dwordx2 v[30:31], v[34:35] offset:256
	v_cvt_pk_bf16_f32 v28, v28, v29
	v_cvt_pk_bf16_f32 v29, v32, v33
	flat_store_dwordx2 v[30:31], v[28:29] offset:288
	ds_read_b32 v28, v135 offset:512
	v_lshlrev_b64 v[30:31], 11, v[226:227]
	v_lshl_add_u64 v[30:31], v[132:133], 0, v[30:31]
	s_waitcnt lgkmcnt(0)
	v_mul_f32_e64 v32, v106, v28
	v_mul_f32_e64 v33, v107, v28
	v_mul_f32_e64 v34, v104, v28
	v_mul_f32_e64 v35, v105, v28
	v_fma_f32 v32, v128, v32, v142
	v_fma_f32 v33, v129, v33, v143
	v_fma_f32 v34, v130, v34, v140
	v_fma_f32 v35, v131, v35, v141
	s_nop 0
	v_cvt_pk_bf16_f32 v34, v34, v35
	v_cvt_pk_bf16_f32 v35, v32, v33
	flat_store_dwordx2 v[30:31], v[34:35]
	v_mul_f32_e64 v32, v98, v28
	v_mul_f32_e64 v33, v99, v28
	v_mul_f32_e64 v34, v96, v28
	v_mul_f32_e64 v35, v97, v28
	v_fma_f32 v32, v146, v32, v162
	v_fma_f32 v33, v147, v33, v163
	v_fma_f32 v34, v144, v34, v160
	v_fma_f32 v35, v145, v35, v161
	s_nop 0
	v_cvt_pk_bf16_f32 v34, v34, v35
	v_cvt_pk_bf16_f32 v35, v32, v33
	flat_store_dwordx2 v[30:31], v[34:35] offset:32
	v_mul_f32_e64 v32, v86, v28
	v_mul_f32_e64 v33, v87, v28
	v_mul_f32_e64 v34, v84, v28
	v_mul_f32_e64 v35, v85, v28
	v_fma_f32 v32, v170, v32, v182
	v_fma_f32 v33, v171, v33, v183
	v_fma_f32 v34, v168, v34, v180
	v_fma_f32 v35, v169, v35, v181
	s_nop 0
	v_cvt_pk_bf16_f32 v34, v34, v35
	v_cvt_pk_bf16_f32 v35, v32, v33
	v_mul_f32_e64 v32, v78, v28
	v_mul_f32_e64 v33, v79, v28
	v_mul_f32_e64 v29, v77, v28
	v_mul_f32_e64 v28, v76, v28
	v_fma_f32 v32, v186, v32, v202
	v_fma_f32 v33, v187, v33, v203
	v_fma_f32 v28, v184, v28, v200
	v_fma_f32 v29, v185, v29, v201
	flat_store_dwordx2 v[30:31], v[34:35] offset:256
	v_cvt_pk_bf16_f32 v28, v28, v29
	v_cvt_pk_bf16_f32 v29, v32, v33
	flat_store_dwordx2 v[30:31], v[28:29] offset:288
	ds_read_b32 v28, v135 offset:576
	v_lshlrev_b64 v[30:31], 11, v[228:229]
	v_lshl_add_u64 v[30:31], v[132:133], 0, v[30:31]
	s_waitcnt lgkmcnt(0)
	v_mul_f32_e64 v32, v70, v28
	v_mul_f32_e64 v33, v71, v28
	v_mul_f32_e64 v34, v68, v28
	v_mul_f32_e64 v35, v69, v28
	v_fma_f32 v32, v128, v32, v142
	v_fma_f32 v33, v129, v33, v143
	v_fma_f32 v34, v130, v34, v140
	v_fma_f32 v35, v131, v35, v141
	s_nop 0
	v_cvt_pk_bf16_f32 v34, v34, v35
	v_cvt_pk_bf16_f32 v35, v32, v33
	flat_store_dwordx2 v[30:31], v[34:35]
	v_mul_f32_e64 v32, v62, v28
	v_mul_f32_e64 v33, v63, v28
	v_mul_f32_e64 v34, v60, v28
	v_mul_f32_e64 v35, v61, v28
	v_fma_f32 v32, v146, v32, v162
	v_fma_f32 v33, v147, v33, v163
	v_fma_f32 v34, v144, v34, v160
	v_fma_f32 v35, v145, v35, v161
	s_nop 0
	v_cvt_pk_bf16_f32 v34, v34, v35
	v_cvt_pk_bf16_f32 v35, v32, v33
	flat_store_dwordx2 v[30:31], v[34:35] offset:32
	v_mul_f32_e64 v32, v54, v28
	v_mul_f32_e64 v33, v55, v28
	v_mul_f32_e64 v34, v52, v28
	v_mul_f32_e64 v35, v53, v28
	v_fma_f32 v32, v170, v32, v182
	v_fma_f32 v33, v171, v33, v183
	v_fma_f32 v34, v168, v34, v180
	v_fma_f32 v35, v169, v35, v181
	s_nop 0
	v_cvt_pk_bf16_f32 v34, v34, v35
	v_cvt_pk_bf16_f32 v35, v32, v33
	v_mul_f32_e64 v32, v46, v28
	v_mul_f32_e64 v33, v47, v28
	v_mul_f32_e64 v29, v45, v28
	v_mul_f32_e64 v28, v44, v28
	v_fma_f32 v32, v186, v32, v202
	v_fma_f32 v33, v187, v33, v203
	v_fma_f32 v28, v184, v28, v200
	v_fma_f32 v29, v185, v29, v201
	flat_store_dwordx2 v[30:31], v[34:35] offset:256
	v_cvt_pk_bf16_f32 v28, v28, v29
	v_cvt_pk_bf16_f32 v29, v32, v33
	flat_store_dwordx2 v[30:31], v[28:29] offset:288
	ds_read_b32 v28, v135 offset:640
	v_lshlrev_b64 v[30:31], 11, v[230:231]
	v_lshl_add_u64 v[30:31], v[132:133], 0, v[30:31]
	s_waitcnt lgkmcnt(0)
	v_mul_f32_e64 v32, v38, v28
	v_mul_f32_e64 v33, v39, v28
	v_mul_f32_e64 v34, v36, v28
	v_mul_f32_e64 v35, v37, v28
	v_mul_f32_e64 v26, v26, v28
	v_mul_f32_e64 v27, v27, v28
	v_mul_f32_e64 v24, v24, v28
	v_mul_f32_e64 v25, v25, v28
	v_mul_f32_e64 v22, v22, v28
	v_mul_f32_e64 v23, v23, v28
	v_mul_f32_e64 v20, v20, v28
	v_mul_f32_e64 v21, v21, v28
	v_mul_f32_e64 v18, v18, v28
	v_mul_f32_e64 v19, v19, v28
	v_mul_f32_e64 v16, v16, v28
	v_mul_f32_e64 v17, v17, v28
	v_fma_f32 v32, v128, v32, v142
	v_fma_f32 v33, v129, v33, v143
	v_fma_f32 v34, v130, v34, v140
	v_fma_f32 v35, v131, v35, v141
	v_fma_f32 v26, v146, v26, v162
	v_fma_f32 v27, v147, v27, v163
	v_fma_f32 v24, v144, v24, v160
	v_fma_f32 v25, v145, v25, v161
	v_fma_f32 v22, v170, v22, v182
	v_fma_f32 v23, v171, v23, v183
	v_fma_f32 v20, v168, v20, v180
	v_fma_f32 v21, v169, v21, v181
	v_fma_f32 v18, v186, v18, v202
	v_fma_f32 v19, v187, v19, v203
	v_fma_f32 v16, v184, v16, v200
	v_fma_f32 v17, v185, v17, v201
	v_cvt_pk_bf16_f32 v34, v34, v35
	v_cvt_pk_bf16_f32 v35, v32, v33
	v_cvt_pk_bf16_f32 v24, v24, v25
	v_cvt_pk_bf16_f32 v25, v26, v27
	v_cvt_pk_bf16_f32 v20, v20, v21
	v_cvt_pk_bf16_f32 v21, v22, v23
	v_cvt_pk_bf16_f32 v16, v16, v17
	v_cvt_pk_bf16_f32 v17, v18, v19
	flat_store_dwordx2 v[30:31], v[34:35]
	flat_store_dwordx2 v[30:31], v[24:25] offset:32
	flat_store_dwordx2 v[30:31], v[20:21] offset:256
	flat_store_dwordx2 v[30:31], v[16:17] offset:288
	ds_read_b32 v16, v135 offset:704
	v_lshlrev_b64 v[18:19], 11, v[232:233]
	v_lshl_add_u64 v[18:19], v[132:133], 0, v[18:19]
	s_waitcnt lgkmcnt(0)
	v_mul_f32_e64 v14, v14, v16
	v_mul_f32_e64 v15, v15, v16
	v_mul_f32_e64 v12, v12, v16
	v_mul_f32_e64 v13, v13, v16
	v_mul_f32_e64 v10, v10, v16
	v_mul_f32_e64 v11, v11, v16
	v_mul_f32_e64 v8, v8, v16
	v_mul_f32_e64 v9, v9, v16
	v_mul_f32_e64 v6, v6, v16
	v_mul_f32_e64 v7, v7, v16
	v_mul_f32_e64 v4, v4, v16
	v_mul_f32_e64 v5, v5, v16
	v_mul_f32_e64 v2, v2, v16
	v_mul_f32_e64 v3, v3, v16
	v_mul_f32_e64 v0, v0, v16
	v_mul_f32_e64 v1, v1, v16
	v_fma_f32 v14, v128, v14, v142
	v_fma_f32 v15, v129, v15, v143
	v_fma_f32 v12, v130, v12, v140
	v_fma_f32 v13, v131, v13, v141
	v_fma_f32 v10, v146, v10, v162
	v_fma_f32 v11, v147, v11, v163
	v_fma_f32 v8, v144, v8, v160
	v_fma_f32 v9, v145, v9, v161
	v_fma_f32 v6, v170, v6, v182
	v_fma_f32 v7, v171, v7, v183
	v_fma_f32 v4, v168, v4, v180
	v_fma_f32 v5, v169, v5, v181
	v_fma_f32 v2, v186, v2, v202
	v_fma_f32 v3, v187, v3, v203
	v_fma_f32 v0, v184, v0, v200
	v_fma_f32 v1, v185, v1, v201
	v_cvt_pk_bf16_f32 v12, v12, v13
	v_cvt_pk_bf16_f32 v13, v14, v15
	v_cvt_pk_bf16_f32 v8, v8, v9
	v_cvt_pk_bf16_f32 v9, v10, v11
	v_cvt_pk_bf16_f32 v4, v4, v5
	v_cvt_pk_bf16_f32 v5, v6, v7
	v_cvt_pk_bf16_f32 v0, v0, v1
	v_cvt_pk_bf16_f32 v1, v2, v3
	flat_store_dwordx2 v[18:19], v[12:13]
	flat_store_dwordx2 v[18:19], v[8:9] offset:32
	flat_store_dwordx2 v[18:19], v[4:5] offset:256
	flat_store_dwordx2 v[18:19], v[0:1] offset:288
	s_cbranch_vccnz .LBB0_1638
	s_andn2_b64 vcc, exec, s[20:21]
	s_cbranch_vccnz .LBB0_1637
	s_barrier
	s_branch .LBB0_1637

.LBB0_1742:
	s_ashr_i32 s7, s6, 31
	s_lshl_b64 s[22:23], s[6:7], 2
	s_add_u32 s24, s5, s22
	s_addc_u32 s25, s17, s23
	global_load_dwordx2 v[60:61], v49, s[24:25]
	s_add_u32 s24, s18, s22
	s_addc_u32 s25, s19, s23
	global_load_dword v59, v49, s[24:25]
	s_add_u32 s22, s20, s22
	s_addc_u32 s23, s21, s23
	s_waitcnt vmcnt(1)
	v_readfirstlane_b32 s26, v60
	s_cmp_eq_u32 s26, 1
	global_load_dword v60, v49, s[22:23]
	s_cselect_b32 s22, s11, 0
	s_cmp_eq_u32 s26, 2
	s_cselect_b32 s22, s12, s22
	s_cmp_eq_u32 s26, 3
	s_cselect_b32 s22, s13, s22
	s_cmp_eq_u32 s26, 4
	s_cselect_b32 s22, s14, s22
	s_cmp_eq_u32 s26, 5
	s_cselect_b32 s22, s15, s22
	s_cmp_eq_u32 s26, 6
	v_readfirstlane_b32 s7, v61
	s_cselect_b64 vcc, -1, 0
	v_mov_b32_e32 v61, s22
	s_cmp_eq_u32 s26, 7
	v_cndmask_b32_e32 v61, v61, v57, vcc
	s_cselect_b64 vcc, -1, 0
	v_cndmask_b32_e32 v61, v61, v58, vcc
	s_waitcnt vmcnt(1)
	v_add_u32_e32 v62, v61, v59
	v_ashrrev_i32_e32 v63, 31, v62
	v_lshlrev_b64 v[62:63], 11, v[62:63]
	v_lshl_add_u64 v[62:63], v[50:51], 0, v[62:63]
	global_load_dwordx2 v[64:65], v[62:63], off
	s_add_i32 s22, s6, 1
	s_ashr_i32 s23, s22, 31
	s_lshl_b64 s[22:23], s[22:23], 2
	s_add_u32 s24, s18, s22
	s_addc_u32 s25, s19, s23
	global_load_dword v59, v49, s[24:25]
	s_add_u32 s22, s20, s22
	s_addc_u32 s23, s21, s23
	s_cmp_eq_u32 s7, 1
	s_waitcnt vmcnt(2)
	v_mul_f32_e64 v66, v2, v60
	v_mul_f32_e64 v67, v3, v60
	v_mul_f32_e64 v68, v0, v60
	v_mul_f32_e64 v69, v1, v60
	s_waitcnt vmcnt(1)
	v_lshlrev_b32_e32 v70, 16, v64
	v_and_b32_e32 v71, 0xffff0000, v64
	v_lshlrev_b32_e32 v64, 16, v65
	v_and_b32_e32 v65, 0xffff0000, v65
	v_fma_f32 v46, v66, v64, v46
	v_fma_f32 v47, v67, v65, v47
	global_load_dwordx2 v[64:65], v[62:63], off offset:512
	v_fma_f32 v44, v68, v70, v44
	v_fma_f32 v45, v69, v71, v45
	v_mul_f32_e64 v66, v6, v60
	v_mul_f32_e64 v67, v7, v60
	v_mul_f32_e64 v68, v4, v60
	v_mul_f32_e64 v69, v5, v60
	s_waitcnt vmcnt(0)
	v_lshlrev_b32_e32 v70, 16, v64
	v_and_b32_e32 v71, 0xffff0000, v64
	v_lshlrev_b32_e32 v64, 16, v65
	v_and_b32_e32 v65, 0xffff0000, v65
	v_fma_f32 v42, v66, v64, v42
	v_fma_f32 v43, v67, v65, v43
	global_load_dwordx2 v[64:65], v[62:63], off offset:1024
	v_fma_f32 v40, v68, v70, v40
	v_fma_f32 v41, v69, v71, v41
	global_load_dwordx2 v[62:63], v[62:63], off offset:1536
	v_mul_f32_e64 v66, v10, v60
	v_mul_f32_e64 v67, v11, v60
	v_mul_f32_e64 v68, v8, v60
	v_mul_f32_e64 v69, v9, v60
	s_waitcnt vmcnt(1)
	v_lshlrev_b32_e32 v70, 16, v64
	v_and_b32_e32 v71, 0xffff0000, v64
	v_lshlrev_b32_e32 v64, 16, v65
	v_and_b32_e32 v65, 0xffff0000, v65
	v_fma_f32 v38, v66, v64, v38
	v_fma_f32 v39, v67, v65, v39
	v_mul_f32_e64 v64, v14, v60
	v_mul_f32_e64 v65, v15, v60
	v_mul_f32_e64 v61, v13, v60
	v_mul_f32_e64 v60, v12, v60
	s_waitcnt vmcnt(0)
	v_lshlrev_b32_e32 v66, 16, v62
	v_and_b32_e32 v67, 0xffff0000, v62
	v_fma_f32 v32, v60, v66, v32
	v_fma_f32 v33, v61, v67, v33
	global_load_dword v60, v49, s[22:23]
	s_cselect_b32 s22, s11, 0
	s_cmp_eq_u32 s7, 2
	s_cselect_b32 s22, s12, s22
	s_cmp_eq_u32 s7, 3
	s_cselect_b32 s22, s13, s22
	s_cmp_eq_u32 s7, 4
	s_cselect_b32 s22, s14, s22
	s_cmp_eq_u32 s7, 5
	s_cselect_b32 s22, s15, s22
	s_cmp_eq_u32 s7, 6
	s_cselect_b64 vcc, -1, 0
	v_mov_b32_e32 v61, s22
	s_cmp_eq_u32 s7, 7
	v_cndmask_b32_e32 v61, v61, v57, vcc
	s_cselect_b64 vcc, -1, 0
	v_lshlrev_b32_e32 v62, 16, v63
	v_and_b32_e32 v63, 0xffff0000, v63
	v_cndmask_b32_e32 v61, v61, v58, vcc
	v_fma_f32 v34, v64, v62, v34
	v_fma_f32 v35, v65, v63, v35
	v_add_u32_e32 v62, v61, v59
	v_ashrrev_i32_e32 v63, 31, v62
	v_lshlrev_b64 v[62:63], 11, v[62:63]
	v_lshl_add_u64 v[62:63], v[50:51], 0, v[62:63]
	global_load_dwordx2 v[64:65], v[62:63], off
	v_fma_f32 v36, v68, v70, v36
	v_fma_f32 v37, v69, v71, v37
	s_add_i32 s6, s6, 2
	s_andn2_b64 vcc, exec, s[8:9]
	s_waitcnt vmcnt(1)
	v_mul_f32_e64 v68, v2, v60
	v_mul_f32_e64 v69, v3, v60
	v_mul_f32_e64 v66, v0, v60
	v_mul_f32_e64 v67, v1, v60
	s_waitcnt vmcnt(0)
	v_lshlrev_b32_e32 v70, 16, v64
	v_and_b32_e32 v71, 0xffff0000, v64
	v_lshlrev_b32_e32 v64, 16, v65
	v_and_b32_e32 v65, 0xffff0000, v65
	v_fma_f32 v46, v68, v64, v46
	v_fma_f32 v47, v69, v65, v47
	global_load_dwordx2 v[64:65], v[62:63], off offset:512
	v_fma_f32 v44, v66, v70, v44
	v_fma_f32 v45, v67, v71, v45
	v_mul_f32_e64 v68, v6, v60
	v_mul_f32_e64 v69, v7, v60
	v_mul_f32_e64 v66, v4, v60
	v_mul_f32_e64 v67, v5, v60
	s_waitcnt vmcnt(0)
	v_lshlrev_b32_e32 v70, 16, v64
	v_and_b32_e32 v71, 0xffff0000, v64
	v_lshlrev_b32_e32 v64, 16, v65
	v_and_b32_e32 v65, 0xffff0000, v65
	v_fma_f32 v42, v68, v64, v42
	v_fma_f32 v43, v69, v65, v43
	global_load_dwordx2 v[64:65], v[62:63], off offset:1024
	v_fma_f32 v40, v66, v70, v40
	v_fma_f32 v41, v67, v71, v41
	global_load_dwordx2 v[62:63], v[62:63], off offset:1536
	v_mul_f32_e64 v66, v8, v60
	v_mul_f32_e64 v67, v9, v60
	v_mul_f32_e64 v68, v10, v60
	v_mul_f32_e64 v69, v11, v60
	s_waitcnt vmcnt(1)
	v_lshlrev_b32_e32 v70, 16, v64
	v_and_b32_e32 v71, 0xffff0000, v64
	v_lshlrev_b32_e32 v64, 16, v65
	v_and_b32_e32 v65, 0xffff0000, v65
	v_fma_f32 v38, v68, v64, v38
	v_fma_f32 v39, v69, v65, v39
	v_fma_f32 v36, v66, v70, v36
	v_fma_f32 v37, v67, v71, v37
	v_mul_f32_e64 v64, v12, v60
	v_mul_f32_e64 v65, v13, v60
	v_mul_f32_e64 v61, v15, v60
	v_mul_f32_e64 v60, v14, v60
	s_waitcnt vmcnt(0)
	v_lshlrev_b32_e32 v66, 16, v62
	v_and_b32_e32 v67, 0xffff0000, v62
	v_lshlrev_b32_e32 v62, 16, v63
	v_and_b32_e32 v63, 0xffff0000, v63
	v_fma_f32 v34, v60, v62, v34
	v_fma_f32 v35, v61, v63, v35
	v_fma_f32 v32, v64, v66, v32
	v_fma_f32 v33, v65, v67, v33
	global_store_dwordx4 v[54:55], v[44:47], off offset:-4096
	global_store_dwordx4 v[54:55], v[40:43], off offset:-3072
	global_store_dwordx4 v[54:55], v[36:39], off offset:-2048
	global_store_dwordx4 v[54:55], v[32:35], off offset:-1024
	v_mov_b64_e32 v[42:43], v[22:23]
	v_mov_b64_e32 v[38:39], v[26:27]
	v_mov_b64_e32 v[34:35], v[30:31]
	v_mov_b64_e32 v[46:47], v[18:19]
	v_lshl_add_u64 v[54:55], v[54:55], 0, s[0:1]
	v_mov_b64_e32 v[32:33], v[28:29]
	v_mov_b64_e32 v[36:37], v[24:25]
	v_mov_b64_e32 v[40:41], v[20:21]
	v_mov_b64_e32 v[44:45], v[16:17]
	s_cbranch_vccz .LBB0_1747
.LBB0_1743:
	s_ashr_i32 s7, s4, 31
	s_lshr_b32 s7, s7, 20
	s_add_i32 s7, s4, s7
	s_ashr_i32 s7, s7, 12
	s_cmp_eq_u32 s7, s16
	s_cbranch_scc1 .LBB0_1745
	s_mul_i32 s8, s7, 0x1800
	s_ashr_i32 s9, s8, 31
	s_lshl_b64 s[8:9], s[8:9], 2
	s_add_u32 s8, s2, s8
	s_addc_u32 s9, s3, s9
	v_lshl_add_u64 v[0:1], s[8:9], 0, v[48:49]
	s_mov_b64 s[8:9], 0x105000
	v_lshl_add_u64 v[16:17], v[0:1], 0, s[8:9]
	v_add_co_u32_e32 v0, vcc, 0x105000, v0
	s_mov_b32 s16, s7
	s_nop 0
	v_addc_co_u32_e32 v1, vcc, 0, v1, vcc
	global_load_dwordx4 v[0:3], v[0:1], off
	s_nop 0
	global_load_dwordx4 v[4:7], v[52:53], off
	s_waitcnt vmcnt(0)
	v_add_f32_e64 v2, v2, v6
	v_add_f32_e64 v3, v3, v7
	v_add_f32_e64 v0, v0, v4
	v_add_f32_e64 v1, v1, v5
	global_load_dwordx4 v[4:7], v[16:17], off offset:1024
	global_load_dwordx4 v[8:11], v[52:53], off offset:1024
	s_waitcnt vmcnt(0)
	v_add_f32_e64 v6, v6, v10
	v_add_f32_e64 v7, v7, v11
	v_add_f32_e64 v4, v4, v8
	v_add_f32_e64 v5, v5, v9
	global_load_dwordx4 v[8:11], v[16:17], off offset:2048
	global_load_dwordx4 v[12:15], v[52:53], off offset:2048
	s_waitcnt vmcnt(0)
	v_add_f32_e64 v10, v10, v14
	v_add_f32_e64 v11, v11, v15
	v_add_f32_e64 v8, v8, v12
	v_add_f32_e64 v9, v9, v13
	global_load_dwordx4 v[12:15], v[16:17], off offset:3072
	s_nop 0
	global_load_dwordx4 v[16:19], v[52:53], off offset:3072
	s_waitcnt vmcnt(0)
	v_add_f32_e64 v14, v14, v18
	v_add_f32_e64 v15, v15, v19
	v_add_f32_e64 v12, v12, v16
	v_add_f32_e64 v13, v13, v17
